# all GEMM epilogue stores nontemporal + deeper epilogue prefetch
# baseline (speedup 1.0000x reference)
; template <class Epi, class Sched, bool GATHER, bool ALIGN_EPI = true, bool SP2 = true, bool REMAP64 = false>
; __device__ __forceinline__ void gemm_phase(LAS unsigned char* lds, const bf16* Ag, const bf16* Btg, const int K, const Sched& S, const Epi& E) {
;     ...
;             constexpr bool RP = REMAP64 && Epi::ROWPAIR;
;             const bool hi = RP && (fr >= 8); const int rsh = hi ? -8 : 0, citx = hi ? cit + 32 : cit;
;             typename Epi::Pre pq[2];
;             { const int r0_ = wr * 64 + fr; pq[0] = E.pre(cur, (r0_ < cur.nrows ? r0_ : cur.nrows - 1) + rsh, citx); }
; #pragma unroll
;             for (int gq = 0; gq < 8; ++gq) { const int ai = gq >> 2, m = gq & 3, r = ai * HALF + wr * 64 + m * 16 + fr;
;                 if (gq + 1 < 8) { const int rn = ((gq + 1) >> 2) * HALF + wr * 64 + ((gq + 1) & 3) * 16 + fr; pq[(gq + 1) & 1] = E.pre(cur, (rn < cur.nrows ? rn : cur.nrows - 1) + rsh, citx); }
;                 __builtin_amdgcn_sched_barrier(0);
;                 if (r < cur.nrows) { float v0[8], v1[8];
; #pragma unroll
;                     for (int i = 0; i < 4; ++i) { v0[i] = acc[ai][0][m][0][i]; v0[4 + i] = acc[ai][0][m][1][i]; v1[i] = acc[ai][1][m][0][i]; v1[4 + i] = acc[ai][1][m][1][i]; }
;                     if constexpr (RP) {
; #pragma unroll
;                         for (int i = 0; i < 8; ++i) { const float snd = hi ? v0[i] : v1[i];
;                             const float rcv = __builtin_bit_cast(float, __builtin_amdgcn_update_dpp(0, __builtin_bit_cast(int, snd), 0x128, 0xf, 0xf, false));
;                             if (hi) v0[i] = rcv; else v1[i] = rcv; } }
;                     E.post(cur, r + rsh, citx, v0, v1, pq[gq & 1]); }
;                 __builtin_amdgcn_sched_barrier(0); }
;     __device__ __forceinline__ Pre pre(const Unit& u, int r, int cit) const { const size_t off = (size_t)(u.arow0 + r) * D + u.pn * 256 + cit; return Pre{__builtin_nontemporal_load((const v4u*)(gp + off)), __builtin_nontemporal_load((const v4u*)(gp + off + (size_t)8 * D))}; }
;     __device__ __forceinline__ void post(const Unit& u, int r, int cit, const float* v0, const float* v1, const Pre& p) const {
;         const size_t off = (size_t)(u.arow0 + r) * D + u.pn * 256 + cit; float g0[8], g1[8], a[8], b[8]; unpack8bf(p.g0, g0); unpack8bf(p.g1, g1);
; #pragma unroll
;         for (int i = 0; i < 8; ++i) { a[i] = g0[i] * v0[i]; b[i] = g1[i] * v1[i]; }
.LBB0_950:
	v_add_u32_e32 v130, s10, v176
	v_ashrrev_i32_e32 v131, 31, v130
	s_lshl_b32 s54, s52, 8
	s_ashr_i32 s55, s54, 31
	v_lshlrev_b64 v[130:131], 12, v[130:131]
	v_lshl_add_u64 v[130:131], s[48:49], 0, v[130:131]
	s_lshl_b64 s[54:55], s[54:55], 1
	v_lshl_add_u64 v[130:131], v[130:131], 0, s[54:55]
	v_lshl_add_u64 v[130:131], v[130:131], 0, v[154:155]
	v_add_co_u32_e32 v132, vcc, 0x8000, v130
	v_add_u32_e32 v188, s10, v175
	s_nop 0
	v_addc_co_u32_e32 v133, vcc, 0, v131, vcc
	global_load_dwordx4 v[142:145], v[130:131], off nt
	global_load_dwordx4 v[138:141], v[132:133], off nt
	v_add_u32_e32 v130, v188, v177
	v_ashrrev_i32_e32 v131, 31, v130
	v_lshl_add_u64 v[172:173], v[156:157], 0, s[54:55]
	v_lshlrev_b64 v[130:131], 12, v[130:131]
	v_lshl_add_u64 v[130:131], v[172:173], 0, v[130:131]
	v_add_co_u32_e32 v132, vcc, 0x8000, v130
	v_lshl_add_u64 v[168:169], v[158:159], 0, s[54:55]
	s_nop 0
	v_addc_co_u32_e32 v133, vcc, 0, v131, vcc
	global_load_dwordx4 v[134:137], v[130:131], off nt
	s_nop 0
	global_load_dwordx4 v[130:133], v[132:133], off nt
	v_add_u32_e32 v187, v188, v171
	s_nop 1
	v_add_u32_e32 v198, v188, v178
	v_ashrrev_i32_e32 v199, 31, v198
	v_lshlrev_b64 v[198:199], 12, v[198:199]
	v_lshl_add_u64 v[198:199], v[172:173], 0, v[198:199]
	v_add_co_u32_e32 v200, vcc, 0x8000, v198
	s_nop 1
	v_addc_co_u32_e32 v201, vcc, 0, v199, vcc
	global_load_dwordx4 v[202:205], v[198:199], off nt
	s_nop 0
	global_load_dwordx4 v[198:201], v[200:201], off nt
	s_nop 1
	v_add_u32_e32 v206, v188, v179
	v_ashrrev_i32_e32 v207, 31, v206
	v_lshlrev_b64 v[206:207], 12, v[206:207]
	v_lshl_add_u64 v[206:207], v[172:173], 0, v[206:207]
	v_add_co_u32_e32 v208, vcc, 0x8000, v206
	s_nop 1
	v_addc_co_u32_e32 v209, vcc, 0, v207, vcc
	global_load_dwordx4 v[210:213], v[206:207], off nt
	s_nop 0
	global_load_dwordx4 v[206:209], v[208:209], off nt
	s_nop 1
	v_add_u32_e32 v214, v188, v180
	v_ashrrev_i32_e32 v215, 31, v214
	v_lshlrev_b64 v[214:215], 12, v[214:215]
	v_lshl_add_u64 v[214:215], v[172:173], 0, v[214:215]
	v_add_co_u32_e32 v216, vcc, 0x8000, v214
	s_nop 1
	v_addc_co_u32_e32 v217, vcc, 0, v215, vcc
	global_load_dwordx4 v[218:221], v[214:215], off nt
	s_nop 0
	global_load_dwordx4 v[214:217], v[216:217], off nt
	s_nop 1
	v_add_u32_e32 v222, v188, v181
	v_ashrrev_i32_e32 v223, 31, v222
	v_lshlrev_b64 v[222:223], 12, v[222:223]
	v_lshl_add_u64 v[222:223], v[172:173], 0, v[222:223]
	v_add_co_u32_e32 v224, vcc, 0x8000, v222
	s_nop 1
	v_addc_co_u32_e32 v225, vcc, 0, v223, vcc
	global_load_dwordx4 v[226:229], v[222:223], off nt
	s_nop 0
	global_load_dwordx4 v[222:225], v[224:225], off nt
	s_nop 1
	v_add_u32_e32 v230, v188, v182
	v_ashrrev_i32_e32 v231, 31, v230
	v_lshlrev_b64 v[230:231], 12, v[230:231]
	v_lshl_add_u64 v[230:231], v[172:173], 0, v[230:231]
	v_add_co_u32_e32 v232, vcc, 0x8000, v230
	s_nop 1
	v_addc_co_u32_e32 v233, vcc, 0, v231, vcc
	global_load_dwordx4 v[234:237], v[230:231], off nt
	s_nop 0
	global_load_dwordx4 v[230:233], v[232:233], off nt
	s_nop 1
	v_add_u32_e32 v238, v188, v183
	v_ashrrev_i32_e32 v239, 31, v238
	v_lshlrev_b64 v[238:239], 12, v[238:239]
	v_lshl_add_u64 v[238:239], v[172:173], 0, v[238:239]
	v_add_co_u32_e32 v240, vcc, 0x8000, v238
	s_nop 1
	v_addc_co_u32_e32 v241, vcc, 0, v239, vcc
	global_load_dwordx4 v[242:245], v[238:239], off nt
	s_nop 0
	global_load_dwordx4 v[238:241], v[240:241], off nt
	s_and_b64 vcc, exec, s[16:17]
	s_cbranch_vccz .LBB0_952
	s_waitcnt vmcnt(14)
	v_cndmask_b32_e64 v189, v118, v126, s[6:7]
	v_mov_b32_e32 v190, v155
	s_nop 0
	v_lshlrev_b32_e32 v194, 16, v139
	v_and_b32_e32 v139, 0xffff0000, v139
	v_mov_b32_dpp v190, v189 row_ror:8 row_mask:0xf bank_mask:0xf
	v_cndmask_b32_e64 v189, v119, v127, s[6:7]
	v_cndmask_b32_e64 v126, v126, v190, s[6:7]
	v_cndmask_b32_e64 v118, v190, v118, s[6:7]
	v_mov_b32_e32 v190, v155
	v_lshlrev_b32_e32 v195, 16, v140
	v_and_b32_e32 v140, 0xffff0000, v140
	v_mov_b32_dpp v190, v189 row_ror:8 row_mask:0xf bank_mask:0xf
	v_cndmask_b32_e64 v189, v120, v128, s[6:7]
	v_cndmask_b32_e64 v127, v127, v190, s[6:7]
	v_cndmask_b32_e64 v119, v190, v119, s[6:7]
	v_mov_b32_e32 v190, v155
	v_lshlrev_b32_e32 v191, 16, v144
	v_and_b32_e32 v144, 0xffff0000, v144
	v_mov_b32_dpp v190, v189 row_ror:8 row_mask:0xf bank_mask:0xf
	v_cndmask_b32_e64 v189, v121, v129, s[6:7]
	v_cndmask_b32_e64 v128, v128, v190, s[6:7]
	v_cndmask_b32_e64 v120, v190, v120, s[6:7]
	v_mov_b32_e32 v190, v155
	v_lshlrev_b32_e32 v192, 16, v145
	v_and_b32_e32 v145, 0xffff0000, v145
	v_mov_b32_dpp v190, v189 row_ror:8 row_mask:0xf bank_mask:0xf
	v_cndmask_b32_e64 v189, v114, v122, s[6:7]
	v_cndmask_b32_e64 v129, v129, v190, s[6:7]
	v_cndmask_b32_e64 v121, v190, v121, s[6:7]
	v_mov_b32_e32 v190, v155
	v_mul_f32_e32 v121, v121, v139
	v_lshlrev_b32_e32 v193, 16, v138
	v_mov_b32_dpp v190, v189 row_ror:8 row_mask:0xf bank_mask:0xf
	v_cndmask_b32_e64 v189, v115, v123, s[6:7]
	v_cndmask_b32_e64 v122, v122, v190, s[6:7]
	v_cndmask_b32_e64 v114, v190, v114, s[6:7]
	v_mov_b32_e32 v190, v155
	v_mul_f32_e32 v139, v114, v195
	v_add_u32_e32 v114, s76, v187
	v_mov_b32_dpp v190, v189 row_ror:8 row_mask:0xf bank_mask:0xf
	v_cndmask_b32_e64 v189, v116, v124, s[6:7]
	v_cndmask_b32_e64 v123, v123, v190, s[6:7]
	v_cndmask_b32_e64 v115, v190, v115, s[6:7]
	v_mov_b32_e32 v190, v155
	v_mul_f32_e32 v140, v115, v140
	v_ashrrev_i32_e32 v115, 31, v114
	v_mov_b32_dpp v190, v189 row_ror:8 row_mask:0xf bank_mask:0xf
	v_cndmask_b32_e64 v189, v117, v125, s[6:7]
	v_cndmask_b32_e64 v124, v124, v190, s[6:7]
	v_cndmask_b32_e64 v116, v190, v116, s[6:7]
	v_mov_b32_e32 v190, v155
	v_and_b32_e32 v138, 0xffff0000, v138
	v_lshlrev_b32_e32 v196, 16, v141
	v_mov_b32_dpp v190, v189 row_ror:8 row_mask:0xf bank_mask:0xf
	v_cndmask_b32_e64 v125, v125, v190, s[6:7]
	v_cndmask_b32_e64 v117, v190, v117, s[6:7]
	v_lshlrev_b32_e32 v189, 16, v142
	v_and_b32_e32 v142, 0xffff0000, v142
	v_lshlrev_b32_e32 v190, 16, v143
	v_and_b32_e32 v143, 0xffff0000, v143
	v_and_b32_e32 v141, 0xffff0000, v141
	v_mul_f32_e32 v126, v126, v189
	v_mul_f32_e32 v127, v127, v142
	v_mul_f32_e32 v128, v128, v190
	v_mul_f32_e32 v129, v129, v143
	v_mul_f32_e32 v122, v122, v191
	v_mul_f32_e32 v123, v123, v144
	v_mul_f32_e32 v124, v124, v192
	v_mul_f32_e32 v125, v125, v145
	v_lshlrev_b64 v[114:115], 12, v[114:115]
	v_mul_f32_e32 v189, v118, v193
	v_mul_f32_e32 v138, v119, v138
	v_mul_f32_e32 v142, v116, v196
	v_mul_f32_e32 v141, v117, v141
	v_lshl_add_u64 v[118:119], v[168:169], 0, v[114:115]
	v_cvt_pk_bf16_f32 v114, v126, v127
	v_cvt_pk_bf16_f32 v115, v128, v129
	v_cvt_pk_bf16_f32 v116, v122, v123
	v_cvt_pk_bf16_f32 v117, v124, v125
	v_mul_f32_e32 v120, v120, v194
	global_store_dwordx4 v[118:119], v[114:117], off nt
	v_add_co_u32_e32 v118, vcc, 0x8000, v118
	s_nop 0
	v_cvt_pk_bf16_f32 v114, v189, v138
	v_cvt_pk_bf16_f32 v115, v120, v121
	v_cvt_pk_bf16_f32 v116, v139, v140
	v_cvt_pk_bf16_f32 v117, v142, v141
	v_addc_co_u32_e32 v119, vcc, 0, v119, vcc
	global_store_dwordx4 v[118:119], v[114:117], off nt
; template <class Epi, class Sched, bool GATHER, bool ALIGN_EPI = true, bool SP2 = true, bool REMAP64 = false>
; __device__ __forceinline__ void gemm_phase(LAS unsigned char* lds, const bf16* Ag, const bf16* Btg, const int K, const Sched& S, const Epi& E) {
;     ...
;             constexpr bool RP = REMAP64 && Epi::ROWPAIR;
;             const bool hi = RP && (fr >= 8); const int rsh = hi ? -8 : 0, citx = hi ? cit + 32 : cit;
;             typename Epi::Pre pq[2];
;             { const int r0_ = wr * 64 + fr; pq[0] = E.pre(cur, (r0_ < cur.nrows ? r0_ : cur.nrows - 1) + rsh, citx); }
; #pragma unroll
;             for (int gq = 0; gq < 8; ++gq) { const int ai = gq >> 2, m = gq & 3, r = ai * HALF + wr * 64 + m * 16 + fr;
;                 if (gq + 1 < 8) { const int rn = ((gq + 1) >> 2) * HALF + wr * 64 + ((gq + 1) & 3) * 16 + fr; pq[(gq + 1) & 1] = E.pre(cur, (rn < cur.nrows ? rn : cur.nrows - 1) + rsh, citx); }
;                 __builtin_amdgcn_sched_barrier(0);
;                 if (r < cur.nrows) { float v0[8], v1[8];
; #pragma unroll
;                     for (int i = 0; i < 4; ++i) { v0[i] = acc[ai][0][m][0][i]; v0[4 + i] = acc[ai][0][m][1][i]; v1[i] = acc[ai][1][m][0][i]; v1[4 + i] = acc[ai][1][m][1][i]; }
;                     if constexpr (RP) {
; #pragma unroll
;                         for (int i = 0; i < 8; ++i) { const float snd = hi ? v0[i] : v1[i];
;                             const float rcv = __builtin_bit_cast(float, __builtin_amdgcn_update_dpp(0, __builtin_bit_cast(int, snd), 0x128, 0xf, 0xf, false));
;                             if (hi) v0[i] = rcv; else v1[i] = rcv; } }
;                     E.post(cur, r + rsh, citx, v0, v1, pq[gq & 1]); }
;                 __builtin_amdgcn_sched_barrier(0); }
;     __device__ __forceinline__ Pre pre(const Unit& u, int r, int cit) const { const size_t off = (size_t)(u.arow0 + r) * D + u.pn * 256 + cit; return Pre{__builtin_nontemporal_load((const v4u*)(gp + off)), __builtin_nontemporal_load((const v4u*)(gp + off + (size_t)8 * D))}; }
;     __device__ __forceinline__ void post(const Unit& u, int r, int cit, const float* v0, const float* v1, const Pre& p) const {
;         const size_t off = (size_t)(u.arow0 + r) * D + u.pn * 256 + cit; float g0[8], g1[8], a[8], b[8]; unpack8bf(p.g0, g0); unpack8bf(p.g1, g1);
; #pragma unroll
;         for (int i = 0; i < 8; ++i) { a[i] = g0[i] * v0[i]; b[i] = g1[i] * v1[i]; }
.LBB0_952:
	v_cndmask_b32_e64 v122, 0, 1, s[16:17]
	v_cmp_ne_u32_e64 s[10:11], 1, v122
	s_andn2_b64 vcc, exec, s[16:17]
	s_cbranch_vccnz .LBB0_954
	s_waitcnt vmcnt(14)
	v_cndmask_b32_e64 v122, v102, v110, s[6:7]
	v_mov_b32_e32 v123, v155
	s_nop 0
	v_lshlrev_b32_e32 v124, 16, v135
	v_lshlrev_b32_e32 v126, 16, v136
	v_mov_b32_dpp v123, v122 row_ror:8 row_mask:0xf bank_mask:0xf
	v_cndmask_b32_e64 v122, v103, v111, s[6:7]
	v_cndmask_b32_e64 v110, v110, v123, s[6:7]
	v_cndmask_b32_e64 v102, v123, v102, s[6:7]
	v_mov_b32_e32 v123, v155
	v_and_b32_e32 v127, 0xffff0000, v136
	v_lshlrev_b32_e32 v136, 16, v132
	v_mov_b32_dpp v123, v122 row_ror:8 row_mask:0xf bank_mask:0xf
	v_cndmask_b32_e64 v122, v104, v112, s[6:7]
	v_cndmask_b32_e64 v111, v111, v123, s[6:7]
	v_cndmask_b32_e64 v103, v123, v103, s[6:7]
	v_mov_b32_e32 v123, v155
	v_and_b32_e32 v125, 0xffff0000, v135
	v_and_b32_e32 v132, 0xffff0000, v132
	v_mov_b32_dpp v123, v122 row_ror:8 row_mask:0xf bank_mask:0xf
	v_cndmask_b32_e64 v122, v105, v113, s[6:7]
	v_cndmask_b32_e64 v112, v112, v123, s[6:7]
	v_cndmask_b32_e64 v104, v123, v104, s[6:7]
	v_mov_b32_e32 v123, v155
	v_mul_f32_e32 v112, v112, v124
	v_lshlrev_b32_e32 v128, 16, v137
	v_mov_b32_dpp v123, v122 row_ror:8 row_mask:0xf bank_mask:0xf
	v_cndmask_b32_e64 v122, v98, v106, s[6:7]
	v_cndmask_b32_e64 v113, v113, v123, s[6:7]
	v_cndmask_b32_e64 v105, v123, v105, s[6:7]
	v_mov_b32_e32 v123, v155
	v_and_b32_e32 v129, 0xffff0000, v137
	v_mul_f32_e32 v113, v113, v125
	v_mov_b32_dpp v123, v122 row_ror:8 row_mask:0xf bank_mask:0xf
	v_cndmask_b32_e64 v122, v99, v107, s[6:7]
	v_cndmask_b32_e64 v106, v106, v123, s[6:7]
	v_cndmask_b32_e64 v98, v123, v98, s[6:7]
	v_mov_b32_e32 v123, v155
	v_mul_f32_e32 v124, v98, v136
	v_add_u32_e32 v98, s80, v187
	v_mov_b32_dpp v123, v122 row_ror:8 row_mask:0xf bank_mask:0xf
	v_cndmask_b32_e64 v122, v100, v108, s[6:7]
	v_cndmask_b32_e64 v107, v107, v123, s[6:7]
	v_cndmask_b32_e64 v99, v123, v99, s[6:7]
	v_mov_b32_e32 v123, v155
	v_mul_f32_e32 v125, v99, v132
	v_ashrrev_i32_e32 v99, 31, v98
	v_mov_b32_dpp v123, v122 row_ror:8 row_mask:0xf bank_mask:0xf
	v_cndmask_b32_e64 v122, v101, v109, s[6:7]
	v_cndmask_b32_e64 v108, v108, v123, s[6:7]
	v_cndmask_b32_e64 v100, v123, v100, s[6:7]
	v_mov_b32_e32 v123, v155
	v_lshlrev_b32_e32 v137, 16, v133
	v_and_b32_e32 v133, 0xffff0000, v133
	v_mov_b32_dpp v123, v122 row_ror:8 row_mask:0xf bank_mask:0xf
	v_cndmask_b32_e64 v109, v109, v123, s[6:7]
	v_cndmask_b32_e64 v101, v123, v101, s[6:7]
	v_lshlrev_b32_e32 v122, 16, v134
	v_and_b32_e32 v123, 0xffff0000, v134
	v_lshlrev_b32_e32 v134, 16, v130
	v_and_b32_e32 v130, 0xffff0000, v130
	v_mul_f32_e32 v110, v110, v122
	v_mul_f32_e32 v111, v111, v123
	v_mul_f32_e32 v106, v106, v126
	v_mul_f32_e32 v107, v107, v127
	v_mul_f32_e32 v108, v108, v128
	v_mul_f32_e32 v109, v109, v129
	v_lshlrev_b64 v[98:99], 12, v[98:99]
	v_lshlrev_b32_e32 v135, 16, v131
	v_and_b32_e32 v131, 0xffff0000, v131
	v_mul_f32_e32 v122, v102, v134
	v_mul_f32_e32 v123, v103, v130
	v_mul_f32_e32 v126, v100, v137
	v_mul_f32_e32 v127, v101, v133
	v_lshl_add_u64 v[102:103], v[168:169], 0, v[98:99]
	v_cvt_pk_bf16_f32 v98, v110, v111
	v_cvt_pk_bf16_f32 v99, v112, v113
	v_cvt_pk_bf16_f32 v100, v106, v107
	v_cvt_pk_bf16_f32 v101, v108, v109
	v_mul_f32_e32 v104, v104, v135
	v_mul_f32_e32 v105, v105, v131
	global_store_dwordx4 v[102:103], v[98:101], off nt
	v_add_co_u32_e32 v102, vcc, 0x8000, v102
	s_nop 0
	v_cvt_pk_bf16_f32 v98, v122, v123
	v_cvt_pk_bf16_f32 v99, v104, v105
	v_cvt_pk_bf16_f32 v100, v124, v125
	v_cvt_pk_bf16_f32 v101, v126, v127
	v_addc_co_u32_e32 v103, vcc, 0, v103, vcc
	global_store_dwordx4 v[102:103], v[98:101], off nt
.LBB0_954:
	s_and_b64 vcc, exec, s[10:11]
	s_cbranch_vccnz .LBB0_956
	s_waitcnt vmcnt(14)
	v_cndmask_b32_e64 v106, v86, v94, s[6:7]
	v_mov_b32_e32 v107, v155
	s_nop 0
	v_lshlrev_b32_e32 v108, 16, v203
	v_lshlrev_b32_e32 v110, 16, v204
	v_mov_b32_dpp v107, v106 row_ror:8 row_mask:0xf bank_mask:0xf
	v_cndmask_b32_e64 v106, v87, v95, s[6:7]
	v_cndmask_b32_e64 v94, v94, v107, s[6:7]
	v_cndmask_b32_e64 v86, v107, v86, s[6:7]
	v_mov_b32_e32 v107, v155
	v_and_b32_e32 v111, 0xffff0000, v204
	v_lshlrev_b32_e32 v204, 16, v200
	v_mov_b32_dpp v107, v106 row_ror:8 row_mask:0xf bank_mask:0xf
	v_cndmask_b32_e64 v106, v88, v96, s[6:7]
	v_cndmask_b32_e64 v95, v95, v107, s[6:7]
	v_cndmask_b32_e64 v87, v107, v87, s[6:7]
	v_mov_b32_e32 v107, v155
	v_and_b32_e32 v109, 0xffff0000, v203
	v_and_b32_e32 v200, 0xffff0000, v200
	v_mov_b32_dpp v107, v106 row_ror:8 row_mask:0xf bank_mask:0xf
	v_cndmask_b32_e64 v106, v89, v97, s[6:7]
	v_cndmask_b32_e64 v96, v96, v107, s[6:7]
	v_cndmask_b32_e64 v88, v107, v88, s[6:7]
	v_mov_b32_e32 v107, v155
	v_mul_f32_e32 v96, v96, v108
	v_lshlrev_b32_e32 v112, 16, v205
	v_mov_b32_dpp v107, v106 row_ror:8 row_mask:0xf bank_mask:0xf
	v_cndmask_b32_e64 v106, v82, v90, s[6:7]
	v_cndmask_b32_e64 v97, v97, v107, s[6:7]
	v_cndmask_b32_e64 v89, v107, v89, s[6:7]
	v_mov_b32_e32 v107, v155
	v_and_b32_e32 v113, 0xffff0000, v205
	v_mul_f32_e32 v97, v97, v109
	v_mov_b32_dpp v107, v106 row_ror:8 row_mask:0xf bank_mask:0xf
	v_cndmask_b32_e64 v106, v83, v91, s[6:7]
	v_cndmask_b32_e64 v90, v90, v107, s[6:7]
	v_cndmask_b32_e64 v82, v107, v82, s[6:7]
	v_mov_b32_e32 v107, v155
	v_mul_f32_e32 v108, v82, v204
	v_add_u32_e32 v82, s81, v187
	v_mov_b32_dpp v107, v106 row_ror:8 row_mask:0xf bank_mask:0xf
	v_cndmask_b32_e64 v106, v84, v92, s[6:7]
	v_cndmask_b32_e64 v91, v91, v107, s[6:7]
	v_cndmask_b32_e64 v83, v107, v83, s[6:7]
	v_mov_b32_e32 v107, v155
	v_mul_f32_e32 v109, v83, v200
	v_ashrrev_i32_e32 v83, 31, v82
	v_mov_b32_dpp v107, v106 row_ror:8 row_mask:0xf bank_mask:0xf
; template <class Epi, class Sched, bool GATHER, bool ALIGN_EPI = true, bool SP2 = true, bool REMAP64 = false>
; __device__ __forceinline__ void gemm_phase(LAS unsigned char* lds, const bf16* Ag, const bf16* Btg, const int K, const Sched& S, const Epi& E) {
;     ...
;             constexpr bool RP = REMAP64 && Epi::ROWPAIR;
;             const bool hi = RP && (fr >= 8); const int rsh = hi ? -8 : 0, citx = hi ? cit + 32 : cit;
;             typename Epi::Pre pq[2];
;             { const int r0_ = wr * 64 + fr; pq[0] = E.pre(cur, (r0_ < cur.nrows ? r0_ : cur.nrows - 1) + rsh, citx); }
; #pragma unroll
;             for (int gq = 0; gq < 8; ++gq) { const int ai = gq >> 2, m = gq & 3, r = ai * HALF + wr * 64 + m * 16 + fr;
;                 if (gq + 1 < 8) { const int rn = ((gq + 1) >> 2) * HALF + wr * 64 + ((gq + 1) & 3) * 16 + fr; pq[(gq + 1) & 1] = E.pre(cur, (rn < cur.nrows ? rn : cur.nrows - 1) + rsh, citx); }
;                 __builtin_amdgcn_sched_barrier(0);
;                 if (r < cur.nrows) { float v0[8], v1[8];
; #pragma unroll
;                     for (int i = 0; i < 4; ++i) { v0[i] = acc[ai][0][m][0][i]; v0[4 + i] = acc[ai][0][m][1][i]; v1[i] = acc[ai][1][m][0][i]; v1[4 + i] = acc[ai][1][m][1][i]; }
;                     if constexpr (RP) {
; #pragma unroll
;                         for (int i = 0; i < 8; ++i) { const float snd = hi ? v0[i] : v1[i];
;                             const float rcv = __builtin_bit_cast(float, __builtin_amdgcn_update_dpp(0, __builtin_bit_cast(int, snd), 0x128, 0xf, 0xf, false));
;                             if (hi) v0[i] = rcv; else v1[i] = rcv; } }
;                     E.post(cur, r + rsh, citx, v0, v1, pq[gq & 1]); }
;                 __builtin_amdgcn_sched_barrier(0); }
;     __device__ __forceinline__ Pre pre(const Unit& u, int r, int cit) const { const size_t off = (size_t)(u.arow0 + r) * D + u.pn * 256 + cit; return Pre{__builtin_nontemporal_load((const v4u*)(gp + off)), __builtin_nontemporal_load((const v4u*)(gp + off + (size_t)8 * D))}; }
;     __device__ __forceinline__ void post(const Unit& u, int r, int cit, const float* v0, const float* v1, const Pre& p) const {
;         const size_t off = (size_t)(u.arow0 + r) * D + u.pn * 256 + cit; float g0[8], g1[8], a[8], b[8]; unpack8bf(p.g0, g0); unpack8bf(p.g1, g1);
; #pragma unroll
;         for (int i = 0; i < 8; ++i) { a[i] = g0[i] * v0[i]; b[i] = g1[i] * v1[i]; }
	v_cndmask_b32_e64 v106, v85, v93, s[6:7]
	v_cndmask_b32_e64 v92, v92, v107, s[6:7]
	v_cndmask_b32_e64 v84, v107, v84, s[6:7]
	v_mov_b32_e32 v107, v155
	v_lshlrev_b32_e32 v205, 16, v201
	v_and_b32_e32 v201, 0xffff0000, v201
	v_mov_b32_dpp v107, v106 row_ror:8 row_mask:0xf bank_mask:0xf
	v_cndmask_b32_e64 v93, v93, v107, s[6:7]
	v_cndmask_b32_e64 v85, v107, v85, s[6:7]
	v_lshlrev_b32_e32 v106, 16, v202
	v_and_b32_e32 v107, 0xffff0000, v202
	v_lshlrev_b32_e32 v202, 16, v198
	v_and_b32_e32 v198, 0xffff0000, v198
	v_mul_f32_e32 v94, v94, v106
	v_mul_f32_e32 v95, v95, v107
	v_mul_f32_e32 v90, v90, v110
	v_mul_f32_e32 v91, v91, v111
	v_mul_f32_e32 v92, v92, v112
	v_mul_f32_e32 v93, v93, v113
	v_lshlrev_b64 v[82:83], 12, v[82:83]
	v_lshlrev_b32_e32 v203, 16, v199
	v_and_b32_e32 v199, 0xffff0000, v199
	v_mul_f32_e32 v106, v86, v202
	v_mul_f32_e32 v107, v87, v198
	v_mul_f32_e32 v110, v84, v205
	v_mul_f32_e32 v111, v85, v201
	v_lshl_add_u64 v[86:87], v[168:169], 0, v[82:83]
	v_cvt_pk_bf16_f32 v82, v94, v95
	v_cvt_pk_bf16_f32 v83, v96, v97
	v_cvt_pk_bf16_f32 v84, v90, v91
	v_cvt_pk_bf16_f32 v85, v92, v93
	v_mul_f32_e32 v88, v88, v203
	v_mul_f32_e32 v89, v89, v199
	global_store_dwordx4 v[86:87], v[82:85], off nt
	v_add_co_u32_e32 v86, vcc, 0x8000, v86
	s_nop 0
	v_cvt_pk_bf16_f32 v82, v106, v107
	v_cvt_pk_bf16_f32 v83, v88, v89
	v_cvt_pk_bf16_f32 v84, v108, v109
	v_cvt_pk_bf16_f32 v85, v110, v111
	v_addc_co_u32_e32 v87, vcc, 0, v87, vcc
	global_store_dwordx4 v[86:87], v[82:85], off nt
.LBB0_956:
	s_and_b64 vcc, exec, s[10:11]
	s_cbranch_vccnz .LBB0_958
	s_waitcnt vmcnt(14)
	v_cndmask_b32_e64 v90, v70, v78, s[6:7]
	v_mov_b32_e32 v91, v155
	s_nop 0
	v_lshlrev_b32_e32 v92, 16, v211
	v_lshlrev_b32_e32 v94, 16, v212
	v_mov_b32_dpp v91, v90 row_ror:8 row_mask:0xf bank_mask:0xf
	v_cndmask_b32_e64 v90, v71, v79, s[6:7]
	v_cndmask_b32_e64 v78, v78, v91, s[6:7]
	v_cndmask_b32_e64 v70, v91, v70, s[6:7]
	v_mov_b32_e32 v91, v155
	v_and_b32_e32 v95, 0xffff0000, v212
	v_lshlrev_b32_e32 v212, 16, v208
	v_mov_b32_dpp v91, v90 row_ror:8 row_mask:0xf bank_mask:0xf
	v_cndmask_b32_e64 v90, v72, v80, s[6:7]
	v_cndmask_b32_e64 v79, v79, v91, s[6:7]
	v_cndmask_b32_e64 v71, v91, v71, s[6:7]
	v_mov_b32_e32 v91, v155
	v_and_b32_e32 v93, 0xffff0000, v211
	v_and_b32_e32 v208, 0xffff0000, v208
	v_mov_b32_dpp v91, v90 row_ror:8 row_mask:0xf bank_mask:0xf
	v_cndmask_b32_e64 v90, v73, v81, s[6:7]
	v_cndmask_b32_e64 v80, v80, v91, s[6:7]
	v_cndmask_b32_e64 v72, v91, v72, s[6:7]
	v_mov_b32_e32 v91, v155
	v_mul_f32_e32 v80, v80, v92
	v_lshlrev_b32_e32 v96, 16, v213
	v_mov_b32_dpp v91, v90 row_ror:8 row_mask:0xf bank_mask:0xf
	v_cndmask_b32_e64 v90, v66, v74, s[6:7]
	v_cndmask_b32_e64 v81, v81, v91, s[6:7]
	v_cndmask_b32_e64 v73, v91, v73, s[6:7]
	v_mov_b32_e32 v91, v155
	v_and_b32_e32 v97, 0xffff0000, v213
	v_mul_f32_e32 v81, v81, v93
	v_mov_b32_dpp v91, v90 row_ror:8 row_mask:0xf bank_mask:0xf
	v_cndmask_b32_e64 v90, v67, v75, s[6:7]
	v_cndmask_b32_e64 v74, v74, v91, s[6:7]
	v_cndmask_b32_e64 v66, v91, v66, s[6:7]
	v_mov_b32_e32 v91, v155
	v_mul_f32_e32 v92, v66, v212
	v_add_u32_e32 v66, s83, v187
	v_mov_b32_dpp v91, v90 row_ror:8 row_mask:0xf bank_mask:0xf
	v_cndmask_b32_e64 v90, v68, v76, s[6:7]
	v_cndmask_b32_e64 v75, v75, v91, s[6:7]
	v_cndmask_b32_e64 v67, v91, v67, s[6:7]
	v_mov_b32_e32 v91, v155
	v_mul_f32_e32 v93, v67, v208
	v_ashrrev_i32_e32 v67, 31, v66
	v_mov_b32_dpp v91, v90 row_ror:8 row_mask:0xf bank_mask:0xf
	v_cndmask_b32_e64 v90, v69, v77, s[6:7]
	v_cndmask_b32_e64 v76, v76, v91, s[6:7]
	v_cndmask_b32_e64 v68, v91, v68, s[6:7]
	v_mov_b32_e32 v91, v155
	v_lshlrev_b32_e32 v213, 16, v209
	v_and_b32_e32 v209, 0xffff0000, v209
	v_mov_b32_dpp v91, v90 row_ror:8 row_mask:0xf bank_mask:0xf
	v_cndmask_b32_e64 v77, v77, v91, s[6:7]
	v_cndmask_b32_e64 v69, v91, v69, s[6:7]
	v_lshlrev_b32_e32 v90, 16, v210
	v_and_b32_e32 v91, 0xffff0000, v210
	v_lshlrev_b32_e32 v210, 16, v206
	v_and_b32_e32 v206, 0xffff0000, v206
	v_mul_f32_e32 v78, v78, v90
	v_mul_f32_e32 v79, v79, v91
	v_mul_f32_e32 v74, v74, v94
	v_mul_f32_e32 v75, v75, v95
	v_mul_f32_e32 v76, v76, v96
	v_mul_f32_e32 v77, v77, v97
	v_lshlrev_b64 v[66:67], 12, v[66:67]
	v_lshlrev_b32_e32 v211, 16, v207
	v_and_b32_e32 v207, 0xffff0000, v207
	v_mul_f32_e32 v90, v70, v210
	v_mul_f32_e32 v91, v71, v206
	v_mul_f32_e32 v94, v68, v213
	v_mul_f32_e32 v95, v69, v209
	v_lshl_add_u64 v[70:71], v[168:169], 0, v[66:67]
	v_cvt_pk_bf16_f32 v66, v78, v79
	v_cvt_pk_bf16_f32 v67, v80, v81
	v_cvt_pk_bf16_f32 v68, v74, v75
	v_cvt_pk_bf16_f32 v69, v76, v77
	v_mul_f32_e32 v72, v72, v211
	v_mul_f32_e32 v73, v73, v207
	global_store_dwordx4 v[70:71], v[66:69], off nt
	v_add_co_u32_e32 v70, vcc, 0x8000, v70
	s_nop 0
	v_cvt_pk_bf16_f32 v66, v90, v91
	v_cvt_pk_bf16_f32 v67, v72, v73
	v_cvt_pk_bf16_f32 v68, v92, v93
	v_cvt_pk_bf16_f32 v69, v94, v95
	v_addc_co_u32_e32 v71, vcc, 0, v71, vcc
	global_store_dwordx4 v[70:71], v[66:69], off nt
; template <class Epi, class Sched, bool GATHER, bool ALIGN_EPI = true, bool SP2 = true, bool REMAP64 = false>
; __device__ __forceinline__ void gemm_phase(LAS unsigned char* lds, const bf16* Ag, const bf16* Btg, const int K, const Sched& S, const Epi& E) {
;     ...
;             constexpr bool RP = REMAP64 && Epi::ROWPAIR;
;             const bool hi = RP && (fr >= 8); const int rsh = hi ? -8 : 0, citx = hi ? cit + 32 : cit;
;             typename Epi::Pre pq[2];
;             { const int r0_ = wr * 64 + fr; pq[0] = E.pre(cur, (r0_ < cur.nrows ? r0_ : cur.nrows - 1) + rsh, citx); }
; #pragma unroll
;             for (int gq = 0; gq < 8; ++gq) { const int ai = gq >> 2, m = gq & 3, r = ai * HALF + wr * 64 + m * 16 + fr;
;                 if (gq + 1 < 8) { const int rn = ((gq + 1) >> 2) * HALF + wr * 64 + ((gq + 1) & 3) * 16 + fr; pq[(gq + 1) & 1] = E.pre(cur, (rn < cur.nrows ? rn : cur.nrows - 1) + rsh, citx); }
;                 __builtin_amdgcn_sched_barrier(0);
;                 if (r < cur.nrows) { float v0[8], v1[8];
; #pragma unroll
;                     for (int i = 0; i < 4; ++i) { v0[i] = acc[ai][0][m][0][i]; v0[4 + i] = acc[ai][0][m][1][i]; v1[i] = acc[ai][1][m][0][i]; v1[4 + i] = acc[ai][1][m][1][i]; }
;                     if constexpr (RP) {
; #pragma unroll
;                         for (int i = 0; i < 8; ++i) { const float snd = hi ? v0[i] : v1[i];
;                             const float rcv = __builtin_bit_cast(float, __builtin_amdgcn_update_dpp(0, __builtin_bit_cast(int, snd), 0x128, 0xf, 0xf, false));
;                             if (hi) v0[i] = rcv; else v1[i] = rcv; } }
;                     E.post(cur, r + rsh, citx, v0, v1, pq[gq & 1]); }
;                 __builtin_amdgcn_sched_barrier(0); }
;     __device__ __forceinline__ Pre pre(const Unit& u, int r, int cit) const { const size_t off = (size_t)(u.arow0 + r) * D + u.pn * 256 + cit; return Pre{__builtin_nontemporal_load((const v4u*)(gp + off)), __builtin_nontemporal_load((const v4u*)(gp + off + (size_t)8 * D))}; }
;     __device__ __forceinline__ void post(const Unit& u, int r, int cit, const float* v0, const float* v1, const Pre& p) const {
;         const size_t off = (size_t)(u.arow0 + r) * D + u.pn * 256 + cit; float g0[8], g1[8], a[8], b[8]; unpack8bf(p.g0, g0); unpack8bf(p.g1, g1);
; #pragma unroll
;         for (int i = 0; i < 8; ++i) { a[i] = g0[i] * v0[i]; b[i] = g1[i] * v1[i]; }
.LBB0_958:
	v_cndmask_b32_e64 v74, 0, 1, s[18:19]
	v_cmp_ne_u32_e64 s[10:11], 1, v74
	s_andn2_b64 vcc, exec, s[18:19]
	s_cbranch_vccnz .LBB0_960
	s_waitcnt vmcnt(14)
	v_cndmask_b32_e64 v74, v54, v62, s[6:7]
	v_mov_b32_e32 v75, v155
	s_nop 0
	v_lshlrev_b32_e32 v76, 16, v219
	v_lshlrev_b32_e32 v78, 16, v220
	v_mov_b32_dpp v75, v74 row_ror:8 row_mask:0xf bank_mask:0xf
	v_cndmask_b32_e64 v74, v55, v63, s[6:7]
	v_cndmask_b32_e64 v62, v62, v75, s[6:7]
	v_cndmask_b32_e64 v54, v75, v54, s[6:7]
	v_mov_b32_e32 v75, v155
	v_and_b32_e32 v79, 0xffff0000, v220
	v_lshlrev_b32_e32 v220, 16, v216
	v_mov_b32_dpp v75, v74 row_ror:8 row_mask:0xf bank_mask:0xf
	v_cndmask_b32_e64 v74, v56, v64, s[6:7]
	v_cndmask_b32_e64 v63, v63, v75, s[6:7]
	v_cndmask_b32_e64 v55, v75, v55, s[6:7]
	v_mov_b32_e32 v75, v155
	v_and_b32_e32 v77, 0xffff0000, v219
	v_and_b32_e32 v216, 0xffff0000, v216
	v_mov_b32_dpp v75, v74 row_ror:8 row_mask:0xf bank_mask:0xf
	v_cndmask_b32_e64 v74, v57, v65, s[6:7]
	v_cndmask_b32_e64 v64, v64, v75, s[6:7]
	v_cndmask_b32_e64 v56, v75, v56, s[6:7]
	v_mov_b32_e32 v75, v155
	v_mul_f32_e32 v64, v64, v76
	v_lshlrev_b32_e32 v80, 16, v221
	v_mov_b32_dpp v75, v74 row_ror:8 row_mask:0xf bank_mask:0xf
	v_cndmask_b32_e64 v74, v50, v58, s[6:7]
	v_cndmask_b32_e64 v65, v65, v75, s[6:7]
	v_cndmask_b32_e64 v57, v75, v57, s[6:7]
	v_mov_b32_e32 v75, v155
	v_and_b32_e32 v81, 0xffff0000, v221
	v_mul_f32_e32 v65, v65, v77
	v_mov_b32_dpp v75, v74 row_ror:8 row_mask:0xf bank_mask:0xf
	v_cndmask_b32_e64 v74, v51, v59, s[6:7]
	v_cndmask_b32_e64 v58, v58, v75, s[6:7]
	v_cndmask_b32_e64 v50, v75, v50, s[6:7]
	v_mov_b32_e32 v75, v155
	v_mul_f32_e32 v76, v50, v220
	v_add_u32_e32 v50, s82, v187
	v_mov_b32_dpp v75, v74 row_ror:8 row_mask:0xf bank_mask:0xf
	v_cndmask_b32_e64 v74, v52, v60, s[6:7]
	v_cndmask_b32_e64 v59, v59, v75, s[6:7]
	v_cndmask_b32_e64 v51, v75, v51, s[6:7]
	v_mov_b32_e32 v75, v155
	v_mul_f32_e32 v77, v51, v216
	v_ashrrev_i32_e32 v51, 31, v50
	v_mov_b32_dpp v75, v74 row_ror:8 row_mask:0xf bank_mask:0xf
	v_cndmask_b32_e64 v74, v53, v61, s[6:7]
	v_cndmask_b32_e64 v60, v60, v75, s[6:7]
	v_cndmask_b32_e64 v52, v75, v52, s[6:7]
	v_mov_b32_e32 v75, v155
	v_lshlrev_b32_e32 v221, 16, v217
	v_and_b32_e32 v217, 0xffff0000, v217
	v_mov_b32_dpp v75, v74 row_ror:8 row_mask:0xf bank_mask:0xf
	v_cndmask_b32_e64 v61, v61, v75, s[6:7]
	v_cndmask_b32_e64 v53, v75, v53, s[6:7]
	v_lshlrev_b32_e32 v74, 16, v218
	v_and_b32_e32 v75, 0xffff0000, v218
	v_lshlrev_b32_e32 v218, 16, v214
	v_and_b32_e32 v214, 0xffff0000, v214
	v_mul_f32_e32 v62, v62, v74
	v_mul_f32_e32 v63, v63, v75
	v_mul_f32_e32 v58, v58, v78
	v_mul_f32_e32 v59, v59, v79
	v_mul_f32_e32 v60, v60, v80
	v_mul_f32_e32 v61, v61, v81
	v_lshlrev_b64 v[50:51], 12, v[50:51]
	v_lshlrev_b32_e32 v219, 16, v215
	v_and_b32_e32 v215, 0xffff0000, v215
	v_mul_f32_e32 v74, v54, v218
	v_mul_f32_e32 v75, v55, v214
	v_mul_f32_e32 v78, v52, v221
	v_mul_f32_e32 v79, v53, v217
	v_lshl_add_u64 v[54:55], v[168:169], 0, v[50:51]
	v_cvt_pk_bf16_f32 v50, v62, v63
	v_cvt_pk_bf16_f32 v51, v64, v65
	v_cvt_pk_bf16_f32 v52, v58, v59
	v_cvt_pk_bf16_f32 v53, v60, v61
	v_mul_f32_e32 v56, v56, v219
	v_mul_f32_e32 v57, v57, v215
	global_store_dwordx4 v[54:55], v[50:53], off nt
	v_add_co_u32_e32 v54, vcc, 0x8000, v54
	s_nop 0
	v_cvt_pk_bf16_f32 v50, v74, v75
	v_cvt_pk_bf16_f32 v51, v56, v57
	v_cvt_pk_bf16_f32 v52, v76, v77
	v_cvt_pk_bf16_f32 v53, v78, v79
	v_addc_co_u32_e32 v55, vcc, 0, v55, vcc
	global_store_dwordx4 v[54:55], v[50:53], off nt
.LBB0_960:
	s_and_b64 vcc, exec, s[10:11]
	s_cbranch_vccnz .LBB0_962
	s_waitcnt vmcnt(14)
	v_cndmask_b32_e64 v58, v38, v46, s[6:7]
	v_mov_b32_e32 v59, v155
	s_nop 0
	v_lshlrev_b32_e32 v60, 16, v227
	v_lshlrev_b32_e32 v62, 16, v228
	v_mov_b32_dpp v59, v58 row_ror:8 row_mask:0xf bank_mask:0xf
	v_cndmask_b32_e64 v58, v39, v47, s[6:7]
	v_cndmask_b32_e64 v46, v46, v59, s[6:7]
	v_cndmask_b32_e64 v38, v59, v38, s[6:7]
	v_mov_b32_e32 v59, v155
	v_and_b32_e32 v63, 0xffff0000, v228
	v_lshlrev_b32_e32 v228, 16, v224
	v_mov_b32_dpp v59, v58 row_ror:8 row_mask:0xf bank_mask:0xf
	v_cndmask_b32_e64 v58, v40, v48, s[6:7]
	v_cndmask_b32_e64 v47, v47, v59, s[6:7]
	v_cndmask_b32_e64 v39, v59, v39, s[6:7]
	v_mov_b32_e32 v59, v155
	v_and_b32_e32 v61, 0xffff0000, v227
	v_and_b32_e32 v224, 0xffff0000, v224
	v_mov_b32_dpp v59, v58 row_ror:8 row_mask:0xf bank_mask:0xf
	v_cndmask_b32_e64 v58, v41, v49, s[6:7]
	v_cndmask_b32_e64 v48, v48, v59, s[6:7]
	v_cndmask_b32_e64 v40, v59, v40, s[6:7]
	v_mov_b32_e32 v59, v155
	v_mul_f32_e32 v48, v48, v60
	v_lshlrev_b32_e32 v64, 16, v229
	v_mov_b32_dpp v59, v58 row_ror:8 row_mask:0xf bank_mask:0xf
	v_cndmask_b32_e64 v58, v34, v42, s[6:7]
	v_cndmask_b32_e64 v49, v49, v59, s[6:7]
	v_cndmask_b32_e64 v41, v59, v41, s[6:7]
	v_mov_b32_e32 v59, v155
	v_and_b32_e32 v65, 0xffff0000, v229
	v_mul_f32_e32 v49, v49, v61
	v_mov_b32_dpp v59, v58 row_ror:8 row_mask:0xf bank_mask:0xf
	v_cndmask_b32_e64 v58, v35, v43, s[6:7]
	v_cndmask_b32_e64 v42, v42, v59, s[6:7]
	v_cndmask_b32_e64 v34, v59, v34, s[6:7]
	v_mov_b32_e32 v59, v155
	v_mul_f32_e32 v60, v34, v228
	v_add_u32_e32 v34, s84, v187
	v_mov_b32_dpp v59, v58 row_ror:8 row_mask:0xf bank_mask:0xf
	v_cndmask_b32_e64 v58, v36, v44, s[6:7]
	v_cndmask_b32_e64 v43, v43, v59, s[6:7]
	v_cndmask_b32_e64 v35, v59, v35, s[6:7]
	v_mov_b32_e32 v59, v155
	v_mul_f32_e32 v61, v35, v224
	v_ashrrev_i32_e32 v35, 31, v34
	v_mov_b32_dpp v59, v58 row_ror:8 row_mask:0xf bank_mask:0xf
	v_cndmask_b32_e64 v58, v37, v45, s[6:7]
	v_cndmask_b32_e64 v44, v44, v59, s[6:7]
	v_cndmask_b32_e64 v36, v59, v36, s[6:7]
	v_mov_b32_e32 v59, v155
	v_lshlrev_b32_e32 v229, 16, v225
	v_and_b32_e32 v225, 0xffff0000, v225
	v_mov_b32_dpp v59, v58 row_ror:8 row_mask:0xf bank_mask:0xf
	v_cndmask_b32_e64 v45, v45, v59, s[6:7]
	v_cndmask_b32_e64 v37, v59, v37, s[6:7]
	v_lshlrev_b32_e32 v58, 16, v226
	v_and_b32_e32 v59, 0xffff0000, v226
	v_lshlrev_b32_e32 v226, 16, v222
	v_and_b32_e32 v222, 0xffff0000, v222
	v_mul_f32_e32 v46, v46, v58
	v_mul_f32_e32 v47, v47, v59
	v_mul_f32_e32 v42, v42, v62
	v_mul_f32_e32 v43, v43, v63
	v_mul_f32_e32 v44, v44, v64
	v_mul_f32_e32 v45, v45, v65
	v_lshlrev_b64 v[34:35], 12, v[34:35]
	v_lshlrev_b32_e32 v227, 16, v223
	v_and_b32_e32 v223, 0xffff0000, v223
	v_mul_f32_e32 v58, v38, v226
	v_mul_f32_e32 v59, v39, v222
	v_mul_f32_e32 v62, v36, v229
	v_mul_f32_e32 v63, v37, v225
	v_lshl_add_u64 v[38:39], v[168:169], 0, v[34:35]
	v_cvt_pk_bf16_f32 v34, v46, v47
	v_cvt_pk_bf16_f32 v35, v48, v49
	v_cvt_pk_bf16_f32 v36, v42, v43
	v_cvt_pk_bf16_f32 v37, v44, v45
	v_mul_f32_e32 v40, v40, v227
	v_mul_f32_e32 v41, v41, v223
	global_store_dwordx4 v[38:39], v[34:37], off nt
	v_add_co_u32_e32 v38, vcc, 0x8000, v38
	s_nop 0
	v_cvt_pk_bf16_f32 v34, v58, v59
	v_cvt_pk_bf16_f32 v35, v40, v41
	v_cvt_pk_bf16_f32 v36, v60, v61
	v_cvt_pk_bf16_f32 v37, v62, v63
	v_addc_co_u32_e32 v39, vcc, 0, v39, vcc
	global_store_dwordx4 v[38:39], v[34:37], off nt
; template <class Epi, class Sched, bool GATHER, bool ALIGN_EPI = true, bool SP2 = true, bool REMAP64 = false>
; __device__ __forceinline__ void gemm_phase(LAS unsigned char* lds, const bf16* Ag, const bf16* Btg, const int K, const Sched& S, const Epi& E) {
;     ...
;             constexpr bool RP = REMAP64 && Epi::ROWPAIR;
;             const bool hi = RP && (fr >= 8); const int rsh = hi ? -8 : 0, citx = hi ? cit + 32 : cit;
;             typename Epi::Pre pq[2];
;             { const int r0_ = wr * 64 + fr; pq[0] = E.pre(cur, (r0_ < cur.nrows ? r0_ : cur.nrows - 1) + rsh, citx); }
; #pragma unroll
;             for (int gq = 0; gq < 8; ++gq) { const int ai = gq >> 2, m = gq & 3, r = ai * HALF + wr * 64 + m * 16 + fr;
;                 if (gq + 1 < 8) { const int rn = ((gq + 1) >> 2) * HALF + wr * 64 + ((gq + 1) & 3) * 16 + fr; pq[(gq + 1) & 1] = E.pre(cur, (rn < cur.nrows ? rn : cur.nrows - 1) + rsh, citx); }
;                 __builtin_amdgcn_sched_barrier(0);
;                 if (r < cur.nrows) { float v0[8], v1[8];
; #pragma unroll
;                     for (int i = 0; i < 4; ++i) { v0[i] = acc[ai][0][m][0][i]; v0[4 + i] = acc[ai][0][m][1][i]; v1[i] = acc[ai][1][m][0][i]; v1[4 + i] = acc[ai][1][m][1][i]; }
;                     if constexpr (RP) {
; #pragma unroll
;                         for (int i = 0; i < 8; ++i) { const float snd = hi ? v0[i] : v1[i];
;                             const float rcv = __builtin_bit_cast(float, __builtin_amdgcn_update_dpp(0, __builtin_bit_cast(int, snd), 0x128, 0xf, 0xf, false));
;                             if (hi) v0[i] = rcv; else v1[i] = rcv; } }
;                     E.post(cur, r + rsh, citx, v0, v1, pq[gq & 1]); }
;                 __builtin_amdgcn_sched_barrier(0); }
;     __device__ __forceinline__ Pre pre(const Unit& u, int r, int cit) const { const size_t off = (size_t)(u.arow0 + r) * D + u.pn * 256 + cit; return Pre{__builtin_nontemporal_load((const v4u*)(gp + off)), __builtin_nontemporal_load((const v4u*)(gp + off + (size_t)8 * D))}; }
;     __device__ __forceinline__ void post(const Unit& u, int r, int cit, const float* v0, const float* v1, const Pre& p) const {
;         const size_t off = (size_t)(u.arow0 + r) * D + u.pn * 256 + cit; float g0[8], g1[8], a[8], b[8]; unpack8bf(p.g0, g0); unpack8bf(p.g1, g1);
; #pragma unroll
;         for (int i = 0; i < 8; ++i) { a[i] = g0[i] * v0[i]; b[i] = g1[i] * v1[i]; }
.LBB0_962:
	s_and_b64 vcc, exec, s[10:11]
	s_cbranch_vccnz .LBB0_964
	s_waitcnt vmcnt(14)
	v_cndmask_b32_e64 v42, v22, v30, s[6:7]
	v_mov_b32_e32 v43, v155
	s_nop 0
	v_lshlrev_b32_e32 v44, 16, v235
	v_lshlrev_b32_e32 v46, 16, v236
	v_mov_b32_dpp v43, v42 row_ror:8 row_mask:0xf bank_mask:0xf
	v_cndmask_b32_e64 v42, v23, v31, s[6:7]
	v_cndmask_b32_e64 v30, v30, v43, s[6:7]
	v_cndmask_b32_e64 v22, v43, v22, s[6:7]
	v_mov_b32_e32 v43, v155
	v_and_b32_e32 v47, 0xffff0000, v236
	v_lshlrev_b32_e32 v236, 16, v232
	v_mov_b32_dpp v43, v42 row_ror:8 row_mask:0xf bank_mask:0xf
	v_cndmask_b32_e64 v42, v24, v32, s[6:7]
	v_cndmask_b32_e64 v31, v31, v43, s[6:7]
	v_cndmask_b32_e64 v23, v43, v23, s[6:7]
	v_mov_b32_e32 v43, v155
	v_and_b32_e32 v45, 0xffff0000, v235
	v_and_b32_e32 v232, 0xffff0000, v232
	v_mov_b32_dpp v43, v42 row_ror:8 row_mask:0xf bank_mask:0xf
	v_cndmask_b32_e64 v42, v25, v33, s[6:7]
	v_cndmask_b32_e64 v32, v32, v43, s[6:7]
	v_cndmask_b32_e64 v24, v43, v24, s[6:7]
	v_mov_b32_e32 v43, v155
	v_mul_f32_e32 v32, v32, v44
	v_lshlrev_b32_e32 v48, 16, v237
	v_mov_b32_dpp v43, v42 row_ror:8 row_mask:0xf bank_mask:0xf
	v_cndmask_b32_e64 v42, v18, v26, s[6:7]
	v_cndmask_b32_e64 v33, v33, v43, s[6:7]
	v_cndmask_b32_e64 v25, v43, v25, s[6:7]
	v_mov_b32_e32 v43, v155
	v_and_b32_e32 v49, 0xffff0000, v237
	v_mul_f32_e32 v33, v33, v45
	v_mov_b32_dpp v43, v42 row_ror:8 row_mask:0xf bank_mask:0xf
	v_cndmask_b32_e64 v42, v19, v27, s[6:7]
	v_cndmask_b32_e64 v26, v26, v43, s[6:7]
	v_cndmask_b32_e64 v18, v43, v18, s[6:7]
	v_mov_b32_e32 v43, v155
	v_mul_f32_e32 v44, v18, v236
	v_add_u32_e32 v18, s85, v187
	v_mov_b32_dpp v43, v42 row_ror:8 row_mask:0xf bank_mask:0xf
	v_cndmask_b32_e64 v42, v20, v28, s[6:7]
	v_cndmask_b32_e64 v27, v27, v43, s[6:7]
	v_cndmask_b32_e64 v19, v43, v19, s[6:7]
	v_mov_b32_e32 v43, v155
	v_mul_f32_e32 v45, v19, v232
	v_ashrrev_i32_e32 v19, 31, v18
	v_mov_b32_dpp v43, v42 row_ror:8 row_mask:0xf bank_mask:0xf
	v_cndmask_b32_e64 v42, v21, v29, s[6:7]
	v_cndmask_b32_e64 v28, v28, v43, s[6:7]
	v_cndmask_b32_e64 v20, v43, v20, s[6:7]
	v_mov_b32_e32 v43, v155
	v_lshlrev_b32_e32 v237, 16, v233
	v_and_b32_e32 v233, 0xffff0000, v233
	v_mov_b32_dpp v43, v42 row_ror:8 row_mask:0xf bank_mask:0xf
	v_cndmask_b32_e64 v29, v29, v43, s[6:7]
	v_cndmask_b32_e64 v21, v43, v21, s[6:7]
	v_lshlrev_b32_e32 v42, 16, v234
	v_and_b32_e32 v43, 0xffff0000, v234
	v_lshlrev_b32_e32 v234, 16, v230
	v_and_b32_e32 v230, 0xffff0000, v230
	v_mul_f32_e32 v30, v30, v42
	v_mul_f32_e32 v31, v31, v43
	v_mul_f32_e32 v26, v26, v46
	v_mul_f32_e32 v27, v27, v47
	v_mul_f32_e32 v28, v28, v48
	v_mul_f32_e32 v29, v29, v49
	v_lshlrev_b64 v[18:19], 12, v[18:19]
	v_lshlrev_b32_e32 v235, 16, v231
	v_and_b32_e32 v231, 0xffff0000, v231
	v_mul_f32_e32 v42, v22, v234
	v_mul_f32_e32 v43, v23, v230
	v_mul_f32_e32 v46, v20, v237
	v_mul_f32_e32 v47, v21, v233
	v_lshl_add_u64 v[22:23], v[168:169], 0, v[18:19]
	v_cvt_pk_bf16_f32 v18, v30, v31
	v_cvt_pk_bf16_f32 v19, v32, v33
	v_cvt_pk_bf16_f32 v20, v26, v27
	v_cvt_pk_bf16_f32 v21, v28, v29
	v_mul_f32_e32 v24, v24, v235
	v_mul_f32_e32 v25, v25, v231
	global_store_dwordx4 v[22:23], v[18:21], off nt
	v_add_co_u32_e32 v22, vcc, 0x8000, v22
	s_nop 0
	v_cvt_pk_bf16_f32 v18, v42, v43
	v_cvt_pk_bf16_f32 v19, v24, v25
	v_cvt_pk_bf16_f32 v20, v44, v45
	v_cvt_pk_bf16_f32 v21, v46, v47
	v_addc_co_u32_e32 v23, vcc, 0, v23, vcc
	global_store_dwordx4 v[22:23], v[18:21], off nt
.LBB0_964:
	s_and_b64 vcc, exec, s[10:11]
	s_cbranch_vccnz .LBB0_966
	s_waitcnt vmcnt(14)
	v_cndmask_b32_e64 v18, v6, v14, s[6:7]
	v_mov_b32_e32 v19, v155
	s_nop 0
	v_lshlrev_b32_e32 v20, 16, v243
	v_lshlrev_b32_e32 v30, 16, v240
	v_mov_b32_dpp v19, v18 row_ror:8 row_mask:0xf bank_mask:0xf
	v_cndmask_b32_e64 v18, v7, v15, s[6:7]
	v_cndmask_b32_e64 v14, v14, v19, s[6:7]
	v_cndmask_b32_e64 v6, v19, v6, s[6:7]
	v_mov_b32_e32 v19, v155
	v_and_b32_e32 v21, 0xffff0000, v243
	v_and_b32_e32 v31, 0xffff0000, v240
	v_mov_b32_dpp v19, v18 row_ror:8 row_mask:0xf bank_mask:0xf
	v_cndmask_b32_e64 v18, v8, v16, s[6:7]
	v_cndmask_b32_e64 v15, v15, v19, s[6:7]
	v_cndmask_b32_e64 v7, v19, v7, s[6:7]
	v_mov_b32_e32 v19, v155
	v_lshlrev_b32_e32 v22, 16, v244
	v_and_b32_e32 v23, 0xffff0000, v244
	v_mov_b32_dpp v19, v18 row_ror:8 row_mask:0xf bank_mask:0xf
	v_cndmask_b32_e64 v18, v9, v17, s[6:7]
	v_cndmask_b32_e64 v16, v16, v19, s[6:7]
	v_cndmask_b32_e64 v8, v19, v8, s[6:7]
	v_mov_b32_e32 v19, v155
	v_mul_f32_e32 v16, v16, v20
	v_lshlrev_b32_e32 v24, 16, v245
	v_mov_b32_dpp v19, v18 row_ror:8 row_mask:0xf bank_mask:0xf
	v_cndmask_b32_e64 v18, v2, v10, s[6:7]
	v_cndmask_b32_e64 v17, v17, v19, s[6:7]
	v_cndmask_b32_e64 v9, v19, v9, s[6:7]
	v_mov_b32_e32 v19, v155
	v_and_b32_e32 v25, 0xffff0000, v245
	v_mul_f32_e32 v17, v17, v21
	v_mov_b32_dpp v19, v18 row_ror:8 row_mask:0xf bank_mask:0xf
	v_cndmask_b32_e64 v18, v3, v11, s[6:7]
	v_cndmask_b32_e64 v10, v10, v19, s[6:7]
	v_cndmask_b32_e64 v2, v19, v2, s[6:7]
	v_mov_b32_e32 v19, v155
	v_mul_f32_e32 v20, v2, v30
	v_add_u32_e32 v2, s86, v187
	v_mov_b32_dpp v19, v18 row_ror:8 row_mask:0xf bank_mask:0xf
	v_cndmask_b32_e64 v18, v4, v12, s[6:7]
	v_cndmask_b32_e64 v11, v11, v19, s[6:7]
	v_cndmask_b32_e64 v3, v19, v3, s[6:7]
	v_mov_b32_e32 v19, v155
	v_mul_f32_e32 v21, v3, v31
	v_ashrrev_i32_e32 v3, 31, v2
	v_mov_b32_dpp v19, v18 row_ror:8 row_mask:0xf bank_mask:0xf
	v_cndmask_b32_e64 v18, v5, v13, s[6:7]
	v_cndmask_b32_e64 v12, v12, v19, s[6:7]
	v_cndmask_b32_e64 v4, v19, v4, s[6:7]
	v_mov_b32_e32 v19, v155
	v_lshlrev_b32_e32 v26, 16, v238
	v_and_b32_e32 v27, 0xffff0000, v238
	v_mov_b32_dpp v19, v18 row_ror:8 row_mask:0xf bank_mask:0xf
	v_cndmask_b32_e64 v13, v13, v19, s[6:7]
	v_cndmask_b32_e64 v5, v19, v5, s[6:7]
	v_lshlrev_b32_e32 v18, 16, v242
	v_and_b32_e32 v19, 0xffff0000, v242
	v_lshlrev_b32_e32 v32, 16, v241
	v_and_b32_e32 v33, 0xffff0000, v241
	v_mul_f32_e32 v14, v14, v18
	v_mul_f32_e32 v15, v15, v19
	v_mul_f32_e32 v10, v10, v22
	v_mul_f32_e32 v11, v11, v23
	v_mul_f32_e32 v12, v12, v24
	v_mul_f32_e32 v13, v13, v25
	v_lshlrev_b64 v[2:3], 12, v[2:3]
	v_lshlrev_b32_e32 v28, 16, v239
	v_and_b32_e32 v29, 0xffff0000, v239
	v_mul_f32_e32 v18, v6, v26
	v_mul_f32_e32 v19, v7, v27
	v_mul_f32_e32 v22, v4, v32
	v_mul_f32_e32 v23, v5, v33
	v_lshl_add_u64 v[6:7], v[168:169], 0, v[2:3]
	v_cvt_pk_bf16_f32 v2, v14, v15
	v_cvt_pk_bf16_f32 v3, v16, v17
	v_cvt_pk_bf16_f32 v4, v10, v11
	v_cvt_pk_bf16_f32 v5, v12, v13
	v_mul_f32_e32 v8, v8, v28
	v_mul_f32_e32 v9, v9, v29
	global_store_dwordx4 v[6:7], v[2:5], off nt
	v_add_co_u32_e32 v6, vcc, 0x8000, v6
	s_nop 0
	v_cvt_pk_bf16_f32 v2, v18, v19
	v_cvt_pk_bf16_f32 v3, v8, v9
	v_cvt_pk_bf16_f32 v4, v20, v21
	v_cvt_pk_bf16_f32 v5, v22, v23
	v_addc_co_u32_e32 v7, vcc, 0, v7, vcc
	global_store_dwordx4 v[6:7], v[2:5], off nt

; template <class Epi, class Sched, bool GATHER, bool ALIGN_EPI = true, bool SP2 = true, bool REMAP64 = false>
; __device__ __forceinline__ void gemm_phase(LAS unsigned char* lds, const bf16* Ag, const bf16* Btg, const int K, const Sched& S, const Epi& E) {
;     ...
;             constexpr bool RP = REMAP64 && Epi::ROWPAIR;
;             const bool hi = RP && (fr >= 8); const int rsh = hi ? -8 : 0, citx = hi ? cit + 32 : cit;
;             typename Epi::Pre pq[2];
;             { const int r0_ = wr * 64 + fr; pq[0] = E.pre(cur, (r0_ < cur.nrows ? r0_ : cur.nrows - 1) + rsh, citx); }
; #pragma unroll
;             for (int gq = 0; gq < 8; ++gq) { const int ai = gq >> 2, m = gq & 3, r = ai * HALF + wr * 64 + m * 16 + fr;
;                 if (gq + 1 < 8) { const int rn = ((gq + 1) >> 2) * HALF + wr * 64 + ((gq + 1) & 3) * 16 + fr; pq[(gq + 1) & 1] = E.pre(cur, (rn < cur.nrows ? rn : cur.nrows - 1) + rsh, citx); }
;                 __builtin_amdgcn_sched_barrier(0);
;                 if (r < cur.nrows) { float v0[8], v1[8];
; #pragma unroll
;                     for (int i = 0; i < 4; ++i) { v0[i] = acc[ai][0][m][0][i]; v0[4 + i] = acc[ai][0][m][1][i]; v1[i] = acc[ai][1][m][0][i]; v1[4 + i] = acc[ai][1][m][1][i]; }
;                     if constexpr (RP) {
; #pragma unroll
;                         for (int i = 0; i < 8; ++i) { const float snd = hi ? v0[i] : v1[i];
;                             const float rcv = __builtin_bit_cast(float, __builtin_amdgcn_update_dpp(0, __builtin_bit_cast(int, snd), 0x128, 0xf, 0xf, false));
;                             if (hi) v0[i] = rcv; else v1[i] = rcv; } }
;                     E.post(cur, r + rsh, citx, v0, v1, pq[gq & 1]); }
;                 __builtin_amdgcn_sched_barrier(0); }
;     __device__ __forceinline__ Pre pre(const Unit& u, int r, int cit) const { const size_t off = (size_t)(u.arow0 + r) * D + u.pn * 256 + cit; return Pre{__builtin_nontemporal_load((const v4u*)(gd + off)), __builtin_nontemporal_load((const v4u*)(gd + off + (size_t)8 * D)), __builtin_nontemporal_load ...
;     __device__ __forceinline__ void post(const Unit& u, int r, int cit, const float* v0, const float* v1, const Pre& p) const {
;         const size_t off = (size_t)(u.arow0 + r) * D + u.pn * 256 + cit; float g0[8], g1[8], m0[8], m1[8]; unpack8bf(p.g0, g0); unpack8bf(p.g1, g1); unpack8bf(p.m0, m0); unpack8bf(p.m1, m1);
; #pragma unroll
.LBB0_1152:
	v_add_u32_e32 v130, s8, v185
	v_ashrrev_i32_e32 v131, 31, v130
	s_lshl_b32 s42, s40, 8
	v_lshlrev_b64 v[130:131], 11, v[130:131]
	s_ashr_i32 s43, s42, 31
	v_lshl_add_u64 v[130:131], v[130:131], 0, s[42:43]
	v_or_b32_e32 v130, v130, v172
	v_lshlrev_b64 v[130:131], 1, v[130:131]
	v_lshl_add_u64 v[132:133], s[50:51], 0, v[130:131]
	v_add_co_u32_e32 v134, vcc, s63, v132
	v_lshl_add_u64 v[130:131], s[20:21], 0, v[130:131]
	s_nop 0
	v_addc_co_u32_e32 v135, vcc, 0, v133, vcc
	global_load_dwordx4 v[158:161], v[132:133], off nt
	global_load_dwordx4 v[154:157], v[134:135], off nt
	v_add_co_u32_e32 v132, vcc, s63, v130
	v_add_u32_e32 v197, s8, v184
	s_nop 0
	v_addc_co_u32_e32 v133, vcc, 0, v131, vcc
	global_load_dwordx4 v[150:153], v[130:131], off nt
	global_load_dwordx4 v[146:149], v[132:133], off nt
	v_add_u32_e32 v130, v197, v186
	v_ashrrev_i32_e32 v131, 31, v130
	v_mov_b32_e32 v183, s43
	v_or_b32_e32 v182, s42, v172
	v_lshlrev_b64 v[130:131], 11, v[130:131]
	v_lshl_add_u64 v[130:131], v[130:131], 0, v[182:183]
	v_lshlrev_b64 v[130:131], 1, v[130:131]
	v_lshl_add_u64 v[132:133], s[50:51], 0, v[130:131]
	v_add_co_u32_e32 v134, vcc, 0x8000, v132
	v_lshl_add_u64 v[130:131], s[20:21], 0, v[130:131]
	s_nop 0
	v_addc_co_u32_e32 v135, vcc, 0, v133, vcc
	global_load_dwordx4 v[142:145], v[132:133], off nt
	global_load_dwordx4 v[138:141], v[134:135], off nt
	v_add_co_u32_e32 v132, vcc, 0x8000, v130
	v_add_u32_e32 v196, v197, v171
	s_nop 0
	v_addc_co_u32_e32 v133, vcc, 0, v131, vcc
	global_load_dwordx4 v[134:137], v[130:131], off nt
	s_nop 0
	global_load_dwordx4 v[130:133], v[132:133], off nt
	s_nop 1
	v_add_u32_e32 v214, v197, v187
	v_ashrrev_i32_e32 v215, 31, v214
	v_lshlrev_b64 v[214:215], 11, v[214:215]
	v_lshl_add_u64 v[214:215], v[214:215], 0, v[182:183]
	v_lshlrev_b64 v[214:215], 1, v[214:215]
	v_lshl_add_u64 v[216:217], s[50:51], 0, v[214:215]
	v_add_co_u32_e32 v218, vcc, 0x8000, v216
	v_lshl_add_u64 v[214:215], s[20:21], 0, v[214:215]
	s_nop 0
	v_addc_co_u32_e32 v219, vcc, 0, v217, vcc
	global_load_dwordx4 v[226:229], v[216:217], off nt
	global_load_dwordx4 v[222:225], v[218:219], off nt
	v_add_co_u32_e32 v216, vcc, 0x8000, v214
	s_nop 1
	v_addc_co_u32_e32 v217, vcc, 0, v215, vcc
	global_load_dwordx4 v[218:221], v[214:215], off nt
	s_nop 0
	global_load_dwordx4 v[214:217], v[216:217], off nt
	s_nop 1
	v_add_u32_e32 v230, v197, v188
	v_ashrrev_i32_e32 v231, 31, v230
	v_lshlrev_b64 v[230:231], 11, v[230:231]
	v_lshl_add_u64 v[230:231], v[230:231], 0, v[182:183]
	v_lshlrev_b64 v[230:231], 1, v[230:231]
	v_lshl_add_u64 v[232:233], s[50:51], 0, v[230:231]
	v_add_co_u32_e32 v234, vcc, 0x8000, v232
	v_lshl_add_u64 v[230:231], s[20:21], 0, v[230:231]
	s_nop 0
	v_addc_co_u32_e32 v235, vcc, 0, v233, vcc
	global_load_dwordx4 v[242:245], v[232:233], off nt
	global_load_dwordx4 v[238:241], v[234:235], off nt
	v_add_co_u32_e32 v232, vcc, 0x8000, v230
	s_nop 1
	v_addc_co_u32_e32 v233, vcc, 0, v231, vcc
	global_load_dwordx4 v[234:237], v[230:231], off nt
	s_nop 0
	global_load_dwordx4 v[230:233], v[232:233], off nt
	s_and_b64 vcc, exec, s[16:17]
	s_cbranch_vccz .LBB0_1154
	s_waitcnt vmcnt(12)
	v_cndmask_b32_e64 v198, v118, v126, s[0:1]
	v_mov_b32_e32 v199, 0
	s_nop 0
	v_lshlrev_b32_e32 v204, 16, v156
	v_lshlrev_b32_e32 v212, 16, v148
	v_mov_b32_dpp v199, v198 row_ror:8 row_mask:0xf bank_mask:0xf
	v_cndmask_b32_e64 v198, v119, v127, s[0:1]
	v_cndmask_b32_e64 v126, v126, v199, s[0:1]
	v_cndmask_b32_e64 v118, v199, v118, s[0:1]
	v_mov_b32_e32 v199, 0
	v_and_b32_e32 v156, 0xffff0000, v156
	v_and_b32_e32 v148, 0xffff0000, v148
	v_mov_b32_dpp v199, v198 row_ror:8 row_mask:0xf bank_mask:0xf
	v_cndmask_b32_e64 v198, v120, v128, s[0:1]
	v_cndmask_b32_e64 v127, v127, v199, s[0:1]
	v_cndmask_b32_e64 v119, v199, v119, s[0:1]
	v_mov_b32_e32 v199, 0
	v_lshlrev_b32_e32 v200, 16, v160
	v_and_b32_e32 v160, 0xffff0000, v160
	v_mov_b32_dpp v199, v198 row_ror:8 row_mask:0xf bank_mask:0xf
	v_cndmask_b32_e64 v198, v121, v129, s[0:1]
	v_cndmask_b32_e64 v128, v128, v199, s[0:1]
	v_cndmask_b32_e64 v120, v199, v120, s[0:1]
	v_mov_b32_e32 v199, 0
	v_lshlrev_b32_e32 v201, 16, v161
	v_and_b32_e32 v161, 0xffff0000, v161
	v_mov_b32_dpp v199, v198 row_ror:8 row_mask:0xf bank_mask:0xf
	v_cndmask_b32_e64 v198, v114, v122, s[0:1]
	v_cndmask_b32_e64 v129, v129, v199, s[0:1]
	v_cndmask_b32_e64 v121, v199, v121, s[0:1]
	v_mov_b32_e32 v199, 0
	v_lshlrev_b32_e32 v206, 16, v150
	v_and_b32_e32 v150, 0xffff0000, v150
	v_mov_b32_dpp v199, v198 row_ror:8 row_mask:0xf bank_mask:0xf
	v_cndmask_b32_e64 v198, v115, v123, s[0:1]
	v_cndmask_b32_e64 v122, v122, v199, s[0:1]
	v_cndmask_b32_e64 v114, v199, v114, s[0:1]
	v_mov_b32_e32 v199, 0
	v_fmac_f32_e32 v212, v114, v204
	v_add_u32_e32 v114, s60, v196
	v_mov_b32_dpp v199, v198 row_ror:8 row_mask:0xf bank_mask:0xf
	v_cndmask_b32_e64 v198, v116, v124, s[0:1]
	v_cndmask_b32_e64 v123, v123, v199, s[0:1]
	v_cndmask_b32_e64 v115, v199, v115, s[0:1]
	v_mov_b32_e32 v199, 0
	v_fmac_f32_e32 v148, v115, v156
	v_ashrrev_i32_e32 v115, 31, v114
	v_mov_b32_dpp v199, v198 row_ror:8 row_mask:0xf bank_mask:0xf
	v_cndmask_b32_e64 v198, v117, v125, s[0:1]
	v_cndmask_b32_e64 v124, v124, v199, s[0:1]
	v_cndmask_b32_e64 v116, v199, v116, s[0:1]
	v_mov_b32_e32 v199, 0
	v_lshlrev_b32_e32 v207, 16, v151
	v_and_b32_e32 v151, 0xffff0000, v151
	v_mov_b32_dpp v199, v198 row_ror:8 row_mask:0xf bank_mask:0xf
	v_cndmask_b32_e64 v125, v125, v199, s[0:1]
	v_cndmask_b32_e64 v117, v199, v117, s[0:1]
	v_lshlrev_b32_e32 v198, 16, v158
	v_and_b32_e32 v158, 0xffff0000, v158
	v_lshlrev_b32_e32 v199, 16, v159
	v_and_b32_e32 v159, 0xffff0000, v159
	v_lshlrev_b32_e32 v208, 16, v152
; template <class Epi, class Sched, bool GATHER, bool ALIGN_EPI = true, bool SP2 = true, bool REMAP64 = false>
; __device__ __forceinline__ void gemm_phase(LAS unsigned char* lds, const bf16* Ag, const bf16* Btg, const int K, const Sched& S, const Epi& E) {
;     ...
;             constexpr bool RP = REMAP64 && Epi::ROWPAIR;
;             const bool hi = RP && (fr >= 8); const int rsh = hi ? -8 : 0, citx = hi ? cit + 32 : cit;
;             typename Epi::Pre pq[2];
;             { const int r0_ = wr * 64 + fr; pq[0] = E.pre(cur, (r0_ < cur.nrows ? r0_ : cur.nrows - 1) + rsh, citx); }
; #pragma unroll
;             for (int gq = 0; gq < 8; ++gq) { const int ai = gq >> 2, m = gq & 3, r = ai * HALF + wr * 64 + m * 16 + fr;
;                 if (gq + 1 < 8) { const int rn = ((gq + 1) >> 2) * HALF + wr * 64 + ((gq + 1) & 3) * 16 + fr; pq[(gq + 1) & 1] = E.pre(cur, (rn < cur.nrows ? rn : cur.nrows - 1) + rsh, citx); }
;                 __builtin_amdgcn_sched_barrier(0);
;                 if (r < cur.nrows) { float v0[8], v1[8];
; #pragma unroll
;                     for (int i = 0; i < 4; ++i) { v0[i] = acc[ai][0][m][0][i]; v0[4 + i] = acc[ai][0][m][1][i]; v1[i] = acc[ai][1][m][0][i]; v1[4 + i] = acc[ai][1][m][1][i]; }
;                     if constexpr (RP) {
; #pragma unroll
;                         for (int i = 0; i < 8; ++i) { const float snd = hi ? v0[i] : v1[i];
;                             const float rcv = __builtin_bit_cast(float, __builtin_amdgcn_update_dpp(0, __builtin_bit_cast(int, snd), 0x128, 0xf, 0xf, false));
;                             if (hi) v0[i] = rcv; else v1[i] = rcv; } }
;                     E.post(cur, r + rsh, citx, v0, v1, pq[gq & 1]); }
;                 __builtin_amdgcn_sched_barrier(0); }
;     __device__ __forceinline__ Pre pre(const Unit& u, int r, int cit) const { const size_t off = (size_t)(u.arow0 + r) * D + u.pn * 256 + cit; return Pre{__builtin_nontemporal_load((const v4u*)(gd + off)), __builtin_nontemporal_load((const v4u*)(gd + off + (size_t)8 * D)), __builtin_nontemporal_load ...
;     __device__ __forceinline__ void post(const Unit& u, int r, int cit, const float* v0, const float* v1, const Pre& p) const {
;         const size_t off = (size_t)(u.arow0 + r) * D + u.pn * 256 + cit; float g0[8], g1[8], m0[8], m1[8]; unpack8bf(p.g0, g0); unpack8bf(p.g1, g1); unpack8bf(p.m0, m0); unpack8bf(p.m1, m1);
; #pragma unroll
	v_and_b32_e32 v152, 0xffff0000, v152
	v_lshlrev_b32_e32 v209, 16, v153
	v_and_b32_e32 v153, 0xffff0000, v153
	v_lshlrev_b64 v[114:115], 12, v[114:115]
	v_lshlrev_b32_e32 v202, 16, v154
	v_and_b32_e32 v154, 0xffff0000, v154
	v_lshlrev_b32_e32 v205, 16, v157
	v_and_b32_e32 v157, 0xffff0000, v157
	v_lshlrev_b32_e32 v210, 16, v146
	v_and_b32_e32 v146, 0xffff0000, v146
	v_lshlrev_b32_e32 v213, 16, v149
	v_and_b32_e32 v149, 0xffff0000, v149
	v_fmac_f32_e32 v206, v126, v198
	v_fmac_f32_e32 v150, v127, v158
	v_fmac_f32_e32 v207, v128, v199
	v_fmac_f32_e32 v151, v129, v159
	v_fmac_f32_e32 v208, v122, v200
	v_fmac_f32_e32 v152, v123, v160
	v_fmac_f32_e32 v209, v124, v201
	v_fmac_f32_e32 v153, v125, v161
	v_lshl_add_u64 v[114:115], s[36:37], 0, v[114:115]
	v_lshlrev_b32_e32 v203, 16, v155
	v_and_b32_e32 v155, 0xffff0000, v155
	v_lshlrev_b32_e32 v211, 16, v147
	v_and_b32_e32 v147, 0xffff0000, v147
	v_fmac_f32_e32 v210, v118, v202
	v_fmac_f32_e32 v146, v119, v154
	v_fmac_f32_e32 v213, v116, v205
	v_fmac_f32_e32 v149, v117, v157
	v_lshl_add_u64 v[118:119], v[182:183], 1, v[114:115]
	v_cvt_pk_bf16_f32 v114, v206, v150
	v_cvt_pk_bf16_f32 v115, v207, v151
	v_cvt_pk_bf16_f32 v116, v208, v152
	v_cvt_pk_bf16_f32 v117, v209, v153
	v_fmac_f32_e32 v211, v120, v203
	v_fmac_f32_e32 v147, v121, v155
	global_store_dwordx4 v[118:119], v[114:117], off nt
	v_add_co_u32_e32 v118, vcc, 0x8000, v118
	s_nop 0
	v_cvt_pk_bf16_f32 v114, v210, v146
	v_cvt_pk_bf16_f32 v115, v211, v147
	v_cvt_pk_bf16_f32 v116, v212, v148
	v_cvt_pk_bf16_f32 v117, v213, v149
	v_addc_co_u32_e32 v119, vcc, 0, v119, vcc
	global_store_dwordx4 v[118:119], v[114:117], off nt
.LBB0_1154:
	s_nop 1
	v_add_u32_e32 v114, v197, v189
	v_ashrrev_i32_e32 v115, 31, v114
	v_lshlrev_b64 v[114:115], 11, v[114:115]
	v_lshl_add_u64 v[114:115], v[114:115], 0, v[182:183]
	v_lshlrev_b64 v[114:115], 1, v[114:115]
	v_lshl_add_u64 v[116:117], s[50:51], 0, v[114:115]
	v_add_co_u32_e32 v118, vcc, 0x8000, v116
	v_lshl_add_u64 v[114:115], s[20:21], 0, v[114:115]
	s_nop 0
	v_addc_co_u32_e32 v119, vcc, 0, v117, vcc
	global_load_dwordx4 v[126:129], v[116:117], off nt
	global_load_dwordx4 v[122:125], v[118:119], off nt
	v_add_co_u32_e32 v116, vcc, 0x8000, v114
	s_nop 1
	v_addc_co_u32_e32 v117, vcc, 0, v115, vcc
	global_load_dwordx4 v[118:121], v[114:115], off nt
	s_nop 0
	global_load_dwordx4 v[114:117], v[116:117], off nt
	s_nop 0
	v_cndmask_b32_e64 v146, 0, 1, s[16:17]
	v_cmp_ne_u32_e64 s[8:9], 1, v146
	s_andn2_b64 vcc, exec, s[16:17]
	s_cbranch_vccnz .LBB0_1156
	s_waitcnt vmcnt(14)
	v_cndmask_b32_e64 v146, v102, v110, s[0:1]
	v_mov_b32_e32 v147, 0
	v_lshlrev_b32_e32 v152, 16, v140
	v_lshlrev_b32_e32 v160, 16, v132
	v_mov_b32_dpp v147, v146 row_ror:8 row_mask:0xf bank_mask:0xf
	v_cndmask_b32_e64 v146, v103, v111, s[0:1]
	v_cndmask_b32_e64 v110, v110, v147, s[0:1]
	v_cndmask_b32_e64 v102, v147, v102, s[0:1]
	v_mov_b32_e32 v147, 0
	v_and_b32_e32 v140, 0xffff0000, v140
	v_and_b32_e32 v132, 0xffff0000, v132
	v_mov_b32_dpp v147, v146 row_ror:8 row_mask:0xf bank_mask:0xf
	v_cndmask_b32_e64 v146, v104, v112, s[0:1]
	v_cndmask_b32_e64 v111, v111, v147, s[0:1]
	v_cndmask_b32_e64 v103, v147, v103, s[0:1]
	v_mov_b32_e32 v147, 0
	v_lshlrev_b32_e32 v148, 16, v144
	v_and_b32_e32 v144, 0xffff0000, v144
	v_mov_b32_dpp v147, v146 row_ror:8 row_mask:0xf bank_mask:0xf
	v_cndmask_b32_e64 v146, v105, v113, s[0:1]
	v_cndmask_b32_e64 v112, v112, v147, s[0:1]
	v_cndmask_b32_e64 v104, v147, v104, s[0:1]
	v_mov_b32_e32 v147, 0
	v_lshlrev_b32_e32 v149, 16, v145
	v_and_b32_e32 v145, 0xffff0000, v145
	v_mov_b32_dpp v147, v146 row_ror:8 row_mask:0xf bank_mask:0xf
	v_cndmask_b32_e64 v146, v98, v106, s[0:1]
	v_cndmask_b32_e64 v113, v113, v147, s[0:1]
	v_cndmask_b32_e64 v105, v147, v105, s[0:1]
	v_mov_b32_e32 v147, 0
	v_lshlrev_b32_e32 v154, 16, v134
	v_and_b32_e32 v134, 0xffff0000, v134
	v_mov_b32_dpp v147, v146 row_ror:8 row_mask:0xf bank_mask:0xf
	v_cndmask_b32_e64 v146, v99, v107, s[0:1]
	v_cndmask_b32_e64 v106, v106, v147, s[0:1]
	v_cndmask_b32_e64 v98, v147, v98, s[0:1]
	v_mov_b32_e32 v147, 0
	v_fmac_f32_e32 v160, v98, v152
	v_add_u32_e32 v98, s64, v196
	v_mov_b32_dpp v147, v146 row_ror:8 row_mask:0xf bank_mask:0xf
	v_cndmask_b32_e64 v146, v100, v108, s[0:1]
	v_cndmask_b32_e64 v107, v107, v147, s[0:1]
	v_cndmask_b32_e64 v99, v147, v99, s[0:1]
	v_mov_b32_e32 v147, 0
	v_fmac_f32_e32 v132, v99, v140
	v_ashrrev_i32_e32 v99, 31, v98
	v_mov_b32_dpp v147, v146 row_ror:8 row_mask:0xf bank_mask:0xf
	v_cndmask_b32_e64 v146, v101, v109, s[0:1]
	v_cndmask_b32_e64 v108, v108, v147, s[0:1]
	v_cndmask_b32_e64 v100, v147, v100, s[0:1]
	v_mov_b32_e32 v147, 0
	v_lshlrev_b32_e32 v155, 16, v135
	v_and_b32_e32 v135, 0xffff0000, v135
	v_mov_b32_dpp v147, v146 row_ror:8 row_mask:0xf bank_mask:0xf
	v_cndmask_b32_e64 v109, v109, v147, s[0:1]
	v_cndmask_b32_e64 v101, v147, v101, s[0:1]
	v_lshlrev_b32_e32 v146, 16, v142
	v_and_b32_e32 v142, 0xffff0000, v142
	v_lshlrev_b32_e32 v147, 16, v143
	v_and_b32_e32 v143, 0xffff0000, v143
	v_lshlrev_b32_e32 v156, 16, v136
	v_and_b32_e32 v136, 0xffff0000, v136
	v_lshlrev_b32_e32 v157, 16, v137
	v_and_b32_e32 v137, 0xffff0000, v137
	v_lshlrev_b64 v[98:99], 12, v[98:99]
	v_lshlrev_b32_e32 v150, 16, v138
	v_and_b32_e32 v138, 0xffff0000, v138
	v_lshlrev_b32_e32 v153, 16, v141
	v_and_b32_e32 v141, 0xffff0000, v141
	v_lshlrev_b32_e32 v158, 16, v130
	v_and_b32_e32 v130, 0xffff0000, v130
	v_lshlrev_b32_e32 v161, 16, v133
	v_and_b32_e32 v133, 0xffff0000, v133
	v_fmac_f32_e32 v154, v110, v146
	v_fmac_f32_e32 v134, v111, v142
	v_fmac_f32_e32 v155, v112, v147
	v_fmac_f32_e32 v135, v113, v143
	v_fmac_f32_e32 v156, v106, v148
	v_fmac_f32_e32 v136, v107, v144
	v_fmac_f32_e32 v157, v108, v149
	v_fmac_f32_e32 v137, v109, v145
	v_lshl_add_u64 v[98:99], s[36:37], 0, v[98:99]
	v_lshlrev_b32_e32 v151, 16, v139
	v_and_b32_e32 v139, 0xffff0000, v139
	v_lshlrev_b32_e32 v159, 16, v131
	v_and_b32_e32 v131, 0xffff0000, v131
	v_fmac_f32_e32 v158, v102, v150
	v_fmac_f32_e32 v130, v103, v138
	v_fmac_f32_e32 v161, v100, v153
	v_fmac_f32_e32 v133, v101, v141
	v_lshl_add_u64 v[102:103], v[182:183], 1, v[98:99]
	v_cvt_pk_bf16_f32 v98, v154, v134
	v_cvt_pk_bf16_f32 v99, v155, v135
	v_cvt_pk_bf16_f32 v100, v156, v136
	v_cvt_pk_bf16_f32 v101, v157, v137
	v_fmac_f32_e32 v159, v104, v151
	v_fmac_f32_e32 v131, v105, v139
	global_store_dwordx4 v[102:103], v[98:101], off nt
	v_add_co_u32_e32 v102, vcc, 0x8000, v102
	s_nop 0
	v_cvt_pk_bf16_f32 v98, v158, v130
	v_cvt_pk_bf16_f32 v99, v159, v131
	v_cvt_pk_bf16_f32 v100, v160, v132
	v_cvt_pk_bf16_f32 v101, v161, v133
	v_addc_co_u32_e32 v103, vcc, 0, v103, vcc
	global_store_dwordx4 v[102:103], v[98:101], off nt
; template <class Epi, class Sched, bool GATHER, bool ALIGN_EPI = true, bool SP2 = true, bool REMAP64 = false>
; __device__ __forceinline__ void gemm_phase(LAS unsigned char* lds, const bf16* Ag, const bf16* Btg, const int K, const Sched& S, const Epi& E) {
;     ...
;             constexpr bool RP = REMAP64 && Epi::ROWPAIR;
;             const bool hi = RP && (fr >= 8); const int rsh = hi ? -8 : 0, citx = hi ? cit + 32 : cit;
;             typename Epi::Pre pq[2];
;             { const int r0_ = wr * 64 + fr; pq[0] = E.pre(cur, (r0_ < cur.nrows ? r0_ : cur.nrows - 1) + rsh, citx); }
; #pragma unroll
;             for (int gq = 0; gq < 8; ++gq) { const int ai = gq >> 2, m = gq & 3, r = ai * HALF + wr * 64 + m * 16 + fr;
;                 if (gq + 1 < 8) { const int rn = ((gq + 1) >> 2) * HALF + wr * 64 + ((gq + 1) & 3) * 16 + fr; pq[(gq + 1) & 1] = E.pre(cur, (rn < cur.nrows ? rn : cur.nrows - 1) + rsh, citx); }
;                 __builtin_amdgcn_sched_barrier(0);
;                 if (r < cur.nrows) { float v0[8], v1[8];
; #pragma unroll
;                     for (int i = 0; i < 4; ++i) { v0[i] = acc[ai][0][m][0][i]; v0[4 + i] = acc[ai][0][m][1][i]; v1[i] = acc[ai][1][m][0][i]; v1[4 + i] = acc[ai][1][m][1][i]; }
;                     if constexpr (RP) {
; #pragma unroll
;                         for (int i = 0; i < 8; ++i) { const float snd = hi ? v0[i] : v1[i];
;                             const float rcv = __builtin_bit_cast(float, __builtin_amdgcn_update_dpp(0, __builtin_bit_cast(int, snd), 0x128, 0xf, 0xf, false));
;                             if (hi) v0[i] = rcv; else v1[i] = rcv; } }
;                     E.post(cur, r + rsh, citx, v0, v1, pq[gq & 1]); }
;                 __builtin_amdgcn_sched_barrier(0); }
;     __device__ __forceinline__ Pre pre(const Unit& u, int r, int cit) const { const size_t off = (size_t)(u.arow0 + r) * D + u.pn * 256 + cit; return Pre{__builtin_nontemporal_load((const v4u*)(gd + off)), __builtin_nontemporal_load((const v4u*)(gd + off + (size_t)8 * D)), __builtin_nontemporal_load ...
;     __device__ __forceinline__ void post(const Unit& u, int r, int cit, const float* v0, const float* v1, const Pre& p) const {
;         const size_t off = (size_t)(u.arow0 + r) * D + u.pn * 256 + cit; float g0[8], g1[8], m0[8], m1[8]; unpack8bf(p.g0, g0); unpack8bf(p.g1, g1); unpack8bf(p.m0, m0); unpack8bf(p.m1, m1);
; #pragma unroll
.LBB0_1156:
	s_nop 1
	v_add_u32_e32 v98, v197, v190
	v_ashrrev_i32_e32 v99, 31, v98
	v_lshlrev_b64 v[98:99], 11, v[98:99]
	v_lshl_add_u64 v[98:99], v[98:99], 0, v[182:183]
	v_lshlrev_b64 v[98:99], 1, v[98:99]
	v_lshl_add_u64 v[100:101], s[50:51], 0, v[98:99]
	v_add_co_u32_e32 v102, vcc, 0x8000, v100
	v_lshl_add_u64 v[98:99], s[20:21], 0, v[98:99]
	s_nop 0
	v_addc_co_u32_e32 v103, vcc, 0, v101, vcc
	global_load_dwordx4 v[110:113], v[100:101], off nt
	global_load_dwordx4 v[106:109], v[102:103], off nt
	v_add_co_u32_e32 v100, vcc, 0x8000, v98
	s_nop 1
	v_addc_co_u32_e32 v101, vcc, 0, v99, vcc
	global_load_dwordx4 v[102:105], v[98:99], off nt
	s_nop 0
	global_load_dwordx4 v[98:101], v[100:101], off nt
	s_and_b64 vcc, exec, s[8:9]
	s_cbranch_vccnz .LBB0_1158
	s_waitcnt vmcnt(16)
	v_cndmask_b32_e64 v130, v86, v94, s[0:1]
	v_mov_b32_e32 v131, 0
	v_lshlrev_b32_e32 v136, 16, v224
	v_lshlrev_b32_e32 v144, 16, v216
	v_mov_b32_dpp v131, v130 row_ror:8 row_mask:0xf bank_mask:0xf
	v_cndmask_b32_e64 v130, v87, v95, s[0:1]
	v_cndmask_b32_e64 v94, v94, v131, s[0:1]
	v_cndmask_b32_e64 v86, v131, v86, s[0:1]
	v_mov_b32_e32 v131, 0
	v_and_b32_e32 v224, 0xffff0000, v224
	v_and_b32_e32 v216, 0xffff0000, v216
	v_mov_b32_dpp v131, v130 row_ror:8 row_mask:0xf bank_mask:0xf
	v_cndmask_b32_e64 v130, v88, v96, s[0:1]
	v_cndmask_b32_e64 v95, v95, v131, s[0:1]
	v_cndmask_b32_e64 v87, v131, v87, s[0:1]
	v_mov_b32_e32 v131, 0
	v_lshlrev_b32_e32 v132, 16, v228
	v_and_b32_e32 v228, 0xffff0000, v228
	v_mov_b32_dpp v131, v130 row_ror:8 row_mask:0xf bank_mask:0xf
	v_cndmask_b32_e64 v130, v89, v97, s[0:1]
	v_cndmask_b32_e64 v96, v96, v131, s[0:1]
	v_cndmask_b32_e64 v88, v131, v88, s[0:1]
	v_mov_b32_e32 v131, 0
	v_lshlrev_b32_e32 v133, 16, v229
	v_and_b32_e32 v229, 0xffff0000, v229
	v_mov_b32_dpp v131, v130 row_ror:8 row_mask:0xf bank_mask:0xf
	v_cndmask_b32_e64 v130, v82, v90, s[0:1]
	v_cndmask_b32_e64 v97, v97, v131, s[0:1]
	v_cndmask_b32_e64 v89, v131, v89, s[0:1]
	v_mov_b32_e32 v131, 0
	v_lshlrev_b32_e32 v138, 16, v218
	v_and_b32_e32 v218, 0xffff0000, v218
	v_mov_b32_dpp v131, v130 row_ror:8 row_mask:0xf bank_mask:0xf
	v_cndmask_b32_e64 v130, v83, v91, s[0:1]
	v_cndmask_b32_e64 v90, v90, v131, s[0:1]
	v_cndmask_b32_e64 v82, v131, v82, s[0:1]
	v_mov_b32_e32 v131, 0
	v_fmac_f32_e32 v144, v82, v136
	v_add_u32_e32 v82, s65, v196
	v_mov_b32_dpp v131, v130 row_ror:8 row_mask:0xf bank_mask:0xf
	v_cndmask_b32_e64 v130, v84, v92, s[0:1]
	v_cndmask_b32_e64 v91, v91, v131, s[0:1]
	v_cndmask_b32_e64 v83, v131, v83, s[0:1]
	v_mov_b32_e32 v131, 0
	v_fmac_f32_e32 v216, v83, v224
	v_ashrrev_i32_e32 v83, 31, v82
	v_mov_b32_dpp v131, v130 row_ror:8 row_mask:0xf bank_mask:0xf
	v_cndmask_b32_e64 v130, v85, v93, s[0:1]
	v_cndmask_b32_e64 v92, v92, v131, s[0:1]
	v_cndmask_b32_e64 v84, v131, v84, s[0:1]
	v_mov_b32_e32 v131, 0
	v_lshlrev_b32_e32 v139, 16, v219
	v_and_b32_e32 v219, 0xffff0000, v219
	v_mov_b32_dpp v131, v130 row_ror:8 row_mask:0xf bank_mask:0xf
	v_cndmask_b32_e64 v93, v93, v131, s[0:1]
	v_cndmask_b32_e64 v85, v131, v85, s[0:1]
	v_lshlrev_b32_e32 v130, 16, v226
	v_and_b32_e32 v226, 0xffff0000, v226
	v_lshlrev_b32_e32 v131, 16, v227
	v_and_b32_e32 v227, 0xffff0000, v227
	v_lshlrev_b32_e32 v140, 16, v220
	v_and_b32_e32 v220, 0xffff0000, v220
	v_lshlrev_b32_e32 v141, 16, v221
	v_and_b32_e32 v221, 0xffff0000, v221
	v_lshlrev_b64 v[82:83], 12, v[82:83]
	v_lshlrev_b32_e32 v134, 16, v222
	v_and_b32_e32 v222, 0xffff0000, v222
	v_lshlrev_b32_e32 v137, 16, v225
	v_and_b32_e32 v225, 0xffff0000, v225
	v_lshlrev_b32_e32 v142, 16, v214
	v_and_b32_e32 v214, 0xffff0000, v214
	v_lshlrev_b32_e32 v145, 16, v217
	v_and_b32_e32 v217, 0xffff0000, v217
	v_fmac_f32_e32 v138, v94, v130
	v_fmac_f32_e32 v218, v95, v226
	v_fmac_f32_e32 v139, v96, v131
	v_fmac_f32_e32 v219, v97, v227
	v_fmac_f32_e32 v140, v90, v132
	v_fmac_f32_e32 v220, v91, v228
	v_fmac_f32_e32 v141, v92, v133
	v_fmac_f32_e32 v221, v93, v229
	v_lshl_add_u64 v[82:83], s[36:37], 0, v[82:83]
	v_lshlrev_b32_e32 v135, 16, v223
	v_and_b32_e32 v223, 0xffff0000, v223
	v_lshlrev_b32_e32 v143, 16, v215
	v_and_b32_e32 v215, 0xffff0000, v215
	v_fmac_f32_e32 v142, v86, v134
	v_fmac_f32_e32 v214, v87, v222
	v_fmac_f32_e32 v145, v84, v137
	v_fmac_f32_e32 v217, v85, v225
	v_lshl_add_u64 v[86:87], v[182:183], 1, v[82:83]
	v_cvt_pk_bf16_f32 v82, v138, v218
	v_cvt_pk_bf16_f32 v83, v139, v219
	v_cvt_pk_bf16_f32 v84, v140, v220
	v_cvt_pk_bf16_f32 v85, v141, v221
	v_fmac_f32_e32 v143, v88, v135
	v_fmac_f32_e32 v215, v89, v223
	global_store_dwordx4 v[86:87], v[82:85], off nt
	v_add_co_u32_e32 v86, vcc, 0x8000, v86
	s_nop 0
	v_cvt_pk_bf16_f32 v82, v142, v214
	v_cvt_pk_bf16_f32 v83, v143, v215
	v_cvt_pk_bf16_f32 v84, v144, v216
	v_cvt_pk_bf16_f32 v85, v145, v217
	v_addc_co_u32_e32 v87, vcc, 0, v87, vcc
	global_store_dwordx4 v[86:87], v[82:85], off nt
; template <class Epi, class Sched, bool GATHER, bool ALIGN_EPI = true, bool SP2 = true, bool REMAP64 = false>
; __device__ __forceinline__ void gemm_phase(LAS unsigned char* lds, const bf16* Ag, const bf16* Btg, const int K, const Sched& S, const Epi& E) {
;     ...
;             constexpr bool RP = REMAP64 && Epi::ROWPAIR;
;             const bool hi = RP && (fr >= 8); const int rsh = hi ? -8 : 0, citx = hi ? cit + 32 : cit;
;             typename Epi::Pre pq[2];
;             { const int r0_ = wr * 64 + fr; pq[0] = E.pre(cur, (r0_ < cur.nrows ? r0_ : cur.nrows - 1) + rsh, citx); }
; #pragma unroll
;             for (int gq = 0; gq < 8; ++gq) { const int ai = gq >> 2, m = gq & 3, r = ai * HALF + wr * 64 + m * 16 + fr;
;                 if (gq + 1 < 8) { const int rn = ((gq + 1) >> 2) * HALF + wr * 64 + ((gq + 1) & 3) * 16 + fr; pq[(gq + 1) & 1] = E.pre(cur, (rn < cur.nrows ? rn : cur.nrows - 1) + rsh, citx); }
;                 __builtin_amdgcn_sched_barrier(0);
;                 if (r < cur.nrows) { float v0[8], v1[8];
; #pragma unroll
;                     for (int i = 0; i < 4; ++i) { v0[i] = acc[ai][0][m][0][i]; v0[4 + i] = acc[ai][0][m][1][i]; v1[i] = acc[ai][1][m][0][i]; v1[4 + i] = acc[ai][1][m][1][i]; }
;                     if constexpr (RP) {
; #pragma unroll
;                         for (int i = 0; i < 8; ++i) { const float snd = hi ? v0[i] : v1[i];
;                             const float rcv = __builtin_bit_cast(float, __builtin_amdgcn_update_dpp(0, __builtin_bit_cast(int, snd), 0x128, 0xf, 0xf, false));
;                             if (hi) v0[i] = rcv; else v1[i] = rcv; } }
;                     E.post(cur, r + rsh, citx, v0, v1, pq[gq & 1]); }
;                 __builtin_amdgcn_sched_barrier(0); }
;     __device__ __forceinline__ Pre pre(const Unit& u, int r, int cit) const { const size_t off = (size_t)(u.arow0 + r) * D + u.pn * 256 + cit; return Pre{__builtin_nontemporal_load((const v4u*)(gd + off)), __builtin_nontemporal_load((const v4u*)(gd + off + (size_t)8 * D)), __builtin_nontemporal_load ...
;     __device__ __forceinline__ void post(const Unit& u, int r, int cit, const float* v0, const float* v1, const Pre& p) const {
;         const size_t off = (size_t)(u.arow0 + r) * D + u.pn * 256 + cit; float g0[8], g1[8], m0[8], m1[8]; unpack8bf(p.g0, g0); unpack8bf(p.g1, g1); unpack8bf(p.m0, m0); unpack8bf(p.m1, m1);
; #pragma unroll
.LBB0_1158:
	s_nop 1
	v_add_u32_e32 v82, v197, v191
	v_ashrrev_i32_e32 v83, 31, v82
	v_lshlrev_b64 v[82:83], 11, v[82:83]
	v_lshl_add_u64 v[82:83], v[82:83], 0, v[182:183]
	v_lshlrev_b64 v[82:83], 1, v[82:83]
	v_lshl_add_u64 v[84:85], s[50:51], 0, v[82:83]
	v_add_co_u32_e32 v86, vcc, 0x8000, v84
	v_lshl_add_u64 v[82:83], s[20:21], 0, v[82:83]
	s_nop 0
	v_addc_co_u32_e32 v87, vcc, 0, v85, vcc
	global_load_dwordx4 v[94:97], v[84:85], off nt
	global_load_dwordx4 v[90:93], v[86:87], off nt
	v_add_co_u32_e32 v84, vcc, 0x8000, v82
	s_nop 1
	v_addc_co_u32_e32 v85, vcc, 0, v83, vcc
	global_load_dwordx4 v[86:89], v[82:83], off nt
	s_nop 0
	global_load_dwordx4 v[82:85], v[84:85], off nt
	s_and_b64 vcc, exec, s[8:9]
	s_cbranch_vccnz .LBB0_1160
	s_waitcnt vmcnt(18)
	v_cndmask_b32_e64 v146, v70, v78, s[0:1]
	v_mov_b32_e32 v147, 0
	s_nop 0
	v_lshlrev_b32_e32 v152, 16, v240
	s_nop 0
	v_lshlrev_b32_e32 v160, 16, v232
	v_mov_b32_dpp v147, v146 row_ror:8 row_mask:0xf bank_mask:0xf
	v_cndmask_b32_e64 v146, v71, v79, s[0:1]
	v_cndmask_b32_e64 v78, v78, v147, s[0:1]
	v_cndmask_b32_e64 v70, v147, v70, s[0:1]
	v_mov_b32_e32 v147, 0
	v_and_b32_e32 v240, 0xffff0000, v240
	v_and_b32_e32 v232, 0xffff0000, v232
	v_mov_b32_dpp v147, v146 row_ror:8 row_mask:0xf bank_mask:0xf
	v_cndmask_b32_e64 v146, v72, v80, s[0:1]
	v_cndmask_b32_e64 v79, v79, v147, s[0:1]
	v_cndmask_b32_e64 v71, v147, v71, s[0:1]
	v_mov_b32_e32 v147, 0
	v_lshlrev_b32_e32 v148, 16, v244
	v_and_b32_e32 v244, 0xffff0000, v244
	v_mov_b32_dpp v147, v146 row_ror:8 row_mask:0xf bank_mask:0xf
	v_cndmask_b32_e64 v146, v73, v81, s[0:1]
	v_cndmask_b32_e64 v80, v80, v147, s[0:1]
	v_cndmask_b32_e64 v72, v147, v72, s[0:1]
	v_mov_b32_e32 v147, 0
	v_lshlrev_b32_e32 v149, 16, v245
	v_and_b32_e32 v245, 0xffff0000, v245
	v_mov_b32_dpp v147, v146 row_ror:8 row_mask:0xf bank_mask:0xf
	v_cndmask_b32_e64 v146, v66, v74, s[0:1]
	v_cndmask_b32_e64 v81, v81, v147, s[0:1]
	v_cndmask_b32_e64 v73, v147, v73, s[0:1]
	v_mov_b32_e32 v147, 0
	v_lshlrev_b32_e32 v154, 16, v234
	v_and_b32_e32 v234, 0xffff0000, v234
	v_mov_b32_dpp v147, v146 row_ror:8 row_mask:0xf bank_mask:0xf
	v_cndmask_b32_e64 v146, v67, v75, s[0:1]
	v_cndmask_b32_e64 v74, v74, v147, s[0:1]
	v_cndmask_b32_e64 v66, v147, v66, s[0:1]
	v_mov_b32_e32 v147, 0
	v_fmac_f32_e32 v160, v66, v152
	v_add_u32_e32 v66, s71, v196
	v_mov_b32_dpp v147, v146 row_ror:8 row_mask:0xf bank_mask:0xf
	v_cndmask_b32_e64 v146, v68, v76, s[0:1]
	v_cndmask_b32_e64 v75, v75, v147, s[0:1]
	v_cndmask_b32_e64 v67, v147, v67, s[0:1]
	v_mov_b32_e32 v147, 0
	v_fmac_f32_e32 v232, v67, v240
	v_ashrrev_i32_e32 v67, 31, v66
	v_mov_b32_dpp v147, v146 row_ror:8 row_mask:0xf bank_mask:0xf
	v_cndmask_b32_e64 v146, v69, v77, s[0:1]
	v_cndmask_b32_e64 v76, v76, v147, s[0:1]
	v_cndmask_b32_e64 v68, v147, v68, s[0:1]
	v_mov_b32_e32 v147, 0
	v_lshlrev_b32_e32 v155, 16, v235
	v_and_b32_e32 v235, 0xffff0000, v235
	v_mov_b32_dpp v147, v146 row_ror:8 row_mask:0xf bank_mask:0xf
	v_cndmask_b32_e64 v77, v77, v147, s[0:1]
	v_cndmask_b32_e64 v69, v147, v69, s[0:1]
	v_lshlrev_b32_e32 v146, 16, v242
	v_and_b32_e32 v242, 0xffff0000, v242
	v_lshlrev_b32_e32 v147, 16, v243
	v_and_b32_e32 v243, 0xffff0000, v243
	v_lshlrev_b32_e32 v156, 16, v236
	v_and_b32_e32 v236, 0xffff0000, v236
	v_lshlrev_b32_e32 v157, 16, v237
	v_and_b32_e32 v237, 0xffff0000, v237
	v_lshlrev_b64 v[66:67], 12, v[66:67]
	v_lshlrev_b32_e32 v150, 16, v238
	v_and_b32_e32 v238, 0xffff0000, v238
	v_lshlrev_b32_e32 v153, 16, v241
	v_and_b32_e32 v241, 0xffff0000, v241
	v_lshlrev_b32_e32 v158, 16, v230
	v_and_b32_e32 v230, 0xffff0000, v230
	v_lshlrev_b32_e32 v161, 16, v233
	v_and_b32_e32 v233, 0xffff0000, v233
	v_fmac_f32_e32 v154, v78, v146
	v_fmac_f32_e32 v234, v79, v242
	v_fmac_f32_e32 v155, v80, v147
	v_fmac_f32_e32 v235, v81, v243
	v_fmac_f32_e32 v156, v74, v148
	v_fmac_f32_e32 v236, v75, v244
	v_fmac_f32_e32 v157, v76, v149
	v_fmac_f32_e32 v237, v77, v245
	v_lshl_add_u64 v[66:67], s[36:37], 0, v[66:67]
	v_lshlrev_b32_e32 v151, 16, v239
	v_and_b32_e32 v239, 0xffff0000, v239
	v_lshlrev_b32_e32 v159, 16, v231
	v_and_b32_e32 v231, 0xffff0000, v231
	v_fmac_f32_e32 v158, v70, v150
	v_fmac_f32_e32 v230, v71, v238
	v_fmac_f32_e32 v161, v68, v153
	v_fmac_f32_e32 v233, v69, v241
	v_lshl_add_u64 v[70:71], v[182:183], 1, v[66:67]
	v_cvt_pk_bf16_f32 v66, v154, v234
	v_cvt_pk_bf16_f32 v67, v155, v235
	v_cvt_pk_bf16_f32 v68, v156, v236
	v_cvt_pk_bf16_f32 v69, v157, v237
	v_fmac_f32_e32 v159, v72, v151
	v_fmac_f32_e32 v231, v73, v239
	global_store_dwordx4 v[70:71], v[66:69], off nt
	v_add_co_u32_e32 v70, vcc, 0x8000, v70
	s_nop 0
	v_cvt_pk_bf16_f32 v66, v158, v230
	v_cvt_pk_bf16_f32 v67, v159, v231
	v_cvt_pk_bf16_f32 v68, v160, v232
	v_cvt_pk_bf16_f32 v69, v161, v233
	v_addc_co_u32_e32 v71, vcc, 0, v71, vcc
	global_store_dwordx4 v[70:71], v[66:69], off nt
; template <class Epi, class Sched, bool GATHER, bool ALIGN_EPI = true, bool SP2 = true, bool REMAP64 = false>
; __device__ __forceinline__ void gemm_phase(LAS unsigned char* lds, const bf16* Ag, const bf16* Btg, const int K, const Sched& S, const Epi& E) {
;     ...
;             constexpr bool RP = REMAP64 && Epi::ROWPAIR;
;             const bool hi = RP && (fr >= 8); const int rsh = hi ? -8 : 0, citx = hi ? cit + 32 : cit;
;             typename Epi::Pre pq[2];
;             { const int r0_ = wr * 64 + fr; pq[0] = E.pre(cur, (r0_ < cur.nrows ? r0_ : cur.nrows - 1) + rsh, citx); }
; #pragma unroll
;             for (int gq = 0; gq < 8; ++gq) { const int ai = gq >> 2, m = gq & 3, r = ai * HALF + wr * 64 + m * 16 + fr;
;                 if (gq + 1 < 8) { const int rn = ((gq + 1) >> 2) * HALF + wr * 64 + ((gq + 1) & 3) * 16 + fr; pq[(gq + 1) & 1] = E.pre(cur, (rn < cur.nrows ? rn : cur.nrows - 1) + rsh, citx); }
;                 __builtin_amdgcn_sched_barrier(0);
;                 if (r < cur.nrows) { float v0[8], v1[8];
; #pragma unroll
;                     for (int i = 0; i < 4; ++i) { v0[i] = acc[ai][0][m][0][i]; v0[4 + i] = acc[ai][0][m][1][i]; v1[i] = acc[ai][1][m][0][i]; v1[4 + i] = acc[ai][1][m][1][i]; }
;                     if constexpr (RP) {
; #pragma unroll
;                         for (int i = 0; i < 8; ++i) { const float snd = hi ? v0[i] : v1[i];
;                             const float rcv = __builtin_bit_cast(float, __builtin_amdgcn_update_dpp(0, __builtin_bit_cast(int, snd), 0x128, 0xf, 0xf, false));
;                             if (hi) v0[i] = rcv; else v1[i] = rcv; } }
;                     E.post(cur, r + rsh, citx, v0, v1, pq[gq & 1]); }
;                 __builtin_amdgcn_sched_barrier(0); }
;     __device__ __forceinline__ Pre pre(const Unit& u, int r, int cit) const { const size_t off = (size_t)(u.arow0 + r) * D + u.pn * 256 + cit; return Pre{__builtin_nontemporal_load((const v4u*)(gd + off)), __builtin_nontemporal_load((const v4u*)(gd + off + (size_t)8 * D)), __builtin_nontemporal_load ...
;     __device__ __forceinline__ void post(const Unit& u, int r, int cit, const float* v0, const float* v1, const Pre& p) const {
;         const size_t off = (size_t)(u.arow0 + r) * D + u.pn * 256 + cit; float g0[8], g1[8], m0[8], m1[8]; unpack8bf(p.g0, g0); unpack8bf(p.g1, g1); unpack8bf(p.m0, m0); unpack8bf(p.m1, m1);
; #pragma unroll
.LBB0_1160:
	s_nop 1
	v_add_u32_e32 v66, v197, v192
	v_ashrrev_i32_e32 v67, 31, v66
	v_lshlrev_b64 v[66:67], 11, v[66:67]
	v_lshl_add_u64 v[66:67], v[66:67], 0, v[182:183]
	v_lshlrev_b64 v[66:67], 1, v[66:67]
	v_lshl_add_u64 v[68:69], s[50:51], 0, v[66:67]
	v_add_co_u32_e32 v70, vcc, 0x8000, v68
	v_lshl_add_u64 v[66:67], s[20:21], 0, v[66:67]
	s_nop 0
	v_addc_co_u32_e32 v71, vcc, 0, v69, vcc
	global_load_dwordx4 v[78:81], v[68:69], off nt
	global_load_dwordx4 v[74:77], v[70:71], off nt
	v_add_co_u32_e32 v68, vcc, 0x8000, v66
	s_nop 1
	v_addc_co_u32_e32 v69, vcc, 0, v67, vcc
	global_load_dwordx4 v[70:73], v[66:67], off nt
	s_nop 0
	global_load_dwordx4 v[66:69], v[68:69], off nt
	s_nop 0
	v_cndmask_b32_e64 v146, 0, 1, s[18:19]
	v_cmp_ne_u32_e64 s[8:9], 1, v146
	s_andn2_b64 vcc, exec, s[18:19]
	s_cbranch_vccnz .LBB0_1162
	s_waitcnt vmcnt(18)
	v_cndmask_b32_e64 v130, v54, v62, s[0:1]
	v_mov_b32_e32 v131, 0
	s_nop 0
	v_lshlrev_b32_e32 v136, 16, v124
	s_nop 0
	v_lshlrev_b32_e32 v144, 16, v116
	v_mov_b32_dpp v131, v130 row_ror:8 row_mask:0xf bank_mask:0xf
	v_cndmask_b32_e64 v130, v55, v63, s[0:1]
	v_cndmask_b32_e64 v62, v62, v131, s[0:1]
	v_cndmask_b32_e64 v54, v131, v54, s[0:1]
	v_mov_b32_e32 v131, 0
	v_and_b32_e32 v124, 0xffff0000, v124
	v_and_b32_e32 v116, 0xffff0000, v116
	v_mov_b32_dpp v131, v130 row_ror:8 row_mask:0xf bank_mask:0xf
	v_cndmask_b32_e64 v130, v56, v64, s[0:1]
	v_cndmask_b32_e64 v63, v63, v131, s[0:1]
	v_cndmask_b32_e64 v55, v131, v55, s[0:1]
	v_mov_b32_e32 v131, 0
	v_lshlrev_b32_e32 v132, 16, v128
	v_and_b32_e32 v128, 0xffff0000, v128
	v_mov_b32_dpp v131, v130 row_ror:8 row_mask:0xf bank_mask:0xf
	v_cndmask_b32_e64 v130, v57, v65, s[0:1]
	v_cndmask_b32_e64 v64, v64, v131, s[0:1]
	v_cndmask_b32_e64 v56, v131, v56, s[0:1]
	v_mov_b32_e32 v131, 0
	v_lshlrev_b32_e32 v133, 16, v129
	v_and_b32_e32 v129, 0xffff0000, v129
	v_mov_b32_dpp v131, v130 row_ror:8 row_mask:0xf bank_mask:0xf
	v_cndmask_b32_e64 v130, v50, v58, s[0:1]
	v_cndmask_b32_e64 v65, v65, v131, s[0:1]
	v_cndmask_b32_e64 v57, v131, v57, s[0:1]
	v_mov_b32_e32 v131, 0
	v_lshlrev_b32_e32 v138, 16, v118
	v_and_b32_e32 v118, 0xffff0000, v118
	v_mov_b32_dpp v131, v130 row_ror:8 row_mask:0xf bank_mask:0xf
	v_cndmask_b32_e64 v130, v51, v59, s[0:1]
	v_cndmask_b32_e64 v58, v58, v131, s[0:1]
	v_cndmask_b32_e64 v50, v131, v50, s[0:1]
	v_mov_b32_e32 v131, 0
	v_fmac_f32_e32 v144, v50, v136
	v_add_u32_e32 v50, s70, v196
	v_mov_b32_dpp v131, v130 row_ror:8 row_mask:0xf bank_mask:0xf
	v_cndmask_b32_e64 v130, v52, v60, s[0:1]
	v_cndmask_b32_e64 v59, v59, v131, s[0:1]
	v_cndmask_b32_e64 v51, v131, v51, s[0:1]
	v_mov_b32_e32 v131, 0
	v_fmac_f32_e32 v116, v51, v124
	v_ashrrev_i32_e32 v51, 31, v50
	v_mov_b32_dpp v131, v130 row_ror:8 row_mask:0xf bank_mask:0xf
	v_cndmask_b32_e64 v130, v53, v61, s[0:1]
	v_cndmask_b32_e64 v60, v60, v131, s[0:1]
	v_cndmask_b32_e64 v52, v131, v52, s[0:1]
	v_mov_b32_e32 v131, 0
	v_lshlrev_b32_e32 v139, 16, v119
	v_and_b32_e32 v119, 0xffff0000, v119
	v_mov_b32_dpp v131, v130 row_ror:8 row_mask:0xf bank_mask:0xf
	v_cndmask_b32_e64 v61, v61, v131, s[0:1]
	v_cndmask_b32_e64 v53, v131, v53, s[0:1]
	v_lshlrev_b32_e32 v130, 16, v126
	v_and_b32_e32 v126, 0xffff0000, v126
	v_lshlrev_b32_e32 v131, 16, v127
	v_and_b32_e32 v127, 0xffff0000, v127
	v_lshlrev_b32_e32 v140, 16, v120
	v_and_b32_e32 v120, 0xffff0000, v120
	v_lshlrev_b32_e32 v141, 16, v121
	v_and_b32_e32 v121, 0xffff0000, v121
	v_lshlrev_b64 v[50:51], 12, v[50:51]
	v_lshlrev_b32_e32 v134, 16, v122
	v_and_b32_e32 v122, 0xffff0000, v122
	v_lshlrev_b32_e32 v137, 16, v125
	v_and_b32_e32 v125, 0xffff0000, v125
	v_lshlrev_b32_e32 v142, 16, v114
	v_and_b32_e32 v114, 0xffff0000, v114
	v_lshlrev_b32_e32 v145, 16, v117
	v_and_b32_e32 v117, 0xffff0000, v117
	v_fmac_f32_e32 v138, v62, v130
	v_fmac_f32_e32 v118, v63, v126
	v_fmac_f32_e32 v139, v64, v131
	v_fmac_f32_e32 v119, v65, v127
	v_fmac_f32_e32 v140, v58, v132
	v_fmac_f32_e32 v120, v59, v128
	v_fmac_f32_e32 v141, v60, v133
	v_fmac_f32_e32 v121, v61, v129
	v_lshl_add_u64 v[50:51], s[36:37], 0, v[50:51]
	v_lshlrev_b32_e32 v135, 16, v123
	v_and_b32_e32 v123, 0xffff0000, v123
	v_lshlrev_b32_e32 v143, 16, v115
	v_and_b32_e32 v115, 0xffff0000, v115
	v_fmac_f32_e32 v142, v54, v134
	v_fmac_f32_e32 v114, v55, v122
	v_fmac_f32_e32 v145, v52, v137
	v_fmac_f32_e32 v117, v53, v125
	v_lshl_add_u64 v[54:55], v[182:183], 1, v[50:51]
	v_cvt_pk_bf16_f32 v50, v138, v118
	v_cvt_pk_bf16_f32 v51, v139, v119
	v_cvt_pk_bf16_f32 v52, v140, v120
	v_cvt_pk_bf16_f32 v53, v141, v121
	v_fmac_f32_e32 v143, v56, v135
	v_fmac_f32_e32 v115, v57, v123
	global_store_dwordx4 v[54:55], v[50:53], off nt
	v_add_co_u32_e32 v54, vcc, 0x8000, v54
	s_nop 0
	v_cvt_pk_bf16_f32 v50, v142, v114
	v_cvt_pk_bf16_f32 v51, v143, v115
	v_cvt_pk_bf16_f32 v52, v144, v116
	v_cvt_pk_bf16_f32 v53, v145, v117
	v_addc_co_u32_e32 v55, vcc, 0, v55, vcc
	global_store_dwordx4 v[54:55], v[50:53], off nt
; template <class Epi, class Sched, bool GATHER, bool ALIGN_EPI = true, bool SP2 = true, bool REMAP64 = false>
; __device__ __forceinline__ void gemm_phase(LAS unsigned char* lds, const bf16* Ag, const bf16* Btg, const int K, const Sched& S, const Epi& E) {
;     ...
;             constexpr bool RP = REMAP64 && Epi::ROWPAIR;
;             const bool hi = RP && (fr >= 8); const int rsh = hi ? -8 : 0, citx = hi ? cit + 32 : cit;
;             typename Epi::Pre pq[2];
;             { const int r0_ = wr * 64 + fr; pq[0] = E.pre(cur, (r0_ < cur.nrows ? r0_ : cur.nrows - 1) + rsh, citx); }
; #pragma unroll
;             for (int gq = 0; gq < 8; ++gq) { const int ai = gq >> 2, m = gq & 3, r = ai * HALF + wr * 64 + m * 16 + fr;
;                 if (gq + 1 < 8) { const int rn = ((gq + 1) >> 2) * HALF + wr * 64 + ((gq + 1) & 3) * 16 + fr; pq[(gq + 1) & 1] = E.pre(cur, (rn < cur.nrows ? rn : cur.nrows - 1) + rsh, citx); }
;                 __builtin_amdgcn_sched_barrier(0);
;                 if (r < cur.nrows) { float v0[8], v1[8];
; #pragma unroll
;                     for (int i = 0; i < 4; ++i) { v0[i] = acc[ai][0][m][0][i]; v0[4 + i] = acc[ai][0][m][1][i]; v1[i] = acc[ai][1][m][0][i]; v1[4 + i] = acc[ai][1][m][1][i]; }
;                     if constexpr (RP) {
; #pragma unroll
;                         for (int i = 0; i < 8; ++i) { const float snd = hi ? v0[i] : v1[i];
;                             const float rcv = __builtin_bit_cast(float, __builtin_amdgcn_update_dpp(0, __builtin_bit_cast(int, snd), 0x128, 0xf, 0xf, false));
;                             if (hi) v0[i] = rcv; else v1[i] = rcv; } }
;                     E.post(cur, r + rsh, citx, v0, v1, pq[gq & 1]); }
;                 __builtin_amdgcn_sched_barrier(0); }
;     __device__ __forceinline__ Pre pre(const Unit& u, int r, int cit) const { const size_t off = (size_t)(u.arow0 + r) * D + u.pn * 256 + cit; return Pre{__builtin_nontemporal_load((const v4u*)(gd + off)), __builtin_nontemporal_load((const v4u*)(gd + off + (size_t)8 * D)), __builtin_nontemporal_load ...
;     __device__ __forceinline__ void post(const Unit& u, int r, int cit, const float* v0, const float* v1, const Pre& p) const {
;         const size_t off = (size_t)(u.arow0 + r) * D + u.pn * 256 + cit; float g0[8], g1[8], m0[8], m1[8]; unpack8bf(p.g0, g0); unpack8bf(p.g1, g1); unpack8bf(p.m0, m0); unpack8bf(p.m1, m1);
; #pragma unroll
.LBB0_1162:
	s_and_b64 vcc, exec, s[8:9]
	s_cbranch_vccnz .LBB0_1164
	s_waitcnt vmcnt(14)
	s_nop 0
	v_cndmask_b32_e64 v146, v38, v46, s[0:1]
	v_mov_b32_e32 v147, 0
	s_nop 0
	v_lshlrev_b32_e32 v152, 16, v108
	s_nop 0
	v_lshlrev_b32_e32 v160, 16, v100
	v_mov_b32_dpp v147, v146 row_ror:8 row_mask:0xf bank_mask:0xf
	v_cndmask_b32_e64 v146, v39, v47, s[0:1]
	v_cndmask_b32_e64 v46, v46, v147, s[0:1]
	v_cndmask_b32_e64 v38, v147, v38, s[0:1]
	v_mov_b32_e32 v147, 0
	v_and_b32_e32 v108, 0xffff0000, v108
	v_and_b32_e32 v100, 0xffff0000, v100
	v_mov_b32_dpp v147, v146 row_ror:8 row_mask:0xf bank_mask:0xf
	v_cndmask_b32_e64 v146, v40, v48, s[0:1]
	v_cndmask_b32_e64 v47, v47, v147, s[0:1]
	v_cndmask_b32_e64 v39, v147, v39, s[0:1]
	v_mov_b32_e32 v147, 0
	v_lshlrev_b32_e32 v148, 16, v112
	v_and_b32_e32 v112, 0xffff0000, v112
	v_mov_b32_dpp v147, v146 row_ror:8 row_mask:0xf bank_mask:0xf
	v_cndmask_b32_e64 v146, v41, v49, s[0:1]
	v_cndmask_b32_e64 v48, v48, v147, s[0:1]
	v_cndmask_b32_e64 v40, v147, v40, s[0:1]
	v_mov_b32_e32 v147, 0
	v_lshlrev_b32_e32 v149, 16, v113
	v_and_b32_e32 v113, 0xffff0000, v113
	v_mov_b32_dpp v147, v146 row_ror:8 row_mask:0xf bank_mask:0xf
	v_cndmask_b32_e64 v146, v34, v42, s[0:1]
	v_cndmask_b32_e64 v49, v49, v147, s[0:1]
	v_cndmask_b32_e64 v41, v147, v41, s[0:1]
	v_mov_b32_e32 v147, 0
	v_lshlrev_b32_e32 v154, 16, v102
	v_and_b32_e32 v102, 0xffff0000, v102
	v_mov_b32_dpp v147, v146 row_ror:8 row_mask:0xf bank_mask:0xf
	v_cndmask_b32_e64 v146, v35, v43, s[0:1]
	v_cndmask_b32_e64 v42, v42, v147, s[0:1]
	v_cndmask_b32_e64 v34, v147, v34, s[0:1]
	v_mov_b32_e32 v147, 0
	v_fmac_f32_e32 v160, v34, v152
	v_add_u32_e32 v34, s72, v196
	v_mov_b32_dpp v147, v146 row_ror:8 row_mask:0xf bank_mask:0xf
	v_cndmask_b32_e64 v146, v36, v44, s[0:1]
	v_cndmask_b32_e64 v43, v43, v147, s[0:1]
	v_cndmask_b32_e64 v35, v147, v35, s[0:1]
	v_mov_b32_e32 v147, 0
	v_fmac_f32_e32 v100, v35, v108
	v_ashrrev_i32_e32 v35, 31, v34
	v_mov_b32_dpp v147, v146 row_ror:8 row_mask:0xf bank_mask:0xf
	v_cndmask_b32_e64 v146, v37, v45, s[0:1]
	v_cndmask_b32_e64 v44, v44, v147, s[0:1]
	v_cndmask_b32_e64 v36, v147, v36, s[0:1]
	v_mov_b32_e32 v147, 0
	v_lshlrev_b32_e32 v155, 16, v103
	v_and_b32_e32 v103, 0xffff0000, v103
	v_mov_b32_dpp v147, v146 row_ror:8 row_mask:0xf bank_mask:0xf
	v_cndmask_b32_e64 v45, v45, v147, s[0:1]
	v_cndmask_b32_e64 v37, v147, v37, s[0:1]
	v_lshlrev_b32_e32 v146, 16, v110
	v_and_b32_e32 v110, 0xffff0000, v110
	v_lshlrev_b32_e32 v147, 16, v111
	v_and_b32_e32 v111, 0xffff0000, v111
	v_lshlrev_b32_e32 v156, 16, v104
	v_and_b32_e32 v104, 0xffff0000, v104
	v_lshlrev_b32_e32 v157, 16, v105
	v_and_b32_e32 v105, 0xffff0000, v105
	v_lshlrev_b64 v[34:35], 12, v[34:35]
	v_lshlrev_b32_e32 v150, 16, v106
	v_and_b32_e32 v106, 0xffff0000, v106
	v_lshlrev_b32_e32 v153, 16, v109
	v_and_b32_e32 v109, 0xffff0000, v109
	v_lshlrev_b32_e32 v158, 16, v98
	v_and_b32_e32 v98, 0xffff0000, v98
	v_lshlrev_b32_e32 v161, 16, v101
	v_and_b32_e32 v101, 0xffff0000, v101
	v_fmac_f32_e32 v154, v46, v146
	v_fmac_f32_e32 v102, v47, v110
	v_fmac_f32_e32 v155, v48, v147
	v_fmac_f32_e32 v103, v49, v111
	v_fmac_f32_e32 v156, v42, v148
	v_fmac_f32_e32 v104, v43, v112
	v_fmac_f32_e32 v157, v44, v149
	v_fmac_f32_e32 v105, v45, v113
	v_lshl_add_u64 v[34:35], s[36:37], 0, v[34:35]
	v_lshlrev_b32_e32 v151, 16, v107
	v_and_b32_e32 v107, 0xffff0000, v107
	v_lshlrev_b32_e32 v159, 16, v99
	v_and_b32_e32 v99, 0xffff0000, v99
	v_fmac_f32_e32 v158, v38, v150
	v_fmac_f32_e32 v98, v39, v106
	v_fmac_f32_e32 v161, v36, v153
	v_fmac_f32_e32 v101, v37, v109
	v_lshl_add_u64 v[38:39], v[182:183], 1, v[34:35]
	v_cvt_pk_bf16_f32 v34, v154, v102
	v_cvt_pk_bf16_f32 v35, v155, v103
	v_cvt_pk_bf16_f32 v36, v156, v104
	v_cvt_pk_bf16_f32 v37, v157, v105
	v_fmac_f32_e32 v159, v40, v151
	v_fmac_f32_e32 v99, v41, v107
	global_store_dwordx4 v[38:39], v[34:37], off nt
	v_add_co_u32_e32 v38, vcc, 0x8000, v38
	s_nop 0
	v_cvt_pk_bf16_f32 v34, v158, v98
	v_cvt_pk_bf16_f32 v35, v159, v99
	v_cvt_pk_bf16_f32 v36, v160, v100
	v_cvt_pk_bf16_f32 v37, v161, v101
	v_addc_co_u32_e32 v39, vcc, 0, v39, vcc
	global_store_dwordx4 v[38:39], v[34:37], off nt
.LBB0_1164:
	s_and_b64 vcc, exec, s[8:9]
	s_cbranch_vccnz .LBB0_1166
	s_waitcnt vmcnt(10)
	s_nop 0
	v_cndmask_b32_e64 v130, v22, v30, s[0:1]
	v_mov_b32_e32 v131, 0
	s_nop 0
	v_lshlrev_b32_e32 v136, 16, v92
	s_nop 0
	v_lshlrev_b32_e32 v144, 16, v84
	v_mov_b32_dpp v131, v130 row_ror:8 row_mask:0xf bank_mask:0xf
	v_cndmask_b32_e64 v130, v23, v31, s[0:1]
	v_cndmask_b32_e64 v30, v30, v131, s[0:1]
	v_cndmask_b32_e64 v22, v131, v22, s[0:1]
	v_mov_b32_e32 v131, 0
	v_and_b32_e32 v92, 0xffff0000, v92
	v_and_b32_e32 v84, 0xffff0000, v84
	v_mov_b32_dpp v131, v130 row_ror:8 row_mask:0xf bank_mask:0xf
	v_cndmask_b32_e64 v130, v24, v32, s[0:1]
	v_cndmask_b32_e64 v31, v31, v131, s[0:1]
	v_cndmask_b32_e64 v23, v131, v23, s[0:1]
	v_mov_b32_e32 v131, 0
	v_lshlrev_b32_e32 v132, 16, v96
	v_and_b32_e32 v96, 0xffff0000, v96
	v_mov_b32_dpp v131, v130 row_ror:8 row_mask:0xf bank_mask:0xf
	v_cndmask_b32_e64 v130, v25, v33, s[0:1]
	v_cndmask_b32_e64 v32, v32, v131, s[0:1]
	v_cndmask_b32_e64 v24, v131, v24, s[0:1]
	v_mov_b32_e32 v131, 0
	v_lshlrev_b32_e32 v133, 16, v97
	v_and_b32_e32 v97, 0xffff0000, v97
	v_mov_b32_dpp v131, v130 row_ror:8 row_mask:0xf bank_mask:0xf
	v_cndmask_b32_e64 v130, v18, v26, s[0:1]
	v_cndmask_b32_e64 v33, v33, v131, s[0:1]
	v_cndmask_b32_e64 v25, v131, v25, s[0:1]
	v_mov_b32_e32 v131, 0
	v_lshlrev_b32_e32 v138, 16, v86
	v_and_b32_e32 v86, 0xffff0000, v86
	v_mov_b32_dpp v131, v130 row_ror:8 row_mask:0xf bank_mask:0xf
	v_cndmask_b32_e64 v130, v19, v27, s[0:1]
	v_cndmask_b32_e64 v26, v26, v131, s[0:1]
; template <class Epi, class Sched, bool GATHER, bool ALIGN_EPI = true, bool SP2 = true, bool REMAP64 = false>
; __device__ __forceinline__ void gemm_phase(LAS unsigned char* lds, const bf16* Ag, const bf16* Btg, const int K, const Sched& S, const Epi& E) {
;     ...
;             constexpr bool RP = REMAP64 && Epi::ROWPAIR;
;             const bool hi = RP && (fr >= 8); const int rsh = hi ? -8 : 0, citx = hi ? cit + 32 : cit;
;             typename Epi::Pre pq[2];
;             { const int r0_ = wr * 64 + fr; pq[0] = E.pre(cur, (r0_ < cur.nrows ? r0_ : cur.nrows - 1) + rsh, citx); }
; #pragma unroll
;             for (int gq = 0; gq < 8; ++gq) { const int ai = gq >> 2, m = gq & 3, r = ai * HALF + wr * 64 + m * 16 + fr;
;                 if (gq + 1 < 8) { const int rn = ((gq + 1) >> 2) * HALF + wr * 64 + ((gq + 1) & 3) * 16 + fr; pq[(gq + 1) & 1] = E.pre(cur, (rn < cur.nrows ? rn : cur.nrows - 1) + rsh, citx); }
;                 __builtin_amdgcn_sched_barrier(0);
;                 if (r < cur.nrows) { float v0[8], v1[8];
; #pragma unroll
;                     for (int i = 0; i < 4; ++i) { v0[i] = acc[ai][0][m][0][i]; v0[4 + i] = acc[ai][0][m][1][i]; v1[i] = acc[ai][1][m][0][i]; v1[4 + i] = acc[ai][1][m][1][i]; }
;                     if constexpr (RP) {
; #pragma unroll
;                         for (int i = 0; i < 8; ++i) { const float snd = hi ? v0[i] : v1[i];
;                             const float rcv = __builtin_bit_cast(float, __builtin_amdgcn_update_dpp(0, __builtin_bit_cast(int, snd), 0x128, 0xf, 0xf, false));
;                             if (hi) v0[i] = rcv; else v1[i] = rcv; } }
;                     E.post(cur, r + rsh, citx, v0, v1, pq[gq & 1]); }
;                 __builtin_amdgcn_sched_barrier(0); }
;     __device__ __forceinline__ Pre pre(const Unit& u, int r, int cit) const { const size_t off = (size_t)(u.arow0 + r) * D + u.pn * 256 + cit; return Pre{__builtin_nontemporal_load((const v4u*)(gd + off)), __builtin_nontemporal_load((const v4u*)(gd + off + (size_t)8 * D)), __builtin_nontemporal_load ...
;     __device__ __forceinline__ void post(const Unit& u, int r, int cit, const float* v0, const float* v1, const Pre& p) const {
;         const size_t off = (size_t)(u.arow0 + r) * D + u.pn * 256 + cit; float g0[8], g1[8], m0[8], m1[8]; unpack8bf(p.g0, g0); unpack8bf(p.g1, g1); unpack8bf(p.m0, m0); unpack8bf(p.m1, m1);
; #pragma unroll
	v_cndmask_b32_e64 v18, v131, v18, s[0:1]
	v_mov_b32_e32 v131, 0
	v_fmac_f32_e32 v144, v18, v136
	v_add_u32_e32 v18, s73, v196
	v_mov_b32_dpp v131, v130 row_ror:8 row_mask:0xf bank_mask:0xf
	v_cndmask_b32_e64 v130, v20, v28, s[0:1]
	v_cndmask_b32_e64 v27, v27, v131, s[0:1]
	v_cndmask_b32_e64 v19, v131, v19, s[0:1]
	v_mov_b32_e32 v131, 0
	v_fmac_f32_e32 v84, v19, v92
	v_ashrrev_i32_e32 v19, 31, v18
	v_mov_b32_dpp v131, v130 row_ror:8 row_mask:0xf bank_mask:0xf
	v_cndmask_b32_e64 v130, v21, v29, s[0:1]
	v_cndmask_b32_e64 v28, v28, v131, s[0:1]
	v_cndmask_b32_e64 v20, v131, v20, s[0:1]
	v_mov_b32_e32 v131, 0
	v_lshlrev_b32_e32 v139, 16, v87
	v_and_b32_e32 v87, 0xffff0000, v87
	v_mov_b32_dpp v131, v130 row_ror:8 row_mask:0xf bank_mask:0xf
	v_cndmask_b32_e64 v29, v29, v131, s[0:1]
	v_cndmask_b32_e64 v21, v131, v21, s[0:1]
	v_lshlrev_b32_e32 v130, 16, v94
	v_and_b32_e32 v94, 0xffff0000, v94
	v_lshlrev_b32_e32 v131, 16, v95
	v_and_b32_e32 v95, 0xffff0000, v95
	v_lshlrev_b32_e32 v140, 16, v88
	v_and_b32_e32 v88, 0xffff0000, v88
	v_lshlrev_b32_e32 v141, 16, v89
	v_and_b32_e32 v89, 0xffff0000, v89
	v_lshlrev_b64 v[18:19], 12, v[18:19]
	v_lshlrev_b32_e32 v134, 16, v90
	v_and_b32_e32 v90, 0xffff0000, v90
	v_lshlrev_b32_e32 v137, 16, v93
	v_and_b32_e32 v93, 0xffff0000, v93
	v_lshlrev_b32_e32 v142, 16, v82
	v_and_b32_e32 v82, 0xffff0000, v82
	v_lshlrev_b32_e32 v145, 16, v85
	v_and_b32_e32 v85, 0xffff0000, v85
	v_fmac_f32_e32 v138, v30, v130
	v_fmac_f32_e32 v86, v31, v94
	v_fmac_f32_e32 v139, v32, v131
	v_fmac_f32_e32 v87, v33, v95
	v_fmac_f32_e32 v140, v26, v132
	v_fmac_f32_e32 v88, v27, v96
	v_fmac_f32_e32 v141, v28, v133
	v_fmac_f32_e32 v89, v29, v97
	v_lshl_add_u64 v[18:19], s[36:37], 0, v[18:19]
	v_lshlrev_b32_e32 v135, 16, v91
	v_and_b32_e32 v91, 0xffff0000, v91
	v_lshlrev_b32_e32 v143, 16, v83
	v_and_b32_e32 v83, 0xffff0000, v83
	v_fmac_f32_e32 v142, v22, v134
	v_fmac_f32_e32 v82, v23, v90
	v_fmac_f32_e32 v145, v20, v137
	v_fmac_f32_e32 v85, v21, v93
	v_lshl_add_u64 v[22:23], v[182:183], 1, v[18:19]
	v_cvt_pk_bf16_f32 v18, v138, v86
	v_cvt_pk_bf16_f32 v19, v139, v87
	v_cvt_pk_bf16_f32 v20, v140, v88
	v_cvt_pk_bf16_f32 v21, v141, v89
	v_fmac_f32_e32 v143, v24, v135
	v_fmac_f32_e32 v83, v25, v91
	global_store_dwordx4 v[22:23], v[18:21], off nt
	v_add_co_u32_e32 v22, vcc, 0x8000, v22
	s_nop 0
	v_cvt_pk_bf16_f32 v18, v142, v82
	v_cvt_pk_bf16_f32 v19, v143, v83
	v_cvt_pk_bf16_f32 v20, v144, v84
	v_cvt_pk_bf16_f32 v21, v145, v85
	v_addc_co_u32_e32 v23, vcc, 0, v23, vcc
	global_store_dwordx4 v[22:23], v[18:21], off nt
.LBB0_1166:
	s_and_b64 vcc, exec, s[8:9]
	s_cbranch_vccnz .LBB0_1168
	s_waitcnt vmcnt(6)
	v_cndmask_b32_e64 v18, v6, v14, s[0:1]
	v_mov_b32_e32 v19, 0
	s_nop 0
	v_lshlrev_b32_e32 v22, 16, v80
	v_and_b32_e32 v23, 0xffff0000, v80
	v_mov_b32_dpp v19, v18 row_ror:8 row_mask:0xf bank_mask:0xf
	v_cndmask_b32_e64 v18, v7, v15, s[0:1]
	v_cndmask_b32_e64 v14, v14, v19, s[0:1]
	v_cndmask_b32_e64 v6, v19, v6, s[0:1]
	v_mov_b32_e32 v19, 0
	s_nop 0
	v_lshlrev_b32_e32 v30, 16, v76
	s_nop 0
	v_lshlrev_b32_e32 v80, 16, v68
	v_mov_b32_dpp v19, v18 row_ror:8 row_mask:0xf bank_mask:0xf
	v_cndmask_b32_e64 v18, v8, v16, s[0:1]
	v_cndmask_b32_e64 v15, v15, v19, s[0:1]
	v_cndmask_b32_e64 v7, v19, v7, s[0:1]
	v_mov_b32_e32 v19, 0
	v_and_b32_e32 v31, 0xffff0000, v76
	v_and_b32_e32 v68, 0xffff0000, v68
	v_mov_b32_dpp v19, v18 row_ror:8 row_mask:0xf bank_mask:0xf
	v_cndmask_b32_e64 v18, v9, v17, s[0:1]
	v_cndmask_b32_e64 v16, v16, v19, s[0:1]
	v_cndmask_b32_e64 v8, v19, v8, s[0:1]
	v_mov_b32_e32 v19, 0
	v_lshlrev_b32_e32 v20, 16, v79
	v_and_b32_e32 v21, 0xffff0000, v79
	v_mov_b32_dpp v19, v18 row_ror:8 row_mask:0xf bank_mask:0xf
	v_cndmask_b32_e64 v18, v2, v10, s[0:1]
	v_cndmask_b32_e64 v17, v17, v19, s[0:1]
	v_cndmask_b32_e64 v9, v19, v9, s[0:1]
	v_mov_b32_e32 v19, 0
	v_lshlrev_b32_e32 v24, 16, v81
	v_and_b32_e32 v25, 0xffff0000, v81
	v_mov_b32_dpp v19, v18 row_ror:8 row_mask:0xf bank_mask:0xf
	v_cndmask_b32_e64 v18, v3, v11, s[0:1]
	v_cndmask_b32_e64 v10, v10, v19, s[0:1]
	v_cndmask_b32_e64 v2, v19, v2, s[0:1]
	v_mov_b32_e32 v19, 0
	v_fmac_f32_e32 v80, v2, v30
	v_add_u32_e32 v2, s74, v196
	v_mov_b32_dpp v19, v18 row_ror:8 row_mask:0xf bank_mask:0xf
	v_cndmask_b32_e64 v18, v4, v12, s[0:1]
	v_cndmask_b32_e64 v11, v11, v19, s[0:1]
	v_cndmask_b32_e64 v3, v19, v3, s[0:1]
	v_mov_b32_e32 v19, 0
	v_fmac_f32_e32 v68, v3, v31
	v_ashrrev_i32_e32 v3, 31, v2
	v_mov_b32_dpp v19, v18 row_ror:8 row_mask:0xf bank_mask:0xf
	v_cndmask_b32_e64 v18, v5, v13, s[0:1]
	v_cndmask_b32_e64 v12, v12, v19, s[0:1]
	v_cndmask_b32_e64 v4, v19, v4, s[0:1]
	v_mov_b32_e32 v19, 0
	v_lshlrev_b32_e32 v26, 16, v74
	v_and_b32_e32 v27, 0xffff0000, v74
	v_mov_b32_dpp v19, v18 row_ror:8 row_mask:0xf bank_mask:0xf
	v_cndmask_b32_e64 v13, v13, v19, s[0:1]
	v_cndmask_b32_e64 v5, v19, v5, s[0:1]
	v_lshlrev_b32_e32 v18, 16, v78
	v_and_b32_e32 v19, 0xffff0000, v78
	v_lshlrev_b32_e32 v28, 16, v75
	v_and_b32_e32 v29, 0xffff0000, v75
	v_lshlrev_b32_e32 v32, 16, v77
	v_and_b32_e32 v33, 0xffff0000, v77
	v_lshlrev_b32_e32 v74, 16, v70
	v_and_b32_e32 v70, 0xffff0000, v70
	v_lshlrev_b32_e32 v75, 16, v71
	v_and_b32_e32 v71, 0xffff0000, v71
	v_lshlrev_b32_e32 v76, 16, v72
	v_and_b32_e32 v72, 0xffff0000, v72
	v_lshlrev_b32_e32 v77, 16, v73
	v_and_b32_e32 v73, 0xffff0000, v73
	v_lshlrev_b64 v[2:3], 12, v[2:3]
	v_lshlrev_b32_e32 v78, 16, v66
	v_and_b32_e32 v66, 0xffff0000, v66
	v_lshlrev_b32_e32 v81, 16, v69
	v_and_b32_e32 v69, 0xffff0000, v69
	v_fmac_f32_e32 v74, v14, v18
	v_fmac_f32_e32 v70, v15, v19
	v_fmac_f32_e32 v75, v16, v20
	v_fmac_f32_e32 v71, v17, v21
	v_fmac_f32_e32 v76, v10, v22
	v_fmac_f32_e32 v72, v11, v23
	v_fmac_f32_e32 v77, v12, v24
	v_fmac_f32_e32 v73, v13, v25
	v_lshl_add_u64 v[2:3], s[36:37], 0, v[2:3]
	v_lshlrev_b32_e32 v79, 16, v67
	v_and_b32_e32 v67, 0xffff0000, v67
	v_fmac_f32_e32 v78, v6, v26
	v_fmac_f32_e32 v66, v7, v27
	v_fmac_f32_e32 v81, v4, v32
	v_fmac_f32_e32 v69, v5, v33
	v_lshl_add_u64 v[6:7], v[182:183], 1, v[2:3]
	v_cvt_pk_bf16_f32 v2, v74, v70
	v_cvt_pk_bf16_f32 v3, v75, v71
	v_cvt_pk_bf16_f32 v4, v76, v72
	v_cvt_pk_bf16_f32 v5, v77, v73
	v_fmac_f32_e32 v79, v8, v28
	v_fmac_f32_e32 v67, v9, v29
	global_store_dwordx4 v[6:7], v[2:5], off nt
	v_add_co_u32_e32 v6, vcc, 0x8000, v6
	s_nop 0
	v_cvt_pk_bf16_f32 v2, v78, v66
	v_cvt_pk_bf16_f32 v3, v79, v67
	v_cvt_pk_bf16_f32 v4, v80, v68
	v_cvt_pk_bf16_f32 v5, v81, v69
	v_addc_co_u32_e32 v7, vcc, 0, v7, vcc
	global_store_dwordx4 v[6:7], v[2:5], off nt

; template <class Epi, class Sched, bool GATHER, bool ALIGN_EPI = true, bool SP2 = true, bool REMAP64 = false>
; __device__ __forceinline__ void gemm_phase(LAS unsigned char* lds, const bf16* Ag, const bf16* Btg, const int K, const Sched& S, const Epi& E) {
;     ...
;             constexpr bool RP = REMAP64 && Epi::ROWPAIR;
;             const bool hi = RP && (fr >= 8); const int rsh = hi ? -8 : 0, citx = hi ? cit + 32 : cit;
;             typename Epi::Pre pq[2];
;             { const int r0_ = wr * 64 + fr; pq[0] = E.pre(cur, (r0_ < cur.nrows ? r0_ : cur.nrows - 1) + rsh, citx); }
; #pragma unroll
;             for (int gq = 0; gq < 8; ++gq) { const int ai = gq >> 2, m = gq & 3, r = ai * HALF + wr * 64 + m * 16 + fr;
;                 if (gq + 1 < 8) { const int rn = ((gq + 1) >> 2) * HALF + wr * 64 + ((gq + 1) & 3) * 16 + fr; pq[(gq + 1) & 1] = E.pre(cur, (rn < cur.nrows ? rn : cur.nrows - 1) + rsh, citx); }
;                 __builtin_amdgcn_sched_barrier(0);
;                 if (r < cur.nrows) { float v0[8], v1[8];
; #pragma unroll
;                     for (int i = 0; i < 4; ++i) { v0[i] = acc[ai][0][m][0][i]; v0[4 + i] = acc[ai][0][m][1][i]; v1[i] = acc[ai][1][m][0][i]; v1[4 + i] = acc[ai][1][m][1][i]; }
;                     if constexpr (RP) {
; #pragma unroll
;                         for (int i = 0; i < 8; ++i) { const float snd = hi ? v0[i] : v1[i];
;                             const float rcv = __builtin_bit_cast(float, __builtin_amdgcn_update_dpp(0, __builtin_bit_cast(int, snd), 0x128, 0xf, 0xf, false));
;                             if (hi) v0[i] = rcv; else v1[i] = rcv; } }
;                     E.post(cur, r + rsh, citx, v0, v1, pq[gq & 1]); }
;                 __builtin_amdgcn_sched_barrier(0); }
;     __device__ __forceinline__ Pre pre(const Unit& u, int r, int cit) const { const size_t off = (size_t)(u.arow0 + r) * D + u.pn * 256 + cit; return Pre{__builtin_nontemporal_load((const f32x4*)(x + off)), __builtin_nontemporal_load((const f32x4*)(x + off + 4)), __builtin_nontemporal_load((const f3 ...
;     __device__ __forceinline__ void post(const Unit& u, int r, int cit, const float* v0, const float* v1, const Pre& p) const {
;         const size_t off = (size_t)(u.arow0 + r) * D + u.pn * 256 + cit; float a[8], b[8];
; #pragma unroll
.LBB0_1249:
	v_add_u32_e32 v130, s8, v192
	v_ashrrev_i32_e32 v131, 31, v130
	s_lshl_b32 s44, s42, 8
	v_readlane_b32 s80, v247, 8
	s_ashr_i32 s45, s44, 31
	v_lshlrev_b64 v[130:131], 13, v[130:131]
	v_readlane_b32 s81, v247, 9
	s_lshl_b64 s[52:53], s[44:45], 2
	v_add_u32_e32 v204, s8, v191
	v_lshl_add_u64 v[130:131], s[80:81], 0, v[130:131]
	v_lshl_add_u64 v[130:131], v[130:131], 0, s[52:53]
	v_lshl_add_u64 v[130:131], v[130:131], 0, v[172:173]
	global_load_dwordx4 v[146:149], v[130:131], off offset:16 nt
	global_load_dwordx4 v[150:153], v[130:131], off nt
	v_lshl_add_u64 v[132:133], v[130:131], 0, s[22:23]
	v_add_co_u32_e32 v130, vcc, 0x10000, v130
	v_lshl_add_u64 v[188:189], v[174:175], 0, s[52:53]
	s_nop 0
	v_addc_co_u32_e32 v131, vcc, 0, v131, vcc
	global_load_dwordx4 v[154:157], v[130:131], off nt
	global_load_dwordx4 v[158:161], v[132:133], off offset:16 nt
	v_add_u32_e32 v130, v204, v193
	v_ashrrev_i32_e32 v131, 31, v130
	v_lshlrev_b64 v[130:131], 13, v[130:131]
	v_lshl_add_u64 v[138:139], v[188:189], 0, v[130:131]
	global_load_dwordx4 v[130:133], v[138:139], off offset:16 nt
	global_load_dwordx4 v[134:137], v[138:139], off nt
	v_lshl_add_u64 v[142:143], v[138:139], 0, s[22:23]
	v_add_co_u32_e32 v138, vcc, 0x10000, v138
	v_lshl_add_u64 v[186:187], s[44:45], 1, v[176:177]
	s_nop 0
	v_addc_co_u32_e32 v139, vcc, 0, v139, vcc
	global_load_dwordx4 v[138:141], v[138:139], off nt
	s_nop 0
	global_load_dwordx4 v[142:145], v[142:143], off offset:16 nt
	v_add_u32_e32 v203, v204, v171
	v_readlane_b32 s82, v247, 10
	v_readlane_b32 s83, v247, 11
	v_readlane_b32 s84, v247, 12
	v_readlane_b32 s85, v247, 13
	v_readlane_b32 s86, v247, 14
	v_readlane_b32 s87, v247, 15
	v_readlane_b32 s88, v247, 16
	v_readlane_b32 s89, v247, 17
	v_readlane_b32 s90, v247, 18
	v_readlane_b32 s91, v247, 19
	v_readlane_b32 s92, v247, 20
	v_readlane_b32 s93, v247, 21
	v_readlane_b32 s94, v247, 22
	v_readlane_b32 s95, v247, 23
	s_nop 1
	v_add_u32_e32 v210, v204, v194
	v_ashrrev_i32_e32 v211, 31, v210
	v_lshlrev_b64 v[210:211], 13, v[210:211]
	v_lshl_add_u64 v[218:219], v[188:189], 0, v[210:211]
	global_load_dwordx4 v[210:213], v[218:219], off offset:16 nt
	global_load_dwordx4 v[214:217], v[218:219], off nt
	v_lshl_add_u64 v[222:223], v[218:219], 0, s[22:23]
	v_add_co_u32_e32 v218, vcc, 0x10000, v218
	s_nop 1
	v_addc_co_u32_e32 v219, vcc, 0, v219, vcc
	global_load_dwordx4 v[218:221], v[218:219], off nt
	s_nop 0
	global_load_dwordx4 v[222:225], v[222:223], off offset:16 nt
	s_nop 1
	v_add_u32_e32 v226, v204, v195
	v_ashrrev_i32_e32 v227, 31, v226
	v_lshlrev_b64 v[226:227], 13, v[226:227]
	v_lshl_add_u64 v[234:235], v[188:189], 0, v[226:227]
	global_load_dwordx4 v[226:229], v[234:235], off offset:16 nt
	global_load_dwordx4 v[230:233], v[234:235], off nt
	v_lshl_add_u64 v[238:239], v[234:235], 0, s[22:23]
	v_add_co_u32_e32 v234, vcc, 0x10000, v234
	s_nop 1
	v_addc_co_u32_e32 v235, vcc, 0, v235, vcc
	global_load_dwordx4 v[234:237], v[234:235], off nt
	s_nop 0
	global_load_dwordx4 v[238:241], v[238:239], off offset:16 nt
	s_and_b64 vcc, exec, s[18:19]
	s_cbranch_vccz .LBB0_1251
	s_waitcnt vmcnt(12)
	v_cndmask_b32_e64 v205, v118, v126, s[0:1]
	v_mov_b32_e32 v206, v173
	s_nop 1
	v_mov_b32_dpp v206, v205 row_ror:8 row_mask:0xf bank_mask:0xf
	v_cndmask_b32_e64 v205, v119, v127, s[0:1]
	v_cndmask_b32_e64 v126, v126, v206, s[0:1]
	v_cndmask_b32_e64 v118, v206, v118, s[0:1]
	v_mov_b32_e32 v206, v173
	s_nop 0
	v_add_f32_e32 v126, v150, v126
	v_mov_b32_dpp v206, v205 row_ror:8 row_mask:0xf bank_mask:0xf
	v_cndmask_b32_e64 v205, v120, v128, s[0:1]
	v_cndmask_b32_e64 v127, v127, v206, s[0:1]
	v_cndmask_b32_e64 v119, v206, v119, s[0:1]
	v_mov_b32_e32 v206, v173
	v_add_f32_e32 v127, v151, v127
	s_nop 0
	v_mov_b32_dpp v206, v205 row_ror:8 row_mask:0xf bank_mask:0xf
	v_cndmask_b32_e64 v205, v121, v129, s[0:1]
	v_cndmask_b32_e64 v128, v128, v206, s[0:1]
	v_cndmask_b32_e64 v120, v206, v120, s[0:1]
	v_mov_b32_e32 v206, v173
	v_add_f32_e32 v128, v152, v128
	v_add_f32_e32 v120, v156, v120
	v_mov_b32_dpp v206, v205 row_ror:8 row_mask:0xf bank_mask:0xf
	v_cndmask_b32_e64 v205, v114, v122, s[0:1]
	v_cndmask_b32_e64 v129, v129, v206, s[0:1]
	v_cndmask_b32_e64 v121, v206, v121, s[0:1]
	v_mov_b32_e32 v206, v173
	v_add_f32_e32 v121, v157, v121
	s_nop 0
	v_mov_b32_dpp v206, v205 row_ror:8 row_mask:0xf bank_mask:0xf
	v_cndmask_b32_e64 v205, v115, v123, s[0:1]
	v_cndmask_b32_e64 v122, v122, v206, s[0:1]
	v_cndmask_b32_e64 v114, v206, v114, s[0:1]
	v_mov_b32_e32 v206, v173
	v_add_f32_e32 v150, v158, v114
	v_add_u32_e32 v114, s62, v203
	v_mov_b32_dpp v206, v205 row_ror:8 row_mask:0xf bank_mask:0xf
	v_cndmask_b32_e64 v205, v116, v124, s[0:1]
	v_cndmask_b32_e64 v123, v123, v206, s[0:1]
	v_cndmask_b32_e64 v115, v206, v115, s[0:1]
	v_mov_b32_e32 v206, v173
	v_add_f32_e32 v151, v159, v115
	v_ashrrev_i32_e32 v115, 31, v114
	v_mov_b32_dpp v206, v205 row_ror:8 row_mask:0xf bank_mask:0xf
	v_cndmask_b32_e64 v205, v117, v125, s[0:1]
	v_cndmask_b32_e64 v124, v124, v206, s[0:1]
	v_cndmask_b32_e64 v116, v206, v116, s[0:1]
	v_mov_b32_e32 v206, v173
	v_add_f32_e32 v122, v146, v122
	v_add_f32_e32 v123, v147, v123
	v_mov_b32_dpp v206, v205 row_ror:8 row_mask:0xf bank_mask:0xf
	v_cndmask_b32_e64 v125, v125, v206, s[0:1]
	v_cndmask_b32_e64 v117, v206, v117, s[0:1]
	v_add_f32_e32 v124, v148, v124
	v_add_f32_e32 v148, v160, v116
	v_add_f32_e32 v116, v153, v129
	v_add_f32_e32 v125, v149, v125
	v_lshlrev_b64 v[114:115], 12, v[114:115]
	v_add_f32_e32 v146, v154, v118
	v_add_f32_e32 v147, v155, v119
	v_add_f32_e32 v129, v161, v117
	v_lshl_add_u64 v[118:119], v[186:187], 0, v[114:115]
	v_cvt_pk_bf16_f32 v114, v126, v127
	v_cvt_pk_bf16_f32 v115, v128, v116
	v_cvt_pk_bf16_f32 v116, v122, v123
	v_cvt_pk_bf16_f32 v117, v124, v125
	global_store_dwordx4 v[118:119], v[114:117], off nt
	v_add_co_u32_e32 v118, vcc, 0x8000, v118
	s_nop 0
	v_cvt_pk_bf16_f32 v114, v146, v147
	v_cvt_pk_bf16_f32 v115, v120, v121
	v_cvt_pk_bf16_f32 v116, v150, v151
	v_cvt_pk_bf16_f32 v117, v148, v129
	v_addc_co_u32_e32 v119, vcc, 0, v119, vcc
	global_store_dwordx4 v[118:119], v[114:117], off nt
; template <class Epi, class Sched, bool GATHER, bool ALIGN_EPI = true, bool SP2 = true, bool REMAP64 = false>
; __device__ __forceinline__ void gemm_phase(LAS unsigned char* lds, const bf16* Ag, const bf16* Btg, const int K, const Sched& S, const Epi& E) {
;     ...
;             constexpr bool RP = REMAP64 && Epi::ROWPAIR;
;             const bool hi = RP && (fr >= 8); const int rsh = hi ? -8 : 0, citx = hi ? cit + 32 : cit;
;             typename Epi::Pre pq[2];
;             { const int r0_ = wr * 64 + fr; pq[0] = E.pre(cur, (r0_ < cur.nrows ? r0_ : cur.nrows - 1) + rsh, citx); }
; #pragma unroll
;             for (int gq = 0; gq < 8; ++gq) { const int ai = gq >> 2, m = gq & 3, r = ai * HALF + wr * 64 + m * 16 + fr;
;                 if (gq + 1 < 8) { const int rn = ((gq + 1) >> 2) * HALF + wr * 64 + ((gq + 1) & 3) * 16 + fr; pq[(gq + 1) & 1] = E.pre(cur, (rn < cur.nrows ? rn : cur.nrows - 1) + rsh, citx); }
;                 __builtin_amdgcn_sched_barrier(0);
;                 if (r < cur.nrows) { float v0[8], v1[8];
; #pragma unroll
;                     for (int i = 0; i < 4; ++i) { v0[i] = acc[ai][0][m][0][i]; v0[4 + i] = acc[ai][0][m][1][i]; v1[i] = acc[ai][1][m][0][i]; v1[4 + i] = acc[ai][1][m][1][i]; }
;                     if constexpr (RP) {
; #pragma unroll
;                         for (int i = 0; i < 8; ++i) { const float snd = hi ? v0[i] : v1[i];
;                             const float rcv = __builtin_bit_cast(float, __builtin_amdgcn_update_dpp(0, __builtin_bit_cast(int, snd), 0x128, 0xf, 0xf, false));
;                             if (hi) v0[i] = rcv; else v1[i] = rcv; } }
;                     E.post(cur, r + rsh, citx, v0, v1, pq[gq & 1]); }
;                 __builtin_amdgcn_sched_barrier(0); }
;     __device__ __forceinline__ Pre pre(const Unit& u, int r, int cit) const { const size_t off = (size_t)(u.arow0 + r) * D + u.pn * 256 + cit; return Pre{__builtin_nontemporal_load((const f32x4*)(x + off)), __builtin_nontemporal_load((const f32x4*)(x + off + 4)), __builtin_nontemporal_load((const f3 ...
;     __device__ __forceinline__ void post(const Unit& u, int r, int cit, const float* v0, const float* v1, const Pre& p) const {
;         const size_t off = (size_t)(u.arow0 + r) * D + u.pn * 256 + cit; float a[8], b[8];
; #pragma unroll
.LBB0_1251:
	s_nop 1
	v_add_u32_e32 v114, v204, v196
	v_ashrrev_i32_e32 v115, 31, v114
	v_lshlrev_b64 v[114:115], 13, v[114:115]
	v_lshl_add_u64 v[122:123], v[188:189], 0, v[114:115]
	global_load_dwordx4 v[114:117], v[122:123], off offset:16 nt
	global_load_dwordx4 v[118:121], v[122:123], off nt
	v_lshl_add_u64 v[126:127], v[122:123], 0, s[22:23]
	v_add_co_u32_e32 v122, vcc, 0x10000, v122
	s_nop 1
	v_addc_co_u32_e32 v123, vcc, 0, v123, vcc
	global_load_dwordx4 v[122:125], v[122:123], off nt
	s_nop 0
	global_load_dwordx4 v[126:129], v[126:127], off offset:16 nt
	s_nop 0
	v_cndmask_b32_e64 v146, 0, 1, s[18:19]
	v_cmp_ne_u32_e64 s[8:9], 1, v146
	s_andn2_b64 vcc, exec, s[18:19]
	s_cbranch_vccnz .LBB0_1253
	s_waitcnt vmcnt(14)
	v_cndmask_b32_e64 v146, v102, v110, s[0:1]
	v_mov_b32_e32 v147, v173
	s_nop 1
	v_mov_b32_dpp v147, v146 row_ror:8 row_mask:0xf bank_mask:0xf
	v_cndmask_b32_e64 v146, v103, v111, s[0:1]
	v_cndmask_b32_e64 v110, v110, v147, s[0:1]
	v_cndmask_b32_e64 v102, v147, v102, s[0:1]
	v_mov_b32_e32 v147, v173
	v_add_f32_e32 v110, v134, v110
	s_nop 0
	v_mov_b32_dpp v147, v146 row_ror:8 row_mask:0xf bank_mask:0xf
	v_cndmask_b32_e64 v146, v104, v112, s[0:1]
	v_cndmask_b32_e64 v111, v111, v147, s[0:1]
	v_cndmask_b32_e64 v103, v147, v103, s[0:1]
	v_mov_b32_e32 v147, v173
	v_add_f32_e32 v111, v135, v111
	s_nop 0
	v_mov_b32_dpp v147, v146 row_ror:8 row_mask:0xf bank_mask:0xf
	v_cndmask_b32_e64 v146, v105, v113, s[0:1]
	v_cndmask_b32_e64 v112, v112, v147, s[0:1]
	v_cndmask_b32_e64 v104, v147, v104, s[0:1]
	v_mov_b32_e32 v147, v173
	v_add_f32_e32 v112, v136, v112
	v_add_f32_e32 v104, v140, v104
	v_mov_b32_dpp v147, v146 row_ror:8 row_mask:0xf bank_mask:0xf
	v_cndmask_b32_e64 v146, v98, v106, s[0:1]
	v_cndmask_b32_e64 v113, v113, v147, s[0:1]
	v_cndmask_b32_e64 v105, v147, v105, s[0:1]
	v_mov_b32_e32 v147, v173
	v_add_f32_e32 v105, v141, v105
	s_nop 0
	v_mov_b32_dpp v147, v146 row_ror:8 row_mask:0xf bank_mask:0xf
	v_cndmask_b32_e64 v146, v99, v107, s[0:1]
	v_cndmask_b32_e64 v106, v106, v147, s[0:1]
	v_cndmask_b32_e64 v98, v147, v98, s[0:1]
	v_mov_b32_e32 v147, v173
	v_add_f32_e32 v134, v142, v98
	v_add_u32_e32 v98, s65, v203
	v_mov_b32_dpp v147, v146 row_ror:8 row_mask:0xf bank_mask:0xf
	v_cndmask_b32_e64 v146, v100, v108, s[0:1]
	v_cndmask_b32_e64 v107, v107, v147, s[0:1]
	v_cndmask_b32_e64 v99, v147, v99, s[0:1]
	v_mov_b32_e32 v147, v173
	v_add_f32_e32 v135, v143, v99
	v_ashrrev_i32_e32 v99, 31, v98
	v_mov_b32_dpp v147, v146 row_ror:8 row_mask:0xf bank_mask:0xf
	v_cndmask_b32_e64 v146, v101, v109, s[0:1]
	v_cndmask_b32_e64 v108, v108, v147, s[0:1]
	v_cndmask_b32_e64 v100, v147, v100, s[0:1]
	v_mov_b32_e32 v147, v173
	v_add_f32_e32 v106, v130, v106
	v_add_f32_e32 v107, v131, v107
	v_mov_b32_dpp v147, v146 row_ror:8 row_mask:0xf bank_mask:0xf
	v_cndmask_b32_e64 v109, v109, v147, s[0:1]
	v_cndmask_b32_e64 v101, v147, v101, s[0:1]
	v_add_f32_e32 v108, v132, v108
	v_add_f32_e32 v132, v144, v100
	v_add_f32_e32 v100, v137, v113
	v_add_f32_e32 v109, v133, v109
	v_lshlrev_b64 v[98:99], 12, v[98:99]
	v_add_f32_e32 v130, v138, v102
	v_add_f32_e32 v131, v139, v103
	v_add_f32_e32 v113, v145, v101
	v_lshl_add_u64 v[102:103], v[186:187], 0, v[98:99]
	v_cvt_pk_bf16_f32 v98, v110, v111
	v_cvt_pk_bf16_f32 v99, v112, v100
	v_cvt_pk_bf16_f32 v100, v106, v107
	v_cvt_pk_bf16_f32 v101, v108, v109
	global_store_dwordx4 v[102:103], v[98:101], off nt
	v_add_co_u32_e32 v102, vcc, 0x8000, v102
	s_nop 0
	v_cvt_pk_bf16_f32 v98, v130, v131
	v_cvt_pk_bf16_f32 v99, v104, v105
	v_cvt_pk_bf16_f32 v100, v134, v135
	v_cvt_pk_bf16_f32 v101, v132, v113
	v_addc_co_u32_e32 v103, vcc, 0, v103, vcc
	global_store_dwordx4 v[102:103], v[98:101], off nt
.LBB0_1253:
	s_nop 1
	v_add_u32_e32 v98, v204, v197
	v_ashrrev_i32_e32 v99, 31, v98
	v_lshlrev_b64 v[98:99], 13, v[98:99]
	v_lshl_add_u64 v[106:107], v[188:189], 0, v[98:99]
	global_load_dwordx4 v[98:101], v[106:107], off offset:16 nt
	global_load_dwordx4 v[102:105], v[106:107], off nt
	v_lshl_add_u64 v[110:111], v[106:107], 0, s[22:23]
	v_add_co_u32_e32 v106, vcc, 0x10000, v106
	s_nop 1
	v_addc_co_u32_e32 v107, vcc, 0, v107, vcc
	global_load_dwordx4 v[106:109], v[106:107], off nt
	s_nop 0
	global_load_dwordx4 v[110:113], v[110:111], off offset:16 nt
	s_and_b64 vcc, exec, s[8:9]
	s_cbranch_vccnz .LBB0_1255
;     __device__ __forceinline__ Pre pre(const Unit& u, int r, int cit) const { const size_t off = (size_t)(u.arow0 + r) * D + u.pn * 256 + cit; return Pre{__builtin_nontemporal_load((const v4u*)(gp + off)), __builtin_nontemporal_load((const v4u*)(gp + off + (size_t)8 * D))}; }
; template <class Epi, class Sched, bool GATHER, bool ALIGN_EPI = true, bool SP2 = true, bool REMAP64 = false>
; __device__ __forceinline__ void gemm_phase(LAS unsigned char* lds, const bf16* Ag, const bf16* Btg, const int K, const Sched& S, const Epi& E) {
;     ...
;             for (int gq = 0; gq < 8; ++gq) { const int ai = gq >> 2, m = gq & 3, r = ai * HALF + wr * 64 + m * 16 + fr;
;                 if (gq + 1 < 8) { const int rn = ((gq + 1) >> 2) * HALF + wr * 64 + ((gq + 1) & 3) * 16 + fr; pq[(gq + 1) & 1] = E.pre(cur, (rn < cur.nrows ? rn : cur.nrows - 1) + rsh, citx); }
;                 __builtin_amdgcn_sched_barrier(0);
;                 if (r < cur.nrows) { float v0[8], v1[8];
; #pragma unroll
;                     for (int i = 0; i < 4; ++i) { v0[i] = acc[ai][0][m][0][i]; v0[4 + i] = acc[ai][0][m][1][i]; v1[i] = acc[ai][1][m][0][i]; v1[4 + i] = acc[ai][1][m][1][i]; }
;                     if constexpr (RP) {
; #pragma unroll
;                         for (int i = 0; i < 8; ++i) { const float snd = hi ? v0[i] : v1[i];
;                             const float rcv = __builtin_bit_cast(float, __builtin_amdgcn_update_dpp(0, __builtin_bit_cast(int, snd), 0x128, 0xf, 0xf, false));
;                             if (hi) v0[i] = rcv; else v1[i] = rcv; } }
;                     E.post(cur, r + rsh, citx, v0, v1, pq[gq & 1]); }
;     __device__ __forceinline__ Pre pre(const Unit& u, int r, int cit) const { const size_t off = (size_t)(u.arow0 + r) * D + u.pn * 256 + cit; return Pre{__builtin_nontemporal_load((const f32x4*)(x + off)), __builtin_nontemporal_load((const f32x4*)(x + off + 4)), __builtin_nontemporal_load((const f3 ...
;     __device__ __forceinline__ void post(const Unit& u, int r, int cit, const float* v0, const float* v1, const Pre& p) const {
;         const size_t off = (size_t)(u.arow0 + r) * D + u.pn * 256 + cit; float a[8], b[8];
; #pragma unroll
;         for (int i = 0; i < 4; ++i) { a[i] = p.a0[i] + v0[i]; a[4 + i] = p.a1[i] + v0[4 + i]; b[i] = p.b0[i] + v1[i]; b[4 + i] = p.b1[i] + v1[4 + i]; }
;         store8bf(h + off, a); store8bf(h + off + (size_t)8 * D, b);
;     }
	s_waitcnt vmcnt(16)
	v_cndmask_b32_e64 v130, v86, v94, s[0:1]
	v_mov_b32_e32 v131, v173
	s_nop 1
	v_mov_b32_dpp v131, v130 row_ror:8 row_mask:0xf bank_mask:0xf
	v_cndmask_b32_e64 v130, v87, v95, s[0:1]
	v_cndmask_b32_e64 v94, v94, v131, s[0:1]
	v_cndmask_b32_e64 v86, v131, v86, s[0:1]
	v_mov_b32_e32 v131, v173
	v_add_f32_e32 v94, v214, v94
	s_nop 0
	v_mov_b32_dpp v131, v130 row_ror:8 row_mask:0xf bank_mask:0xf
	v_cndmask_b32_e64 v130, v88, v96, s[0:1]
	v_cndmask_b32_e64 v95, v95, v131, s[0:1]
	v_cndmask_b32_e64 v87, v131, v87, s[0:1]
	v_mov_b32_e32 v131, v173
	v_add_f32_e32 v95, v215, v95
	s_nop 0
	v_mov_b32_dpp v131, v130 row_ror:8 row_mask:0xf bank_mask:0xf
	v_cndmask_b32_e64 v130, v89, v97, s[0:1]
	v_cndmask_b32_e64 v96, v96, v131, s[0:1]
	v_cndmask_b32_e64 v88, v131, v88, s[0:1]
	v_mov_b32_e32 v131, v173
	v_add_f32_e32 v96, v216, v96
	v_add_f32_e32 v88, v220, v88
	v_mov_b32_dpp v131, v130 row_ror:8 row_mask:0xf bank_mask:0xf
	v_cndmask_b32_e64 v130, v82, v90, s[0:1]
	v_cndmask_b32_e64 v97, v97, v131, s[0:1]
	v_cndmask_b32_e64 v89, v131, v89, s[0:1]
	v_mov_b32_e32 v131, v173
	v_add_f32_e32 v89, v221, v89
	s_nop 0
	v_mov_b32_dpp v131, v130 row_ror:8 row_mask:0xf bank_mask:0xf
	v_cndmask_b32_e64 v130, v83, v91, s[0:1]
	v_cndmask_b32_e64 v90, v90, v131, s[0:1]
	v_cndmask_b32_e64 v82, v131, v82, s[0:1]
	v_mov_b32_e32 v131, v173
	v_add_f32_e32 v214, v222, v82
	v_add_u32_e32 v82, s70, v203
	v_mov_b32_dpp v131, v130 row_ror:8 row_mask:0xf bank_mask:0xf
	v_cndmask_b32_e64 v130, v84, v92, s[0:1]
	v_cndmask_b32_e64 v91, v91, v131, s[0:1]
	v_cndmask_b32_e64 v83, v131, v83, s[0:1]
	v_mov_b32_e32 v131, v173
	v_add_f32_e32 v215, v223, v83
	v_ashrrev_i32_e32 v83, 31, v82
	v_mov_b32_dpp v131, v130 row_ror:8 row_mask:0xf bank_mask:0xf
	v_cndmask_b32_e64 v130, v85, v93, s[0:1]
	v_cndmask_b32_e64 v92, v92, v131, s[0:1]
	v_cndmask_b32_e64 v84, v131, v84, s[0:1]
	v_mov_b32_e32 v131, v173
	v_add_f32_e32 v90, v210, v90
	v_add_f32_e32 v91, v211, v91
	v_mov_b32_dpp v131, v130 row_ror:8 row_mask:0xf bank_mask:0xf
	v_cndmask_b32_e64 v93, v93, v131, s[0:1]
	v_cndmask_b32_e64 v85, v131, v85, s[0:1]
	v_add_f32_e32 v92, v212, v92
	v_add_f32_e32 v212, v224, v84
	v_add_f32_e32 v84, v217, v97
	v_add_f32_e32 v93, v213, v93
	v_lshlrev_b64 v[82:83], 12, v[82:83]
	v_add_f32_e32 v210, v218, v86
	v_add_f32_e32 v211, v219, v87
	v_add_f32_e32 v97, v225, v85
	v_lshl_add_u64 v[86:87], v[186:187], 0, v[82:83]
	v_cvt_pk_bf16_f32 v82, v94, v95
	v_cvt_pk_bf16_f32 v83, v96, v84
	v_cvt_pk_bf16_f32 v84, v90, v91
	v_cvt_pk_bf16_f32 v85, v92, v93
	global_store_dwordx4 v[86:87], v[82:85], off nt
	v_add_co_u32_e32 v86, vcc, 0x8000, v86
	s_nop 0
	v_cvt_pk_bf16_f32 v82, v210, v211
	v_cvt_pk_bf16_f32 v83, v88, v89
	v_cvt_pk_bf16_f32 v84, v214, v215
	v_cvt_pk_bf16_f32 v85, v212, v97
	v_addc_co_u32_e32 v87, vcc, 0, v87, vcc
	global_store_dwordx4 v[86:87], v[82:85], off nt
.LBB0_1255:
	s_nop 1
	v_add_u32_e32 v82, v204, v198
	v_ashrrev_i32_e32 v83, 31, v82
	v_lshlrev_b64 v[82:83], 13, v[82:83]
	v_lshl_add_u64 v[90:91], v[188:189], 0, v[82:83]
	global_load_dwordx4 v[82:85], v[90:91], off offset:16 nt
	global_load_dwordx4 v[86:89], v[90:91], off nt
	v_lshl_add_u64 v[94:95], v[90:91], 0, s[22:23]
	v_add_co_u32_e32 v90, vcc, 0x10000, v90
	s_nop 1
	v_addc_co_u32_e32 v91, vcc, 0, v91, vcc
	global_load_dwordx4 v[90:93], v[90:91], off nt
	s_nop 0
	global_load_dwordx4 v[94:97], v[94:95], off offset:16 nt
	s_and_b64 vcc, exec, s[8:9]
	s_cbranch_vccnz .LBB0_1257
	s_waitcnt vmcnt(18)
	v_cndmask_b32_e64 v146, v70, v78, s[0:1]
	v_mov_b32_e32 v147, v173
	s_nop 1
	v_mov_b32_dpp v147, v146 row_ror:8 row_mask:0xf bank_mask:0xf
	v_cndmask_b32_e64 v146, v71, v79, s[0:1]
	v_cndmask_b32_e64 v78, v78, v147, s[0:1]
	v_cndmask_b32_e64 v70, v147, v70, s[0:1]
	v_mov_b32_e32 v147, v173
	s_nop 0
	v_add_f32_e32 v78, v230, v78
	v_mov_b32_dpp v147, v146 row_ror:8 row_mask:0xf bank_mask:0xf
	v_cndmask_b32_e64 v146, v72, v80, s[0:1]
	v_cndmask_b32_e64 v79, v79, v147, s[0:1]
	v_cndmask_b32_e64 v71, v147, v71, s[0:1]
	v_mov_b32_e32 v147, v173
	v_add_f32_e32 v79, v231, v79
	s_nop 0
	v_mov_b32_dpp v147, v146 row_ror:8 row_mask:0xf bank_mask:0xf
	v_cndmask_b32_e64 v146, v73, v81, s[0:1]
	v_cndmask_b32_e64 v80, v80, v147, s[0:1]
	v_cndmask_b32_e64 v72, v147, v72, s[0:1]
	v_mov_b32_e32 v147, v173
	v_add_f32_e32 v80, v232, v80
	s_nop 0
	v_add_f32_e32 v72, v236, v72
	v_mov_b32_dpp v147, v146 row_ror:8 row_mask:0xf bank_mask:0xf
	v_cndmask_b32_e64 v146, v66, v74, s[0:1]
	v_cndmask_b32_e64 v81, v81, v147, s[0:1]
	v_cndmask_b32_e64 v73, v147, v73, s[0:1]
	v_mov_b32_e32 v147, v173
	v_add_f32_e32 v73, v237, v73
	s_nop 0
	v_mov_b32_dpp v147, v146 row_ror:8 row_mask:0xf bank_mask:0xf
	v_cndmask_b32_e64 v146, v67, v75, s[0:1]
	v_cndmask_b32_e64 v74, v74, v147, s[0:1]
	v_cndmask_b32_e64 v66, v147, v66, s[0:1]
	v_mov_b32_e32 v147, v173
	s_nop 0
	v_add_f32_e32 v230, v238, v66
	v_add_u32_e32 v66, s72, v203
	v_mov_b32_dpp v147, v146 row_ror:8 row_mask:0xf bank_mask:0xf
	v_cndmask_b32_e64 v146, v68, v76, s[0:1]
	v_cndmask_b32_e64 v75, v75, v147, s[0:1]
	v_cndmask_b32_e64 v67, v147, v67, s[0:1]
	v_mov_b32_e32 v147, v173
	v_add_f32_e32 v231, v239, v67
	v_ashrrev_i32_e32 v67, 31, v66
	v_mov_b32_dpp v147, v146 row_ror:8 row_mask:0xf bank_mask:0xf
	v_cndmask_b32_e64 v146, v69, v77, s[0:1]
	v_cndmask_b32_e64 v76, v76, v147, s[0:1]
	v_cndmask_b32_e64 v68, v147, v68, s[0:1]
	v_mov_b32_e32 v147, v173
	v_add_f32_e32 v74, v226, v74
	v_add_f32_e32 v75, v227, v75
	v_mov_b32_dpp v147, v146 row_ror:8 row_mask:0xf bank_mask:0xf
	v_cndmask_b32_e64 v77, v77, v147, s[0:1]
	v_cndmask_b32_e64 v69, v147, v69, s[0:1]
	v_add_f32_e32 v76, v228, v76
	v_add_f32_e32 v228, v240, v68
	v_add_f32_e32 v68, v233, v81
	v_add_f32_e32 v77, v229, v77
	v_lshlrev_b64 v[66:67], 12, v[66:67]
	v_add_f32_e32 v226, v234, v70
	v_add_f32_e32 v227, v235, v71
	v_add_f32_e32 v81, v241, v69
	v_lshl_add_u64 v[70:71], v[186:187], 0, v[66:67]
	v_cvt_pk_bf16_f32 v66, v78, v79
	v_cvt_pk_bf16_f32 v67, v80, v68
	v_cvt_pk_bf16_f32 v68, v74, v75
	v_cvt_pk_bf16_f32 v69, v76, v77
	global_store_dwordx4 v[70:71], v[66:69], off nt
	v_add_co_u32_e32 v70, vcc, 0x8000, v70
	s_nop 0
	v_cvt_pk_bf16_f32 v66, v226, v227
	v_cvt_pk_bf16_f32 v67, v72, v73
	v_cvt_pk_bf16_f32 v68, v230, v231
	v_cvt_pk_bf16_f32 v69, v228, v81
	v_addc_co_u32_e32 v71, vcc, 0, v71, vcc
	global_store_dwordx4 v[70:71], v[66:69], off nt
;     __device__ __forceinline__ Pre pre(const Unit& u, int r, int cit) const { const size_t off = (size_t)(u.arow0 + r) * D + u.pn * 256 + cit; return Pre{__builtin_nontemporal_load((const v4u*)(gp + off)), __builtin_nontemporal_load((const v4u*)(gp + off + (size_t)8 * D))}; }
; template <class Epi, class Sched, bool GATHER, bool ALIGN_EPI = true, bool SP2 = true, bool REMAP64 = false>
; __device__ __forceinline__ void gemm_phase(LAS unsigned char* lds, const bf16* Ag, const bf16* Btg, const int K, const Sched& S, const Epi& E) {
;     ...
;             for (int gq = 0; gq < 8; ++gq) { const int ai = gq >> 2, m = gq & 3, r = ai * HALF + wr * 64 + m * 16 + fr;
;                 if (gq + 1 < 8) { const int rn = ((gq + 1) >> 2) * HALF + wr * 64 + ((gq + 1) & 3) * 16 + fr; pq[(gq + 1) & 1] = E.pre(cur, (rn < cur.nrows ? rn : cur.nrows - 1) + rsh, citx); }
;                 __builtin_amdgcn_sched_barrier(0);
;                 if (r < cur.nrows) { float v0[8], v1[8];
; #pragma unroll
;                     for (int i = 0; i < 4; ++i) { v0[i] = acc[ai][0][m][0][i]; v0[4 + i] = acc[ai][0][m][1][i]; v1[i] = acc[ai][1][m][0][i]; v1[4 + i] = acc[ai][1][m][1][i]; }
;                     if constexpr (RP) {
; #pragma unroll
;                         for (int i = 0; i < 8; ++i) { const float snd = hi ? v0[i] : v1[i];
;                             const float rcv = __builtin_bit_cast(float, __builtin_amdgcn_update_dpp(0, __builtin_bit_cast(int, snd), 0x128, 0xf, 0xf, false));
;                             if (hi) v0[i] = rcv; else v1[i] = rcv; } }
;                     E.post(cur, r + rsh, citx, v0, v1, pq[gq & 1]); }
;     __device__ __forceinline__ Pre pre(const Unit& u, int r, int cit) const { const size_t off = (size_t)(u.arow0 + r) * D + u.pn * 256 + cit; return Pre{__builtin_nontemporal_load((const f32x4*)(x + off)), __builtin_nontemporal_load((const f32x4*)(x + off + 4)), __builtin_nontemporal_load((const f3 ...
;     __device__ __forceinline__ void post(const Unit& u, int r, int cit, const float* v0, const float* v1, const Pre& p) const {
;         const size_t off = (size_t)(u.arow0 + r) * D + u.pn * 256 + cit; float a[8], b[8];
; #pragma unroll
;         for (int i = 0; i < 4; ++i) { a[i] = p.a0[i] + v0[i]; a[4 + i] = p.a1[i] + v0[4 + i]; b[i] = p.b0[i] + v1[i]; b[4 + i] = p.b1[i] + v1[4 + i]; }
;         store8bf(h + off, a); store8bf(h + off + (size_t)8 * D, b);
;     }
.LBB0_1257:
	s_nop 1
	v_add_u32_e32 v66, v204, v199
	v_ashrrev_i32_e32 v67, 31, v66
	v_lshlrev_b64 v[66:67], 13, v[66:67]
	v_lshl_add_u64 v[74:75], v[188:189], 0, v[66:67]
	global_load_dwordx4 v[66:69], v[74:75], off offset:16 nt
	global_load_dwordx4 v[70:73], v[74:75], off nt
	v_lshl_add_u64 v[78:79], v[74:75], 0, s[22:23]
	v_add_co_u32_e32 v74, vcc, 0x10000, v74
	s_nop 1
	v_addc_co_u32_e32 v75, vcc, 0, v75, vcc
	global_load_dwordx4 v[74:77], v[74:75], off nt
	s_nop 0
	global_load_dwordx4 v[78:81], v[78:79], off offset:16 nt
	s_nop 0
	v_cndmask_b32_e64 v146, 0, 1, s[20:21]
	v_cmp_ne_u32_e64 s[8:9], 1, v146
	s_andn2_b64 vcc, exec, s[20:21]
	s_cbranch_vccnz .LBB0_1259
	s_waitcnt vmcnt(18)
	v_cndmask_b32_e64 v130, v54, v62, s[0:1]
	v_mov_b32_e32 v131, v173
	s_nop 1
	v_mov_b32_dpp v131, v130 row_ror:8 row_mask:0xf bank_mask:0xf
	v_cndmask_b32_e64 v130, v55, v63, s[0:1]
	v_cndmask_b32_e64 v62, v62, v131, s[0:1]
	v_cndmask_b32_e64 v54, v131, v54, s[0:1]
	v_mov_b32_e32 v131, v173
	s_nop 0
	v_add_f32_e32 v62, v118, v62
	v_mov_b32_dpp v131, v130 row_ror:8 row_mask:0xf bank_mask:0xf
	v_cndmask_b32_e64 v130, v56, v64, s[0:1]
	v_cndmask_b32_e64 v63, v63, v131, s[0:1]
	v_cndmask_b32_e64 v55, v131, v55, s[0:1]
	v_mov_b32_e32 v131, v173
	v_add_f32_e32 v63, v119, v63
	s_nop 0
	v_mov_b32_dpp v131, v130 row_ror:8 row_mask:0xf bank_mask:0xf
	v_cndmask_b32_e64 v130, v57, v65, s[0:1]
	v_cndmask_b32_e64 v64, v64, v131, s[0:1]
	v_cndmask_b32_e64 v56, v131, v56, s[0:1]
	v_mov_b32_e32 v131, v173
	v_add_f32_e32 v64, v120, v64
	s_nop 0
	v_add_f32_e32 v56, v124, v56
	v_mov_b32_dpp v131, v130 row_ror:8 row_mask:0xf bank_mask:0xf
	v_cndmask_b32_e64 v130, v50, v58, s[0:1]
	v_cndmask_b32_e64 v65, v65, v131, s[0:1]
	v_cndmask_b32_e64 v57, v131, v57, s[0:1]
	v_mov_b32_e32 v131, v173
	v_add_f32_e32 v57, v125, v57
	s_nop 0
	v_mov_b32_dpp v131, v130 row_ror:8 row_mask:0xf bank_mask:0xf
	v_cndmask_b32_e64 v130, v51, v59, s[0:1]
	v_cndmask_b32_e64 v58, v58, v131, s[0:1]
	v_cndmask_b32_e64 v50, v131, v50, s[0:1]
	v_mov_b32_e32 v131, v173
	s_nop 0
	v_add_f32_e32 v118, v126, v50
	v_add_u32_e32 v50, s71, v203
	v_mov_b32_dpp v131, v130 row_ror:8 row_mask:0xf bank_mask:0xf
	v_cndmask_b32_e64 v130, v52, v60, s[0:1]
	v_cndmask_b32_e64 v59, v59, v131, s[0:1]
	v_cndmask_b32_e64 v51, v131, v51, s[0:1]
	v_mov_b32_e32 v131, v173
	v_add_f32_e32 v119, v127, v51
	v_ashrrev_i32_e32 v51, 31, v50
	v_mov_b32_dpp v131, v130 row_ror:8 row_mask:0xf bank_mask:0xf
	v_cndmask_b32_e64 v130, v53, v61, s[0:1]
	v_cndmask_b32_e64 v60, v60, v131, s[0:1]
	v_cndmask_b32_e64 v52, v131, v52, s[0:1]
	v_mov_b32_e32 v131, v173
	v_add_f32_e32 v58, v114, v58
	v_add_f32_e32 v59, v115, v59
	v_mov_b32_dpp v131, v130 row_ror:8 row_mask:0xf bank_mask:0xf
	v_cndmask_b32_e64 v61, v61, v131, s[0:1]
	v_cndmask_b32_e64 v53, v131, v53, s[0:1]
	v_add_f32_e32 v60, v116, v60
	v_add_f32_e32 v116, v128, v52
	v_add_f32_e32 v52, v121, v65
	v_add_f32_e32 v61, v117, v61
	v_lshlrev_b64 v[50:51], 12, v[50:51]
	v_add_f32_e32 v114, v122, v54
	v_add_f32_e32 v115, v123, v55
	v_add_f32_e32 v65, v129, v53
	v_lshl_add_u64 v[54:55], v[186:187], 0, v[50:51]
	v_cvt_pk_bf16_f32 v50, v62, v63
	v_cvt_pk_bf16_f32 v51, v64, v52
	v_cvt_pk_bf16_f32 v52, v58, v59
	v_cvt_pk_bf16_f32 v53, v60, v61
	global_store_dwordx4 v[54:55], v[50:53], off nt
	v_add_co_u32_e32 v54, vcc, 0x8000, v54
	s_nop 0
	v_cvt_pk_bf16_f32 v50, v114, v115
	v_cvt_pk_bf16_f32 v51, v56, v57
	v_cvt_pk_bf16_f32 v52, v118, v119
	v_cvt_pk_bf16_f32 v53, v116, v65
	v_addc_co_u32_e32 v55, vcc, 0, v55, vcc
	global_store_dwordx4 v[54:55], v[50:53], off nt
.LBB0_1259:
	s_and_b64 vcc, exec, s[8:9]
	s_cbranch_vccnz .LBB0_1261
	s_waitcnt vmcnt(14)
	s_nop 0
	v_cndmask_b32_e64 v146, v38, v46, s[0:1]
	v_mov_b32_e32 v147, v173
	s_nop 1
	v_mov_b32_dpp v147, v146 row_ror:8 row_mask:0xf bank_mask:0xf
	v_cndmask_b32_e64 v146, v39, v47, s[0:1]
	v_cndmask_b32_e64 v46, v46, v147, s[0:1]
	v_cndmask_b32_e64 v38, v147, v38, s[0:1]
	v_mov_b32_e32 v147, v173
	s_nop 0
	v_add_f32_e32 v46, v102, v46
	v_mov_b32_dpp v147, v146 row_ror:8 row_mask:0xf bank_mask:0xf
	v_cndmask_b32_e64 v146, v40, v48, s[0:1]
	v_cndmask_b32_e64 v47, v47, v147, s[0:1]
	v_cndmask_b32_e64 v39, v147, v39, s[0:1]
	v_mov_b32_e32 v147, v173
	v_add_f32_e32 v47, v103, v47
	s_nop 0
	v_mov_b32_dpp v147, v146 row_ror:8 row_mask:0xf bank_mask:0xf
	v_cndmask_b32_e64 v146, v41, v49, s[0:1]
	v_cndmask_b32_e64 v48, v48, v147, s[0:1]
	v_cndmask_b32_e64 v40, v147, v40, s[0:1]
	v_mov_b32_e32 v147, v173
	v_add_f32_e32 v48, v104, v48
	s_nop 0
	v_add_f32_e32 v40, v108, v40
	v_mov_b32_dpp v147, v146 row_ror:8 row_mask:0xf bank_mask:0xf
	v_cndmask_b32_e64 v146, v34, v42, s[0:1]
	v_cndmask_b32_e64 v49, v49, v147, s[0:1]
	v_cndmask_b32_e64 v41, v147, v41, s[0:1]
	v_mov_b32_e32 v147, v173
	v_add_f32_e32 v41, v109, v41
	s_nop 0
	v_mov_b32_dpp v147, v146 row_ror:8 row_mask:0xf bank_mask:0xf
	v_cndmask_b32_e64 v146, v35, v43, s[0:1]
	v_cndmask_b32_e64 v42, v42, v147, s[0:1]
	v_cndmask_b32_e64 v34, v147, v34, s[0:1]
	v_mov_b32_e32 v147, v173
	s_nop 0
	v_add_f32_e32 v102, v110, v34
	v_add_u32_e32 v34, s73, v203
	v_mov_b32_dpp v147, v146 row_ror:8 row_mask:0xf bank_mask:0xf
	v_cndmask_b32_e64 v146, v36, v44, s[0:1]
	v_cndmask_b32_e64 v43, v43, v147, s[0:1]
	v_cndmask_b32_e64 v35, v147, v35, s[0:1]
	v_mov_b32_e32 v147, v173
	v_add_f32_e32 v103, v111, v35
	v_ashrrev_i32_e32 v35, 31, v34
	v_mov_b32_dpp v147, v146 row_ror:8 row_mask:0xf bank_mask:0xf
	v_cndmask_b32_e64 v146, v37, v45, s[0:1]
	v_cndmask_b32_e64 v44, v44, v147, s[0:1]
	v_cndmask_b32_e64 v36, v147, v36, s[0:1]
	v_mov_b32_e32 v147, v173
	v_add_f32_e32 v42, v98, v42
	v_add_f32_e32 v43, v99, v43
	v_mov_b32_dpp v147, v146 row_ror:8 row_mask:0xf bank_mask:0xf
	v_cndmask_b32_e64 v45, v45, v147, s[0:1]
	v_cndmask_b32_e64 v37, v147, v37, s[0:1]
	v_add_f32_e32 v44, v100, v44
	v_add_f32_e32 v100, v112, v36
	v_add_f32_e32 v36, v105, v49
	v_add_f32_e32 v45, v101, v45
	v_lshlrev_b64 v[34:35], 12, v[34:35]
	v_add_f32_e32 v98, v106, v38
	v_add_f32_e32 v99, v107, v39
	v_add_f32_e32 v49, v113, v37
	v_lshl_add_u64 v[38:39], v[186:187], 0, v[34:35]
	v_cvt_pk_bf16_f32 v34, v46, v47
	v_cvt_pk_bf16_f32 v35, v48, v36
	v_cvt_pk_bf16_f32 v36, v42, v43
	v_cvt_pk_bf16_f32 v37, v44, v45
	global_store_dwordx4 v[38:39], v[34:37], off nt
	v_add_co_u32_e32 v38, vcc, 0x8000, v38
	s_nop 0
	v_cvt_pk_bf16_f32 v34, v98, v99
	v_cvt_pk_bf16_f32 v35, v40, v41
	v_cvt_pk_bf16_f32 v36, v102, v103
	v_cvt_pk_bf16_f32 v37, v100, v49
	v_addc_co_u32_e32 v39, vcc, 0, v39, vcc
	global_store_dwordx4 v[38:39], v[34:37], off nt
;     __device__ __forceinline__ Pre pre(const Unit& u, int r, int cit) const { const size_t off = (size_t)(u.arow0 + r) * D + u.pn * 256 + cit; return Pre{__builtin_nontemporal_load((const v4u*)(gp + off)), __builtin_nontemporal_load((const v4u*)(gp + off + (size_t)8 * D))}; }
; template <class Epi, class Sched, bool GATHER, bool ALIGN_EPI = true, bool SP2 = true, bool REMAP64 = false>
; __device__ __forceinline__ void gemm_phase(LAS unsigned char* lds, const bf16* Ag, const bf16* Btg, const int K, const Sched& S, const Epi& E) {
;     ...
;             for (int gq = 0; gq < 8; ++gq) { const int ai = gq >> 2, m = gq & 3, r = ai * HALF + wr * 64 + m * 16 + fr;
;                 if (gq + 1 < 8) { const int rn = ((gq + 1) >> 2) * HALF + wr * 64 + ((gq + 1) & 3) * 16 + fr; pq[(gq + 1) & 1] = E.pre(cur, (rn < cur.nrows ? rn : cur.nrows - 1) + rsh, citx); }
;                 __builtin_amdgcn_sched_barrier(0);
;                 if (r < cur.nrows) { float v0[8], v1[8];
; #pragma unroll
;                     for (int i = 0; i < 4; ++i) { v0[i] = acc[ai][0][m][0][i]; v0[4 + i] = acc[ai][0][m][1][i]; v1[i] = acc[ai][1][m][0][i]; v1[4 + i] = acc[ai][1][m][1][i]; }
;                     if constexpr (RP) {
; #pragma unroll
;                         for (int i = 0; i < 8; ++i) { const float snd = hi ? v0[i] : v1[i];
;                             const float rcv = __builtin_bit_cast(float, __builtin_amdgcn_update_dpp(0, __builtin_bit_cast(int, snd), 0x128, 0xf, 0xf, false));
;                             if (hi) v0[i] = rcv; else v1[i] = rcv; } }
;                     E.post(cur, r + rsh, citx, v0, v1, pq[gq & 1]); }
;     __device__ __forceinline__ Pre pre(const Unit& u, int r, int cit) const { const size_t off = (size_t)(u.arow0 + r) * D + u.pn * 256 + cit; return Pre{__builtin_nontemporal_load((const f32x4*)(x + off)), __builtin_nontemporal_load((const f32x4*)(x + off + 4)), __builtin_nontemporal_load((const f3 ...
;     __device__ __forceinline__ void post(const Unit& u, int r, int cit, const float* v0, const float* v1, const Pre& p) const {
;         const size_t off = (size_t)(u.arow0 + r) * D + u.pn * 256 + cit; float a[8], b[8];
; #pragma unroll
;         for (int i = 0; i < 4; ++i) { a[i] = p.a0[i] + v0[i]; a[4 + i] = p.a1[i] + v0[4 + i]; b[i] = p.b0[i] + v1[i]; b[4 + i] = p.b1[i] + v1[4 + i]; }
;         store8bf(h + off, a); store8bf(h + off + (size_t)8 * D, b);
;     }
.LBB0_1261:
	s_and_b64 vcc, exec, s[8:9]
	s_cbranch_vccnz .LBB0_1263
	s_waitcnt vmcnt(10)
	s_nop 0
	v_cndmask_b32_e64 v130, v22, v30, s[0:1]
	v_mov_b32_e32 v131, v173
	s_nop 1
	v_mov_b32_dpp v131, v130 row_ror:8 row_mask:0xf bank_mask:0xf
	v_cndmask_b32_e64 v130, v23, v31, s[0:1]
	v_cndmask_b32_e64 v30, v30, v131, s[0:1]
	v_cndmask_b32_e64 v22, v131, v22, s[0:1]
	v_mov_b32_e32 v131, v173
	s_nop 0
	v_add_f32_e32 v30, v86, v30
	v_mov_b32_dpp v131, v130 row_ror:8 row_mask:0xf bank_mask:0xf
	v_cndmask_b32_e64 v130, v24, v32, s[0:1]
	v_cndmask_b32_e64 v31, v31, v131, s[0:1]
	v_cndmask_b32_e64 v23, v131, v23, s[0:1]
	v_mov_b32_e32 v131, v173
	v_add_f32_e32 v31, v87, v31
	s_nop 0
	v_mov_b32_dpp v131, v130 row_ror:8 row_mask:0xf bank_mask:0xf
	v_cndmask_b32_e64 v130, v25, v33, s[0:1]
	v_cndmask_b32_e64 v32, v32, v131, s[0:1]
	v_cndmask_b32_e64 v24, v131, v24, s[0:1]
	v_mov_b32_e32 v131, v173
	v_add_f32_e32 v32, v88, v32
	s_nop 0
	v_add_f32_e32 v24, v92, v24
	v_mov_b32_dpp v131, v130 row_ror:8 row_mask:0xf bank_mask:0xf
	v_cndmask_b32_e64 v130, v18, v26, s[0:1]
	v_cndmask_b32_e64 v33, v33, v131, s[0:1]
	v_cndmask_b32_e64 v25, v131, v25, s[0:1]
	v_mov_b32_e32 v131, v173
	v_add_f32_e32 v25, v93, v25
	s_nop 0
	v_mov_b32_dpp v131, v130 row_ror:8 row_mask:0xf bank_mask:0xf
	v_cndmask_b32_e64 v130, v19, v27, s[0:1]
	v_cndmask_b32_e64 v26, v26, v131, s[0:1]
	v_cndmask_b32_e64 v18, v131, v18, s[0:1]
	v_mov_b32_e32 v131, v173
	s_nop 0
	v_add_f32_e32 v86, v94, v18
	v_add_u32_e32 v18, s74, v203
	v_mov_b32_dpp v131, v130 row_ror:8 row_mask:0xf bank_mask:0xf
	v_cndmask_b32_e64 v130, v20, v28, s[0:1]
	v_cndmask_b32_e64 v27, v27, v131, s[0:1]
	v_cndmask_b32_e64 v19, v131, v19, s[0:1]
	v_mov_b32_e32 v131, v173
	v_add_f32_e32 v87, v95, v19
	v_ashrrev_i32_e32 v19, 31, v18
	v_mov_b32_dpp v131, v130 row_ror:8 row_mask:0xf bank_mask:0xf
	v_cndmask_b32_e64 v130, v21, v29, s[0:1]
	v_cndmask_b32_e64 v28, v28, v131, s[0:1]
	v_cndmask_b32_e64 v20, v131, v20, s[0:1]
	v_mov_b32_e32 v131, v173
	v_add_f32_e32 v26, v82, v26
	v_add_f32_e32 v27, v83, v27
	v_mov_b32_dpp v131, v130 row_ror:8 row_mask:0xf bank_mask:0xf
	v_cndmask_b32_e64 v29, v29, v131, s[0:1]
	v_cndmask_b32_e64 v21, v131, v21, s[0:1]
	v_add_f32_e32 v28, v84, v28
	v_add_f32_e32 v84, v96, v20
	v_add_f32_e32 v20, v89, v33
	v_add_f32_e32 v29, v85, v29
	v_lshlrev_b64 v[18:19], 12, v[18:19]
	v_add_f32_e32 v82, v90, v22
	v_add_f32_e32 v83, v91, v23
	v_add_f32_e32 v33, v97, v21
	v_lshl_add_u64 v[22:23], v[186:187], 0, v[18:19]
	v_cvt_pk_bf16_f32 v18, v30, v31
	v_cvt_pk_bf16_f32 v19, v32, v20
	v_cvt_pk_bf16_f32 v20, v26, v27
	v_cvt_pk_bf16_f32 v21, v28, v29
	global_store_dwordx4 v[22:23], v[18:21], off nt
	v_add_co_u32_e32 v22, vcc, 0x8000, v22
	s_nop 0
	v_cvt_pk_bf16_f32 v18, v82, v83
	v_cvt_pk_bf16_f32 v19, v24, v25
	v_cvt_pk_bf16_f32 v20, v86, v87
	v_cvt_pk_bf16_f32 v21, v84, v33
	v_addc_co_u32_e32 v23, vcc, 0, v23, vcc
	global_store_dwordx4 v[22:23], v[18:21], off nt
.LBB0_1263:
	s_and_b64 vcc, exec, s[8:9]
	s_cbranch_vccnz .LBB0_1265
	s_waitcnt vmcnt(6)
	v_cndmask_b32_e64 v18, v6, v14, s[0:1]
	v_mov_b32_e32 v19, v173
	s_nop 1
	v_mov_b32_dpp v19, v18 row_ror:8 row_mask:0xf bank_mask:0xf
	v_cndmask_b32_e64 v18, v7, v15, s[0:1]
	v_cndmask_b32_e64 v14, v14, v19, s[0:1]
	v_cndmask_b32_e64 v6, v19, v6, s[0:1]
	v_mov_b32_e32 v19, v173
	s_nop 0
	v_add_f32_e32 v14, v70, v14
	v_mov_b32_dpp v19, v18 row_ror:8 row_mask:0xf bank_mask:0xf
	v_cndmask_b32_e64 v18, v8, v16, s[0:1]
	v_cndmask_b32_e64 v15, v15, v19, s[0:1]
	v_cndmask_b32_e64 v7, v19, v7, s[0:1]
	v_mov_b32_e32 v19, v173
	v_add_f32_e32 v15, v71, v15
	s_nop 0
	v_add_f32_e32 v20, v75, v7
	v_mov_b32_dpp v19, v18 row_ror:8 row_mask:0xf bank_mask:0xf
	v_cndmask_b32_e64 v18, v9, v17, s[0:1]
	v_cndmask_b32_e64 v16, v16, v19, s[0:1]
	v_cndmask_b32_e64 v8, v19, v8, s[0:1]
	v_mov_b32_e32 v19, v173
	v_add_f32_e32 v16, v72, v16
	v_add_f32_e32 v8, v76, v8
	v_mov_b32_dpp v19, v18 row_ror:8 row_mask:0xf bank_mask:0xf
	v_cndmask_b32_e64 v18, v2, v10, s[0:1]
	v_cndmask_b32_e64 v17, v17, v19, s[0:1]
	v_cndmask_b32_e64 v9, v19, v9, s[0:1]
	v_mov_b32_e32 v19, v173
	v_add_f32_e32 v9, v77, v9
	s_nop 0
	v_mov_b32_dpp v19, v18 row_ror:8 row_mask:0xf bank_mask:0xf
	v_cndmask_b32_e64 v18, v3, v11, s[0:1]
	v_cndmask_b32_e64 v10, v10, v19, s[0:1]
	v_cndmask_b32_e64 v2, v19, v2, s[0:1]
	v_mov_b32_e32 v19, v173
	v_add_f32_e32 v10, v66, v10
	s_nop 0
	v_mov_b32_dpp v19, v18 row_ror:8 row_mask:0xf bank_mask:0xf
	v_cndmask_b32_e64 v18, v4, v12, s[0:1]
	v_cndmask_b32_e64 v11, v11, v19, s[0:1]
	v_cndmask_b32_e64 v3, v19, v3, s[0:1]
	v_mov_b32_e32 v19, v173
	s_nop 0
	v_add_f32_e32 v21, v79, v3
	v_add_f32_e32 v11, v67, v11
	v_mov_b32_dpp v19, v18 row_ror:8 row_mask:0xf bank_mask:0xf
	v_cndmask_b32_e64 v18, v5, v13, s[0:1]
	v_cndmask_b32_e64 v12, v12, v19, s[0:1]
	v_cndmask_b32_e64 v4, v19, v4, s[0:1]
	v_mov_b32_e32 v19, v173
	v_add_f32_e32 v12, v68, v12
	v_add_f32_e32 v22, v80, v4
	v_mov_b32_dpp v19, v18 row_ror:8 row_mask:0xf bank_mask:0xf
	v_cndmask_b32_e64 v13, v13, v19, s[0:1]
	v_cndmask_b32_e64 v5, v19, v5, s[0:1]
	v_add_f32_e32 v19, v78, v2
	v_add_u32_e32 v2, s75, v203
	v_ashrrev_i32_e32 v3, 31, v2
	v_add_f32_e32 v4, v73, v17
	v_add_f32_e32 v13, v69, v13
	v_lshlrev_b64 v[2:3], 12, v[2:3]
	v_add_f32_e32 v18, v74, v6
	v_add_f32_e32 v17, v81, v5
	v_lshl_add_u64 v[6:7], v[186:187], 0, v[2:3]
	v_cvt_pk_bf16_f32 v2, v14, v15
	v_cvt_pk_bf16_f32 v3, v16, v4
	v_cvt_pk_bf16_f32 v4, v10, v11
	v_cvt_pk_bf16_f32 v5, v12, v13
	global_store_dwordx4 v[6:7], v[2:5], off nt
	v_add_co_u32_e32 v6, vcc, 0x8000, v6
	s_nop 0
	v_cvt_pk_bf16_f32 v2, v18, v20
	v_cvt_pk_bf16_f32 v3, v8, v9
	v_cvt_pk_bf16_f32 v4, v19, v21
	v_cvt_pk_bf16_f32 v5, v22, v17
	v_addc_co_u32_e32 v7, vcc, 0, v7, vcc
	global_store_dwordx4 v[6:7], v[2:5], off nt

; __device__ __forceinline__ float siluf_(float x) { return x * __builtin_amdgcn_rcpf(1.0f + __builtin_amdgcn_exp2f(-1.4426950408889634f * x)); }
;     __device__ __forceinline__ Pre pre(const Unit& u, int r, int cit) const { const size_t off = (size_t)(u.arow0 + r) * D + u.pn * 256 + cit; return Pre{__builtin_nontemporal_load((const v4u*)(gp + off)), __builtin_nontemporal_load((const v4u*)(gp + off + (size_t)8 * D))}; }
; template <class Epi, class Sched, bool GATHER, bool ALIGN_EPI = true, bool SP2 = true, bool REMAP64 = false>
; __device__ __forceinline__ void gemm_phase(LAS unsigned char* lds, const bf16* Ag, const bf16* Btg, const int K, const Sched& S, const Epi& E) {
;     ...
;             for (int gq = 0; gq < 8; ++gq) { const int ai = gq >> 2, m = gq & 3, r = ai * HALF + wr * 64 + m * 16 + fr;
;                 if (gq + 1 < 8) { const int rn = ((gq + 1) >> 2) * HALF + wr * 64 + ((gq + 1) & 3) * 16 + fr; pq[(gq + 1) & 1] = E.pre(cur, (rn < cur.nrows ? rn : cur.nrows - 1) + rsh, citx); }
;                 __builtin_amdgcn_sched_barrier(0);
;                 if (r < cur.nrows) { float v0[8], v1[8];
; #pragma unroll
;                     for (int i = 0; i < 4; ++i) { v0[i] = acc[ai][0][m][0][i]; v0[4 + i] = acc[ai][0][m][1][i]; v1[i] = acc[ai][1][m][0][i]; v1[4 + i] = acc[ai][1][m][1][i]; }
;                     if constexpr (RP) {
; #pragma unroll
;                         for (int i = 0; i < 8; ++i) { const float snd = hi ? v0[i] : v1[i];
;                             const float rcv = __builtin_bit_cast(float, __builtin_amdgcn_update_dpp(0, __builtin_bit_cast(int, snd), 0x128, 0xf, 0xf, false));
;                             if (hi) v0[i] = rcv; else v1[i] = rcv; } }
;                     E.post(cur, r + rsh, citx, v0, v1, pq[gq & 1]); }
;     __device__ __forceinline__ void post(const Unit& u, int r, int cit, const float* v0, const float* v1, const Pre&) const {
;         float a[8];
; #pragma unroll
;         for (int i = 0; i < 8; ++i) a[i] = siluf_(v0[i]) * v1[i];
;         store8bf(hmid + (size_t)(u.arow0 + r) * DE + u.pn * 128 + cit, a);
;     }
.LBB0_1437:
	s_lshl_b32 s6, s26, 7
	s_ashr_i32 s7, s6, 31
	v_lshl_add_u64 v[138:139], s[6:7], 1, v[136:137]
	v_cmp_gt_i32_e32 vcc, s52, v143
	s_and_saveexec_b64 s[6:7], vcc
	s_cbranch_execz .LBB0_1439
	v_mul_f32_e32 v134, 0xbfb8aa3b, v126
	v_mul_f32_e32 v140, 0xbfb8aa3b, v127
	v_exp_f32_e32 v134, v134
	v_exp_f32_e32 v140, v140
	v_add_f32_e32 v134, 1.0, v134
	v_add_f32_e32 v141, 1.0, v140
	v_rcp_f32_e32 v140, v134
	v_rcp_f32_e32 v141, v141
	v_mul_f32_e32 v134, 0xbfb8aa3b, v128
	v_exp_f32_e32 v134, v134
	v_pk_mul_f32 v[126:127], v[126:127], v[140:141]
	v_mul_f32_e32 v140, 0xbfb8aa3b, v129
	v_exp_f32_e32 v140, v140
	v_pk_mul_f32 v[118:119], v[126:127], v[118:119]
	v_add_f32_e32 v126, 1.0, v134
	v_mul_f32_e32 v134, 0xbfb8aa3b, v122
	v_add_f32_e32 v127, 1.0, v140
	v_rcp_f32_e32 v126, v126
	v_rcp_f32_e32 v127, v127
	v_exp_f32_e32 v134, v134
	v_mul_f32_e32 v140, 0xbfb8aa3b, v123
	v_exp_f32_e32 v140, v140
	v_pk_mul_f32 v[126:127], v[128:129], v[126:127]
	v_add_f32_e32 v128, 1.0, v134
	v_mul_f32_e32 v134, 0xbfb8aa3b, v124
	v_add_f32_e32 v129, 1.0, v140
	v_exp_f32_e32 v134, v134
	v_mul_f32_e32 v140, 0xbfb8aa3b, v125
	v_exp_f32_e32 v141, v140
	v_rcp_f32_e32 v128, v128
	v_add_f32_e32 v134, 1.0, v134
	v_rcp_f32_e32 v129, v129
	v_rcp_f32_e32 v140, v134
	v_add_f32_e32 v134, 1.0, v141
	v_rcp_f32_e32 v141, v134
	v_pk_mul_f32 v[122:123], v[122:123], v[128:129]
	v_pk_mul_f32 v[120:121], v[126:127], v[120:121]
	v_pk_mul_f32 v[122:123], v[122:123], v[114:115]
	v_pk_mul_f32 v[114:115], v[124:125], v[140:141]
	s_nop 0
	v_pk_mul_f32 v[124:125], v[114:115], v[116:117]
	v_add_u32_e32 v114, s33, v143
	v_ashrrev_i32_e32 v115, 31, v114
	v_lshlrev_b64 v[114:115], 10, v[114:115]
	v_lshl_add_u64 v[126:127], v[138:139], 0, v[114:115]
	v_cvt_pk_bf16_f32 v114, v118, v119
	v_cvt_pk_bf16_f32 v115, v120, v121
	v_cvt_pk_bf16_f32 v116, v122, v123
	v_cvt_pk_bf16_f32 v117, v124, v125
	global_store_dwordx4 v[126:127], v[114:117], off nt
.LBB0_1439:
	s_or_b64 exec, exec, s[6:7]
	v_cmp_gt_i32_e32 vcc, s52, v155
	s_and_saveexec_b64 s[6:7], vcc
	s_cbranch_execz .LBB0_1441
	v_mul_f32_e32 v114, 0xbfb8aa3b, v110
	v_mul_f32_e32 v115, 0xbfb8aa3b, v111
	v_exp_f32_e32 v114, v114
	v_exp_f32_e32 v115, v115
	v_mul_f32_e32 v116, 0xbfb8aa3b, v112
	v_exp_f32_e32 v116, v116
	v_add_f32_e32 v114, 1.0, v114
	v_add_f32_e32 v115, 1.0, v115
	v_rcp_f32_e32 v114, v114
	v_rcp_f32_e32 v115, v115
	s_nop 0
	v_pk_mul_f32 v[110:111], v[110:111], v[114:115]
	v_mul_f32_e32 v114, 0xbfb8aa3b, v113
	v_exp_f32_e32 v114, v114
	v_pk_mul_f32 v[102:103], v[110:111], v[102:103]
	v_add_f32_e32 v110, 1.0, v116
	v_mul_f32_e32 v115, 0xbfb8aa3b, v107
	v_add_f32_e32 v111, 1.0, v114
	v_mul_f32_e32 v114, 0xbfb8aa3b, v106
	v_rcp_f32_e32 v110, v110
	v_rcp_f32_e32 v111, v111
	v_exp_f32_e32 v114, v114
	v_exp_f32_e32 v115, v115
	v_pk_mul_f32 v[110:111], v[112:113], v[110:111]
	v_add_f32_e32 v112, 1.0, v114
	v_add_f32_e32 v113, 1.0, v115
	v_mul_f32_e32 v114, 0xbfb8aa3b, v108
	v_mul_f32_e32 v115, 0xbfb8aa3b, v109
	v_exp_f32_e32 v114, v114
	v_exp_f32_e32 v115, v115
	v_rcp_f32_e32 v112, v112
	v_rcp_f32_e32 v113, v113
	v_add_f32_e32 v114, 1.0, v114
	v_add_f32_e32 v115, 1.0, v115
	v_rcp_f32_e32 v114, v114
	v_rcp_f32_e32 v115, v115
	v_pk_mul_f32 v[106:107], v[106:107], v[112:113]
	v_pk_mul_f32 v[104:105], v[110:111], v[104:105]
	v_pk_mul_f32 v[106:107], v[106:107], v[98:99]
	v_pk_mul_f32 v[98:99], v[108:109], v[114:115]
	s_nop 0
	v_pk_mul_f32 v[108:109], v[98:99], v[100:101]
	v_add_u32_e32 v98, s33, v155
	v_ashrrev_i32_e32 v99, 31, v98
	v_lshlrev_b64 v[98:99], 10, v[98:99]
	v_lshl_add_u64 v[110:111], v[138:139], 0, v[98:99]
	v_cvt_pk_bf16_f32 v98, v102, v103
	v_cvt_pk_bf16_f32 v99, v104, v105
	v_cvt_pk_bf16_f32 v100, v106, v107
	v_cvt_pk_bf16_f32 v101, v108, v109
	global_store_dwordx4 v[110:111], v[98:101], off nt
.LBB0_1441:
	s_or_b64 exec, exec, s[6:7]
	v_cmp_gt_i32_e32 vcc, s52, v156
	s_and_saveexec_b64 s[6:7], vcc
	s_cbranch_execz .LBB0_1443
	v_mul_f32_e32 v98, 0xbfb8aa3b, v94
	v_mul_f32_e32 v99, 0xbfb8aa3b, v95
	v_exp_f32_e32 v98, v98
	v_exp_f32_e32 v99, v99
	v_mul_f32_e32 v100, 0xbfb8aa3b, v96
	v_exp_f32_e32 v100, v100
	v_add_f32_e32 v98, 1.0, v98
	v_add_f32_e32 v99, 1.0, v99
	v_rcp_f32_e32 v98, v98
	v_rcp_f32_e32 v99, v99
	s_nop 0
	v_pk_mul_f32 v[94:95], v[94:95], v[98:99]
	v_mul_f32_e32 v98, 0xbfb8aa3b, v97
	v_exp_f32_e32 v98, v98
	v_pk_mul_f32 v[86:87], v[94:95], v[86:87]
	v_add_f32_e32 v94, 1.0, v100
	v_mul_f32_e32 v99, 0xbfb8aa3b, v91
	v_add_f32_e32 v95, 1.0, v98
	v_mul_f32_e32 v98, 0xbfb8aa3b, v90
	v_rcp_f32_e32 v94, v94
	v_rcp_f32_e32 v95, v95
	v_exp_f32_e32 v98, v98
	v_exp_f32_e32 v99, v99
	v_pk_mul_f32 v[94:95], v[96:97], v[94:95]
	v_add_f32_e32 v96, 1.0, v98
	v_add_f32_e32 v97, 1.0, v99
	v_mul_f32_e32 v98, 0xbfb8aa3b, v92
	v_mul_f32_e32 v99, 0xbfb8aa3b, v93
	v_exp_f32_e32 v98, v98
	v_exp_f32_e32 v99, v99
	v_rcp_f32_e32 v96, v96
	v_rcp_f32_e32 v97, v97
	v_add_f32_e32 v98, 1.0, v98
	v_add_f32_e32 v99, 1.0, v99
	v_rcp_f32_e32 v98, v98
	v_rcp_f32_e32 v99, v99
	v_pk_mul_f32 v[90:91], v[90:91], v[96:97]
	v_pk_mul_f32 v[88:89], v[94:95], v[88:89]
	v_pk_mul_f32 v[90:91], v[90:91], v[82:83]
	v_pk_mul_f32 v[82:83], v[92:93], v[98:99]
	s_nop 0
	v_pk_mul_f32 v[92:93], v[82:83], v[84:85]
	v_add_u32_e32 v82, s33, v156
	v_ashrrev_i32_e32 v83, 31, v82
	v_lshlrev_b64 v[82:83], 10, v[82:83]
	v_lshl_add_u64 v[94:95], v[138:139], 0, v[82:83]
	v_cvt_pk_bf16_f32 v82, v86, v87
	v_cvt_pk_bf16_f32 v83, v88, v89
	v_cvt_pk_bf16_f32 v84, v90, v91
	v_cvt_pk_bf16_f32 v85, v92, v93
	global_store_dwordx4 v[94:95], v[82:85], off nt
; __device__ __forceinline__ float siluf_(float x) { return x * __builtin_amdgcn_rcpf(1.0f + __builtin_amdgcn_exp2f(-1.4426950408889634f * x)); }
;     __device__ __forceinline__ Pre pre(const Unit& u, int r, int cit) const { const size_t off = (size_t)(u.arow0 + r) * D + u.pn * 256 + cit; return Pre{__builtin_nontemporal_load((const v4u*)(gp + off)), __builtin_nontemporal_load((const v4u*)(gp + off + (size_t)8 * D))}; }
; template <class Epi, class Sched, bool GATHER, bool ALIGN_EPI = true, bool SP2 = true, bool REMAP64 = false>
; __device__ __forceinline__ void gemm_phase(LAS unsigned char* lds, const bf16* Ag, const bf16* Btg, const int K, const Sched& S, const Epi& E) {
;     ...
;             for (int gq = 0; gq < 8; ++gq) { const int ai = gq >> 2, m = gq & 3, r = ai * HALF + wr * 64 + m * 16 + fr;
;                 if (gq + 1 < 8) { const int rn = ((gq + 1) >> 2) * HALF + wr * 64 + ((gq + 1) & 3) * 16 + fr; pq[(gq + 1) & 1] = E.pre(cur, (rn < cur.nrows ? rn : cur.nrows - 1) + rsh, citx); }
;                 __builtin_amdgcn_sched_barrier(0);
;                 if (r < cur.nrows) { float v0[8], v1[8];
; #pragma unroll
;                     for (int i = 0; i < 4; ++i) { v0[i] = acc[ai][0][m][0][i]; v0[4 + i] = acc[ai][0][m][1][i]; v1[i] = acc[ai][1][m][0][i]; v1[4 + i] = acc[ai][1][m][1][i]; }
;                     if constexpr (RP) {
; #pragma unroll
;                         for (int i = 0; i < 8; ++i) { const float snd = hi ? v0[i] : v1[i];
;                             const float rcv = __builtin_bit_cast(float, __builtin_amdgcn_update_dpp(0, __builtin_bit_cast(int, snd), 0x128, 0xf, 0xf, false));
;                             if (hi) v0[i] = rcv; else v1[i] = rcv; } }
;                     E.post(cur, r + rsh, citx, v0, v1, pq[gq & 1]); }
;     __device__ __forceinline__ void post(const Unit& u, int r, int cit, const float* v0, const float* v1, const Pre&) const {
;         float a[8];
; #pragma unroll
;         for (int i = 0; i < 8; ++i) a[i] = siluf_(v0[i]) * v1[i];
;         store8bf(hmid + (size_t)(u.arow0 + r) * DE + u.pn * 128 + cit, a);
;     }
.LBB0_1443:
	s_or_b64 exec, exec, s[6:7]
	v_cmp_gt_i32_e32 vcc, s52, v157
	s_and_saveexec_b64 s[6:7], vcc
	s_cbranch_execz .LBB0_1445
	v_mul_f32_e32 v82, 0xbfb8aa3b, v78
	v_mul_f32_e32 v83, 0xbfb8aa3b, v79
	v_exp_f32_e32 v82, v82
	v_exp_f32_e32 v83, v83
	v_mul_f32_e32 v84, 0xbfb8aa3b, v80
	v_exp_f32_e32 v84, v84
	v_add_f32_e32 v82, 1.0, v82
	v_add_f32_e32 v83, 1.0, v83
	v_rcp_f32_e32 v82, v82
	v_rcp_f32_e32 v83, v83
	s_nop 0
	v_pk_mul_f32 v[78:79], v[78:79], v[82:83]
	v_mul_f32_e32 v82, 0xbfb8aa3b, v81
	v_exp_f32_e32 v82, v82
	v_pk_mul_f32 v[70:71], v[78:79], v[70:71]
	v_add_f32_e32 v78, 1.0, v84
	v_mul_f32_e32 v83, 0xbfb8aa3b, v75
	v_add_f32_e32 v79, 1.0, v82
	v_mul_f32_e32 v82, 0xbfb8aa3b, v74
	v_rcp_f32_e32 v78, v78
	v_rcp_f32_e32 v79, v79
	v_exp_f32_e32 v82, v82
	v_exp_f32_e32 v83, v83
	v_pk_mul_f32 v[78:79], v[80:81], v[78:79]
	v_add_f32_e32 v80, 1.0, v82
	v_add_f32_e32 v81, 1.0, v83
	v_mul_f32_e32 v82, 0xbfb8aa3b, v76
	v_mul_f32_e32 v83, 0xbfb8aa3b, v77
	v_exp_f32_e32 v82, v82
	v_exp_f32_e32 v83, v83
	v_rcp_f32_e32 v80, v80
	v_rcp_f32_e32 v81, v81
	v_add_f32_e32 v82, 1.0, v82
	v_add_f32_e32 v83, 1.0, v83
	v_rcp_f32_e32 v82, v82
	v_rcp_f32_e32 v83, v83
	v_pk_mul_f32 v[74:75], v[74:75], v[80:81]
	v_pk_mul_f32 v[72:73], v[78:79], v[72:73]
	v_pk_mul_f32 v[74:75], v[74:75], v[66:67]
	v_pk_mul_f32 v[66:67], v[76:77], v[82:83]
	s_nop 0
	v_pk_mul_f32 v[76:77], v[66:67], v[68:69]
	v_add_u32_e32 v66, s33, v157
	v_ashrrev_i32_e32 v67, 31, v66
	v_lshlrev_b64 v[66:67], 10, v[66:67]
	v_lshl_add_u64 v[78:79], v[138:139], 0, v[66:67]
	v_cvt_pk_bf16_f32 v66, v70, v71
	v_cvt_pk_bf16_f32 v67, v72, v73
	v_cvt_pk_bf16_f32 v68, v74, v75
	v_cvt_pk_bf16_f32 v69, v76, v77
	global_store_dwordx4 v[78:79], v[66:69], off nt
.LBB0_1445:
	s_or_b64 exec, exec, s[6:7]
	v_cmp_gt_i32_e32 vcc, s52, v158
	s_and_saveexec_b64 s[6:7], vcc
	s_cbranch_execz .LBB0_1447
	v_mul_f32_e32 v66, 0xbfb8aa3b, v54
	v_mul_f32_e32 v67, 0xbfb8aa3b, v55
	v_exp_f32_e32 v66, v66
	v_exp_f32_e32 v67, v67
	v_mul_f32_e32 v68, 0xbfb8aa3b, v56
	v_exp_f32_e32 v68, v68
	v_add_f32_e32 v66, 1.0, v66
	v_add_f32_e32 v67, 1.0, v67
	v_rcp_f32_e32 v66, v66
	v_rcp_f32_e32 v67, v67
	s_nop 0
	v_pk_mul_f32 v[54:55], v[54:55], v[66:67]
	v_mul_f32_e32 v66, 0xbfb8aa3b, v57
	v_exp_f32_e32 v66, v66
	v_pk_mul_f32 v[54:55], v[54:55], v[62:63]
	v_add_f32_e32 v62, 1.0, v68
	v_mul_f32_e32 v67, 0xbfb8aa3b, v43
	v_add_f32_e32 v63, 1.0, v66
	v_mul_f32_e32 v66, 0xbfb8aa3b, v42
	v_rcp_f32_e32 v62, v62
	v_rcp_f32_e32 v63, v63
	v_exp_f32_e32 v66, v66
	v_exp_f32_e32 v67, v67
	v_pk_mul_f32 v[56:57], v[56:57], v[62:63]
	v_add_f32_e32 v62, 1.0, v66
	v_add_f32_e32 v63, 1.0, v67
	v_mul_f32_e32 v66, 0xbfb8aa3b, v44
	v_mul_f32_e32 v67, 0xbfb8aa3b, v45
	v_exp_f32_e32 v66, v66
	v_exp_f32_e32 v67, v67
	v_rcp_f32_e32 v62, v62
	v_rcp_f32_e32 v63, v63
	v_add_f32_e32 v66, 1.0, v66
	v_add_f32_e32 v67, 1.0, v67
	v_rcp_f32_e32 v66, v66
	v_rcp_f32_e32 v67, v67
	v_pk_mul_f32 v[42:43], v[42:43], v[62:63]
	v_pk_mul_f32 v[56:57], v[56:57], v[64:65]
	v_pk_mul_f32 v[58:59], v[42:43], v[58:59]
	v_pk_mul_f32 v[42:43], v[44:45], v[66:67]
	v_cvt_pk_bf16_f32 v44, v58, v59
	v_pk_mul_f32 v[60:61], v[42:43], v[60:61]
	v_add_u32_e32 v42, s33, v158
	v_ashrrev_i32_e32 v43, 31, v42
	v_lshlrev_b64 v[42:43], 10, v[42:43]
	v_lshl_add_u64 v[62:63], v[138:139], 0, v[42:43]
	v_cvt_pk_bf16_f32 v42, v54, v55
	v_cvt_pk_bf16_f32 v43, v56, v57
	v_cvt_pk_bf16_f32 v45, v60, v61
	global_store_dwordx4 v[62:63], v[42:45], off nt
; __device__ __forceinline__ float siluf_(float x) { return x * __builtin_amdgcn_rcpf(1.0f + __builtin_amdgcn_exp2f(-1.4426950408889634f * x)); }
;     __device__ __forceinline__ Pre pre(const Unit& u, int r, int cit) const { const size_t off = (size_t)(u.arow0 + r) * D + u.pn * 256 + cit; return Pre{__builtin_nontemporal_load((const v4u*)(gp + off)), __builtin_nontemporal_load((const v4u*)(gp + off + (size_t)8 * D))}; }
; template <class Epi, class Sched, bool GATHER, bool ALIGN_EPI = true, bool SP2 = true, bool REMAP64 = false>
; __device__ __forceinline__ void gemm_phase(LAS unsigned char* lds, const bf16* Ag, const bf16* Btg, const int K, const Sched& S, const Epi& E) {
;     ...
;             for (int gq = 0; gq < 8; ++gq) { const int ai = gq >> 2, m = gq & 3, r = ai * HALF + wr * 64 + m * 16 + fr;
;                 if (gq + 1 < 8) { const int rn = ((gq + 1) >> 2) * HALF + wr * 64 + ((gq + 1) & 3) * 16 + fr; pq[(gq + 1) & 1] = E.pre(cur, (rn < cur.nrows ? rn : cur.nrows - 1) + rsh, citx); }
;                 __builtin_amdgcn_sched_barrier(0);
;                 if (r < cur.nrows) { float v0[8], v1[8];
; #pragma unroll
;                     for (int i = 0; i < 4; ++i) { v0[i] = acc[ai][0][m][0][i]; v0[4 + i] = acc[ai][0][m][1][i]; v1[i] = acc[ai][1][m][0][i]; v1[4 + i] = acc[ai][1][m][1][i]; }
;                     if constexpr (RP) {
; #pragma unroll
;                         for (int i = 0; i < 8; ++i) { const float snd = hi ? v0[i] : v1[i];
;                             const float rcv = __builtin_bit_cast(float, __builtin_amdgcn_update_dpp(0, __builtin_bit_cast(int, snd), 0x128, 0xf, 0xf, false));
;                             if (hi) v0[i] = rcv; else v1[i] = rcv; } }
;                     E.post(cur, r + rsh, citx, v0, v1, pq[gq & 1]); }
;     __device__ __forceinline__ void post(const Unit& u, int r, int cit, const float* v0, const float* v1, const Pre&) const {
;         float a[8];
; #pragma unroll
;         for (int i = 0; i < 8; ++i) a[i] = siluf_(v0[i]) * v1[i];
;         store8bf(hmid + (size_t)(u.arow0 + r) * DE + u.pn * 128 + cit, a);
;     }
.LBB0_1447:
	s_or_b64 exec, exec, s[6:7]
	v_cmp_gt_i32_e32 vcc, s52, v159
	s_and_saveexec_b64 s[6:7], vcc
	s_cbranch_execz .LBB0_1449
	v_mul_f32_e32 v42, 0xbfb8aa3b, v38
	v_mul_f32_e32 v43, 0xbfb8aa3b, v39
	v_exp_f32_e32 v42, v42
	v_exp_f32_e32 v43, v43
	v_mul_f32_e32 v44, 0xbfb8aa3b, v40
	v_exp_f32_e32 v44, v44
	v_add_f32_e32 v42, 1.0, v42
	v_add_f32_e32 v43, 1.0, v43
	v_rcp_f32_e32 v42, v42
	v_rcp_f32_e32 v43, v43
	v_mul_f32_e32 v45, 0xbfb8aa3b, v23
	v_exp_f32_e32 v45, v45
	v_pk_mul_f32 v[38:39], v[38:39], v[42:43]
	v_mul_f32_e32 v42, 0xbfb8aa3b, v41
	v_exp_f32_e32 v43, v42
	v_add_f32_e32 v42, 1.0, v44
	v_mul_f32_e32 v44, 0xbfb8aa3b, v22
	v_rcp_f32_e32 v42, v42
	v_add_f32_e32 v43, 1.0, v43
	v_rcp_f32_e32 v43, v43
	v_exp_f32_e32 v44, v44
	v_pk_mul_f32 v[38:39], v[38:39], v[50:51]
	v_pk_mul_f32 v[40:41], v[40:41], v[42:43]
	v_add_f32_e32 v42, 1.0, v44
	v_add_f32_e32 v43, 1.0, v45
	v_mul_f32_e32 v44, 0xbfb8aa3b, v24
	v_mul_f32_e32 v45, 0xbfb8aa3b, v25
	v_exp_f32_e32 v44, v44
	v_exp_f32_e32 v45, v45
	v_rcp_f32_e32 v42, v42
	v_rcp_f32_e32 v43, v43
	v_add_f32_e32 v44, 1.0, v44
	v_add_f32_e32 v45, 1.0, v45
	v_rcp_f32_e32 v44, v44
	v_rcp_f32_e32 v45, v45
	v_pk_mul_f32 v[22:23], v[22:23], v[42:43]
	v_pk_mul_f32 v[40:41], v[40:41], v[52:53]
	v_pk_mul_f32 v[42:43], v[22:23], v[46:47]
	v_pk_mul_f32 v[22:23], v[24:25], v[44:45]
	v_cvt_pk_bf16_f32 v24, v42, v43
	v_pk_mul_f32 v[44:45], v[22:23], v[48:49]
	v_add_u32_e32 v22, s33, v159
	v_ashrrev_i32_e32 v23, 31, v22
	v_lshlrev_b64 v[22:23], 10, v[22:23]
	v_lshl_add_u64 v[46:47], v[138:139], 0, v[22:23]
	v_cvt_pk_bf16_f32 v22, v38, v39
	v_cvt_pk_bf16_f32 v23, v40, v41
	v_cvt_pk_bf16_f32 v25, v44, v45
	global_store_dwordx4 v[46:47], v[22:25], off nt
.LBB0_1449:
	s_or_b64 exec, exec, s[6:7]
	v_cmp_gt_i32_e32 vcc, s52, v160
	s_and_saveexec_b64 s[6:7], vcc
	s_cbranch_execz .LBB0_1451
	v_mul_f32_e32 v22, 0xbfb8aa3b, v26
	v_mul_f32_e32 v23, 0xbfb8aa3b, v27
	v_exp_f32_e32 v22, v22
	v_exp_f32_e32 v23, v23
	v_mul_f32_e32 v24, 0xbfb8aa3b, v28
	v_mul_f32_e32 v25, 0xbfb8aa3b, v29
	v_exp_f32_e32 v24, v24
	v_exp_f32_e32 v25, v25
	v_add_f32_e32 v22, 1.0, v22
	v_add_f32_e32 v23, 1.0, v23
	v_rcp_f32_e32 v22, v22
	v_rcp_f32_e32 v23, v23
	v_add_f32_e32 v24, 1.0, v24
	v_add_f32_e32 v25, 1.0, v25
	v_rcp_f32_e32 v24, v24
	v_rcp_f32_e32 v25, v25
	v_pk_mul_f32 v[22:23], v[26:27], v[22:23]
	v_mul_f32_e32 v26, 0xbfb8aa3b, v18
	v_mul_f32_e32 v27, 0xbfb8aa3b, v19
	v_exp_f32_e32 v26, v26
	v_exp_f32_e32 v27, v27
	v_pk_mul_f32 v[24:25], v[28:29], v[24:25]
	v_mul_f32_e32 v28, 0xbfb8aa3b, v20
	v_mul_f32_e32 v29, 0xbfb8aa3b, v21
	v_exp_f32_e32 v28, v28
	v_exp_f32_e32 v29, v29
	v_add_f32_e32 v26, 1.0, v26
	v_add_f32_e32 v27, 1.0, v27
	v_rcp_f32_e32 v26, v26
	v_rcp_f32_e32 v27, v27
	v_add_f32_e32 v28, 1.0, v28
	v_add_f32_e32 v29, 1.0, v29
	v_rcp_f32_e32 v28, v28
	v_rcp_f32_e32 v29, v29
	v_pk_mul_f32 v[18:19], v[18:19], v[26:27]
	v_pk_mul_f32 v[22:23], v[22:23], v[34:35]
	v_pk_mul_f32 v[26:27], v[18:19], v[30:31]
	v_pk_mul_f32 v[18:19], v[20:21], v[28:29]
	v_pk_mul_f32 v[24:25], v[24:25], v[36:37]
	v_pk_mul_f32 v[28:29], v[18:19], v[32:33]
	v_add_u32_e32 v18, s33, v160
	v_ashrrev_i32_e32 v19, 31, v18
	v_lshlrev_b64 v[18:19], 10, v[18:19]
	v_lshl_add_u64 v[30:31], v[138:139], 0, v[18:19]
	v_cvt_pk_bf16_f32 v18, v22, v23
	v_cvt_pk_bf16_f32 v19, v24, v25
	v_cvt_pk_bf16_f32 v20, v26, v27
	v_cvt_pk_bf16_f32 v21, v28, v29
	global_store_dwordx4 v[30:31], v[18:21], off nt
.LBB0_1451:
	s_or_b64 exec, exec, s[6:7]
	v_cmp_gt_i32_e32 vcc, s52, v161
	s_and_saveexec_b64 s[6:7], vcc
	s_cbranch_execz .LBB0_1453
	v_mul_f32_e32 v18, 0xbfb8aa3b, v6
	v_mul_f32_e32 v19, 0xbfb8aa3b, v7
	v_exp_f32_e32 v18, v18
	v_exp_f32_e32 v19, v19
	v_mul_f32_e32 v20, 0xbfb8aa3b, v8
	v_exp_f32_e32 v20, v20
	v_add_f32_e32 v18, 1.0, v18
	v_add_f32_e32 v19, 1.0, v19
	v_rcp_f32_e32 v18, v18
	v_rcp_f32_e32 v19, v19
	s_nop 0
	v_pk_mul_f32 v[6:7], v[6:7], v[18:19]
	v_mul_f32_e32 v18, 0xbfb8aa3b, v9
	v_exp_f32_e32 v18, v18
	v_pk_mul_f32 v[6:7], v[6:7], v[14:15]
	v_add_f32_e32 v14, 1.0, v20
	v_mul_f32_e32 v19, 0xbfb8aa3b, v3
	v_add_f32_e32 v15, 1.0, v18
	v_mul_f32_e32 v18, 0xbfb8aa3b, v2
	v_rcp_f32_e32 v14, v14
	v_rcp_f32_e32 v15, v15
	v_exp_f32_e32 v18, v18
	v_exp_f32_e32 v19, v19
	v_pk_mul_f32 v[8:9], v[8:9], v[14:15]
	v_add_f32_e32 v14, 1.0, v18
	v_add_f32_e32 v15, 1.0, v19
	v_mul_f32_e32 v18, 0xbfb8aa3b, v4
	v_mul_f32_e32 v19, 0xbfb8aa3b, v5
	v_exp_f32_e32 v18, v18
	v_exp_f32_e32 v19, v19
	v_rcp_f32_e32 v14, v14
	v_rcp_f32_e32 v15, v15
	v_add_f32_e32 v18, 1.0, v18
	v_add_f32_e32 v19, 1.0, v19
	v_rcp_f32_e32 v18, v18
	v_rcp_f32_e32 v19, v19
	v_pk_mul_f32 v[2:3], v[2:3], v[14:15]
	v_pk_mul_f32 v[8:9], v[8:9], v[16:17]
	v_pk_mul_f32 v[10:11], v[2:3], v[10:11]
	v_pk_mul_f32 v[2:3], v[4:5], v[18:19]
	v_cvt_pk_bf16_f32 v4, v10, v11
	v_pk_mul_f32 v[12:13], v[2:3], v[12:13]
	v_add_u32_e32 v2, s33, v161
	v_ashrrev_i32_e32 v3, 31, v2
	v_lshlrev_b64 v[2:3], 10, v[2:3]
	v_lshl_add_u64 v[14:15], v[138:139], 0, v[2:3]
	v_cvt_pk_bf16_f32 v2, v6, v7
	v_cvt_pk_bf16_f32 v3, v8, v9
	v_cvt_pk_bf16_f32 v5, v12, v13
	global_store_dwordx4 v[14:15], v[2:5], off nt

;     __device__ __forceinline__ Pre pre(const Unit& u, int r, int cit) const { const size_t off = (size_t)(u.arow0 + r) * D + u.pn * 256 + cit; return Pre{__builtin_nontemporal_load((const v4u*)(gp + off)), __builtin_nontemporal_load((const v4u*)(gp + off + (size_t)8 * D))}; }
;     __device__ __forceinline__ Pre pre(const Unit& u, int r, int cit) const { const size_t off = (size_t)(u.arow0 + r) * D + u.pn * 256 + cit; return Pre{__builtin_nontemporal_load((const v4u*)(gd + off)), __builtin_nontemporal_load((const v4u*)(gd + off + (size_t)8 * D)), __builtin_nontemporal_load((const v4u*)(mp + off)), __builtin_nontemporal_load((const v4u*)(mp + off + (size_t)8 * D))}; }
; template <class Epi, class Sched, bool GATHER, bool ALIGN_EPI = true, bool SP2 = true, bool REMAP64 = false>
; __device__ __forceinline__ void gemm_phase(LAS unsigned char* lds, const bf16* Ag, const bf16* Btg, const int K, const Sched& S, const Epi& E) {
;     ...
;             for (int gq = 0; gq < 8; ++gq) { const int ai = gq >> 2, m = gq & 3, r = ai * HALF + wr * 64 + m * 16 + fr;
;                 if (gq + 1 < 8) { const int rn = ((gq + 1) >> 2) * HALF + wr * 64 + ((gq + 1) & 3) * 16 + fr; pq[(gq + 1) & 1] = E.pre(cur, (rn < cur.nrows ? rn : cur.nrows - 1) + rsh, citx); }
;                 __builtin_amdgcn_sched_barrier(0);
;                 if (r < cur.nrows) { float v0[8], v1[8];
; #pragma unroll
;                     for (int i = 0; i < 4; ++i) { v0[i] = acc[ai][0][m][0][i]; v0[4 + i] = acc[ai][0][m][1][i]; v1[i] = acc[ai][1][m][0][i]; v1[4 + i] = acc[ai][1][m][1][i]; }
;                     if constexpr (RP) {
; #pragma unroll
;                         for (int i = 0; i < 8; ++i) { const float snd = hi ? v0[i] : v1[i];
;                             const float rcv = __builtin_bit_cast(float, __builtin_amdgcn_update_dpp(0, __builtin_bit_cast(int, snd), 0x128, 0xf, 0xf, false));
;                             if (hi) v0[i] = rcv; else v1[i] = rcv; } }
;                     E.post(cur, r + rsh, citx, v0, v1, pq[gq & 1]); }
;     __device__ __forceinline__ void post(const Unit& u, int r, int cit, const float* v0, const float* v1, const Pre&) const {
;         bf16* p = o + (size_t)(u.arow0 + r) * D + u.pn * 256 + cit; store8bf(p, v0); store8bf(p + 128, v1);
;     }
.LBB0_1489:
	s_lshl_b32 s0, s0, 8
	s_ashr_i32 s1, s0, 31
	v_add_u32_e32 v148, s24, v1
	v_lshl_add_u64 v[142:143], s[0:1], 1, v[138:139]
	s_and_b64 vcc, exec, s[16:17]
	s_cbranch_vccz .LBB0_1491
	v_add_u32_e32 v150, s75, v148
	v_ashrrev_i32_e32 v151, 31, v150
	v_lshlrev_b64 v[150:151], 12, v[150:151]
	v_lshl_add_u64 v[150:151], v[142:143], 0, v[150:151]
	v_cvt_pk_bf16_f32 v126, v126, v127
	v_cvt_pk_bf16_f32 v127, v128, v129
	v_cvt_pk_bf16_f32 v128, v122, v123
	v_cvt_pk_bf16_f32 v129, v124, v125
	v_cvt_pk_bf16_f32 v114, v114, v115
	v_cvt_pk_bf16_f32 v115, v116, v117
	v_cvt_pk_bf16_f32 v116, v106, v107
	v_cvt_pk_bf16_f32 v117, v108, v109
	global_store_dwordx4 v[150:151], v[126:129], off nt
	global_store_dwordx4 v[150:151], v[114:117], off offset:256 nt
.LBB0_1491:
	v_cndmask_b32_e64 v106, 0, 1, s[16:17]
	v_cmp_ne_u32_e64 s[0:1], 1, v106
	s_andn2_b64 vcc, exec, s[16:17]
	s_cbranch_vccnz .LBB0_1493
	v_add_u32_e32 v106, s78, v148
	v_ashrrev_i32_e32 v107, 31, v106
	v_lshlrev_b64 v[106:107], 12, v[106:107]
	v_lshl_add_u64 v[114:115], v[142:143], 0, v[106:107]
	v_cvt_pk_bf16_f32 v106, v118, v119
	v_cvt_pk_bf16_f32 v107, v120, v121
	v_cvt_pk_bf16_f32 v108, v110, v111
	v_cvt_pk_bf16_f32 v109, v112, v113
	v_cvt_pk_bf16_f32 v98, v98, v99
	v_cvt_pk_bf16_f32 v99, v100, v101
	v_cvt_pk_bf16_f32 v100, v90, v91
	v_cvt_pk_bf16_f32 v101, v92, v93
	global_store_dwordx4 v[114:115], v[106:109], off nt
	global_store_dwordx4 v[114:115], v[98:101], off offset:256 nt
.LBB0_1493:
	s_and_b64 vcc, exec, s[0:1]
	s_mov_b32 s96, s8
	s_cbranch_vccnz .LBB0_1495
	v_add_u32_e32 v90, s79, v148
	v_ashrrev_i32_e32 v91, 31, v90
	v_lshlrev_b64 v[90:91], 12, v[90:91]
	v_lshl_add_u64 v[98:99], v[142:143], 0, v[90:91]
	v_cvt_pk_bf16_f32 v90, v102, v103
	v_cvt_pk_bf16_f32 v91, v104, v105
	v_cvt_pk_bf16_f32 v92, v94, v95
	v_cvt_pk_bf16_f32 v93, v96, v97
	v_cvt_pk_bf16_f32 v82, v82, v83
	v_cvt_pk_bf16_f32 v83, v84, v85
	v_cvt_pk_bf16_f32 v84, v74, v75
	v_cvt_pk_bf16_f32 v85, v76, v77
	global_store_dwordx4 v[98:99], v[90:93], off nt
	global_store_dwordx4 v[98:99], v[82:85], off offset:256 nt
.LBB0_1495:
	s_and_b64 vcc, exec, s[0:1]
	s_cbranch_vccnz .LBB0_1497
	v_add_u32_e32 v74, s80, v148
	v_ashrrev_i32_e32 v75, 31, v74
	v_lshlrev_b64 v[74:75], 12, v[74:75]
	v_lshl_add_u64 v[82:83], v[142:143], 0, v[74:75]
	v_cvt_pk_bf16_f32 v74, v86, v87
	v_cvt_pk_bf16_f32 v75, v88, v89
	v_cvt_pk_bf16_f32 v76, v78, v79
	v_cvt_pk_bf16_f32 v77, v80, v81
	v_cvt_pk_bf16_f32 v70, v70, v71
	v_cvt_pk_bf16_f32 v71, v72, v73
	v_cvt_pk_bf16_f32 v72, v66, v67
	v_cvt_pk_bf16_f32 v73, v68, v69
	global_store_dwordx4 v[82:83], v[74:77], off nt
	global_store_dwordx4 v[82:83], v[70:73], off offset:256 nt
.LBB0_1497:
	v_cndmask_b32_e64 v66, 0, 1, s[18:19]
	v_cmp_ne_u32_e64 s[0:1], 1, v66
	s_andn2_b64 vcc, exec, s[18:19]
	s_cbranch_vccnz .LBB0_1499
	v_add_u32_e32 v66, s81, v148
	v_ashrrev_i32_e32 v67, 31, v66
	v_lshlrev_b64 v[66:67], 12, v[66:67]
	v_lshl_add_u64 v[66:67], v[142:143], 0, v[66:67]
	v_cvt_pk_bf16_f32 v62, v62, v63
	v_cvt_pk_bf16_f32 v63, v64, v65
	v_cvt_pk_bf16_f32 v64, v58, v59
	v_cvt_pk_bf16_f32 v65, v60, v61
	v_cvt_pk_bf16_f32 v50, v50, v51
	v_cvt_pk_bf16_f32 v51, v52, v53
	v_cvt_pk_bf16_f32 v52, v42, v43
	v_cvt_pk_bf16_f32 v53, v44, v45
	global_store_dwordx4 v[66:67], v[62:65], off nt
	global_store_dwordx4 v[66:67], v[50:53], off offset:256 nt
.LBB0_1499:
	s_and_b64 vcc, exec, s[0:1]
	s_cbranch_vccnz .LBB0_1501
	v_add_u32_e32 v42, s82, v148
	v_ashrrev_i32_e32 v43, 31, v42
	v_lshlrev_b64 v[42:43], 12, v[42:43]
	v_lshl_add_u64 v[50:51], v[142:143], 0, v[42:43]
	v_cvt_pk_bf16_f32 v42, v54, v55
	v_cvt_pk_bf16_f32 v43, v56, v57
	v_cvt_pk_bf16_f32 v44, v46, v47
	v_cvt_pk_bf16_f32 v45, v48, v49
	v_cvt_pk_bf16_f32 v34, v34, v35
	v_cvt_pk_bf16_f32 v35, v36, v37
	v_cvt_pk_bf16_f32 v36, v26, v27
	v_cvt_pk_bf16_f32 v37, v28, v29
	global_store_dwordx4 v[50:51], v[42:45], off nt
	global_store_dwordx4 v[50:51], v[34:37], off offset:256 nt
.LBB0_1501:
	s_and_b64 vcc, exec, s[0:1]
	s_cbranch_vccnz .LBB0_1503
	v_add_u32_e32 v26, s83, v148
	v_ashrrev_i32_e32 v27, 31, v26
	v_lshlrev_b64 v[26:27], 12, v[26:27]
	v_lshl_add_u64 v[34:35], v[142:143], 0, v[26:27]
	v_cvt_pk_bf16_f32 v26, v38, v39
	v_cvt_pk_bf16_f32 v27, v40, v41
	v_cvt_pk_bf16_f32 v28, v30, v31
	v_cvt_pk_bf16_f32 v29, v32, v33
	v_cvt_pk_bf16_f32 v18, v18, v19
	v_cvt_pk_bf16_f32 v19, v20, v21
	v_cvt_pk_bf16_f32 v20, v10, v11
	v_cvt_pk_bf16_f32 v21, v12, v13
	global_store_dwordx4 v[34:35], v[26:29], off nt
	global_store_dwordx4 v[34:35], v[18:21], off offset:256 nt
.LBB0_1503:
	s_and_b64 vcc, exec, s[0:1]
	s_cbranch_vccnz .LBB0_1505
	v_add_u32_e32 v10, s84, v148
	v_ashrrev_i32_e32 v11, 31, v10
	v_lshlrev_b64 v[10:11], 12, v[10:11]
	v_lshl_add_u64 v[18:19], v[142:143], 0, v[10:11]
	v_cvt_pk_bf16_f32 v10, v22, v23
	v_cvt_pk_bf16_f32 v11, v24, v25
	v_cvt_pk_bf16_f32 v12, v14, v15
	v_cvt_pk_bf16_f32 v13, v16, v17
	v_cvt_pk_bf16_f32 v6, v6, v7
	v_cvt_pk_bf16_f32 v7, v8, v9
	v_cvt_pk_bf16_f32 v8, v2, v3
	v_cvt_pk_bf16_f32 v9, v4, v5
	global_store_dwordx4 v[18:19], v[10:13], off nt
	global_store_dwordx4 v[18:19], v[6:9], off offset:256 nt

;     __device__ __forceinline__ Pre pre(const Unit& u, int r, int cit) const { const size_t off = (size_t)(u.arow0 + r) * D + u.pn * 256 + cit; return Pre{__builtin_nontemporal_load((const v4u*)(gp + off)), __builtin_nontemporal_load((const v4u*)(gp + off + (size_t)8 * D))}; }
;     __device__ __forceinline__ Pre pre(const Unit& u, int r, int cit) const { const size_t off = (size_t)(u.arow0 + r) * D + u.pn * 256 + cit; return Pre{__builtin_nontemporal_load((const v4u*)(gd + off)), __builtin_nontemporal_load((const v4u*)(gd + off + (size_t)8 * D)), __builtin_nontemporal_load((const v4u*)(mp + off)), __builtin_nontemporal_load((const v4u*)(mp + off + (size_t)8 * D))}; }
; template <class Epi, class Sched, bool GATHER, bool ALIGN_EPI = true, bool SP2 = true, bool REMAP64 = false>
; __device__ __forceinline__ void gemm_phase(LAS unsigned char* lds, const bf16* Ag, const bf16* Btg, const int K, const Sched& S, const Epi& E) {
;     ...
;             if constexpr (Epi::PRE_ALL) {
;                 typename Epi::Pre pa[8];
; #pragma unroll
;                 for (int gq = 0; gq < 8; ++gq) { const int rn = (gq >> 2) * HALF + wr * 64 + (gq & 3) * 16 + fr; pa[gq] = E.pre(cur, rn < cur.nrows ? rn : cur.nrows - 1, cit); }
; #pragma unroll
;                 for (int gq = 0; gq < 8; ++gq) { const int ai = gq >> 2, m = gq & 3, r = ai * HALF + wr * 64 + m * 16 + fr;
;                     if (r < cur.nrows) { float v0[8], v1[8];
; #pragma unroll
;                         for (int i = 0; i < 4; ++i) { v0[i] = acc[ai][0][m][0][i]; v0[4 + i] = acc[ai][0][m][1][i]; v1[i] = acc[ai][1][m][0][i]; v1[4 + i] = acc[ai][1][m][1][i]; }
;                         E.post(cur, r, cit, v0, v1, pa[gq]); } }
;     __device__ __forceinline__ void post(const Unit& u, int, int cit, const float* v0, const float* v1, const Pre& p) const {
;         bf16* y = ((p.tk & 1) ? y1 : y0) + (size_t)(p.tk >> 1) * D + u.pn * 256 + cit; float a[8], b[8];
; #pragma unroll
;         for (int i = 0; i < 8; ++i) { a[i] = p.w * v0[i]; b[i] = p.w * v1[i]; }
;         store8bf(y, a); store8bf(y + 128, b);
;     }
.LBB0_1591:
	v_lshl_add_u64 v[172:173], s[26:27], 0, v[140:141]
	v_lshlrev_b64 v[172:173], 2, v[172:173]
	v_lshl_add_u64 v[174:175], s[42:43], 0, v[172:173]
	v_lshl_add_u64 v[172:173], s[40:41], 0, v[172:173]
	global_load_dword v171, v[172:173], off
	s_nop 0
	global_load_dword v172, v[174:175], off
	v_mov_b32_e32 v177, s51
	v_mov_b32_e32 v178, s49
	v_mov_b32_e32 v180, s50
	v_mov_b32_e32 v181, s48
	s_waitcnt vmcnt(0)
	v_and_b32_e32 v179, 1, v171
	v_ashrrev_i32_e32 v176, 1, v171
	v_cmp_eq_u32_e32 vcc, 0, v179
	v_pk_mul_f32 v[122:123], v[122:123], v[172:173] op_sel_hi:[1,0]
	v_pk_mul_f32 v[126:127], v[126:127], v[172:173] op_sel_hi:[1,0]
	v_cndmask_b32_e32 v179, v177, v178, vcc
	v_ashrrev_i32_e32 v177, 31, v176
	v_pk_mul_f32 v[118:119], v[118:119], v[172:173] op_sel_hi:[1,0]
	v_pk_mul_f32 v[128:129], v[128:129], v[172:173] op_sel_hi:[1,0]
	v_pk_mul_f32 v[120:121], v[120:121], v[172:173] op_sel_hi:[1,0]
	v_pk_mul_f32 v[174:175], v[114:115], v[172:173] op_sel_hi:[1,0]
	v_pk_mul_f32 v[124:125], v[124:125], v[172:173] op_sel_hi:[1,0]
	v_pk_mul_f32 v[172:173], v[116:117], v[172:173] op_sel_hi:[1,0]
	v_cvt_pk_bf16_f32 v116, v122, v123
	v_cndmask_b32_e32 v178, v180, v181, vcc
	v_lshlrev_b64 v[122:123], 12, v[176:177]
	v_lshl_add_u64 v[122:123], v[178:179], 0, v[122:123]
	v_lshl_add_u64 v[122:123], s[24:25], 1, v[122:123]
	v_cvt_pk_bf16_f32 v114, v126, v127
	v_cvt_pk_bf16_f32 v115, v128, v129
	v_cvt_pk_bf16_f32 v117, v124, v125
	v_lshl_add_u64 v[122:123], v[122:123], 0, v[138:139]
	v_cvt_pk_bf16_f32 v118, v118, v119
	v_cvt_pk_bf16_f32 v119, v120, v121
	v_cvt_pk_bf16_f32 v120, v174, v175
	v_cvt_pk_bf16_f32 v121, v172, v173
	global_store_dwordx4 v[122:123], v[114:117], off nt
	global_store_dwordx4 v[122:123], v[118:121], off offset:256 nt
	s_or_b64 exec, exec, s[28:29]
	v_cmp_gt_i32_e32 vcc, s55, v143
	s_and_saveexec_b64 s[26:27], vcc
	s_cbranch_execz .LBB0_1584
.LBB0_1592:
	s_waitcnt vmcnt(0)
	v_and_b32_e32 v114, 1, v169
	v_mov_b32_e32 v115, s51
	v_mov_b32_e32 v116, s49
	v_cmp_eq_u32_e32 vcc, 0, v114
	v_mov_b32_e32 v114, s50
	v_pk_mul_f32 v[110:111], v[110:111], v[160:161] op_sel_hi:[1,0]
	v_cndmask_b32_e32 v115, v115, v116, vcc
	v_mov_b32_e32 v116, s48
	v_cndmask_b32_e32 v114, v114, v116, vcc
	v_pk_mul_f32 v[116:117], v[98:99], v[160:161] op_sel_hi:[1,0]
	v_ashrrev_i32_e32 v98, 1, v169
	v_ashrrev_i32_e32 v99, 31, v98
	v_lshlrev_b64 v[98:99], 12, v[98:99]
	v_lshl_add_u64 v[98:99], v[114:115], 0, v[98:99]
	v_pk_mul_f32 v[112:113], v[112:113], v[160:161] op_sel_hi:[1,0]
	v_pk_mul_f32 v[106:107], v[106:107], v[160:161] op_sel_hi:[1,0]
	v_pk_mul_f32 v[108:109], v[108:109], v[160:161] op_sel_hi:[1,0]
	v_lshl_add_u64 v[98:99], s[24:25], 1, v[98:99]
	v_pk_mul_f32 v[102:103], v[102:103], v[160:161] op_sel_hi:[1,0]
	v_pk_mul_f32 v[104:105], v[104:105], v[160:161] op_sel_hi:[1,0]
	v_pk_mul_f32 v[118:119], v[100:101], v[160:161] op_sel_hi:[1,0]
	v_lshl_add_u64 v[114:115], v[98:99], 0, v[138:139]
	v_cvt_pk_bf16_f32 v98, v110, v111
	v_cvt_pk_bf16_f32 v99, v112, v113
	v_cvt_pk_bf16_f32 v100, v106, v107
	v_cvt_pk_bf16_f32 v101, v108, v109
	global_store_dwordx4 v[114:115], v[98:101], off nt
	s_nop 1
	v_cvt_pk_bf16_f32 v98, v102, v103
	v_cvt_pk_bf16_f32 v99, v104, v105
	v_cvt_pk_bf16_f32 v100, v116, v117
	v_cvt_pk_bf16_f32 v101, v118, v119
	global_store_dwordx4 v[114:115], v[98:101], off offset:256 nt
	s_or_b64 exec, exec, s[26:27]
	v_cmp_gt_i32_e32 vcc, s55, v153
	s_and_saveexec_b64 s[26:27], vcc
	s_cbranch_execz .LBB0_1585
.LBB0_1593:
	s_waitcnt vmcnt(0)
	v_and_b32_e32 v98, 1, v168
	v_mov_b32_e32 v99, s51
	v_mov_b32_e32 v100, s49
	v_cmp_eq_u32_e32 vcc, 0, v98
	v_mov_b32_e32 v98, s50
	v_pk_mul_f32 v[94:95], v[94:95], v[158:159] op_sel_hi:[1,0]
	v_cndmask_b32_e32 v99, v99, v100, vcc
	v_mov_b32_e32 v100, s48
	v_cndmask_b32_e32 v98, v98, v100, vcc
	v_pk_mul_f32 v[100:101], v[82:83], v[158:159] op_sel_hi:[1,0]
	v_ashrrev_i32_e32 v82, 1, v168
	v_ashrrev_i32_e32 v83, 31, v82
	v_lshlrev_b64 v[82:83], 12, v[82:83]
	v_lshl_add_u64 v[82:83], v[98:99], 0, v[82:83]
	v_pk_mul_f32 v[96:97], v[96:97], v[158:159] op_sel_hi:[1,0]
	v_pk_mul_f32 v[90:91], v[90:91], v[158:159] op_sel_hi:[1,0]
	v_pk_mul_f32 v[92:93], v[92:93], v[158:159] op_sel_hi:[1,0]
	v_lshl_add_u64 v[82:83], s[24:25], 1, v[82:83]
	v_pk_mul_f32 v[86:87], v[86:87], v[158:159] op_sel_hi:[1,0]
	v_pk_mul_f32 v[88:89], v[88:89], v[158:159] op_sel_hi:[1,0]
	v_pk_mul_f32 v[102:103], v[84:85], v[158:159] op_sel_hi:[1,0]
	v_lshl_add_u64 v[98:99], v[82:83], 0, v[138:139]
	v_cvt_pk_bf16_f32 v82, v94, v95
	v_cvt_pk_bf16_f32 v83, v96, v97
	v_cvt_pk_bf16_f32 v84, v90, v91
	v_cvt_pk_bf16_f32 v85, v92, v93
	global_store_dwordx4 v[98:99], v[82:85], off nt
	s_nop 1
	v_cvt_pk_bf16_f32 v82, v86, v87
	v_cvt_pk_bf16_f32 v83, v88, v89
	v_cvt_pk_bf16_f32 v84, v100, v101
	v_cvt_pk_bf16_f32 v85, v102, v103
	global_store_dwordx4 v[98:99], v[82:85], off offset:256 nt
	s_or_b64 exec, exec, s[26:27]
	v_cmp_gt_i32_e32 vcc, s55, v155
	s_and_saveexec_b64 s[26:27], vcc
	s_cbranch_execz .LBB0_1586
;     __device__ __forceinline__ Pre pre(const Unit& u, int r, int cit) const { const size_t off = (size_t)(u.arow0 + r) * D + u.pn * 256 + cit; return Pre{__builtin_nontemporal_load((const v4u*)(gp + off)), __builtin_nontemporal_load((const v4u*)(gp + off + (size_t)8 * D))}; }
;     __device__ __forceinline__ Pre pre(const Unit& u, int r, int cit) const { const size_t off = (size_t)(u.arow0 + r) * D + u.pn * 256 + cit; return Pre{__builtin_nontemporal_load((const v4u*)(gd + off)), __builtin_nontemporal_load((const v4u*)(gd + off + (size_t)8 * D)), __builtin_nontemporal_load((const v4u*)(mp + off)), __builtin_nontemporal_load((const v4u*)(mp + off + (size_t)8 * D))}; }
; template <class Epi, class Sched, bool GATHER, bool ALIGN_EPI = true, bool SP2 = true, bool REMAP64 = false>
; __device__ __forceinline__ void gemm_phase(LAS unsigned char* lds, const bf16* Ag, const bf16* Btg, const int K, const Sched& S, const Epi& E) {
;     ...
;             if constexpr (Epi::PRE_ALL) {
;                 typename Epi::Pre pa[8];
; #pragma unroll
;                 for (int gq = 0; gq < 8; ++gq) { const int rn = (gq >> 2) * HALF + wr * 64 + (gq & 3) * 16 + fr; pa[gq] = E.pre(cur, rn < cur.nrows ? rn : cur.nrows - 1, cit); }
; #pragma unroll
;                 for (int gq = 0; gq < 8; ++gq) { const int ai = gq >> 2, m = gq & 3, r = ai * HALF + wr * 64 + m * 16 + fr;
;                     if (r < cur.nrows) { float v0[8], v1[8];
; #pragma unroll
;                         for (int i = 0; i < 4; ++i) { v0[i] = acc[ai][0][m][0][i]; v0[4 + i] = acc[ai][0][m][1][i]; v1[i] = acc[ai][1][m][0][i]; v1[4 + i] = acc[ai][1][m][1][i]; }
;                         E.post(cur, r, cit, v0, v1, pa[gq]); } }
;     __device__ __forceinline__ void post(const Unit& u, int, int cit, const float* v0, const float* v1, const Pre& p) const {
;         bf16* y = ((p.tk & 1) ? y1 : y0) + (size_t)(p.tk >> 1) * D + u.pn * 256 + cit; float a[8], b[8];
; #pragma unroll
;         for (int i = 0; i < 8; ++i) { a[i] = p.w * v0[i]; b[i] = p.w * v1[i]; }
;         store8bf(y, a); store8bf(y + 128, b);
;     }
.LBB0_1594:
	s_waitcnt vmcnt(0)
	v_and_b32_e32 v82, 1, v167
	v_mov_b32_e32 v83, s51
	v_mov_b32_e32 v84, s49
	v_cmp_eq_u32_e32 vcc, 0, v82
	v_mov_b32_e32 v82, s50
	v_pk_mul_f32 v[78:79], v[78:79], v[156:157] op_sel_hi:[1,0]
	v_cndmask_b32_e32 v83, v83, v84, vcc
	v_mov_b32_e32 v84, s48
	v_cndmask_b32_e32 v82, v82, v84, vcc
	v_pk_mul_f32 v[84:85], v[50:51], v[156:157] op_sel_hi:[1,0]
	v_ashrrev_i32_e32 v50, 1, v167
	v_ashrrev_i32_e32 v51, 31, v50
	v_lshlrev_b64 v[50:51], 12, v[50:51]
	v_lshl_add_u64 v[50:51], v[82:83], 0, v[50:51]
	v_pk_mul_f32 v[80:81], v[80:81], v[156:157] op_sel_hi:[1,0]
	v_pk_mul_f32 v[70:71], v[70:71], v[156:157] op_sel_hi:[1,0]
	v_pk_mul_f32 v[72:73], v[72:73], v[156:157] op_sel_hi:[1,0]
	v_lshl_add_u64 v[50:51], s[24:25], 1, v[50:51]
	v_pk_mul_f32 v[62:63], v[62:63], v[156:157] op_sel_hi:[1,0]
	v_pk_mul_f32 v[64:65], v[64:65], v[156:157] op_sel_hi:[1,0]
	v_pk_mul_f32 v[86:87], v[52:53], v[156:157] op_sel_hi:[1,0]
	v_lshl_add_u64 v[82:83], v[50:51], 0, v[138:139]
	v_cvt_pk_bf16_f32 v50, v78, v79
	v_cvt_pk_bf16_f32 v51, v80, v81
	v_cvt_pk_bf16_f32 v52, v70, v71
	v_cvt_pk_bf16_f32 v53, v72, v73
	global_store_dwordx4 v[82:83], v[50:53], off nt
	s_nop 1
	v_cvt_pk_bf16_f32 v50, v62, v63
	v_cvt_pk_bf16_f32 v51, v64, v65
	v_cvt_pk_bf16_f32 v52, v84, v85
	v_cvt_pk_bf16_f32 v53, v86, v87
	global_store_dwordx4 v[82:83], v[50:53], off offset:256 nt
	s_or_b64 exec, exec, s[26:27]
	v_cmp_gt_i32_e32 vcc, s55, v157
	s_and_saveexec_b64 s[26:27], vcc
	s_cbranch_execz .LBB0_1587
.LBB0_1595:
	s_waitcnt vmcnt(0)
	v_and_b32_e32 v50, 1, v166
	v_mov_b32_e32 v51, s51
	v_mov_b32_e32 v52, s49
	v_cmp_eq_u32_e32 vcc, 0, v50
	v_pk_mul_f32 v[64:65], v[66:67], v[154:155] op_sel_hi:[1,0]
	v_pk_mul_f32 v[66:67], v[68:69], v[154:155] op_sel_hi:[1,0]
	v_ashrrev_i32_e32 v68, 1, v166
	v_cndmask_b32_e32 v51, v51, v52, vcc
	v_mov_b32_e32 v50, s50
	v_mov_b32_e32 v52, s48
	v_ashrrev_i32_e32 v69, 31, v68
	v_cndmask_b32_e32 v50, v50, v52, vcc
	v_lshlrev_b64 v[68:69], 12, v[68:69]
	v_lshl_add_u64 v[50:51], v[50:51], 0, v[68:69]
	v_pk_mul_f32 v[52:53], v[58:59], v[154:155] op_sel_hi:[1,0]
	v_pk_mul_f32 v[60:61], v[60:61], v[154:155] op_sel_hi:[1,0]
	v_pk_mul_f32 v[54:55], v[54:55], v[154:155] op_sel_hi:[1,0]
	v_pk_mul_f32 v[56:57], v[56:57], v[154:155] op_sel_hi:[1,0]
	v_lshl_add_u64 v[50:51], s[24:25], 1, v[50:51]
	v_pk_mul_f32 v[58:59], v[74:75], v[154:155] op_sel_hi:[1,0]
	v_pk_mul_f32 v[62:63], v[76:77], v[154:155] op_sel_hi:[1,0]
	v_lshl_add_u64 v[68:69], v[50:51], 0, v[138:139]
	v_cvt_pk_bf16_f32 v50, v52, v53
	v_cvt_pk_bf16_f32 v51, v60, v61
	v_cvt_pk_bf16_f32 v52, v54, v55
	v_cvt_pk_bf16_f32 v53, v56, v57
	global_store_dwordx4 v[68:69], v[50:53], off nt
	s_nop 1
	v_cvt_pk_bf16_f32 v50, v58, v59
	v_cvt_pk_bf16_f32 v51, v62, v63
	v_cvt_pk_bf16_f32 v52, v64, v65
	v_cvt_pk_bf16_f32 v53, v66, v67
	global_store_dwordx4 v[68:69], v[50:53], off offset:256 nt
	s_or_b64 exec, exec, s[26:27]
	v_cmp_gt_i32_e32 vcc, s55, v159
	s_and_saveexec_b64 s[26:27], vcc
	s_cbranch_execz .LBB0_1588
;     __device__ __forceinline__ Pre pre(const Unit& u, int r, int cit) const { const size_t off = (size_t)(u.arow0 + r) * D + u.pn * 256 + cit; return Pre{__builtin_nontemporal_load((const v4u*)(gp + off)), __builtin_nontemporal_load((const v4u*)(gp + off + (size_t)8 * D))}; }
;     __device__ __forceinline__ Pre pre(const Unit& u, int r, int cit) const { const size_t off = (size_t)(u.arow0 + r) * D + u.pn * 256 + cit; return Pre{__builtin_nontemporal_load((const v4u*)(gd + off)), __builtin_nontemporal_load((const v4u*)(gd + off + (size_t)8 * D)), __builtin_nontemporal_load((const v4u*)(mp + off)), __builtin_nontemporal_load((const v4u*)(mp + off + (size_t)8 * D))}; }
; template <class Epi, class Sched, bool GATHER, bool ALIGN_EPI = true, bool SP2 = true, bool REMAP64 = false>
; __device__ __forceinline__ void gemm_phase(LAS unsigned char* lds, const bf16* Ag, const bf16* Btg, const int K, const Sched& S, const Epi& E) {
;     ...
;             if constexpr (Epi::PRE_ALL) {
;                 typename Epi::Pre pa[8];
; #pragma unroll
;                 for (int gq = 0; gq < 8; ++gq) { const int rn = (gq >> 2) * HALF + wr * 64 + (gq & 3) * 16 + fr; pa[gq] = E.pre(cur, rn < cur.nrows ? rn : cur.nrows - 1, cit); }
; #pragma unroll
;                 for (int gq = 0; gq < 8; ++gq) { const int ai = gq >> 2, m = gq & 3, r = ai * HALF + wr * 64 + m * 16 + fr;
;                     if (r < cur.nrows) { float v0[8], v1[8];
; #pragma unroll
;                         for (int i = 0; i < 4; ++i) { v0[i] = acc[ai][0][m][0][i]; v0[4 + i] = acc[ai][0][m][1][i]; v1[i] = acc[ai][1][m][0][i]; v1[4 + i] = acc[ai][1][m][1][i]; }
;                         E.post(cur, r, cit, v0, v1, pa[gq]); } }
;     __device__ __forceinline__ void post(const Unit& u, int, int cit, const float* v0, const float* v1, const Pre& p) const {
;         bf16* y = ((p.tk & 1) ? y1 : y0) + (size_t)(p.tk >> 1) * D + u.pn * 256 + cit; float a[8], b[8];
; #pragma unroll
;         for (int i = 0; i < 8; ++i) { a[i] = p.w * v0[i]; b[i] = p.w * v1[i]; }
;         store8bf(y, a); store8bf(y + 128, b);
;     }
.LBB0_1596:
	s_waitcnt vmcnt(0)
	v_and_b32_e32 v50, 1, v165
	v_mov_b32_e32 v51, s51
	v_mov_b32_e32 v52, s49
	v_cmp_eq_u32_e32 vcc, 0, v50
	v_mov_b32_e32 v50, s50
	v_pk_mul_f32 v[38:39], v[38:39], v[152:153] op_sel_hi:[1,0]
	v_cndmask_b32_e32 v51, v51, v52, vcc
	v_mov_b32_e32 v52, s48
	v_cndmask_b32_e32 v50, v50, v52, vcc
	v_pk_mul_f32 v[52:53], v[34:35], v[152:153] op_sel_hi:[1,0]
	v_ashrrev_i32_e32 v34, 1, v165
	v_ashrrev_i32_e32 v35, 31, v34
	v_lshlrev_b64 v[34:35], 12, v[34:35]
	v_lshl_add_u64 v[34:35], v[50:51], 0, v[34:35]
	v_pk_mul_f32 v[40:41], v[40:41], v[152:153] op_sel_hi:[1,0]
	v_pk_mul_f32 v[54:55], v[36:37], v[152:153] op_sel_hi:[1,0]
	v_lshl_add_u64 v[34:35], s[24:25], 1, v[34:35]
	v_pk_mul_f32 v[46:47], v[46:47], v[152:153] op_sel_hi:[1,0]
	v_pk_mul_f32 v[48:49], v[48:49], v[152:153] op_sel_hi:[1,0]
	v_pk_mul_f32 v[42:43], v[42:43], v[152:153] op_sel_hi:[1,0]
	v_pk_mul_f32 v[44:45], v[44:45], v[152:153] op_sel_hi:[1,0]
	v_lshl_add_u64 v[50:51], v[34:35], 0, v[138:139]
	v_cvt_pk_bf16_f32 v34, v38, v39
	v_cvt_pk_bf16_f32 v35, v40, v41
	v_cvt_pk_bf16_f32 v36, v52, v53
	v_cvt_pk_bf16_f32 v37, v54, v55
	global_store_dwordx4 v[50:51], v[34:37], off nt
	s_nop 1
	v_cvt_pk_bf16_f32 v34, v46, v47
	v_cvt_pk_bf16_f32 v35, v48, v49
	v_cvt_pk_bf16_f32 v36, v42, v43
	v_cvt_pk_bf16_f32 v37, v44, v45
	global_store_dwordx4 v[50:51], v[34:37], off offset:256 nt
	s_or_b64 exec, exec, s[26:27]
	v_cmp_gt_i32_e32 vcc, s55, v161
	s_and_saveexec_b64 s[26:27], vcc
	s_cbranch_execz .LBB0_1589
.LBB0_1597:
	s_waitcnt vmcnt(0)
	v_and_b32_e32 v34, 1, v151
	v_mov_b32_e32 v35, s51
	v_mov_b32_e32 v36, s49
	v_cmp_eq_u32_e32 vcc, 0, v34
	v_mov_b32_e32 v34, s50
	v_pk_mul_f32 v[22:23], v[22:23], v[150:151] op_sel_hi:[1,0]
	v_cndmask_b32_e32 v35, v35, v36, vcc
	v_mov_b32_e32 v36, s48
	v_cndmask_b32_e32 v34, v34, v36, vcc
	v_pk_mul_f32 v[36:37], v[18:19], v[150:151] op_sel_hi:[1,0]
	v_ashrrev_i32_e32 v18, 1, v151
	v_ashrrev_i32_e32 v19, 31, v18
	v_lshlrev_b64 v[18:19], 12, v[18:19]
	v_lshl_add_u64 v[18:19], v[34:35], 0, v[18:19]
	v_pk_mul_f32 v[24:25], v[24:25], v[150:151] op_sel_hi:[1,0]
	v_pk_mul_f32 v[38:39], v[20:21], v[150:151] op_sel_hi:[1,0]
	v_lshl_add_u64 v[18:19], s[24:25], 1, v[18:19]
	v_pk_mul_f32 v[30:31], v[30:31], v[150:151] op_sel_hi:[1,0]
	v_pk_mul_f32 v[32:33], v[32:33], v[150:151] op_sel_hi:[1,0]
	v_pk_mul_f32 v[26:27], v[26:27], v[150:151] op_sel_hi:[1,0]
	v_pk_mul_f32 v[28:29], v[28:29], v[150:151] op_sel_hi:[1,0]
	v_lshl_add_u64 v[34:35], v[18:19], 0, v[138:139]
	v_cvt_pk_bf16_f32 v18, v22, v23
	v_cvt_pk_bf16_f32 v19, v24, v25
	v_cvt_pk_bf16_f32 v20, v36, v37
	v_cvt_pk_bf16_f32 v21, v38, v39
	global_store_dwordx4 v[34:35], v[18:21], off nt
	s_nop 1
	v_cvt_pk_bf16_f32 v18, v30, v31
	v_cvt_pk_bf16_f32 v19, v32, v33
	v_cvt_pk_bf16_f32 v20, v26, v27
	v_cvt_pk_bf16_f32 v21, v28, v29
	global_store_dwordx4 v[34:35], v[18:21], off offset:256 nt
	s_or_b64 exec, exec, s[26:27]
	v_cmp_gt_i32_e32 vcc, s55, v162
	s_and_saveexec_b64 s[26:27], vcc
	s_cbranch_execz .LBB0_1590
.LBB0_1598:
	s_waitcnt vmcnt(0)
	v_and_b32_e32 v18, 1, v149
	v_mov_b32_e32 v19, s51
	v_mov_b32_e32 v20, s49
	v_cmp_eq_u32_e32 vcc, 0, v18
	v_mov_b32_e32 v18, s50
	v_pk_mul_f32 v[6:7], v[6:7], v[148:149] op_sel_hi:[1,0]
	v_cndmask_b32_e32 v19, v19, v20, vcc
	v_mov_b32_e32 v20, s48
	v_cndmask_b32_e32 v18, v18, v20, vcc
	v_pk_mul_f32 v[20:21], v[2:3], v[148:149] op_sel_hi:[1,0]
	v_ashrrev_i32_e32 v2, 1, v149
	v_ashrrev_i32_e32 v3, 31, v2
	v_lshlrev_b64 v[2:3], 12, v[2:3]
	v_lshl_add_u64 v[2:3], v[18:19], 0, v[2:3]
	v_pk_mul_f32 v[8:9], v[8:9], v[148:149] op_sel_hi:[1,0]
	v_pk_mul_f32 v[22:23], v[4:5], v[148:149] op_sel_hi:[1,0]
	v_lshl_add_u64 v[2:3], s[24:25], 1, v[2:3]
	v_pk_mul_f32 v[14:15], v[14:15], v[148:149] op_sel_hi:[1,0]
	v_pk_mul_f32 v[16:17], v[16:17], v[148:149] op_sel_hi:[1,0]
	v_pk_mul_f32 v[10:11], v[10:11], v[148:149] op_sel_hi:[1,0]
	v_pk_mul_f32 v[12:13], v[12:13], v[148:149] op_sel_hi:[1,0]
	v_lshl_add_u64 v[18:19], v[2:3], 0, v[138:139]
	v_cvt_pk_bf16_f32 v2, v6, v7
	v_cvt_pk_bf16_f32 v3, v8, v9
	v_cvt_pk_bf16_f32 v4, v20, v21
	v_cvt_pk_bf16_f32 v5, v22, v23
	global_store_dwordx4 v[18:19], v[2:5], off nt
	s_nop 1
	v_cvt_pk_bf16_f32 v2, v14, v15
	v_cvt_pk_bf16_f32 v3, v16, v17
	v_cvt_pk_bf16_f32 v4, v10, v11
	v_cvt_pk_bf16_f32 v5, v12, v13
	global_store_dwordx4 v[18:19], v[2:5], off offset:256 nt
	s_or_b64 exec, exec, s[26:27]
	s_mov_b64 s[24:25], -1
	s_and_b64 vcc, exec, s[0:1]
	s_cbranch_vccz .LBB0_1573

; template <class Epi, class Sched, bool GATHER, bool ALIGN_EPI = true, bool SP2 = true, bool REMAP64 = false>
; __device__ __forceinline__ void gemm_phase(LAS unsigned char* lds, const bf16* Ag, const bf16* Btg, const int K, const Sched& S, const Epi& E) {
;     ...
;             const bool hi = RP && (fr >= 8); const int rsh = hi ? -8 : 0, citx = hi ? cit + 32 : cit;
;             typename Epi::Pre pq[2];
;             { const int r0_ = wr * 64 + fr; pq[0] = E.pre(cur, (r0_ < cur.nrows ? r0_ : cur.nrows - 1) + rsh, citx); }
; #pragma unroll
;             for (int gq = 0; gq < 8; ++gq) { const int ai = gq >> 2, m = gq & 3, r = ai * HALF + wr * 64 + m * 16 + fr;
;                 if (gq + 1 < 8) { const int rn = ((gq + 1) >> 2) * HALF + wr * 64 + ((gq + 1) & 3) * 16 + fr; pq[(gq + 1) & 1] = E.pre(cur, (rn < cur.nrows ? rn : cur.nrows - 1) + rsh, citx); }
;                 __builtin_amdgcn_sched_barrier(0);
;                 if (r < cur.nrows) { float v0[8], v1[8];
; #pragma unroll
;                     for (int i = 0; i < 4; ++i) { v0[i] = acc[ai][0][m][0][i]; v0[4 + i] = acc[ai][0][m][1][i]; v1[i] = acc[ai][1][m][0][i]; v1[4 + i] = acc[ai][1][m][1][i]; }
;                     if constexpr (RP) {
; #pragma unroll
;                         for (int i = 0; i < 8; ++i) { const float snd = hi ? v0[i] : v1[i];
;                             const float rcv = __builtin_bit_cast(float, __builtin_amdgcn_update_dpp(0, __builtin_bit_cast(int, snd), 0x128, 0xf, 0xf, false));
;     __device__ __forceinline__ Pre pre(const Unit& u, int r, int cit) const { const size_t off = (size_t)(u.arow0 + r) * D + u.pn * 256 + cit;
;         return Pre{__builtin_nontemporal_load((const v4u*)(pp + off)), __builtin_nontemporal_load((const v4u*)(pp + off + (size_t)8 * D)), *(const v4u*)(h + off), *(const v4u*)(h + off + (size_t)8 * D)}; }
;     __device__ __forceinline__ void post(const Unit& u, int r, int cit, const float* v0, const float* v1, const Pre& p) const {
;         const size_t off = (size_t)(u.arow0 + r) * D + u.pn * 256 + cit; float p0[8], p1[8], a[8], b[8]; unpack8bf(p.p0, p0); unpack8bf(p.p1, p1); unpack8bf(p.h0, a); unpack8bf(p.h1, b);
; #pragma unroll
;         for (int i = 0; i < 8; ++i) { a[i] += sigmoidf_(v0[i]) * p0[i]; b[i] += sigmoidf_(v1[i]) * p1[i]; }
;         store8bf(h + off, a); store8bf(h + off + (size_t)8 * D, b);
;     }
.LBB0_1736:
	v_add_u32_e32 v128, s8, v189
	v_ashrrev_i32_e32 v129, 31, v128
	s_lshl_b32 s42, s40, 8
	v_lshlrev_b64 v[128:129], 11, v[128:129]
	s_ashr_i32 s43, s42, 31
	v_lshl_add_u64 v[128:129], v[128:129], 0, s[42:43]
	v_or_b32_e32 v128, v128, v172
	v_lshlrev_b64 v[128:129], 1, v[128:129]
	v_lshl_add_u64 v[130:131], s[36:37], 0, v[128:129]
	v_add_co_u32_e32 v132, vcc, s57, v130
	v_lshl_add_u64 v[128:129], s[4:5], 0, v[128:129]
	s_nop 0
	v_addc_co_u32_e32 v133, vcc, 0, v131, vcc
	global_load_dwordx4 v[156:159], v[130:131], off nt
	global_load_dwordx4 v[144:147], v[132:133], off nt
	v_add_co_u32_e32 v130, vcc, s57, v128
	v_add_u32_e32 v201, s8, v188
	s_nop 0
	v_addc_co_u32_e32 v131, vcc, 0, v129, vcc
	global_load_dwordx4 v[152:155], v[128:129], off
	global_load_dwordx4 v[148:151], v[130:131], off
	v_add_u32_e32 v128, v201, v190
	v_ashrrev_i32_e32 v129, 31, v128
	v_mov_b32_e32 v187, s43
	v_or_b32_e32 v186, s42, v172
	v_lshlrev_b64 v[128:129], 11, v[128:129]
	v_lshl_add_u64 v[128:129], v[128:129], 0, v[186:187]
	v_lshlrev_b64 v[132:133], 1, v[128:129]
	v_lshl_add_u64 v[128:129], s[36:37], 0, v[132:133]
	v_add_co_u32_e32 v130, vcc, 0x8000, v128
	v_lshl_add_u64 v[132:133], s[4:5], 0, v[132:133]
	s_nop 0
	v_addc_co_u32_e32 v131, vcc, 0, v129, vcc
	v_add_co_u32_e32 v134, vcc, 0x8000, v132
	global_load_dwordx4 v[140:143], v[128:129], off nt
	s_nop 0
	global_load_dwordx4 v[128:131], v[130:131], off nt
	v_addc_co_u32_e32 v135, vcc, 0, v133, vcc
	global_load_dwordx4 v[136:139], v[132:133], off
	s_nop 0
	global_load_dwordx4 v[132:135], v[134:135], off
	v_lshl_add_u64 v[184:185], s[42:43], 1, v[174:175]
	v_add_u32_e32 v200, v201, v161
	s_nop 1
	v_add_u32_e32 v214, v201, v191
	v_ashrrev_i32_e32 v215, 31, v214
	v_lshlrev_b64 v[214:215], 11, v[214:215]
	v_lshl_add_u64 v[214:215], v[214:215], 0, v[186:187]
	v_lshlrev_b64 v[218:219], 1, v[214:215]
	v_lshl_add_u64 v[214:215], s[36:37], 0, v[218:219]
	v_add_co_u32_e32 v216, vcc, 0x8000, v214
	v_lshl_add_u64 v[218:219], s[4:5], 0, v[218:219]
	s_nop 0
	v_addc_co_u32_e32 v217, vcc, 0, v215, vcc
	v_add_co_u32_e32 v220, vcc, 0x8000, v218
	global_load_dwordx4 v[226:229], v[214:215], off nt
	s_nop 0
	global_load_dwordx4 v[214:217], v[216:217], off nt
	v_addc_co_u32_e32 v221, vcc, 0, v219, vcc
	global_load_dwordx4 v[222:225], v[218:219], off
	s_nop 0
	global_load_dwordx4 v[218:221], v[220:221], off
	s_nop 1
	v_add_u32_e32 v230, v201, v192
	v_ashrrev_i32_e32 v231, 31, v230
	v_lshlrev_b64 v[230:231], 11, v[230:231]
	v_lshl_add_u64 v[230:231], v[230:231], 0, v[186:187]
	v_lshlrev_b64 v[234:235], 1, v[230:231]
	v_lshl_add_u64 v[230:231], s[36:37], 0, v[234:235]
	v_add_co_u32_e32 v232, vcc, 0x8000, v230
	v_lshl_add_u64 v[234:235], s[4:5], 0, v[234:235]
	s_nop 0
	v_addc_co_u32_e32 v233, vcc, 0, v231, vcc
	v_add_co_u32_e32 v236, vcc, 0x8000, v234
	global_load_dwordx4 v[242:245], v[230:231], off nt
	s_nop 0
	global_load_dwordx4 v[230:233], v[232:233], off nt
	v_addc_co_u32_e32 v237, vcc, 0, v235, vcc
	global_load_dwordx4 v[238:241], v[234:235], off
	s_nop 0
	global_load_dwordx4 v[234:237], v[236:237], off
	s_and_b64 vcc, exec, s[20:21]
	s_cbranch_vccz .LBB0_1738
	s_waitcnt vmcnt(12)
	v_cndmask_b32_e64 v202, v116, v124, s[0:1]
	v_mov_b32_e32 v203, 0
	s_nop 1
	v_mov_b32_dpp v203, v202 row_ror:8 row_mask:0xf bank_mask:0xf
	v_cndmask_b32_e64 v202, v117, v125, s[0:1]
	v_cndmask_b32_e64 v124, v124, v203, s[0:1]
	v_cndmask_b32_e64 v116, v203, v116, s[0:1]
	v_mov_b32_e32 v203, 0
	s_nop 1
	v_mov_b32_dpp v203, v202 row_ror:8 row_mask:0xf bank_mask:0xf
	v_cndmask_b32_e64 v202, v118, v126, s[0:1]
	v_cndmask_b32_e64 v125, v125, v203, s[0:1]
	v_cndmask_b32_e64 v203, v203, v117, s[0:1]
	v_mov_b32_e32 v117, 0
	s_nop 1
	v_mov_b32_dpp v117, v202 row_ror:8 row_mask:0xf bank_mask:0xf
	v_cndmask_b32_e64 v202, v119, v127, s[0:1]
	v_cndmask_b32_e64 v126, v126, v117, s[0:1]
	v_cndmask_b32_e64 v204, v117, v118, s[0:1]
	v_mov_b32_e32 v117, 0
	v_cndmask_b32_e64 v118, v112, v120, s[0:1]
	s_nop 0
	v_mov_b32_dpp v117, v202 row_ror:8 row_mask:0xf bank_mask:0xf
	v_cndmask_b32_e64 v127, v127, v117, s[0:1]
	v_cndmask_b32_e64 v202, v117, v119, s[0:1]
	v_mov_b32_e32 v117, 0
	s_nop 0
	v_and_b32_e32 v119, 0xffff0000, v152
	v_mov_b32_dpp v117, v118 row_ror:8 row_mask:0xf bank_mask:0xf
	v_cndmask_b32_e64 v118, v113, v121, s[0:1]
	v_cndmask_b32_e64 v206, v117, v112, s[0:1]
	v_mov_b32_e32 v112, 0
	v_cndmask_b32_e64 v205, v120, v117, s[0:1]
	v_cndmask_b32_e64 v117, v114, v122, s[0:1]
	v_mov_b32_dpp v112, v118 row_ror:8 row_mask:0xf bank_mask:0xf
	v_cndmask_b32_e64 v207, v121, v112, s[0:1]
	v_cndmask_b32_e64 v208, v112, v113, s[0:1]
	v_mov_b32_e32 v112, 0
	v_cndmask_b32_e64 v113, v115, v123, s[0:1]
	v_lshlrev_b32_e32 v118, 16, v152
	v_mov_b32_dpp v112, v117 row_ror:8 row_mask:0xf bank_mask:0xf
	v_cndmask_b32_e64 v210, v112, v114, s[0:1]
	v_mul_f32_e32 v114, 0xbfb8aa3b, v124
	v_exp_f32_e32 v114, v114
	v_cndmask_b32_e64 v209, v122, v112, s[0:1]
	v_mov_b32_e32 v112, 0
	v_and_b32_e32 v117, 0xffff0000, v156
	v_and_b32_e32 v121, 0xffff0000, v157
	v_mov_b32_dpp v112, v113 row_ror:8 row_mask:0xf bank_mask:0xf
	v_mul_f32_e32 v113, 0xbfb8aa3b, v116
	v_cndmask_b32_e64 v211, v123, v112, s[0:1]
	v_cndmask_b32_e64 v212, v112, v115, s[0:1]
	v_add_f32_e32 v112, 1.0, v114
	v_exp_f32_e32 v113, v113
	v_mul_f32_e32 v114, 0xbfb8aa3b, v125
	v_exp_f32_e32 v115, v114
	v_rcp_f32_e32 v112, v112
	v_add_f32_e32 v113, 1.0, v113
	v_rcp_f32_e32 v114, v113
	v_add_f32_e32 v113, 1.0, v115
	v_mul_f32_e32 v115, 0xbfb8aa3b, v203
	v_exp_f32_e32 v115, v115
	v_rcp_f32_e32 v113, v113
	v_lshlrev_b32_e32 v116, 16, v156
	v_lshlrev_b32_e32 v122, 16, v153
	v_add_f32_e32 v115, 1.0, v115
	v_rcp_f32_e32 v115, v115
; template <class Epi, class Sched, bool GATHER, bool ALIGN_EPI = true, bool SP2 = true, bool REMAP64 = false>
; __device__ __forceinline__ void gemm_phase(LAS unsigned char* lds, const bf16* Ag, const bf16* Btg, const int K, const Sched& S, const Epi& E) {
;     ...
;             const bool hi = RP && (fr >= 8); const int rsh = hi ? -8 : 0, citx = hi ? cit + 32 : cit;
;             typename Epi::Pre pq[2];
;             { const int r0_ = wr * 64 + fr; pq[0] = E.pre(cur, (r0_ < cur.nrows ? r0_ : cur.nrows - 1) + rsh, citx); }
; #pragma unroll
;             for (int gq = 0; gq < 8; ++gq) { const int ai = gq >> 2, m = gq & 3, r = ai * HALF + wr * 64 + m * 16 + fr;
;                 if (gq + 1 < 8) { const int rn = ((gq + 1) >> 2) * HALF + wr * 64 + ((gq + 1) & 3) * 16 + fr; pq[(gq + 1) & 1] = E.pre(cur, (rn < cur.nrows ? rn : cur.nrows - 1) + rsh, citx); }
;                 __builtin_amdgcn_sched_barrier(0);
;                 if (r < cur.nrows) { float v0[8], v1[8];
; #pragma unroll
;                     for (int i = 0; i < 4; ++i) { v0[i] = acc[ai][0][m][0][i]; v0[4 + i] = acc[ai][0][m][1][i]; v1[i] = acc[ai][1][m][0][i]; v1[4 + i] = acc[ai][1][m][1][i]; }
;                     if constexpr (RP) {
; #pragma unroll
;                         for (int i = 0; i < 8; ++i) { const float snd = hi ? v0[i] : v1[i];
;                             const float rcv = __builtin_bit_cast(float, __builtin_amdgcn_update_dpp(0, __builtin_bit_cast(int, snd), 0x128, 0xf, 0xf, false));
;     __device__ __forceinline__ Pre pre(const Unit& u, int r, int cit) const { const size_t off = (size_t)(u.arow0 + r) * D + u.pn * 256 + cit;
;         return Pre{__builtin_nontemporal_load((const v4u*)(pp + off)), __builtin_nontemporal_load((const v4u*)(pp + off + (size_t)8 * D)), *(const v4u*)(h + off), *(const v4u*)(h + off + (size_t)8 * D)}; }
;     __device__ __forceinline__ void post(const Unit& u, int r, int cit, const float* v0, const float* v1, const Pre& p) const {
;         const size_t off = (size_t)(u.arow0 + r) * D + u.pn * 256 + cit; float p0[8], p1[8], a[8], b[8]; unpack8bf(p.p0, p0); unpack8bf(p.p1, p1); unpack8bf(p.h0, a); unpack8bf(p.h1, b);
; #pragma unroll
;         for (int i = 0; i < 8; ++i) { a[i] += sigmoidf_(v0[i]) * p0[i]; b[i] += sigmoidf_(v1[i]) * p1[i]; }
;         store8bf(h + off, a); store8bf(h + off + (size_t)8 * D, b);
;     }
	v_pk_fma_f32 v[112:113], v[112:113], v[116:117], v[118:119]
	v_mul_f32_e32 v118, 0xbfb8aa3b, v126
	v_lshlrev_b32_e32 v116, 16, v144
	v_and_b32_e32 v117, 0xffff0000, v144
	v_exp_f32_e32 v120, v118
	v_lshlrev_b32_e32 v118, 16, v148
	v_and_b32_e32 v119, 0xffff0000, v148
	v_pk_fma_f32 v[116:117], v[114:115], v[116:117], v[118:119]
	v_mul_f32_e32 v115, 0xbfb8aa3b, v204
	v_exp_f32_e32 v115, v115
	v_mul_f32_e32 v118, 0xbfb8aa3b, v127
	v_exp_f32_e32 v119, v118
	v_add_f32_e32 v114, 1.0, v120
	v_add_f32_e32 v115, 1.0, v115
	v_rcp_f32_e32 v118, v115
	v_add_f32_e32 v115, 1.0, v119
	v_mul_f32_e32 v119, 0xbfb8aa3b, v202
	v_exp_f32_e32 v119, v119
	v_rcp_f32_e32 v114, v114
	v_rcp_f32_e32 v115, v115
	v_lshlrev_b32_e32 v120, 16, v157
	v_add_f32_e32 v119, 1.0, v119
	v_rcp_f32_e32 v119, v119
	v_and_b32_e32 v123, 0xffff0000, v153
	v_pk_fma_f32 v[114:115], v[114:115], v[120:121], v[122:123]
	v_mul_f32_e32 v122, 0xbfb8aa3b, v205
	v_lshlrev_b32_e32 v120, 16, v145
	v_and_b32_e32 v121, 0xffff0000, v145
	v_exp_f32_e32 v124, v122
	v_lshlrev_b32_e32 v122, 16, v149
	v_and_b32_e32 v123, 0xffff0000, v149
	v_pk_fma_f32 v[118:119], v[118:119], v[120:121], v[122:123]
	v_mul_f32_e32 v121, 0xbfb8aa3b, v206
	v_exp_f32_e32 v121, v121
	v_mul_f32_e32 v122, 0xbfb8aa3b, v207
	v_exp_f32_e32 v123, v122
	v_add_f32_e32 v120, 1.0, v124
	v_add_f32_e32 v121, 1.0, v121
	v_rcp_f32_e32 v122, v121
	v_add_f32_e32 v121, 1.0, v123
	v_mul_f32_e32 v123, 0xbfb8aa3b, v208
	v_exp_f32_e32 v123, v123
	v_rcp_f32_e32 v120, v120
	v_rcp_f32_e32 v121, v121
	v_lshlrev_b32_e32 v124, 16, v158
	v_add_f32_e32 v123, 1.0, v123
	v_rcp_f32_e32 v123, v123
	v_and_b32_e32 v125, 0xffff0000, v158
	v_lshlrev_b32_e32 v126, 16, v154
	v_and_b32_e32 v127, 0xffff0000, v154
	v_pk_fma_f32 v[120:121], v[120:121], v[124:125], v[126:127]
	v_mul_f32_e32 v126, 0xbfb8aa3b, v209
	v_lshlrev_b32_e32 v124, 16, v146
	v_and_b32_e32 v125, 0xffff0000, v146
	v_exp_f32_e32 v144, v126
	v_lshlrev_b32_e32 v126, 16, v150
	v_and_b32_e32 v127, 0xffff0000, v150
	v_pk_fma_f32 v[122:123], v[122:123], v[124:125], v[126:127]
	v_mul_f32_e32 v125, 0xbfb8aa3b, v210
	v_exp_f32_e32 v125, v125
	v_mul_f32_e32 v126, 0xbfb8aa3b, v211
	v_exp_f32_e32 v127, v126
	v_add_f32_e32 v124, 1.0, v144
	v_add_f32_e32 v125, 1.0, v125
	v_rcp_f32_e32 v126, v125
	v_add_f32_e32 v125, 1.0, v127
	v_mul_f32_e32 v127, 0xbfb8aa3b, v212
	v_exp_f32_e32 v127, v127
	v_rcp_f32_e32 v124, v124
	v_rcp_f32_e32 v125, v125
	v_lshlrev_b32_e32 v144, 16, v159
	v_add_f32_e32 v127, 1.0, v127
	v_rcp_f32_e32 v127, v127
	v_and_b32_e32 v145, 0xffff0000, v159
	v_lshlrev_b32_e32 v148, 16, v155
	v_and_b32_e32 v149, 0xffff0000, v155
	v_pk_fma_f32 v[124:125], v[124:125], v[144:145], v[148:149]
	v_lshlrev_b32_e32 v144, 16, v147
	v_and_b32_e32 v145, 0xffff0000, v147
	v_lshlrev_b32_e32 v146, 16, v151
	v_and_b32_e32 v147, 0xffff0000, v151
	v_pk_fma_f32 v[126:127], v[126:127], v[144:145], v[146:147]
	v_add_u32_e32 v144, s54, v200
	v_ashrrev_i32_e32 v145, 31, v144
	v_lshlrev_b64 v[144:145], 12, v[144:145]
	v_lshl_add_u64 v[144:145], v[184:185], 0, v[144:145]
	v_cvt_pk_bf16_f32 v112, v112, v113
	v_cvt_pk_bf16_f32 v113, v114, v115
	v_cvt_pk_bf16_f32 v114, v120, v121
	v_cvt_pk_bf16_f32 v115, v124, v125
	global_store_dwordx4 v[144:145], v[112:115], off nt
	s_nop 1
	v_cvt_pk_bf16_f32 v112, v116, v117
	v_add_co_u32_e32 v116, vcc, 0x8000, v144
	v_cvt_pk_bf16_f32 v113, v118, v119
	v_cvt_pk_bf16_f32 v114, v122, v123
	v_cvt_pk_bf16_f32 v115, v126, v127
	v_addc_co_u32_e32 v117, vcc, 0, v145, vcc
	global_store_dwordx4 v[116:117], v[112:115], off nt
.LBB0_1738:
	s_nop 1
	v_add_u32_e32 v112, v201, v193
	v_ashrrev_i32_e32 v113, 31, v112
	v_lshlrev_b64 v[112:113], 11, v[112:113]
	v_lshl_add_u64 v[112:113], v[112:113], 0, v[186:187]
	v_lshlrev_b64 v[116:117], 1, v[112:113]
	v_lshl_add_u64 v[112:113], s[36:37], 0, v[116:117]
	v_add_co_u32_e32 v114, vcc, 0x8000, v112
	v_lshl_add_u64 v[116:117], s[4:5], 0, v[116:117]
	s_nop 0
	v_addc_co_u32_e32 v115, vcc, 0, v113, vcc
	v_add_co_u32_e32 v118, vcc, 0x8000, v116
	global_load_dwordx4 v[124:127], v[112:113], off nt
	s_nop 0
	global_load_dwordx4 v[112:115], v[114:115], off nt
	v_addc_co_u32_e32 v119, vcc, 0, v117, vcc
	global_load_dwordx4 v[120:123], v[116:117], off
	s_nop 0
	global_load_dwordx4 v[116:119], v[118:119], off
	s_nop 0
	v_cndmask_b32_e64 v144, 0, 1, s[20:21]
	v_cmp_ne_u32_e64 s[8:9], 1, v144
	s_andn2_b64 vcc, exec, s[20:21]
	s_cbranch_vccnz .LBB0_1740
; template <class Epi, class Sched, bool GATHER, bool ALIGN_EPI = true, bool SP2 = true, bool REMAP64 = false>
; __device__ __forceinline__ void gemm_phase(LAS unsigned char* lds, const bf16* Ag, const bf16* Btg, const int K, const Sched& S, const Epi& E) {
;     ...
;             const bool hi = RP && (fr >= 8); const int rsh = hi ? -8 : 0, citx = hi ? cit + 32 : cit;
;             typename Epi::Pre pq[2];
;             { const int r0_ = wr * 64 + fr; pq[0] = E.pre(cur, (r0_ < cur.nrows ? r0_ : cur.nrows - 1) + rsh, citx); }
; #pragma unroll
;             for (int gq = 0; gq < 8; ++gq) { const int ai = gq >> 2, m = gq & 3, r = ai * HALF + wr * 64 + m * 16 + fr;
;                 if (gq + 1 < 8) { const int rn = ((gq + 1) >> 2) * HALF + wr * 64 + ((gq + 1) & 3) * 16 + fr; pq[(gq + 1) & 1] = E.pre(cur, (rn < cur.nrows ? rn : cur.nrows - 1) + rsh, citx); }
;                 __builtin_amdgcn_sched_barrier(0);
;                 if (r < cur.nrows) { float v0[8], v1[8];
; #pragma unroll
;                     for (int i = 0; i < 4; ++i) { v0[i] = acc[ai][0][m][0][i]; v0[4 + i] = acc[ai][0][m][1][i]; v1[i] = acc[ai][1][m][0][i]; v1[4 + i] = acc[ai][1][m][1][i]; }
;                     if constexpr (RP) {
; #pragma unroll
;                         for (int i = 0; i < 8; ++i) { const float snd = hi ? v0[i] : v1[i];
;                             const float rcv = __builtin_bit_cast(float, __builtin_amdgcn_update_dpp(0, __builtin_bit_cast(int, snd), 0x128, 0xf, 0xf, false));
;     __device__ __forceinline__ Pre pre(const Unit& u, int r, int cit) const { const size_t off = (size_t)(u.arow0 + r) * D + u.pn * 256 + cit;
;         return Pre{__builtin_nontemporal_load((const v4u*)(pp + off)), __builtin_nontemporal_load((const v4u*)(pp + off + (size_t)8 * D)), *(const v4u*)(h + off), *(const v4u*)(h + off + (size_t)8 * D)}; }
;     __device__ __forceinline__ void post(const Unit& u, int r, int cit, const float* v0, const float* v1, const Pre& p) const {
;         const size_t off = (size_t)(u.arow0 + r) * D + u.pn * 256 + cit; float p0[8], p1[8], a[8], b[8]; unpack8bf(p.p0, p0); unpack8bf(p.p1, p1); unpack8bf(p.h0, a); unpack8bf(p.h1, b);
; #pragma unroll
;         for (int i = 0; i < 8; ++i) { a[i] += sigmoidf_(v0[i]) * p0[i]; b[i] += sigmoidf_(v1[i]) * p1[i]; }
;         store8bf(h + off, a); store8bf(h + off + (size_t)8 * D, b);
;     }
	s_waitcnt vmcnt(14)
	v_cndmask_b32_e64 v144, v100, v108, s[0:1]
	v_mov_b32_e32 v145, 0
	s_nop 1
	v_mov_b32_dpp v145, v144 row_ror:8 row_mask:0xf bank_mask:0xf
	v_cndmask_b32_e64 v144, v101, v109, s[0:1]
	v_cndmask_b32_e64 v108, v108, v145, s[0:1]
	v_cndmask_b32_e64 v100, v145, v100, s[0:1]
	v_mov_b32_e32 v145, 0
	s_nop 1
	v_mov_b32_dpp v145, v144 row_ror:8 row_mask:0xf bank_mask:0xf
	v_cndmask_b32_e64 v144, v102, v110, s[0:1]
	v_cndmask_b32_e64 v109, v109, v145, s[0:1]
	v_cndmask_b32_e64 v145, v145, v101, s[0:1]
	v_mov_b32_e32 v101, 0
	s_nop 1
	v_mov_b32_dpp v101, v144 row_ror:8 row_mask:0xf bank_mask:0xf
	v_cndmask_b32_e64 v144, v103, v111, s[0:1]
	v_cndmask_b32_e64 v110, v110, v101, s[0:1]
	v_cndmask_b32_e64 v146, v101, v102, s[0:1]
	v_mov_b32_e32 v101, 0
	v_cndmask_b32_e64 v102, v96, v104, s[0:1]
	s_nop 0
	v_mov_b32_dpp v101, v144 row_ror:8 row_mask:0xf bank_mask:0xf
	v_cndmask_b32_e64 v111, v111, v101, s[0:1]
	v_cndmask_b32_e64 v144, v101, v103, s[0:1]
	v_mov_b32_e32 v101, 0
	v_and_b32_e32 v103, 0xffff0000, v136
	s_nop 0
	v_mov_b32_dpp v101, v102 row_ror:8 row_mask:0xf bank_mask:0xf
	v_cndmask_b32_e64 v102, v97, v105, s[0:1]
	v_cndmask_b32_e64 v148, v101, v96, s[0:1]
	v_mov_b32_e32 v96, 0
	v_cndmask_b32_e64 v147, v104, v101, s[0:1]
	v_cndmask_b32_e64 v101, v98, v106, s[0:1]
	v_mov_b32_dpp v96, v102 row_ror:8 row_mask:0xf bank_mask:0xf
	v_cndmask_b32_e64 v149, v105, v96, s[0:1]
	v_cndmask_b32_e64 v150, v96, v97, s[0:1]
	v_mov_b32_e32 v96, 0
	v_cndmask_b32_e64 v97, v99, v107, s[0:1]
	v_lshlrev_b32_e32 v102, 16, v136
	v_mov_b32_dpp v96, v101 row_ror:8 row_mask:0xf bank_mask:0xf
	v_cndmask_b32_e64 v152, v96, v98, s[0:1]
	v_mul_f32_e32 v98, 0xbfb8aa3b, v108
	v_exp_f32_e32 v98, v98
	v_cndmask_b32_e64 v151, v106, v96, s[0:1]
	v_mov_b32_e32 v96, 0
	v_and_b32_e32 v101, 0xffff0000, v140
	v_and_b32_e32 v105, 0xffff0000, v141
	v_mov_b32_dpp v96, v97 row_ror:8 row_mask:0xf bank_mask:0xf
	v_mul_f32_e32 v97, 0xbfb8aa3b, v100
	v_cndmask_b32_e64 v153, v107, v96, s[0:1]
	v_cndmask_b32_e64 v154, v96, v99, s[0:1]
	v_add_f32_e32 v96, 1.0, v98
	v_exp_f32_e32 v97, v97
	v_mul_f32_e32 v98, 0xbfb8aa3b, v109
	v_exp_f32_e32 v99, v98
	v_rcp_f32_e32 v96, v96
	v_add_f32_e32 v97, 1.0, v97
	v_rcp_f32_e32 v98, v97
	v_add_f32_e32 v97, 1.0, v99
	v_mul_f32_e32 v99, 0xbfb8aa3b, v145
	v_exp_f32_e32 v99, v99
	v_rcp_f32_e32 v97, v97
	v_lshlrev_b32_e32 v100, 16, v140
	v_lshlrev_b32_e32 v106, 16, v137
	v_add_f32_e32 v99, 1.0, v99
	v_rcp_f32_e32 v99, v99
	v_pk_fma_f32 v[96:97], v[96:97], v[100:101], v[102:103]
	v_mul_f32_e32 v102, 0xbfb8aa3b, v110
	v_lshlrev_b32_e32 v100, 16, v128
	v_and_b32_e32 v101, 0xffff0000, v128
	v_exp_f32_e32 v104, v102
	v_lshlrev_b32_e32 v102, 16, v132
	v_and_b32_e32 v103, 0xffff0000, v132
	v_pk_fma_f32 v[100:101], v[98:99], v[100:101], v[102:103]
	v_mul_f32_e32 v99, 0xbfb8aa3b, v146
	v_exp_f32_e32 v99, v99
	v_mul_f32_e32 v102, 0xbfb8aa3b, v111
	v_exp_f32_e32 v103, v102
	v_add_f32_e32 v98, 1.0, v104
	v_add_f32_e32 v99, 1.0, v99
	v_rcp_f32_e32 v102, v99
	v_add_f32_e32 v99, 1.0, v103
	v_mul_f32_e32 v103, 0xbfb8aa3b, v144
	v_exp_f32_e32 v103, v103
	v_rcp_f32_e32 v98, v98
	v_rcp_f32_e32 v99, v99
	v_lshlrev_b32_e32 v104, 16, v141
	v_add_f32_e32 v103, 1.0, v103
	v_rcp_f32_e32 v103, v103
	v_and_b32_e32 v107, 0xffff0000, v137
	v_pk_fma_f32 v[98:99], v[98:99], v[104:105], v[106:107]
	v_mul_f32_e32 v106, 0xbfb8aa3b, v147
	v_lshlrev_b32_e32 v104, 16, v129
	v_and_b32_e32 v105, 0xffff0000, v129
	v_exp_f32_e32 v108, v106
	v_lshlrev_b32_e32 v106, 16, v133
	v_and_b32_e32 v107, 0xffff0000, v133
	v_pk_fma_f32 v[102:103], v[102:103], v[104:105], v[106:107]
	v_mul_f32_e32 v105, 0xbfb8aa3b, v148
	v_exp_f32_e32 v105, v105
	v_mul_f32_e32 v106, 0xbfb8aa3b, v149
	v_exp_f32_e32 v107, v106
	v_add_f32_e32 v104, 1.0, v108
	v_add_f32_e32 v105, 1.0, v105
	v_rcp_f32_e32 v106, v105
	v_add_f32_e32 v105, 1.0, v107
	v_mul_f32_e32 v107, 0xbfb8aa3b, v150
	v_exp_f32_e32 v107, v107
	v_rcp_f32_e32 v104, v104
	v_rcp_f32_e32 v105, v105
	v_lshlrev_b32_e32 v108, 16, v142
	v_add_f32_e32 v107, 1.0, v107
	v_rcp_f32_e32 v107, v107
	v_and_b32_e32 v109, 0xffff0000, v142
	v_lshlrev_b32_e32 v110, 16, v138
	v_and_b32_e32 v111, 0xffff0000, v138
	v_pk_fma_f32 v[104:105], v[104:105], v[108:109], v[110:111]
	v_mul_f32_e32 v110, 0xbfb8aa3b, v151
	v_lshlrev_b32_e32 v108, 16, v130
	v_and_b32_e32 v109, 0xffff0000, v130
	v_exp_f32_e32 v128, v110
	v_lshlrev_b32_e32 v110, 16, v134
	v_and_b32_e32 v111, 0xffff0000, v134
	v_pk_fma_f32 v[106:107], v[106:107], v[108:109], v[110:111]
	v_mul_f32_e32 v109, 0xbfb8aa3b, v152
	v_exp_f32_e32 v109, v109
	v_mul_f32_e32 v110, 0xbfb8aa3b, v153
	v_exp_f32_e32 v111, v110
	v_add_f32_e32 v108, 1.0, v128
	v_add_f32_e32 v109, 1.0, v109
	v_rcp_f32_e32 v110, v109
	v_add_f32_e32 v109, 1.0, v111
	v_mul_f32_e32 v111, 0xbfb8aa3b, v154
	v_exp_f32_e32 v111, v111
	v_rcp_f32_e32 v108, v108
	v_rcp_f32_e32 v109, v109
	v_lshlrev_b32_e32 v128, 16, v143
	v_add_f32_e32 v111, 1.0, v111
	v_rcp_f32_e32 v111, v111
	v_and_b32_e32 v129, 0xffff0000, v143
	v_lshlrev_b32_e32 v132, 16, v139
	v_and_b32_e32 v133, 0xffff0000, v139
	v_pk_fma_f32 v[108:109], v[108:109], v[128:129], v[132:133]
	v_lshlrev_b32_e32 v128, 16, v131
	v_and_b32_e32 v129, 0xffff0000, v131
	v_lshlrev_b32_e32 v130, 16, v135
	v_and_b32_e32 v131, 0xffff0000, v135
	v_pk_fma_f32 v[110:111], v[110:111], v[128:129], v[130:131]
	v_add_u32_e32 v128, s58, v200
	v_ashrrev_i32_e32 v129, 31, v128
	v_lshlrev_b64 v[128:129], 12, v[128:129]
	v_lshl_add_u64 v[128:129], v[184:185], 0, v[128:129]
	v_cvt_pk_bf16_f32 v96, v96, v97
	v_cvt_pk_bf16_f32 v97, v98, v99
	v_cvt_pk_bf16_f32 v98, v104, v105
	v_cvt_pk_bf16_f32 v99, v108, v109
	global_store_dwordx4 v[128:129], v[96:99], off nt
	s_nop 1
	v_cvt_pk_bf16_f32 v96, v100, v101
	v_add_co_u32_e32 v100, vcc, 0x8000, v128
	v_cvt_pk_bf16_f32 v97, v102, v103
	v_cvt_pk_bf16_f32 v98, v106, v107
	v_cvt_pk_bf16_f32 v99, v110, v111
	v_addc_co_u32_e32 v101, vcc, 0, v129, vcc
	global_store_dwordx4 v[100:101], v[96:99], off nt
; template <class Epi, class Sched, bool GATHER, bool ALIGN_EPI = true, bool SP2 = true, bool REMAP64 = false>
; __device__ __forceinline__ void gemm_phase(LAS unsigned char* lds, const bf16* Ag, const bf16* Btg, const int K, const Sched& S, const Epi& E) {
;     ...
;             const bool hi = RP && (fr >= 8); const int rsh = hi ? -8 : 0, citx = hi ? cit + 32 : cit;
;             typename Epi::Pre pq[2];
;             { const int r0_ = wr * 64 + fr; pq[0] = E.pre(cur, (r0_ < cur.nrows ? r0_ : cur.nrows - 1) + rsh, citx); }
; #pragma unroll
;             for (int gq = 0; gq < 8; ++gq) { const int ai = gq >> 2, m = gq & 3, r = ai * HALF + wr * 64 + m * 16 + fr;
;                 if (gq + 1 < 8) { const int rn = ((gq + 1) >> 2) * HALF + wr * 64 + ((gq + 1) & 3) * 16 + fr; pq[(gq + 1) & 1] = E.pre(cur, (rn < cur.nrows ? rn : cur.nrows - 1) + rsh, citx); }
;                 __builtin_amdgcn_sched_barrier(0);
;                 if (r < cur.nrows) { float v0[8], v1[8];
; #pragma unroll
;                     for (int i = 0; i < 4; ++i) { v0[i] = acc[ai][0][m][0][i]; v0[4 + i] = acc[ai][0][m][1][i]; v1[i] = acc[ai][1][m][0][i]; v1[4 + i] = acc[ai][1][m][1][i]; }
;                     if constexpr (RP) {
; #pragma unroll
;                         for (int i = 0; i < 8; ++i) { const float snd = hi ? v0[i] : v1[i];
;                             const float rcv = __builtin_bit_cast(float, __builtin_amdgcn_update_dpp(0, __builtin_bit_cast(int, snd), 0x128, 0xf, 0xf, false));
;     __device__ __forceinline__ Pre pre(const Unit& u, int r, int cit) const { const size_t off = (size_t)(u.arow0 + r) * D + u.pn * 256 + cit;
;         return Pre{__builtin_nontemporal_load((const v4u*)(pp + off)), __builtin_nontemporal_load((const v4u*)(pp + off + (size_t)8 * D)), *(const v4u*)(h + off), *(const v4u*)(h + off + (size_t)8 * D)}; }
;     __device__ __forceinline__ void post(const Unit& u, int r, int cit, const float* v0, const float* v1, const Pre& p) const {
;         const size_t off = (size_t)(u.arow0 + r) * D + u.pn * 256 + cit; float p0[8], p1[8], a[8], b[8]; unpack8bf(p.p0, p0); unpack8bf(p.p1, p1); unpack8bf(p.h0, a); unpack8bf(p.h1, b);
; #pragma unroll
;         for (int i = 0; i < 8; ++i) { a[i] += sigmoidf_(v0[i]) * p0[i]; b[i] += sigmoidf_(v1[i]) * p1[i]; }
;         store8bf(h + off, a); store8bf(h + off + (size_t)8 * D, b);
;     }
.LBB0_1740:
	s_nop 1
	v_add_u32_e32 v96, v201, v194
	v_ashrrev_i32_e32 v97, 31, v96
	v_lshlrev_b64 v[96:97], 11, v[96:97]
	v_lshl_add_u64 v[96:97], v[96:97], 0, v[186:187]
	v_lshlrev_b64 v[100:101], 1, v[96:97]
	v_lshl_add_u64 v[96:97], s[36:37], 0, v[100:101]
	v_add_co_u32_e32 v98, vcc, 0x8000, v96
	v_lshl_add_u64 v[100:101], s[4:5], 0, v[100:101]
	s_nop 0
	v_addc_co_u32_e32 v99, vcc, 0, v97, vcc
	v_add_co_u32_e32 v102, vcc, 0x8000, v100
	global_load_dwordx4 v[108:111], v[96:97], off nt
	s_nop 0
	global_load_dwordx4 v[96:99], v[98:99], off nt
	v_addc_co_u32_e32 v103, vcc, 0, v101, vcc
	global_load_dwordx4 v[104:107], v[100:101], off
	s_nop 0
	global_load_dwordx4 v[100:103], v[102:103], off
	s_and_b64 vcc, exec, s[8:9]
	s_cbranch_vccnz .LBB0_1742
	s_waitcnt vmcnt(16)
	v_cndmask_b32_e64 v128, v84, v92, s[0:1]
	v_mov_b32_e32 v129, 0
	s_nop 1
	v_mov_b32_dpp v129, v128 row_ror:8 row_mask:0xf bank_mask:0xf
	v_cndmask_b32_e64 v128, v85, v93, s[0:1]
	v_cndmask_b32_e64 v92, v92, v129, s[0:1]
	v_cndmask_b32_e64 v84, v129, v84, s[0:1]
	v_mov_b32_e32 v129, 0
	s_nop 1
	v_mov_b32_dpp v129, v128 row_ror:8 row_mask:0xf bank_mask:0xf
	v_cndmask_b32_e64 v128, v86, v94, s[0:1]
	v_cndmask_b32_e64 v93, v93, v129, s[0:1]
	v_cndmask_b32_e64 v129, v129, v85, s[0:1]
	v_mov_b32_e32 v85, 0
	s_nop 1
	v_mov_b32_dpp v85, v128 row_ror:8 row_mask:0xf bank_mask:0xf
	v_cndmask_b32_e64 v128, v87, v95, s[0:1]
	v_cndmask_b32_e64 v94, v94, v85, s[0:1]
	v_cndmask_b32_e64 v130, v85, v86, s[0:1]
	v_mov_b32_e32 v85, 0
	v_cndmask_b32_e64 v86, v80, v88, s[0:1]
	s_nop 0
	v_mov_b32_dpp v85, v128 row_ror:8 row_mask:0xf bank_mask:0xf
	v_cndmask_b32_e64 v95, v95, v85, s[0:1]
	v_cndmask_b32_e64 v128, v85, v87, s[0:1]
	v_mov_b32_e32 v85, 0
	v_and_b32_e32 v87, 0xffff0000, v222
	s_nop 0
	v_mov_b32_dpp v85, v86 row_ror:8 row_mask:0xf bank_mask:0xf
	v_cndmask_b32_e64 v86, v81, v89, s[0:1]
	v_cndmask_b32_e64 v132, v85, v80, s[0:1]
	v_mov_b32_e32 v80, 0
	v_cndmask_b32_e64 v131, v88, v85, s[0:1]
	v_cndmask_b32_e64 v85, v82, v90, s[0:1]
	v_mov_b32_dpp v80, v86 row_ror:8 row_mask:0xf bank_mask:0xf
	v_cndmask_b32_e64 v133, v89, v80, s[0:1]
	v_cndmask_b32_e64 v134, v80, v81, s[0:1]
	v_mov_b32_e32 v80, 0
	v_cndmask_b32_e64 v81, v83, v91, s[0:1]
	v_lshlrev_b32_e32 v86, 16, v222
	v_mov_b32_dpp v80, v85 row_ror:8 row_mask:0xf bank_mask:0xf
	v_cndmask_b32_e64 v136, v80, v82, s[0:1]
	v_mul_f32_e32 v82, 0xbfb8aa3b, v92
	v_exp_f32_e32 v82, v82
	v_cndmask_b32_e64 v135, v90, v80, s[0:1]
	v_mov_b32_e32 v80, 0
	v_and_b32_e32 v85, 0xffff0000, v226
	v_and_b32_e32 v89, 0xffff0000, v227
	v_mov_b32_dpp v80, v81 row_ror:8 row_mask:0xf bank_mask:0xf
	v_mul_f32_e32 v81, 0xbfb8aa3b, v84
	v_cndmask_b32_e64 v137, v91, v80, s[0:1]
	v_cndmask_b32_e64 v138, v80, v83, s[0:1]
	v_add_f32_e32 v80, 1.0, v82
	v_exp_f32_e32 v81, v81
	v_mul_f32_e32 v82, 0xbfb8aa3b, v93
	v_exp_f32_e32 v83, v82
	v_rcp_f32_e32 v80, v80
	v_add_f32_e32 v81, 1.0, v81
	v_rcp_f32_e32 v82, v81
	v_add_f32_e32 v81, 1.0, v83
	v_mul_f32_e32 v83, 0xbfb8aa3b, v129
	v_exp_f32_e32 v83, v83
	v_rcp_f32_e32 v81, v81
	v_lshlrev_b32_e32 v84, 16, v226
	v_lshlrev_b32_e32 v90, 16, v223
	v_add_f32_e32 v83, 1.0, v83
	v_rcp_f32_e32 v83, v83
	v_pk_fma_f32 v[80:81], v[80:81], v[84:85], v[86:87]
	v_mul_f32_e32 v86, 0xbfb8aa3b, v94
	v_lshlrev_b32_e32 v84, 16, v214
	v_and_b32_e32 v85, 0xffff0000, v214
	v_exp_f32_e32 v88, v86
	v_lshlrev_b32_e32 v86, 16, v218
	v_and_b32_e32 v87, 0xffff0000, v218
	v_pk_fma_f32 v[84:85], v[82:83], v[84:85], v[86:87]
	v_mul_f32_e32 v83, 0xbfb8aa3b, v130
	v_exp_f32_e32 v83, v83
	v_mul_f32_e32 v86, 0xbfb8aa3b, v95
	v_exp_f32_e32 v87, v86
	v_add_f32_e32 v82, 1.0, v88
	v_add_f32_e32 v83, 1.0, v83
	v_rcp_f32_e32 v86, v83
	v_add_f32_e32 v83, 1.0, v87
	v_mul_f32_e32 v87, 0xbfb8aa3b, v128
	v_exp_f32_e32 v87, v87
	v_rcp_f32_e32 v82, v82
	v_rcp_f32_e32 v83, v83
	v_lshlrev_b32_e32 v88, 16, v227
	v_add_f32_e32 v87, 1.0, v87
	v_rcp_f32_e32 v87, v87
	v_and_b32_e32 v91, 0xffff0000, v223
	v_pk_fma_f32 v[82:83], v[82:83], v[88:89], v[90:91]
	v_mul_f32_e32 v90, 0xbfb8aa3b, v131
	v_lshlrev_b32_e32 v88, 16, v215
	v_and_b32_e32 v89, 0xffff0000, v215
	v_exp_f32_e32 v92, v90
	v_lshlrev_b32_e32 v90, 16, v219
	v_and_b32_e32 v91, 0xffff0000, v219
	v_pk_fma_f32 v[86:87], v[86:87], v[88:89], v[90:91]
	v_mul_f32_e32 v89, 0xbfb8aa3b, v132
	v_exp_f32_e32 v89, v89
	v_mul_f32_e32 v90, 0xbfb8aa3b, v133
	v_exp_f32_e32 v91, v90
	v_add_f32_e32 v88, 1.0, v92
	v_add_f32_e32 v89, 1.0, v89
	v_rcp_f32_e32 v90, v89
	v_add_f32_e32 v89, 1.0, v91
	v_mul_f32_e32 v91, 0xbfb8aa3b, v134
	v_exp_f32_e32 v91, v91
	v_rcp_f32_e32 v88, v88
	v_rcp_f32_e32 v89, v89
	v_lshlrev_b32_e32 v92, 16, v228
	v_add_f32_e32 v91, 1.0, v91
	v_rcp_f32_e32 v91, v91
	v_and_b32_e32 v93, 0xffff0000, v228
	v_lshlrev_b32_e32 v94, 16, v224
	v_and_b32_e32 v95, 0xffff0000, v224
	v_pk_fma_f32 v[88:89], v[88:89], v[92:93], v[94:95]
	v_mul_f32_e32 v94, 0xbfb8aa3b, v135
	v_lshlrev_b32_e32 v92, 16, v216
	v_and_b32_e32 v93, 0xffff0000, v216
	v_exp_f32_e32 v214, v94
	v_lshlrev_b32_e32 v94, 16, v220
	v_and_b32_e32 v95, 0xffff0000, v220
	v_pk_fma_f32 v[90:91], v[90:91], v[92:93], v[94:95]
	v_mul_f32_e32 v93, 0xbfb8aa3b, v136
	v_exp_f32_e32 v93, v93
	v_mul_f32_e32 v94, 0xbfb8aa3b, v137
	v_exp_f32_e32 v95, v94
	v_add_f32_e32 v92, 1.0, v214
	v_add_f32_e32 v93, 1.0, v93
	v_rcp_f32_e32 v94, v93
	v_add_f32_e32 v93, 1.0, v95
	v_mul_f32_e32 v95, 0xbfb8aa3b, v138
	v_exp_f32_e32 v95, v95
	v_rcp_f32_e32 v92, v92
	v_rcp_f32_e32 v93, v93
	v_lshlrev_b32_e32 v214, 16, v229
	v_add_f32_e32 v95, 1.0, v95
	v_rcp_f32_e32 v95, v95
	v_and_b32_e32 v215, 0xffff0000, v229
	v_lshlrev_b32_e32 v218, 16, v225
	v_and_b32_e32 v219, 0xffff0000, v225
	v_pk_fma_f32 v[92:93], v[92:93], v[214:215], v[218:219]
	v_lshlrev_b32_e32 v214, 16, v217
	v_and_b32_e32 v215, 0xffff0000, v217
	v_lshlrev_b32_e32 v216, 16, v221
	v_and_b32_e32 v217, 0xffff0000, v221
	v_pk_fma_f32 v[94:95], v[94:95], v[214:215], v[216:217]
	v_add_u32_e32 v214, s59, v200
	v_ashrrev_i32_e32 v215, 31, v214
	v_lshlrev_b64 v[214:215], 12, v[214:215]
	v_lshl_add_u64 v[214:215], v[184:185], 0, v[214:215]
	v_cvt_pk_bf16_f32 v80, v80, v81
	v_cvt_pk_bf16_f32 v81, v82, v83
	v_cvt_pk_bf16_f32 v82, v88, v89
	v_cvt_pk_bf16_f32 v83, v92, v93
	global_store_dwordx4 v[214:215], v[80:83], off nt
	s_nop 1
	v_cvt_pk_bf16_f32 v80, v84, v85
	v_add_co_u32_e32 v84, vcc, 0x8000, v214
	v_cvt_pk_bf16_f32 v81, v86, v87
	v_cvt_pk_bf16_f32 v82, v90, v91
	v_cvt_pk_bf16_f32 v83, v94, v95
	v_addc_co_u32_e32 v85, vcc, 0, v215, vcc
	global_store_dwordx4 v[84:85], v[80:83], off nt
; template <class Epi, class Sched, bool GATHER, bool ALIGN_EPI = true, bool SP2 = true, bool REMAP64 = false>
; __device__ __forceinline__ void gemm_phase(LAS unsigned char* lds, const bf16* Ag, const bf16* Btg, const int K, const Sched& S, const Epi& E) {
;     ...
;             const bool hi = RP && (fr >= 8); const int rsh = hi ? -8 : 0, citx = hi ? cit + 32 : cit;
;             typename Epi::Pre pq[2];
;             { const int r0_ = wr * 64 + fr; pq[0] = E.pre(cur, (r0_ < cur.nrows ? r0_ : cur.nrows - 1) + rsh, citx); }
; #pragma unroll
;             for (int gq = 0; gq < 8; ++gq) { const int ai = gq >> 2, m = gq & 3, r = ai * HALF + wr * 64 + m * 16 + fr;
;                 if (gq + 1 < 8) { const int rn = ((gq + 1) >> 2) * HALF + wr * 64 + ((gq + 1) & 3) * 16 + fr; pq[(gq + 1) & 1] = E.pre(cur, (rn < cur.nrows ? rn : cur.nrows - 1) + rsh, citx); }
;                 __builtin_amdgcn_sched_barrier(0);
;                 if (r < cur.nrows) { float v0[8], v1[8];
; #pragma unroll
;                     for (int i = 0; i < 4; ++i) { v0[i] = acc[ai][0][m][0][i]; v0[4 + i] = acc[ai][0][m][1][i]; v1[i] = acc[ai][1][m][0][i]; v1[4 + i] = acc[ai][1][m][1][i]; }
;                     if constexpr (RP) {
; #pragma unroll
;                         for (int i = 0; i < 8; ++i) { const float snd = hi ? v0[i] : v1[i];
;                             const float rcv = __builtin_bit_cast(float, __builtin_amdgcn_update_dpp(0, __builtin_bit_cast(int, snd), 0x128, 0xf, 0xf, false));
;     __device__ __forceinline__ Pre pre(const Unit& u, int r, int cit) const { const size_t off = (size_t)(u.arow0 + r) * D + u.pn * 256 + cit;
;         return Pre{__builtin_nontemporal_load((const v4u*)(pp + off)), __builtin_nontemporal_load((const v4u*)(pp + off + (size_t)8 * D)), *(const v4u*)(h + off), *(const v4u*)(h + off + (size_t)8 * D)}; }
;     __device__ __forceinline__ void post(const Unit& u, int r, int cit, const float* v0, const float* v1, const Pre& p) const {
;         const size_t off = (size_t)(u.arow0 + r) * D + u.pn * 256 + cit; float p0[8], p1[8], a[8], b[8]; unpack8bf(p.p0, p0); unpack8bf(p.p1, p1); unpack8bf(p.h0, a); unpack8bf(p.h1, b);
; #pragma unroll
;         for (int i = 0; i < 8; ++i) { a[i] += sigmoidf_(v0[i]) * p0[i]; b[i] += sigmoidf_(v1[i]) * p1[i]; }
;         store8bf(h + off, a); store8bf(h + off + (size_t)8 * D, b);
;     }
.LBB0_1742:
	s_nop 1
	v_add_u32_e32 v80, v201, v195
	v_ashrrev_i32_e32 v81, 31, v80
	v_lshlrev_b64 v[80:81], 11, v[80:81]
	v_lshl_add_u64 v[80:81], v[80:81], 0, v[186:187]
	v_lshlrev_b64 v[84:85], 1, v[80:81]
	v_lshl_add_u64 v[80:81], s[36:37], 0, v[84:85]
	v_add_co_u32_e32 v82, vcc, 0x8000, v80
	v_lshl_add_u64 v[84:85], s[4:5], 0, v[84:85]
	s_nop 0
	v_addc_co_u32_e32 v83, vcc, 0, v81, vcc
	v_add_co_u32_e32 v86, vcc, 0x8000, v84
	global_load_dwordx4 v[92:95], v[80:81], off nt
	s_nop 0
	global_load_dwordx4 v[80:83], v[82:83], off nt
	v_addc_co_u32_e32 v87, vcc, 0, v85, vcc
	global_load_dwordx4 v[88:91], v[84:85], off
	s_nop 0
	global_load_dwordx4 v[84:87], v[86:87], off
	s_and_b64 vcc, exec, s[8:9]
	s_cbranch_vccnz .LBB0_1744
	s_waitcnt vmcnt(18)
	v_cndmask_b32_e64 v144, v68, v76, s[0:1]
	v_mov_b32_e32 v145, 0
	s_nop 1
	v_mov_b32_dpp v145, v144 row_ror:8 row_mask:0xf bank_mask:0xf
	v_cndmask_b32_e64 v144, v69, v77, s[0:1]
	v_cndmask_b32_e64 v76, v76, v145, s[0:1]
	v_cndmask_b32_e64 v68, v145, v68, s[0:1]
	v_mov_b32_e32 v145, 0
	s_nop 1
	v_mov_b32_dpp v145, v144 row_ror:8 row_mask:0xf bank_mask:0xf
	v_cndmask_b32_e64 v144, v70, v78, s[0:1]
	v_cndmask_b32_e64 v77, v77, v145, s[0:1]
	v_cndmask_b32_e64 v145, v145, v69, s[0:1]
	v_mov_b32_e32 v69, 0
	s_nop 1
	v_mov_b32_dpp v69, v144 row_ror:8 row_mask:0xf bank_mask:0xf
	v_cndmask_b32_e64 v144, v71, v79, s[0:1]
	v_cndmask_b32_e64 v78, v78, v69, s[0:1]
	v_cndmask_b32_e64 v146, v69, v70, s[0:1]
	v_mov_b32_e32 v69, 0
	v_cndmask_b32_e64 v70, v64, v72, s[0:1]
	s_nop 0
	v_mov_b32_dpp v69, v144 row_ror:8 row_mask:0xf bank_mask:0xf
	v_cndmask_b32_e64 v79, v79, v69, s[0:1]
	v_cndmask_b32_e64 v144, v69, v71, s[0:1]
	v_mov_b32_e32 v69, 0
	s_nop 0
	v_and_b32_e32 v71, 0xffff0000, v238
	v_mov_b32_dpp v69, v70 row_ror:8 row_mask:0xf bank_mask:0xf
	v_cndmask_b32_e64 v70, v65, v73, s[0:1]
	v_cndmask_b32_e64 v148, v69, v64, s[0:1]
	v_mov_b32_e32 v64, 0
	v_cndmask_b32_e64 v147, v72, v69, s[0:1]
	v_cndmask_b32_e64 v69, v66, v74, s[0:1]
	v_mov_b32_dpp v64, v70 row_ror:8 row_mask:0xf bank_mask:0xf
	v_cndmask_b32_e64 v149, v73, v64, s[0:1]
	v_cndmask_b32_e64 v150, v64, v65, s[0:1]
	v_mov_b32_e32 v64, 0
	v_cndmask_b32_e64 v65, v67, v75, s[0:1]
	v_lshlrev_b32_e32 v70, 16, v238
	v_mov_b32_dpp v64, v69 row_ror:8 row_mask:0xf bank_mask:0xf
	v_cndmask_b32_e64 v152, v64, v66, s[0:1]
	v_mul_f32_e32 v66, 0xbfb8aa3b, v76
	v_exp_f32_e32 v66, v66
	v_cndmask_b32_e64 v151, v74, v64, s[0:1]
	v_mov_b32_e32 v64, 0
	v_and_b32_e32 v69, 0xffff0000, v242
	v_and_b32_e32 v73, 0xffff0000, v243
	v_mov_b32_dpp v64, v65 row_ror:8 row_mask:0xf bank_mask:0xf
	v_mul_f32_e32 v65, 0xbfb8aa3b, v68
	v_cndmask_b32_e64 v153, v75, v64, s[0:1]
	v_cndmask_b32_e64 v154, v64, v67, s[0:1]
	v_add_f32_e32 v64, 1.0, v66
	v_exp_f32_e32 v65, v65
	v_mul_f32_e32 v66, 0xbfb8aa3b, v77
	v_exp_f32_e32 v67, v66
	v_rcp_f32_e32 v64, v64
	v_add_f32_e32 v65, 1.0, v65
	v_rcp_f32_e32 v66, v65
	v_add_f32_e32 v65, 1.0, v67
	v_mul_f32_e32 v67, 0xbfb8aa3b, v145
	v_exp_f32_e32 v67, v67
	v_rcp_f32_e32 v65, v65
	v_lshlrev_b32_e32 v68, 16, v242
	v_lshlrev_b32_e32 v74, 16, v239
	v_add_f32_e32 v67, 1.0, v67
	v_rcp_f32_e32 v67, v67
	v_pk_fma_f32 v[64:65], v[64:65], v[68:69], v[70:71]
	v_mul_f32_e32 v70, 0xbfb8aa3b, v78
	v_lshlrev_b32_e32 v68, 16, v230
	v_and_b32_e32 v69, 0xffff0000, v230
	v_exp_f32_e32 v72, v70
	s_nop 0
	v_lshlrev_b32_e32 v70, 16, v234
	v_and_b32_e32 v71, 0xffff0000, v234
	v_pk_fma_f32 v[68:69], v[66:67], v[68:69], v[70:71]
	v_mul_f32_e32 v67, 0xbfb8aa3b, v146
	v_exp_f32_e32 v67, v67
	v_mul_f32_e32 v70, 0xbfb8aa3b, v79
	v_exp_f32_e32 v71, v70
	v_add_f32_e32 v66, 1.0, v72
	v_add_f32_e32 v67, 1.0, v67
	v_rcp_f32_e32 v70, v67
	v_add_f32_e32 v67, 1.0, v71
	v_mul_f32_e32 v71, 0xbfb8aa3b, v144
	v_exp_f32_e32 v71, v71
	v_rcp_f32_e32 v66, v66
	v_rcp_f32_e32 v67, v67
	v_lshlrev_b32_e32 v72, 16, v243
	v_add_f32_e32 v71, 1.0, v71
	v_rcp_f32_e32 v71, v71
	v_and_b32_e32 v75, 0xffff0000, v239
	v_pk_fma_f32 v[66:67], v[66:67], v[72:73], v[74:75]
	v_mul_f32_e32 v74, 0xbfb8aa3b, v147
	v_lshlrev_b32_e32 v72, 16, v231
	v_and_b32_e32 v73, 0xffff0000, v231
	v_exp_f32_e32 v76, v74
	v_lshlrev_b32_e32 v74, 16, v235
	v_and_b32_e32 v75, 0xffff0000, v235
	v_pk_fma_f32 v[70:71], v[70:71], v[72:73], v[74:75]
	v_mul_f32_e32 v73, 0xbfb8aa3b, v148
	v_exp_f32_e32 v73, v73
	v_mul_f32_e32 v74, 0xbfb8aa3b, v149
	v_exp_f32_e32 v75, v74
	v_add_f32_e32 v72, 1.0, v76
	v_add_f32_e32 v73, 1.0, v73
	v_rcp_f32_e32 v74, v73
	v_add_f32_e32 v73, 1.0, v75
	v_mul_f32_e32 v75, 0xbfb8aa3b, v150
	v_exp_f32_e32 v75, v75
	v_rcp_f32_e32 v72, v72
	v_rcp_f32_e32 v73, v73
	v_lshlrev_b32_e32 v76, 16, v244
	v_add_f32_e32 v75, 1.0, v75
	v_rcp_f32_e32 v75, v75
	v_and_b32_e32 v77, 0xffff0000, v244
	v_lshlrev_b32_e32 v78, 16, v240
	v_and_b32_e32 v79, 0xffff0000, v240
	v_pk_fma_f32 v[72:73], v[72:73], v[76:77], v[78:79]
	v_mul_f32_e32 v78, 0xbfb8aa3b, v151
	v_lshlrev_b32_e32 v76, 16, v232
	v_and_b32_e32 v77, 0xffff0000, v232
	v_exp_f32_e32 v230, v78
	v_lshlrev_b32_e32 v78, 16, v236
	v_and_b32_e32 v79, 0xffff0000, v236
	v_pk_fma_f32 v[74:75], v[74:75], v[76:77], v[78:79]
	v_mul_f32_e32 v77, 0xbfb8aa3b, v152
	v_exp_f32_e32 v77, v77
	v_mul_f32_e32 v78, 0xbfb8aa3b, v153
	v_exp_f32_e32 v79, v78
	v_add_f32_e32 v76, 1.0, v230
	v_add_f32_e32 v77, 1.0, v77
	v_rcp_f32_e32 v78, v77
	v_add_f32_e32 v77, 1.0, v79
	v_mul_f32_e32 v79, 0xbfb8aa3b, v154
	v_exp_f32_e32 v79, v79
	v_rcp_f32_e32 v76, v76
	v_rcp_f32_e32 v77, v77
	v_lshlrev_b32_e32 v230, 16, v245
	v_add_f32_e32 v79, 1.0, v79
	v_rcp_f32_e32 v79, v79
	v_and_b32_e32 v231, 0xffff0000, v245
	v_lshlrev_b32_e32 v234, 16, v241
	v_and_b32_e32 v235, 0xffff0000, v241
	v_pk_fma_f32 v[76:77], v[76:77], v[230:231], v[234:235]
	v_lshlrev_b32_e32 v230, 16, v233
	v_and_b32_e32 v231, 0xffff0000, v233
	v_lshlrev_b32_e32 v232, 16, v237
	v_and_b32_e32 v233, 0xffff0000, v237
	v_pk_fma_f32 v[78:79], v[78:79], v[230:231], v[232:233]
	v_add_u32_e32 v230, s61, v200
	v_ashrrev_i32_e32 v231, 31, v230
	v_lshlrev_b64 v[230:231], 12, v[230:231]
	v_lshl_add_u64 v[230:231], v[184:185], 0, v[230:231]
	v_cvt_pk_bf16_f32 v64, v64, v65
	v_cvt_pk_bf16_f32 v65, v66, v67
	v_cvt_pk_bf16_f32 v66, v72, v73
	v_cvt_pk_bf16_f32 v67, v76, v77
	global_store_dwordx4 v[230:231], v[64:67], off nt
	s_nop 1
	v_cvt_pk_bf16_f32 v64, v68, v69
	v_add_co_u32_e32 v68, vcc, 0x8000, v230
	v_cvt_pk_bf16_f32 v65, v70, v71
	v_cvt_pk_bf16_f32 v66, v74, v75
	v_cvt_pk_bf16_f32 v67, v78, v79
	v_addc_co_u32_e32 v69, vcc, 0, v231, vcc
	global_store_dwordx4 v[68:69], v[64:67], off nt
; template <class Epi, class Sched, bool GATHER, bool ALIGN_EPI = true, bool SP2 = true, bool REMAP64 = false>
; __device__ __forceinline__ void gemm_phase(LAS unsigned char* lds, const bf16* Ag, const bf16* Btg, const int K, const Sched& S, const Epi& E) {
;     ...
;             const bool hi = RP && (fr >= 8); const int rsh = hi ? -8 : 0, citx = hi ? cit + 32 : cit;
;             typename Epi::Pre pq[2];
;             { const int r0_ = wr * 64 + fr; pq[0] = E.pre(cur, (r0_ < cur.nrows ? r0_ : cur.nrows - 1) + rsh, citx); }
; #pragma unroll
;             for (int gq = 0; gq < 8; ++gq) { const int ai = gq >> 2, m = gq & 3, r = ai * HALF + wr * 64 + m * 16 + fr;
;                 if (gq + 1 < 8) { const int rn = ((gq + 1) >> 2) * HALF + wr * 64 + ((gq + 1) & 3) * 16 + fr; pq[(gq + 1) & 1] = E.pre(cur, (rn < cur.nrows ? rn : cur.nrows - 1) + rsh, citx); }
;                 __builtin_amdgcn_sched_barrier(0);
;                 if (r < cur.nrows) { float v0[8], v1[8];
; #pragma unroll
;                     for (int i = 0; i < 4; ++i) { v0[i] = acc[ai][0][m][0][i]; v0[4 + i] = acc[ai][0][m][1][i]; v1[i] = acc[ai][1][m][0][i]; v1[4 + i] = acc[ai][1][m][1][i]; }
;                     if constexpr (RP) {
; #pragma unroll
;                         for (int i = 0; i < 8; ++i) { const float snd = hi ? v0[i] : v1[i];
;                             const float rcv = __builtin_bit_cast(float, __builtin_amdgcn_update_dpp(0, __builtin_bit_cast(int, snd), 0x128, 0xf, 0xf, false));
;     __device__ __forceinline__ Pre pre(const Unit& u, int r, int cit) const { const size_t off = (size_t)(u.arow0 + r) * D + u.pn * 256 + cit;
;         return Pre{__builtin_nontemporal_load((const v4u*)(pp + off)), __builtin_nontemporal_load((const v4u*)(pp + off + (size_t)8 * D)), *(const v4u*)(h + off), *(const v4u*)(h + off + (size_t)8 * D)}; }
;     __device__ __forceinline__ void post(const Unit& u, int r, int cit, const float* v0, const float* v1, const Pre& p) const {
;         const size_t off = (size_t)(u.arow0 + r) * D + u.pn * 256 + cit; float p0[8], p1[8], a[8], b[8]; unpack8bf(p.p0, p0); unpack8bf(p.p1, p1); unpack8bf(p.h0, a); unpack8bf(p.h1, b);
; #pragma unroll
;         for (int i = 0; i < 8; ++i) { a[i] += sigmoidf_(v0[i]) * p0[i]; b[i] += sigmoidf_(v1[i]) * p1[i]; }
;         store8bf(h + off, a); store8bf(h + off + (size_t)8 * D, b);
;     }
.LBB0_1744:
	s_nop 1
	v_add_u32_e32 v64, v201, v196
	v_ashrrev_i32_e32 v65, 31, v64
	v_lshlrev_b64 v[64:65], 11, v[64:65]
	v_lshl_add_u64 v[64:65], v[64:65], 0, v[186:187]
	v_lshlrev_b64 v[68:69], 1, v[64:65]
	v_lshl_add_u64 v[64:65], s[36:37], 0, v[68:69]
	v_add_co_u32_e32 v66, vcc, 0x8000, v64
	v_lshl_add_u64 v[68:69], s[4:5], 0, v[68:69]
	s_nop 0
	v_addc_co_u32_e32 v67, vcc, 0, v65, vcc
	v_add_co_u32_e32 v70, vcc, 0x8000, v68
	global_load_dwordx4 v[76:79], v[64:65], off nt
	s_nop 0
	global_load_dwordx4 v[64:67], v[66:67], off nt
	v_addc_co_u32_e32 v71, vcc, 0, v69, vcc
	global_load_dwordx4 v[72:75], v[68:69], off
	s_nop 0
	global_load_dwordx4 v[68:71], v[70:71], off
	s_nop 0
	v_cndmask_b32_e64 v144, 0, 1, s[22:23]
	v_cmp_ne_u32_e64 s[8:9], 1, v144
	s_andn2_b64 vcc, exec, s[22:23]
	s_cbranch_vccnz .LBB0_1746
	s_waitcnt vmcnt(18)
	v_cndmask_b32_e64 v128, v52, v60, s[0:1]
	v_mov_b32_e32 v129, 0
	s_nop 1
	v_mov_b32_dpp v129, v128 row_ror:8 row_mask:0xf bank_mask:0xf
	v_cndmask_b32_e64 v128, v53, v61, s[0:1]
	v_cndmask_b32_e64 v60, v60, v129, s[0:1]
	v_cndmask_b32_e64 v52, v129, v52, s[0:1]
	v_mov_b32_e32 v129, 0
	s_nop 1
	v_mov_b32_dpp v129, v128 row_ror:8 row_mask:0xf bank_mask:0xf
	v_cndmask_b32_e64 v128, v54, v62, s[0:1]
	v_cndmask_b32_e64 v61, v61, v129, s[0:1]
	v_cndmask_b32_e64 v129, v129, v53, s[0:1]
	v_mov_b32_e32 v53, 0
	s_nop 1
	v_mov_b32_dpp v53, v128 row_ror:8 row_mask:0xf bank_mask:0xf
	v_cndmask_b32_e64 v128, v55, v63, s[0:1]
	v_cndmask_b32_e64 v62, v62, v53, s[0:1]
	v_cndmask_b32_e64 v130, v53, v54, s[0:1]
	v_mov_b32_e32 v53, 0
	v_cndmask_b32_e64 v54, v48, v56, s[0:1]
	s_nop 0
	v_mov_b32_dpp v53, v128 row_ror:8 row_mask:0xf bank_mask:0xf
	v_cndmask_b32_e64 v63, v63, v53, s[0:1]
	v_cndmask_b32_e64 v128, v53, v55, s[0:1]
	v_mov_b32_e32 v53, 0
	s_nop 0
	v_and_b32_e32 v55, 0xffff0000, v120
	v_mov_b32_dpp v53, v54 row_ror:8 row_mask:0xf bank_mask:0xf
	v_cndmask_b32_e64 v54, v49, v57, s[0:1]
	v_cndmask_b32_e64 v132, v53, v48, s[0:1]
	v_mov_b32_e32 v48, 0
	v_cndmask_b32_e64 v131, v56, v53, s[0:1]
	v_cndmask_b32_e64 v53, v50, v58, s[0:1]
	v_mov_b32_dpp v48, v54 row_ror:8 row_mask:0xf bank_mask:0xf
	v_cndmask_b32_e64 v133, v57, v48, s[0:1]
	v_cndmask_b32_e64 v134, v48, v49, s[0:1]
	v_mov_b32_e32 v48, 0
	v_cndmask_b32_e64 v49, v51, v59, s[0:1]
	v_lshlrev_b32_e32 v54, 16, v120
	v_mov_b32_dpp v48, v53 row_ror:8 row_mask:0xf bank_mask:0xf
	v_cndmask_b32_e64 v136, v48, v50, s[0:1]
	v_mul_f32_e32 v50, 0xbfb8aa3b, v60
	v_exp_f32_e32 v50, v50
	v_cndmask_b32_e64 v135, v58, v48, s[0:1]
	v_mov_b32_e32 v48, 0
	v_and_b32_e32 v53, 0xffff0000, v124
	v_and_b32_e32 v57, 0xffff0000, v125
	v_mov_b32_dpp v48, v49 row_ror:8 row_mask:0xf bank_mask:0xf
	v_mul_f32_e32 v49, 0xbfb8aa3b, v52
	v_cndmask_b32_e64 v137, v59, v48, s[0:1]
	v_cndmask_b32_e64 v138, v48, v51, s[0:1]
	v_add_f32_e32 v48, 1.0, v50
	v_exp_f32_e32 v49, v49
	v_mul_f32_e32 v50, 0xbfb8aa3b, v61
	v_exp_f32_e32 v51, v50
	v_rcp_f32_e32 v48, v48
	v_add_f32_e32 v49, 1.0, v49
	v_rcp_f32_e32 v50, v49
	v_add_f32_e32 v49, 1.0, v51
	v_mul_f32_e32 v51, 0xbfb8aa3b, v129
	v_exp_f32_e32 v51, v51
	v_rcp_f32_e32 v49, v49
	v_lshlrev_b32_e32 v52, 16, v124
	v_lshlrev_b32_e32 v58, 16, v121
	v_add_f32_e32 v51, 1.0, v51
	v_rcp_f32_e32 v51, v51
	v_pk_fma_f32 v[48:49], v[48:49], v[52:53], v[54:55]
	v_mul_f32_e32 v54, 0xbfb8aa3b, v62
	v_lshlrev_b32_e32 v52, 16, v112
	v_and_b32_e32 v53, 0xffff0000, v112
	v_exp_f32_e32 v56, v54
	s_nop 0
	v_lshlrev_b32_e32 v54, 16, v116
	v_and_b32_e32 v55, 0xffff0000, v116
	v_pk_fma_f32 v[52:53], v[50:51], v[52:53], v[54:55]
	v_mul_f32_e32 v51, 0xbfb8aa3b, v130
	v_exp_f32_e32 v51, v51
	v_mul_f32_e32 v54, 0xbfb8aa3b, v63
	v_exp_f32_e32 v55, v54
	v_add_f32_e32 v50, 1.0, v56
	v_add_f32_e32 v51, 1.0, v51
	v_rcp_f32_e32 v54, v51
	v_add_f32_e32 v51, 1.0, v55
	v_mul_f32_e32 v55, 0xbfb8aa3b, v128
	v_exp_f32_e32 v55, v55
	v_rcp_f32_e32 v50, v50
	v_rcp_f32_e32 v51, v51
	v_lshlrev_b32_e32 v56, 16, v125
	v_add_f32_e32 v55, 1.0, v55
	v_rcp_f32_e32 v55, v55
	v_and_b32_e32 v59, 0xffff0000, v121
	v_pk_fma_f32 v[50:51], v[50:51], v[56:57], v[58:59]
	v_mul_f32_e32 v58, 0xbfb8aa3b, v131
	v_lshlrev_b32_e32 v56, 16, v113
	v_and_b32_e32 v57, 0xffff0000, v113
	v_exp_f32_e32 v60, v58
	v_lshlrev_b32_e32 v58, 16, v117
	v_and_b32_e32 v59, 0xffff0000, v117
	v_pk_fma_f32 v[54:55], v[54:55], v[56:57], v[58:59]
	v_mul_f32_e32 v57, 0xbfb8aa3b, v132
	v_exp_f32_e32 v57, v57
	v_mul_f32_e32 v58, 0xbfb8aa3b, v133
	v_exp_f32_e32 v59, v58
	v_add_f32_e32 v56, 1.0, v60
	v_add_f32_e32 v57, 1.0, v57
	v_rcp_f32_e32 v58, v57
	v_add_f32_e32 v57, 1.0, v59
	v_mul_f32_e32 v59, 0xbfb8aa3b, v134
	v_exp_f32_e32 v59, v59
	v_rcp_f32_e32 v56, v56
	v_rcp_f32_e32 v57, v57
	v_lshlrev_b32_e32 v60, 16, v126
	v_add_f32_e32 v59, 1.0, v59
	v_rcp_f32_e32 v59, v59
	v_and_b32_e32 v61, 0xffff0000, v126
	v_lshlrev_b32_e32 v62, 16, v122
	v_and_b32_e32 v63, 0xffff0000, v122
	v_pk_fma_f32 v[56:57], v[56:57], v[60:61], v[62:63]
	v_mul_f32_e32 v62, 0xbfb8aa3b, v135
	v_lshlrev_b32_e32 v60, 16, v114
	v_and_b32_e32 v61, 0xffff0000, v114
	v_exp_f32_e32 v112, v62
	v_lshlrev_b32_e32 v62, 16, v118
	v_and_b32_e32 v63, 0xffff0000, v118
	v_pk_fma_f32 v[58:59], v[58:59], v[60:61], v[62:63]
	v_mul_f32_e32 v61, 0xbfb8aa3b, v136
	v_exp_f32_e32 v61, v61
	v_mul_f32_e32 v62, 0xbfb8aa3b, v137
	v_exp_f32_e32 v63, v62
	v_add_f32_e32 v60, 1.0, v112
	v_add_f32_e32 v61, 1.0, v61
	v_rcp_f32_e32 v62, v61
	v_add_f32_e32 v61, 1.0, v63
	v_mul_f32_e32 v63, 0xbfb8aa3b, v138
	v_exp_f32_e32 v63, v63
	v_rcp_f32_e32 v60, v60
	v_rcp_f32_e32 v61, v61
	v_lshlrev_b32_e32 v112, 16, v127
	v_add_f32_e32 v63, 1.0, v63
	v_rcp_f32_e32 v63, v63
	v_and_b32_e32 v113, 0xffff0000, v127
	v_lshlrev_b32_e32 v116, 16, v123
	v_and_b32_e32 v117, 0xffff0000, v123
	v_pk_fma_f32 v[60:61], v[60:61], v[112:113], v[116:117]
	v_lshlrev_b32_e32 v112, 16, v115
	v_and_b32_e32 v113, 0xffff0000, v115
	v_lshlrev_b32_e32 v114, 16, v119
	v_and_b32_e32 v115, 0xffff0000, v119
	v_pk_fma_f32 v[62:63], v[62:63], v[112:113], v[114:115]
	v_add_u32_e32 v112, s60, v200
	v_ashrrev_i32_e32 v113, 31, v112
	v_lshlrev_b64 v[112:113], 12, v[112:113]
	v_lshl_add_u64 v[112:113], v[184:185], 0, v[112:113]
	v_cvt_pk_bf16_f32 v48, v48, v49
	v_cvt_pk_bf16_f32 v49, v50, v51
	v_cvt_pk_bf16_f32 v50, v56, v57
	v_cvt_pk_bf16_f32 v51, v60, v61
	global_store_dwordx4 v[112:113], v[48:51], off nt
	s_nop 1
	v_cvt_pk_bf16_f32 v48, v52, v53
	v_add_co_u32_e32 v52, vcc, 0x8000, v112
	v_cvt_pk_bf16_f32 v49, v54, v55
	v_cvt_pk_bf16_f32 v50, v58, v59
	v_cvt_pk_bf16_f32 v51, v62, v63
	v_addc_co_u32_e32 v53, vcc, 0, v113, vcc
	global_store_dwordx4 v[52:53], v[48:51], off nt
; template <class Epi, class Sched, bool GATHER, bool ALIGN_EPI = true, bool SP2 = true, bool REMAP64 = false>
; __device__ __forceinline__ void gemm_phase(LAS unsigned char* lds, const bf16* Ag, const bf16* Btg, const int K, const Sched& S, const Epi& E) {
;     ...
;             const bool hi = RP && (fr >= 8); const int rsh = hi ? -8 : 0, citx = hi ? cit + 32 : cit;
;             typename Epi::Pre pq[2];
;             { const int r0_ = wr * 64 + fr; pq[0] = E.pre(cur, (r0_ < cur.nrows ? r0_ : cur.nrows - 1) + rsh, citx); }
; #pragma unroll
;             for (int gq = 0; gq < 8; ++gq) { const int ai = gq >> 2, m = gq & 3, r = ai * HALF + wr * 64 + m * 16 + fr;
;                 if (gq + 1 < 8) { const int rn = ((gq + 1) >> 2) * HALF + wr * 64 + ((gq + 1) & 3) * 16 + fr; pq[(gq + 1) & 1] = E.pre(cur, (rn < cur.nrows ? rn : cur.nrows - 1) + rsh, citx); }
;                 __builtin_amdgcn_sched_barrier(0);
;                 if (r < cur.nrows) { float v0[8], v1[8];
; #pragma unroll
;                     for (int i = 0; i < 4; ++i) { v0[i] = acc[ai][0][m][0][i]; v0[4 + i] = acc[ai][0][m][1][i]; v1[i] = acc[ai][1][m][0][i]; v1[4 + i] = acc[ai][1][m][1][i]; }
;                     if constexpr (RP) {
; #pragma unroll
;                         for (int i = 0; i < 8; ++i) { const float snd = hi ? v0[i] : v1[i];
;                             const float rcv = __builtin_bit_cast(float, __builtin_amdgcn_update_dpp(0, __builtin_bit_cast(int, snd), 0x128, 0xf, 0xf, false));
;     __device__ __forceinline__ Pre pre(const Unit& u, int r, int cit) const { const size_t off = (size_t)(u.arow0 + r) * D + u.pn * 256 + cit;
;         return Pre{__builtin_nontemporal_load((const v4u*)(pp + off)), __builtin_nontemporal_load((const v4u*)(pp + off + (size_t)8 * D)), *(const v4u*)(h + off), *(const v4u*)(h + off + (size_t)8 * D)}; }
;     __device__ __forceinline__ void post(const Unit& u, int r, int cit, const float* v0, const float* v1, const Pre& p) const {
;         const size_t off = (size_t)(u.arow0 + r) * D + u.pn * 256 + cit; float p0[8], p1[8], a[8], b[8]; unpack8bf(p.p0, p0); unpack8bf(p.p1, p1); unpack8bf(p.h0, a); unpack8bf(p.h1, b);
; #pragma unroll
;         for (int i = 0; i < 8; ++i) { a[i] += sigmoidf_(v0[i]) * p0[i]; b[i] += sigmoidf_(v1[i]) * p1[i]; }
;         store8bf(h + off, a); store8bf(h + off + (size_t)8 * D, b);
;     }
.LBB0_1746:
	s_and_b64 vcc, exec, s[8:9]
	s_cbranch_vccnz .LBB0_1748
	s_waitcnt vmcnt(14)
	s_nop 0
	v_cndmask_b32_e64 v144, v36, v44, s[0:1]
	v_mov_b32_e32 v145, 0
	s_nop 1
	v_mov_b32_dpp v145, v144 row_ror:8 row_mask:0xf bank_mask:0xf
	v_cndmask_b32_e64 v144, v37, v45, s[0:1]
	v_cndmask_b32_e64 v44, v44, v145, s[0:1]
	v_cndmask_b32_e64 v36, v145, v36, s[0:1]
	v_mov_b32_e32 v145, 0
	s_nop 1
	v_mov_b32_dpp v145, v144 row_ror:8 row_mask:0xf bank_mask:0xf
	v_cndmask_b32_e64 v144, v38, v46, s[0:1]
	v_cndmask_b32_e64 v45, v45, v145, s[0:1]
	v_cndmask_b32_e64 v145, v145, v37, s[0:1]
	v_mov_b32_e32 v37, 0
	s_nop 1
	v_mov_b32_dpp v37, v144 row_ror:8 row_mask:0xf bank_mask:0xf
	v_cndmask_b32_e64 v144, v39, v47, s[0:1]
	v_cndmask_b32_e64 v46, v46, v37, s[0:1]
	v_cndmask_b32_e64 v146, v37, v38, s[0:1]
	v_mov_b32_e32 v37, 0
	v_cndmask_b32_e64 v38, v32, v40, s[0:1]
	s_nop 0
	v_mov_b32_dpp v37, v144 row_ror:8 row_mask:0xf bank_mask:0xf
	v_cndmask_b32_e64 v47, v47, v37, s[0:1]
	v_cndmask_b32_e64 v144, v37, v39, s[0:1]
	v_mov_b32_e32 v37, 0
	s_nop 0
	v_and_b32_e32 v39, 0xffff0000, v104
	v_mov_b32_dpp v37, v38 row_ror:8 row_mask:0xf bank_mask:0xf
	v_cndmask_b32_e64 v38, v33, v41, s[0:1]
	v_cndmask_b32_e64 v148, v37, v32, s[0:1]
	v_mov_b32_e32 v32, 0
	v_cndmask_b32_e64 v147, v40, v37, s[0:1]
	v_cndmask_b32_e64 v37, v34, v42, s[0:1]
	v_mov_b32_dpp v32, v38 row_ror:8 row_mask:0xf bank_mask:0xf
	v_cndmask_b32_e64 v149, v41, v32, s[0:1]
	v_cndmask_b32_e64 v150, v32, v33, s[0:1]
	v_mov_b32_e32 v32, 0
	v_cndmask_b32_e64 v33, v35, v43, s[0:1]
	v_lshlrev_b32_e32 v38, 16, v104
	v_mov_b32_dpp v32, v37 row_ror:8 row_mask:0xf bank_mask:0xf
	v_cndmask_b32_e64 v152, v32, v34, s[0:1]
	v_mul_f32_e32 v34, 0xbfb8aa3b, v44
	v_exp_f32_e32 v34, v34
	v_cndmask_b32_e64 v151, v42, v32, s[0:1]
	v_mov_b32_e32 v32, 0
	v_and_b32_e32 v37, 0xffff0000, v108
	v_and_b32_e32 v41, 0xffff0000, v109
	v_mov_b32_dpp v32, v33 row_ror:8 row_mask:0xf bank_mask:0xf
	v_mul_f32_e32 v33, 0xbfb8aa3b, v36
	v_cndmask_b32_e64 v153, v43, v32, s[0:1]
	v_cndmask_b32_e64 v154, v32, v35, s[0:1]
	v_add_f32_e32 v32, 1.0, v34
	v_exp_f32_e32 v33, v33
	v_mul_f32_e32 v34, 0xbfb8aa3b, v45
	v_exp_f32_e32 v35, v34
	v_rcp_f32_e32 v32, v32
	v_add_f32_e32 v33, 1.0, v33
	v_rcp_f32_e32 v34, v33
	v_add_f32_e32 v33, 1.0, v35
	v_mul_f32_e32 v35, 0xbfb8aa3b, v145
	v_exp_f32_e32 v35, v35
	v_rcp_f32_e32 v33, v33
	v_lshlrev_b32_e32 v36, 16, v108
	v_lshlrev_b32_e32 v42, 16, v105
	v_add_f32_e32 v35, 1.0, v35
	v_rcp_f32_e32 v35, v35
	v_pk_fma_f32 v[32:33], v[32:33], v[36:37], v[38:39]
	v_mul_f32_e32 v38, 0xbfb8aa3b, v46
	v_lshlrev_b32_e32 v36, 16, v96
	v_and_b32_e32 v37, 0xffff0000, v96
	v_exp_f32_e32 v40, v38
	s_nop 0
	v_lshlrev_b32_e32 v38, 16, v100
	v_and_b32_e32 v39, 0xffff0000, v100
	v_pk_fma_f32 v[36:37], v[34:35], v[36:37], v[38:39]
	v_mul_f32_e32 v35, 0xbfb8aa3b, v146
	v_exp_f32_e32 v35, v35
	v_mul_f32_e32 v38, 0xbfb8aa3b, v47
	v_exp_f32_e32 v39, v38
	v_add_f32_e32 v34, 1.0, v40
	v_add_f32_e32 v35, 1.0, v35
	v_rcp_f32_e32 v38, v35
	v_add_f32_e32 v35, 1.0, v39
	v_mul_f32_e32 v39, 0xbfb8aa3b, v144
	v_exp_f32_e32 v39, v39
	v_rcp_f32_e32 v34, v34
	v_rcp_f32_e32 v35, v35
	v_lshlrev_b32_e32 v40, 16, v109
	v_add_f32_e32 v39, 1.0, v39
	v_rcp_f32_e32 v39, v39
	v_and_b32_e32 v43, 0xffff0000, v105
	v_pk_fma_f32 v[34:35], v[34:35], v[40:41], v[42:43]
	v_mul_f32_e32 v42, 0xbfb8aa3b, v147
	v_lshlrev_b32_e32 v40, 16, v97
	v_and_b32_e32 v41, 0xffff0000, v97
	v_exp_f32_e32 v44, v42
	v_lshlrev_b32_e32 v42, 16, v101
	v_and_b32_e32 v43, 0xffff0000, v101
	v_pk_fma_f32 v[38:39], v[38:39], v[40:41], v[42:43]
	v_mul_f32_e32 v41, 0xbfb8aa3b, v148
	v_exp_f32_e32 v41, v41
	v_mul_f32_e32 v42, 0xbfb8aa3b, v149
	v_exp_f32_e32 v43, v42
	v_add_f32_e32 v40, 1.0, v44
	v_add_f32_e32 v41, 1.0, v41
	v_rcp_f32_e32 v42, v41
	v_add_f32_e32 v41, 1.0, v43
	v_mul_f32_e32 v43, 0xbfb8aa3b, v150
	v_exp_f32_e32 v43, v43
	v_rcp_f32_e32 v40, v40
	v_rcp_f32_e32 v41, v41
	v_lshlrev_b32_e32 v44, 16, v110
	v_add_f32_e32 v43, 1.0, v43
	v_rcp_f32_e32 v43, v43
	v_and_b32_e32 v45, 0xffff0000, v110
	v_lshlrev_b32_e32 v46, 16, v106
	v_and_b32_e32 v47, 0xffff0000, v106
	v_pk_fma_f32 v[40:41], v[40:41], v[44:45], v[46:47]
	v_mul_f32_e32 v46, 0xbfb8aa3b, v151
	v_lshlrev_b32_e32 v44, 16, v98
	v_and_b32_e32 v45, 0xffff0000, v98
	v_exp_f32_e32 v96, v46
	v_lshlrev_b32_e32 v46, 16, v102
	v_and_b32_e32 v47, 0xffff0000, v102
	v_pk_fma_f32 v[42:43], v[42:43], v[44:45], v[46:47]
	v_mul_f32_e32 v45, 0xbfb8aa3b, v152
	v_exp_f32_e32 v45, v45
	v_mul_f32_e32 v46, 0xbfb8aa3b, v153
	v_exp_f32_e32 v47, v46
	v_add_f32_e32 v44, 1.0, v96
	v_add_f32_e32 v45, 1.0, v45
	v_rcp_f32_e32 v46, v45
	v_add_f32_e32 v45, 1.0, v47
	v_mul_f32_e32 v47, 0xbfb8aa3b, v154
	v_exp_f32_e32 v47, v47
	v_rcp_f32_e32 v44, v44
	v_rcp_f32_e32 v45, v45
	v_lshlrev_b32_e32 v96, 16, v111
	v_add_f32_e32 v47, 1.0, v47
	v_rcp_f32_e32 v47, v47
	v_and_b32_e32 v97, 0xffff0000, v111
	v_lshlrev_b32_e32 v100, 16, v107
	v_and_b32_e32 v101, 0xffff0000, v107
	v_pk_fma_f32 v[44:45], v[44:45], v[96:97], v[100:101]
	v_lshlrev_b32_e32 v96, 16, v99
	v_and_b32_e32 v97, 0xffff0000, v99
	v_lshlrev_b32_e32 v98, 16, v103
	v_and_b32_e32 v99, 0xffff0000, v103
	v_pk_fma_f32 v[46:47], v[46:47], v[96:97], v[98:99]
	v_add_u32_e32 v96, s62, v200
	v_ashrrev_i32_e32 v97, 31, v96
	v_lshlrev_b64 v[96:97], 12, v[96:97]
	v_lshl_add_u64 v[96:97], v[184:185], 0, v[96:97]
	v_cvt_pk_bf16_f32 v32, v32, v33
	v_cvt_pk_bf16_f32 v33, v34, v35
	v_cvt_pk_bf16_f32 v34, v40, v41
	v_cvt_pk_bf16_f32 v35, v44, v45
	global_store_dwordx4 v[96:97], v[32:35], off nt
	s_nop 1
	v_cvt_pk_bf16_f32 v32, v36, v37
	v_add_co_u32_e32 v36, vcc, 0x8000, v96
	v_cvt_pk_bf16_f32 v33, v38, v39
	v_cvt_pk_bf16_f32 v34, v42, v43
	v_cvt_pk_bf16_f32 v35, v46, v47
	v_addc_co_u32_e32 v37, vcc, 0, v97, vcc
	global_store_dwordx4 v[36:37], v[32:35], off nt
; template <class Epi, class Sched, bool GATHER, bool ALIGN_EPI = true, bool SP2 = true, bool REMAP64 = false>
; __device__ __forceinline__ void gemm_phase(LAS unsigned char* lds, const bf16* Ag, const bf16* Btg, const int K, const Sched& S, const Epi& E) {
;     ...
;             const bool hi = RP && (fr >= 8); const int rsh = hi ? -8 : 0, citx = hi ? cit + 32 : cit;
;             typename Epi::Pre pq[2];
;             { const int r0_ = wr * 64 + fr; pq[0] = E.pre(cur, (r0_ < cur.nrows ? r0_ : cur.nrows - 1) + rsh, citx); }
; #pragma unroll
;             for (int gq = 0; gq < 8; ++gq) { const int ai = gq >> 2, m = gq & 3, r = ai * HALF + wr * 64 + m * 16 + fr;
;                 if (gq + 1 < 8) { const int rn = ((gq + 1) >> 2) * HALF + wr * 64 + ((gq + 1) & 3) * 16 + fr; pq[(gq + 1) & 1] = E.pre(cur, (rn < cur.nrows ? rn : cur.nrows - 1) + rsh, citx); }
;                 __builtin_amdgcn_sched_barrier(0);
;                 if (r < cur.nrows) { float v0[8], v1[8];
; #pragma unroll
;                     for (int i = 0; i < 4; ++i) { v0[i] = acc[ai][0][m][0][i]; v0[4 + i] = acc[ai][0][m][1][i]; v1[i] = acc[ai][1][m][0][i]; v1[4 + i] = acc[ai][1][m][1][i]; }
;                     if constexpr (RP) {
; #pragma unroll
;                         for (int i = 0; i < 8; ++i) { const float snd = hi ? v0[i] : v1[i];
;                             const float rcv = __builtin_bit_cast(float, __builtin_amdgcn_update_dpp(0, __builtin_bit_cast(int, snd), 0x128, 0xf, 0xf, false));
;     __device__ __forceinline__ Pre pre(const Unit& u, int r, int cit) const { const size_t off = (size_t)(u.arow0 + r) * D + u.pn * 256 + cit;
;         return Pre{__builtin_nontemporal_load((const v4u*)(pp + off)), __builtin_nontemporal_load((const v4u*)(pp + off + (size_t)8 * D)), *(const v4u*)(h + off), *(const v4u*)(h + off + (size_t)8 * D)}; }
;     __device__ __forceinline__ void post(const Unit& u, int r, int cit, const float* v0, const float* v1, const Pre& p) const {
;         const size_t off = (size_t)(u.arow0 + r) * D + u.pn * 256 + cit; float p0[8], p1[8], a[8], b[8]; unpack8bf(p.p0, p0); unpack8bf(p.p1, p1); unpack8bf(p.h0, a); unpack8bf(p.h1, b);
; #pragma unroll
;         for (int i = 0; i < 8; ++i) { a[i] += sigmoidf_(v0[i]) * p0[i]; b[i] += sigmoidf_(v1[i]) * p1[i]; }
;         store8bf(h + off, a); store8bf(h + off + (size_t)8 * D, b);
;     }
.LBB0_1748:
	s_and_b64 vcc, exec, s[8:9]
	s_cbranch_vccnz .LBB0_1750
	s_waitcnt vmcnt(10)
	s_nop 0
	v_cndmask_b32_e64 v128, v20, v28, s[0:1]
	v_mov_b32_e32 v129, 0
	s_nop 1
	v_mov_b32_dpp v129, v128 row_ror:8 row_mask:0xf bank_mask:0xf
	v_cndmask_b32_e64 v128, v21, v29, s[0:1]
	v_cndmask_b32_e64 v28, v28, v129, s[0:1]
	v_cndmask_b32_e64 v20, v129, v20, s[0:1]
	v_mov_b32_e32 v129, 0
	s_nop 1
	v_mov_b32_dpp v129, v128 row_ror:8 row_mask:0xf bank_mask:0xf
	v_cndmask_b32_e64 v128, v22, v30, s[0:1]
	v_cndmask_b32_e64 v29, v29, v129, s[0:1]
	v_cndmask_b32_e64 v129, v129, v21, s[0:1]
	v_mov_b32_e32 v21, 0
	s_nop 1
	v_mov_b32_dpp v21, v128 row_ror:8 row_mask:0xf bank_mask:0xf
	v_cndmask_b32_e64 v128, v23, v31, s[0:1]
	v_cndmask_b32_e64 v30, v30, v21, s[0:1]
	v_cndmask_b32_e64 v130, v21, v22, s[0:1]
	v_mov_b32_e32 v21, 0
	v_cndmask_b32_e64 v22, v16, v24, s[0:1]
	s_nop 0
	v_mov_b32_dpp v21, v128 row_ror:8 row_mask:0xf bank_mask:0xf
	v_cndmask_b32_e64 v31, v31, v21, s[0:1]
	v_cndmask_b32_e64 v128, v21, v23, s[0:1]
	v_mov_b32_e32 v21, 0
	s_nop 0
	v_and_b32_e32 v23, 0xffff0000, v88
	v_mov_b32_dpp v21, v22 row_ror:8 row_mask:0xf bank_mask:0xf
	v_cndmask_b32_e64 v22, v17, v25, s[0:1]
	v_cndmask_b32_e64 v132, v21, v16, s[0:1]
	v_mov_b32_e32 v16, 0
	v_cndmask_b32_e64 v131, v24, v21, s[0:1]
	v_cndmask_b32_e64 v21, v18, v26, s[0:1]
	v_mov_b32_dpp v16, v22 row_ror:8 row_mask:0xf bank_mask:0xf
	v_cndmask_b32_e64 v133, v25, v16, s[0:1]
	v_cndmask_b32_e64 v134, v16, v17, s[0:1]
	v_mov_b32_e32 v16, 0
	v_cndmask_b32_e64 v17, v19, v27, s[0:1]
	v_lshlrev_b32_e32 v22, 16, v88
	v_mov_b32_dpp v16, v21 row_ror:8 row_mask:0xf bank_mask:0xf
	v_cndmask_b32_e64 v136, v16, v18, s[0:1]
	v_mul_f32_e32 v18, 0xbfb8aa3b, v28
	v_exp_f32_e32 v18, v18
	v_cndmask_b32_e64 v135, v26, v16, s[0:1]
	v_mov_b32_e32 v16, 0
	v_and_b32_e32 v21, 0xffff0000, v92
	v_and_b32_e32 v25, 0xffff0000, v93
	v_mov_b32_dpp v16, v17 row_ror:8 row_mask:0xf bank_mask:0xf
	v_mul_f32_e32 v17, 0xbfb8aa3b, v20
	v_cndmask_b32_e64 v137, v27, v16, s[0:1]
	v_cndmask_b32_e64 v138, v16, v19, s[0:1]
	v_add_f32_e32 v16, 1.0, v18
	v_exp_f32_e32 v17, v17
	v_mul_f32_e32 v18, 0xbfb8aa3b, v29
	v_exp_f32_e32 v19, v18
	v_rcp_f32_e32 v16, v16
	v_add_f32_e32 v17, 1.0, v17
	v_rcp_f32_e32 v18, v17
	v_add_f32_e32 v17, 1.0, v19
	v_mul_f32_e32 v19, 0xbfb8aa3b, v129
	v_exp_f32_e32 v19, v19
	v_rcp_f32_e32 v17, v17
	v_lshlrev_b32_e32 v20, 16, v92
	v_lshlrev_b32_e32 v26, 16, v89
	v_add_f32_e32 v19, 1.0, v19
	v_rcp_f32_e32 v19, v19
	v_pk_fma_f32 v[16:17], v[16:17], v[20:21], v[22:23]
	v_mul_f32_e32 v22, 0xbfb8aa3b, v30
	v_lshlrev_b32_e32 v20, 16, v80
	v_and_b32_e32 v21, 0xffff0000, v80
	v_exp_f32_e32 v24, v22
	s_nop 0
	v_lshlrev_b32_e32 v22, 16, v84
	v_and_b32_e32 v23, 0xffff0000, v84
	v_pk_fma_f32 v[20:21], v[18:19], v[20:21], v[22:23]
	v_mul_f32_e32 v19, 0xbfb8aa3b, v130
	v_exp_f32_e32 v19, v19
	v_mul_f32_e32 v22, 0xbfb8aa3b, v31
	v_exp_f32_e32 v23, v22
	v_add_f32_e32 v18, 1.0, v24
	v_add_f32_e32 v19, 1.0, v19
	v_rcp_f32_e32 v22, v19
	v_add_f32_e32 v19, 1.0, v23
	v_mul_f32_e32 v23, 0xbfb8aa3b, v128
	v_exp_f32_e32 v23, v23
	v_rcp_f32_e32 v18, v18
	v_rcp_f32_e32 v19, v19
	v_lshlrev_b32_e32 v24, 16, v93
	v_add_f32_e32 v23, 1.0, v23
	v_rcp_f32_e32 v23, v23
	v_and_b32_e32 v27, 0xffff0000, v89
	v_pk_fma_f32 v[18:19], v[18:19], v[24:25], v[26:27]
	v_mul_f32_e32 v26, 0xbfb8aa3b, v131
	v_lshlrev_b32_e32 v24, 16, v81
	v_and_b32_e32 v25, 0xffff0000, v81
	v_exp_f32_e32 v28, v26
	v_lshlrev_b32_e32 v26, 16, v85
	v_and_b32_e32 v27, 0xffff0000, v85
	v_pk_fma_f32 v[22:23], v[22:23], v[24:25], v[26:27]
	v_mul_f32_e32 v25, 0xbfb8aa3b, v132
	v_exp_f32_e32 v25, v25
	v_mul_f32_e32 v26, 0xbfb8aa3b, v133
	v_exp_f32_e32 v27, v26
	v_add_f32_e32 v24, 1.0, v28
	v_add_f32_e32 v25, 1.0, v25
	v_rcp_f32_e32 v26, v25
	v_add_f32_e32 v25, 1.0, v27
	v_mul_f32_e32 v27, 0xbfb8aa3b, v134
	v_exp_f32_e32 v27, v27
	v_rcp_f32_e32 v24, v24
	v_rcp_f32_e32 v25, v25
	v_lshlrev_b32_e32 v28, 16, v94
	v_add_f32_e32 v27, 1.0, v27
	v_rcp_f32_e32 v27, v27
	v_and_b32_e32 v29, 0xffff0000, v94
	v_lshlrev_b32_e32 v30, 16, v90
	v_and_b32_e32 v31, 0xffff0000, v90
	v_pk_fma_f32 v[24:25], v[24:25], v[28:29], v[30:31]
	v_mul_f32_e32 v30, 0xbfb8aa3b, v135
	v_lshlrev_b32_e32 v28, 16, v82
	v_and_b32_e32 v29, 0xffff0000, v82
	v_exp_f32_e32 v80, v30
	v_lshlrev_b32_e32 v30, 16, v86
	v_and_b32_e32 v31, 0xffff0000, v86
	v_pk_fma_f32 v[26:27], v[26:27], v[28:29], v[30:31]
	v_mul_f32_e32 v29, 0xbfb8aa3b, v136
	v_exp_f32_e32 v29, v29
	v_mul_f32_e32 v30, 0xbfb8aa3b, v137
	v_exp_f32_e32 v31, v30
	v_add_f32_e32 v28, 1.0, v80
	v_add_f32_e32 v29, 1.0, v29
	v_rcp_f32_e32 v30, v29
	v_add_f32_e32 v29, 1.0, v31
	v_mul_f32_e32 v31, 0xbfb8aa3b, v138
	v_exp_f32_e32 v31, v31
	v_rcp_f32_e32 v28, v28
	v_rcp_f32_e32 v29, v29
	v_lshlrev_b32_e32 v80, 16, v95
	v_add_f32_e32 v31, 1.0, v31
	v_rcp_f32_e32 v31, v31
	v_and_b32_e32 v81, 0xffff0000, v95
	v_lshlrev_b32_e32 v84, 16, v91
	v_and_b32_e32 v85, 0xffff0000, v91
	v_pk_fma_f32 v[28:29], v[28:29], v[80:81], v[84:85]
	v_lshlrev_b32_e32 v80, 16, v83
	v_and_b32_e32 v81, 0xffff0000, v83
	v_lshlrev_b32_e32 v82, 16, v87
	v_and_b32_e32 v83, 0xffff0000, v87
	v_pk_fma_f32 v[30:31], v[30:31], v[80:81], v[82:83]
	v_add_u32_e32 v80, s63, v200
	v_ashrrev_i32_e32 v81, 31, v80
	v_lshlrev_b64 v[80:81], 12, v[80:81]
	v_lshl_add_u64 v[80:81], v[184:185], 0, v[80:81]
	v_cvt_pk_bf16_f32 v16, v16, v17
	v_cvt_pk_bf16_f32 v17, v18, v19
	v_cvt_pk_bf16_f32 v18, v24, v25
	v_cvt_pk_bf16_f32 v19, v28, v29
	global_store_dwordx4 v[80:81], v[16:19], off nt
	s_nop 1
	v_cvt_pk_bf16_f32 v16, v20, v21
	v_add_co_u32_e32 v20, vcc, 0x8000, v80
	v_cvt_pk_bf16_f32 v17, v22, v23
	v_cvt_pk_bf16_f32 v18, v26, v27
	v_cvt_pk_bf16_f32 v19, v30, v31
	v_addc_co_u32_e32 v21, vcc, 0, v81, vcc
	global_store_dwordx4 v[20:21], v[16:19], off nt
; template <class Epi, class Sched, bool GATHER, bool ALIGN_EPI = true, bool SP2 = true, bool REMAP64 = false>
; __device__ __forceinline__ void gemm_phase(LAS unsigned char* lds, const bf16* Ag, const bf16* Btg, const int K, const Sched& S, const Epi& E) {
;     ...
;             const bool hi = RP && (fr >= 8); const int rsh = hi ? -8 : 0, citx = hi ? cit + 32 : cit;
;             typename Epi::Pre pq[2];
;             { const int r0_ = wr * 64 + fr; pq[0] = E.pre(cur, (r0_ < cur.nrows ? r0_ : cur.nrows - 1) + rsh, citx); }
; #pragma unroll
;             for (int gq = 0; gq < 8; ++gq) { const int ai = gq >> 2, m = gq & 3, r = ai * HALF + wr * 64 + m * 16 + fr;
;                 if (gq + 1 < 8) { const int rn = ((gq + 1) >> 2) * HALF + wr * 64 + ((gq + 1) & 3) * 16 + fr; pq[(gq + 1) & 1] = E.pre(cur, (rn < cur.nrows ? rn : cur.nrows - 1) + rsh, citx); }
;                 __builtin_amdgcn_sched_barrier(0);
;                 if (r < cur.nrows) { float v0[8], v1[8];
; #pragma unroll
;                     for (int i = 0; i < 4; ++i) { v0[i] = acc[ai][0][m][0][i]; v0[4 + i] = acc[ai][0][m][1][i]; v1[i] = acc[ai][1][m][0][i]; v1[4 + i] = acc[ai][1][m][1][i]; }
;                     if constexpr (RP) {
; #pragma unroll
;                         for (int i = 0; i < 8; ++i) { const float snd = hi ? v0[i] : v1[i];
;                             const float rcv = __builtin_bit_cast(float, __builtin_amdgcn_update_dpp(0, __builtin_bit_cast(int, snd), 0x128, 0xf, 0xf, false));
;     __device__ __forceinline__ Pre pre(const Unit& u, int r, int cit) const { const size_t off = (size_t)(u.arow0 + r) * D + u.pn * 256 + cit;
;         return Pre{__builtin_nontemporal_load((const v4u*)(pp + off)), __builtin_nontemporal_load((const v4u*)(pp + off + (size_t)8 * D)), *(const v4u*)(h + off), *(const v4u*)(h + off + (size_t)8 * D)}; }
;     __device__ __forceinline__ void post(const Unit& u, int r, int cit, const float* v0, const float* v1, const Pre& p) const {
;         const size_t off = (size_t)(u.arow0 + r) * D + u.pn * 256 + cit; float p0[8], p1[8], a[8], b[8]; unpack8bf(p.p0, p0); unpack8bf(p.p1, p1); unpack8bf(p.h0, a); unpack8bf(p.h1, b);
; #pragma unroll
;         for (int i = 0; i < 8; ++i) { a[i] += sigmoidf_(v0[i]) * p0[i]; b[i] += sigmoidf_(v1[i]) * p1[i]; }
;         store8bf(h + off, a); store8bf(h + off + (size_t)8 * D, b);
;     }
.LBB0_1750:
	s_and_b64 vcc, exec, s[8:9]
	s_cbranch_vccnz .LBB0_1752
	s_waitcnt vmcnt(6)
	v_cndmask_b32_e64 v16, v4, v12, s[0:1]
	v_mov_b32_e32 v17, 0
	s_nop 1
	v_mov_b32_dpp v17, v16 row_ror:8 row_mask:0xf bank_mask:0xf
	v_cndmask_b32_e64 v16, v5, v13, s[0:1]
	v_cndmask_b32_e64 v12, v12, v17, s[0:1]
	v_cndmask_b32_e64 v4, v17, v4, s[0:1]
	v_mov_b32_e32 v17, 0
	s_nop 1
	v_mov_b32_dpp v17, v16 row_ror:8 row_mask:0xf bank_mask:0xf
	v_cndmask_b32_e64 v16, v6, v14, s[0:1]
	v_cndmask_b32_e64 v13, v13, v17, s[0:1]
	v_cndmask_b32_e64 v17, v17, v5, s[0:1]
	v_mov_b32_e32 v5, 0
	s_nop 1
	v_mov_b32_dpp v5, v16 row_ror:8 row_mask:0xf bank_mask:0xf
	v_cndmask_b32_e64 v16, v7, v15, s[0:1]
	v_cndmask_b32_e64 v14, v14, v5, s[0:1]
	v_cndmask_b32_e64 v18, v5, v6, s[0:1]
	v_mov_b32_e32 v5, 0
	v_cndmask_b32_e64 v6, v0, v8, s[0:1]
	s_nop 0
	v_mov_b32_dpp v5, v16 row_ror:8 row_mask:0xf bank_mask:0xf
	v_cndmask_b32_e64 v15, v15, v5, s[0:1]
	v_cndmask_b32_e64 v16, v5, v7, s[0:1]
	v_mov_b32_e32 v5, 0
	s_nop 0
	v_and_b32_e32 v7, 0xffff0000, v72
	v_mov_b32_dpp v5, v6 row_ror:8 row_mask:0xf bank_mask:0xf
	v_cndmask_b32_e64 v6, v1, v9, s[0:1]
	v_cndmask_b32_e64 v20, v5, v0, s[0:1]
	v_mov_b32_e32 v0, 0
	v_cndmask_b32_e64 v19, v8, v5, s[0:1]
	v_cndmask_b32_e64 v5, v2, v10, s[0:1]
	v_mov_b32_dpp v0, v6 row_ror:8 row_mask:0xf bank_mask:0xf
	v_cndmask_b32_e64 v21, v9, v0, s[0:1]
	v_cndmask_b32_e64 v22, v0, v1, s[0:1]
	v_mov_b32_e32 v0, 0
	v_cndmask_b32_e64 v1, v3, v11, s[0:1]
	v_lshlrev_b32_e32 v6, 16, v72
	v_mov_b32_dpp v0, v5 row_ror:8 row_mask:0xf bank_mask:0xf
	v_cndmask_b32_e64 v24, v0, v2, s[0:1]
	v_mul_f32_e32 v2, 0xbfb8aa3b, v12
	v_exp_f32_e32 v2, v2
	v_cndmask_b32_e64 v23, v10, v0, s[0:1]
	v_mov_b32_e32 v0, 0
	v_and_b32_e32 v5, 0xffff0000, v76
	v_and_b32_e32 v9, 0xffff0000, v77
	v_mov_b32_dpp v0, v1 row_ror:8 row_mask:0xf bank_mask:0xf
	v_mul_f32_e32 v1, 0xbfb8aa3b, v4
	v_cndmask_b32_e64 v25, v11, v0, s[0:1]
	v_cndmask_b32_e64 v26, v0, v3, s[0:1]
	v_add_f32_e32 v0, 1.0, v2
	v_exp_f32_e32 v1, v1
	v_mul_f32_e32 v2, 0xbfb8aa3b, v13
	v_exp_f32_e32 v3, v2
	v_rcp_f32_e32 v0, v0
	v_add_f32_e32 v1, 1.0, v1
	v_rcp_f32_e32 v2, v1
	v_add_f32_e32 v1, 1.0, v3
	v_mul_f32_e32 v3, 0xbfb8aa3b, v17
	v_exp_f32_e32 v3, v3
	v_rcp_f32_e32 v1, v1
	v_lshlrev_b32_e32 v4, 16, v76
	v_lshlrev_b32_e32 v10, 16, v73
	v_add_f32_e32 v3, 1.0, v3
	v_rcp_f32_e32 v3, v3
	v_pk_fma_f32 v[0:1], v[0:1], v[4:5], v[6:7]
	v_mul_f32_e32 v6, 0xbfb8aa3b, v14
	v_lshlrev_b32_e32 v4, 16, v64
	v_and_b32_e32 v5, 0xffff0000, v64
	v_exp_f32_e32 v8, v6
	s_nop 0
	v_lshlrev_b32_e32 v6, 16, v68
	v_and_b32_e32 v7, 0xffff0000, v68
	v_pk_fma_f32 v[4:5], v[2:3], v[4:5], v[6:7]
	v_mul_f32_e32 v3, 0xbfb8aa3b, v18
	v_exp_f32_e32 v3, v3
	v_mul_f32_e32 v6, 0xbfb8aa3b, v15
	v_exp_f32_e32 v7, v6
	v_add_f32_e32 v2, 1.0, v8
	v_add_f32_e32 v3, 1.0, v3
	v_rcp_f32_e32 v6, v3
	v_add_f32_e32 v3, 1.0, v7
	v_mul_f32_e32 v7, 0xbfb8aa3b, v16
	v_exp_f32_e32 v7, v7
	v_rcp_f32_e32 v2, v2
	v_rcp_f32_e32 v3, v3
	v_lshlrev_b32_e32 v8, 16, v77
	v_add_f32_e32 v7, 1.0, v7
	v_rcp_f32_e32 v7, v7
	v_and_b32_e32 v11, 0xffff0000, v73
	v_pk_fma_f32 v[2:3], v[2:3], v[8:9], v[10:11]
	v_mul_f32_e32 v10, 0xbfb8aa3b, v19
	v_lshlrev_b32_e32 v8, 16, v65
	v_and_b32_e32 v9, 0xffff0000, v65
	v_exp_f32_e32 v12, v10
	v_lshlrev_b32_e32 v10, 16, v69
	v_and_b32_e32 v11, 0xffff0000, v69
	v_pk_fma_f32 v[6:7], v[6:7], v[8:9], v[10:11]
	v_mul_f32_e32 v9, 0xbfb8aa3b, v20
	v_exp_f32_e32 v9, v9
	v_mul_f32_e32 v10, 0xbfb8aa3b, v21
	v_exp_f32_e32 v11, v10
	v_add_f32_e32 v8, 1.0, v12
	v_add_f32_e32 v9, 1.0, v9
	v_rcp_f32_e32 v10, v9
	v_add_f32_e32 v9, 1.0, v11
	v_mul_f32_e32 v11, 0xbfb8aa3b, v22
	v_exp_f32_e32 v11, v11
	v_rcp_f32_e32 v8, v8
	v_rcp_f32_e32 v9, v9
	v_lshlrev_b32_e32 v12, 16, v78
	v_add_f32_e32 v11, 1.0, v11
	v_rcp_f32_e32 v11, v11
	v_and_b32_e32 v13, 0xffff0000, v78
	v_lshlrev_b32_e32 v14, 16, v74
	v_and_b32_e32 v15, 0xffff0000, v74
	v_pk_fma_f32 v[8:9], v[8:9], v[12:13], v[14:15]
	v_mul_f32_e32 v14, 0xbfb8aa3b, v23
	v_lshlrev_b32_e32 v12, 16, v66
	v_and_b32_e32 v13, 0xffff0000, v66
	v_exp_f32_e32 v16, v14
	v_lshlrev_b32_e32 v14, 16, v70
	v_and_b32_e32 v15, 0xffff0000, v70
	v_pk_fma_f32 v[10:11], v[10:11], v[12:13], v[14:15]
	v_mul_f32_e32 v13, 0xbfb8aa3b, v24
	v_exp_f32_e32 v13, v13
	v_mul_f32_e32 v14, 0xbfb8aa3b, v25
	v_exp_f32_e32 v15, v14
	v_add_f32_e32 v12, 1.0, v16
	v_add_f32_e32 v13, 1.0, v13
	v_rcp_f32_e32 v14, v13
	v_add_f32_e32 v13, 1.0, v15
	v_mul_f32_e32 v15, 0xbfb8aa3b, v26
	v_exp_f32_e32 v15, v15
	v_rcp_f32_e32 v12, v12
	v_rcp_f32_e32 v13, v13
	v_lshlrev_b32_e32 v16, 16, v79
	v_add_f32_e32 v15, 1.0, v15
	v_rcp_f32_e32 v15, v15
	v_and_b32_e32 v17, 0xffff0000, v79
	v_lshlrev_b32_e32 v18, 16, v75
	v_and_b32_e32 v19, 0xffff0000, v75
	v_pk_fma_f32 v[12:13], v[12:13], v[16:17], v[18:19]
	v_lshlrev_b32_e32 v16, 16, v67
	v_and_b32_e32 v17, 0xffff0000, v67
	v_lshlrev_b32_e32 v18, 16, v71
	v_and_b32_e32 v19, 0xffff0000, v71
	v_pk_fma_f32 v[14:15], v[14:15], v[16:17], v[18:19]
	v_add_u32_e32 v16, s64, v200
	v_ashrrev_i32_e32 v17, 31, v16
	v_lshlrev_b64 v[16:17], 12, v[16:17]
	v_lshl_add_u64 v[16:17], v[184:185], 0, v[16:17]
	v_cvt_pk_bf16_f32 v0, v0, v1
	v_cvt_pk_bf16_f32 v1, v2, v3
	v_cvt_pk_bf16_f32 v2, v8, v9
	v_cvt_pk_bf16_f32 v3, v12, v13
	global_store_dwordx4 v[16:17], v[0:3], off nt
	s_nop 1
	v_cvt_pk_bf16_f32 v0, v4, v5
	v_add_co_u32_e32 v4, vcc, 0x8000, v16
	v_cvt_pk_bf16_f32 v1, v6, v7
	v_cvt_pk_bf16_f32 v2, v10, v11
	v_cvt_pk_bf16_f32 v3, v14, v15
	v_addc_co_u32_e32 v5, vcc, 0, v17, vcc
	global_store_dwordx4 v[4:5], v[0:3], off nt
